# GEMM units: lagging wave half no longer waits for the leading half's epilogue (lag barrier moved in front of each K loop)
# speedup vs baseline: 1.0143x; 1.0024x over previous
; #define PG8_BAR __builtin_amdgcn_s_barrier()
; template <class Epi, class Sched>
; __device__ __forceinline__ void gemm_phase(LAS unsigned char* lds, const bf16_t* A, const int K, const Sched& S, const Epi& E, const int wv) {
;     int tid = mk_tid(wv); asm volatile("" : "+v"(tid));
;     const int wid = __builtin_amdgcn_readfirstlane(tid >> 6), lane = tid & 63, wr = wid >> 2, wc = wid & 3, fr = lane & 15, fq = lane >> 4;
;     const int nt = K / BK;
;     unsigned voffA[2], voffB[2];
; #pragma unroll
;     for (int i = 0; i < 2; ++i) { int R, C; stage_rc(tid * 16 + i * 8192, R, C); const int Rb = Epi::PERM ? ((R & ~31) + perm32(R & 31)) : R;
;         voffA[i] = (unsigned)(R * K + C) * 2u; voffB[i] = (unsigned)(Rb * K + C) * 2u; }
;     const size_t kstep = (size_t)(BK * 2);
;     const size_t hstep = (size_t)HALF * K * 2;
;     const size_t tstep = 2 * hstep;
;     const unsigned ldsw = (unsigned)wid * 1024u;
;     const int aoff = lds_byte(wr * 64 + fr, fq * 8), boff = lds_byte(wc * 32 + fr, fq * 8);
;     Unit cur, nxt; int ui = 0;
;     if (!S.next(0, cur)) return;
;     f32x4 acc[2][2][4][2];
; #pragma unroll
;     for (int a_ = 0; a_ < 2; ++a_)
; #pragma unroll
;         for (int b_ = 0; b_ < 2; ++b_)
; #pragma unroll
;             for (int m = 0; m < 4; ++m)
; #pragma unroll
;                 for (int n = 0; n < 2; ++n) acc[a_][b_][m][n] = (f32x4){0.f, 0.f, 0.f, 0.f};
;     bf16x8 At[4][2], B0[2][2], B1[2][2];
;     unsigned ao0[2] = {0u, 0u}, ao1[2] = {0u, 0u}, no0[2] = {0u, 0u}, no1[2] = {0u, 0u};
;     const char* Ab = (const char*)A;
;     const char* cA = Ab; const char* nA = Ab;
;     if constexpr (Sched::GATHER) {
; #pragma unroll
;         for (int i = 0; i < 2; ++i) { int R, C; stage_rc(tid * 16 + i * 8192, R, C);
;             ao0[i] = (S.arow(cur, R) * (unsigned)K + (unsigned)C) * 2u; ao1[i] = (S.arow(cur, HALF + R) * (unsigned)K + (unsigned)C) * 2u; }
;     } else cA = Ab + (size_t)cur.pm * tstep;
;     const char* cB = S.bptr(cur);
;     PG8_STAGE(PG8_SB(0, 0), cB, voffB); PG8_STAGE_A(PG8_SA(0, 0), 0, false, 0); PG8_STAGE(PG8_SB(0, 1), cB + hstep, voffB); PG8_STAGE_A(PG8_SA(0, 1), 1, false, 0);
;     if (wr == 1) PG8_BAR;
;     PG8_WAIT_V(4); PG8_BAR;
;     PG8_STAGE(PG8_SB(1, 0), cB + kstep, voffB); PG8_STAGE_A(PG8_SA(1, 0), 0, false, kstep); PG8_STAGE(PG8_SB(1, 1), cB + hstep + kstep, voffB);
;     PG8_WAIT_V(6); PG8_BAR;
.LBB0_310:
	s_andn2_b64 vcc, exec, s[0:1]
	s_cbranch_vccnz .LBB0_575
	v_ashrrev_i32_e32 v1, 31, v8
	v_lshrrev_b32_e32 v1, 26, v1
	v_add_u32_e32 v1, v8, v1
	v_ashrrev_i32_e32 v9, 6, v1
	v_bfe_i32 v1, v8, 27, 1
	v_lshlrev_b32_e32 v0, 4, v8
	v_lshrrev_b32_e32 v1, 22, v1
	v_add_u32_e32 v1, v0, v1
	v_and_b32_e32 v1, 0xfffffc00, v1
	v_sub_u32_e32 v1, v0, v1
	v_lshrrev_b32_e32 v2, 4, v1
	v_bitop3_b32 v1, v2, v1, 32 bitop3:0x6c
	v_ashrrev_i32_e32 v3, 31, v1
	v_lshrrev_b32_e32 v3, 26, v3
	v_add_u32_e32 v3, v1, v3
	v_lshlrev_b32_e32 v2, 3, v9
	v_ashrrev_i32_e32 v10, 6, v3
	v_and_b32_e32 v3, 0xc0, v3
	v_and_b32_e32 v2, -16, v2
	v_sub_u32_e32 v1, v1, v3
	v_mov_b32_e32 v3, 1
	v_add_u32_e32 v2, v10, v2
	v_ashrrev_i16_sdwa v1, v3, sext(v1) dst_sel:DWORD dst_unused:UNUSED_PAD src0_sel:DWORD src1_sel:BYTE_0
	v_lshlrev_b32_e32 v4, 5, v9
	v_bfe_i32 v11, v1, 0, 16
	v_lshlrev_b32_e32 v1, 1, v2
	v_lshrrev_b32_e32 v5, 2, v2
	v_and_b32_e32 v6, 3, v10
	s_mov_b32 s1, 0xfffe0
	v_and_b32_e32 v4, 32, v4
	v_and_b32_e32 v1, 24, v1
	v_and_b32_e32 v5, 4, v5
	v_and_or_b32 v6, v2, s1, v6
	v_or3_b32 v1, v6, v5, v1
	v_add_lshl_u32 v4, v4, v11, 1
	v_add_u32_e32 v0, 0x2000, v0
	v_lshl_add_u32 v162, v1, 12, v4
	v_ashrrev_i32_e32 v1, 31, v0
	v_lshrrev_b32_e32 v1, 22, v1
	v_add_u32_e32 v1, v0, v1
	v_ashrrev_i32_e32 v12, 10, v1
	v_mul_i32_i24_e32 v1, 0x400, v12
	v_sub_u32_e32 v0, v0, v1
	v_lshrrev_b32_e32 v1, 4, v0
	v_bitop3_b32 v0, v1, v0, 32 bitop3:0x6c
	v_lshl_add_u32 v160, v2, 12, v4
	v_ashrrev_i32_e32 v2, 31, v0
	v_lshrrev_b32_e32 v2, 26, v2
	s_add_u32 s60, s76, 0x188000
	v_add_u32_e32 v2, v0, v2
	s_addc_u32 s61, s77, 0
	v_lshlrev_b32_e32 v1, 3, v12
	v_ashrrev_i32_e32 v13, 6, v2
	v_and_b32_e32 v2, 0xc0, v2
	s_add_u32 s62, s76, 0x3c188000
	v_and_b32_e32 v1, -16, v1
	v_sub_u32_e32 v0, v0, v2
	s_addc_u32 s63, s77, 0
	s_ashr_i32 s0, s35, 6
	v_add_u32_e32 v1, v13, v1
	v_ashrrev_i16_sdwa v0, v3, sext(v0) dst_sel:DWORD dst_unused:UNUSED_PAD src0_sel:DWORD src1_sel:BYTE_0
	v_and_b32_e32 v3, 3, v13
	s_ashr_i32 s17, s16, 31
	s_ashr_i32 s15, s14, 31
	v_and_or_b32 v3, v1, s1, v3
	s_ashr_i32 s1, s35, 8
	s_lshl_b32 s64, s0, 10
	s_lshl_b64 s[2:3], s[16:17], 20
	s_lshl_b64 s[4:5], s[14:15], 20
	s_add_u32 s24, s60, s4
	v_lshlrev_b32_e32 v4, 5, v12
	v_bfe_i32 v14, v0, 0, 16
	v_lshlrev_b32_e32 v0, 1, v1
	v_lshrrev_b32_e32 v2, 2, v1
	s_addc_u32 s25, s61, s5
	s_add_i32 s65, s64, 0
	v_and_b32_e32 v4, 32, v4
	v_and_b32_e32 v0, 24, v0
	v_and_b32_e32 v2, 4, v2
	s_add_i32 m0, s65, 0x10000
	v_or3_b32 v0, v3, v2, v0
	v_add_lshl_u32 v2, v4, v14, 1
	global_load_lds_dwordx4 v162, s[24:25]
	s_add_i32 m0, s65, 0x12000
	v_lshl_add_u32 v166, v0, 12, v2
	s_add_u32 s28, s62, s2
	global_load_lds_dwordx4 v166, s[24:25]
	s_addc_u32 s29, s63, s3
	s_mov_b32 m0, s65
	s_add_i32 s66, s65, 0x2000
	v_lshl_add_u32 v164, v1, 12, v2
	global_load_lds_dwordx4 v160, s[28:29]
	s_mov_b32 m0, s66
	s_add_u32 s2, s24, 0x80000
	global_load_lds_dwordx4 v164, s[28:29]
	s_addc_u32 s3, s25, 0
	s_add_i32 m0, s65, 0x14000
	v_mov_b32_e32 v169, 0
	global_load_lds_dwordx4 v162, s[2:3]
	s_add_i32 m0, s65, 0x16000
	v_mov_b32_e32 v163, v169
	global_load_lds_dwordx4 v166, s[2:3]
	s_add_u32 s2, s28, 0x80000
	s_addc_u32 s3, s29, 0
	s_add_i32 s67, s65, 0x4000
	s_mov_b32 m0, s67
	s_add_i32 s68, s65, 0x6000
	global_load_lds_dwordx4 v160, s[2:3]
	s_mov_b32 m0, s68
	v_mov_b32_e32 v167, v169
	global_load_lds_dwordx4 v164, s[2:3]
	v_mov_b32_e32 v161, v169
	v_mov_b32_e32 v165, v169
	s_mov_b32 s19, 0
	v_lshl_add_u64 v[6:7], s[24:25], 0, v[162:163]
	v_lshl_add_u64 v[4:5], s[24:25], 0, v[166:167]
	v_lshl_add_u64 v[2:3], s[28:29], 0, v[160:161]
	s_cmp_lg_u32 s1, 1
	v_lshl_add_u64 v[0:1], s[28:29], 0, v[164:165]
	s_cbranch_scc1 .LBB0_313
.LBB0_313:
	s_add_u32 s20, s76, 0xc8000
	s_addc_u32 s21, s77, 0
	s_add_u32 s22, s76, 0x4c188000
	s_mov_b64 s[26:27], 0x80
	s_addc_u32 s23, s77, 0
	s_and_b32 s4, s0, 3
	s_add_i32 m0, s65, 0x18000
	v_lshl_add_u64 v[6:7], v[6:7], 0, s[26:27]
	s_lshl_b32 s69, s1, 6
	s_lshl_b32 s2, s1, 13
	s_lshl_b32 s3, s4, 12
	s_waitcnt vmcnt(4)
	s_barrier
	global_load_lds_dwordx4 v[6:7], off
	v_lshl_add_u64 v[4:5], v[4:5], 0, s[26:27]
	s_add_i32 m0, s65, 0x1a000
	s_add_i32 s70, s65, 0x8000
	s_add_i32 s71, s65, 0xa000
	global_load_lds_dwordx4 v[4:5], off
	v_lshl_add_u64 v[2:3], v[2:3], 0, s[26:27]
	s_mov_b32 m0, s70
	s_add_u32 s0, s24, 0x80080
	global_load_lds_dwordx4 v[2:3], off
	v_lshl_add_u64 v[0:1], v[0:1], 0, s[26:27]
	s_mov_b32 m0, s71
	s_addc_u32 s1, s25, 0
	global_load_lds_dwordx4 v[0:1], off
	s_add_i32 m0, s65, 0x1c000
	v_lshl_add_u64 v[0:1], s[0:1], 0, v[162:163]
	global_load_lds_dwordx4 v[0:1], off
	v_lshl_add_u64 v[0:1], s[0:1], 0, v[166:167]
	s_add_i32 m0, s65, 0x1e000
	s_mov_b64 s[6:7], 0x108000
	global_load_lds_dwordx4 v[0:1], off
	v_bfe_u32 v0, v8, 4, 2
	v_lshlrev_b32_e32 v1, 3, v0
	v_lshl_or_b32 v170, s4, 5, v1
	v_and_b32_e32 v172, 8, v1
	v_lshlrev_b32_e32 v168, 1, v170
	v_lshl_add_u64 v[174:175], s[76:77], 0, v[168:169]
	v_lshlrev_b32_e32 v168, 2, v172
	v_lshl_add_u64 v[176:177], s[20:21], 0, v[168:169]
	v_lshlrev_b32_e32 v168, 2, v170
	v_lshlrev_b32_e32 v2, 4, v0
	v_cmp_gt_u32_e64 s[0:1], 2, v0
	v_lshl_add_u64 v[0:1], s[76:77], 0, v[168:169]
	v_lshl_add_u64 v[178:179], v[0:1], 0, s[6:7]
	v_lshlrev_b32_e32 v0, 15, v9
	v_and_b32_e32 v0, 0xffff0000, v0
	v_lshl_add_u32 v0, v10, 12, v0
	v_and_b32_e32 v1, 1, v9
	v_lshl_or_b32 v0, v1, 6, v0
	v_lshl_add_u32 v168, v11, 1, v0
	v_lshlrev_b32_e32 v0, 15, v12
	v_and_b32_e32 v171, 15, v8
	v_lshlrev_b32_e32 v3, 2, v8
	v_and_b32_e32 v0, 0xffff0000, v0
	v_lshl_or_b32 v2, v171, 6, v2
	v_and_b32_e32 v3, 32, v3
	v_lshl_add_u32 v0, v13, 12, v0
	v_and_b32_e32 v1, 1, v12
	v_bitop3_b32 v4, v2, s2, v3 bitop3:0xde
	v_bitop3_b32 v173, v2, s3, v3 bitop3:0xde
	s_mov_b64 s[2:3], 0x80080
	s_waitcnt vmcnt(6)
	s_cmp_eq_u32 s4, 0
	v_lshl_or_b32 v0, v1, 6, v0
	s_cselect_b64 s[30:31], -1, 0
	s_mov_b64 s[6:7], 0x44188000
	v_lshl_add_u64 v[182:183], v[168:169], 0, s[2:3]
	v_lshl_add_u32 v168, v14, 1, v0
	s_add_i32 s74, 0, 0x10000
	s_add_i32 s75, 0, 0x14000
	v_mbcnt_lo_u32_b32 v0, -1, 0
	v_cmp_eq_u32_e64 s[4:5], 0, v171
	s_waitcnt lgkmcnt(0)
	s_ashr_i32 s72, s93, 31
	s_ashr_i32 s73, s94, 31
	v_lshl_add_u64 v[180:181], v[174:175], 0, s[6:7]
	v_lshl_add_u64 v[184:185], v[168:169], 0, s[2:3]
	v_mov_b64_e32 v[186:187], 0x600
	v_mov_b64_e32 v[188:189], 0x5ff
	v_add_u32_e32 v208, s74, v173
	v_add_u32_e32 v209, 0, v4
	v_add_u32_e32 v210, s75, v173
	s_mov_b32 s34, 0x3db504f3
	s_mov_b64 s[36:37], 0x1000
	s_mov_b64 s[38:39], 0x2000
	s_mov_b64 s[40:41], 0x3000
	s_mov_b64 s[50:51], 0x1800
	v_mov_b32_e32 v191, 0x3db504f3
	v_mbcnt_hi_u32_b32 v211, -1, v0
	v_mov_b32_e32 v212, 0x3e0293ee
	v_mov_b32_e32 v213, 0x1000
	s_mov_b32 s76, 0
	s_barrier
	s_branch .LBB0_316

; #define PG8_WAIT_V(n) asm volatile("s_waitcnt vmcnt(" #n ")" ::: "memory")
; #define PG8_WAIT_L(n) asm volatile("s_waitcnt lgkmcnt(" #n ")" ::: "memory")
; #define PG8_BAR __builtin_amdgcn_s_barrier()
; template <class Epi, class Sched>
; __device__ __forceinline__ void gemm_phase(LAS unsigned char* lds, const bf16_t* A, const int K, const Sched& S, const Epi& E, const int wv) {
;     ...
;         for (int t = 0; t < nt; t += 2) {
;             const bool last = (t == nt - 2);
;             const size_t k1 = (size_t)(t + 1) * kstep;
;             const size_t k2 = last ? 0 : (size_t)(t + 2) * kstep, k3 = k2 + kstep;
;             const char* b2 = last ? nB : cB + (size_t)(t + 2) * kstep; const char* b3 = b2 + kstep;
;             PG8_LDB(B0, 0, 0); PG8_SCHED; PG8_LDA(At, 0, 0); PG8_STAGE_A(PG8_SA(1, 1), 1, false, k1);
;             PG8_WAIT_L(8); PG8_BAR; PG8_WAIT_L(0); PG8_MMA(0, 0, At, B0); PG8_BAR; PG8_SCHED;
;             PG8_LDB(B1, 0, 1); PG8_STAGE(PG8_SB(0, 0), b2, voffB);
;             PG8_BAR; PG8_WAIT_L(0); PG8_MMA(0, 1, At, B1); PG8_BAR;
;             PG8_LDA(At, 0, 1); PG8_STAGE_A(PG8_SA(0, 0), 0, last, k2);
;             PG8_BAR; PG8_WAIT_L(0); PG8_MMA(1, 0, At, B0); PG8_BAR; PG8_SCHED;
;             PG8_STAGE(PG8_SB(0, 1), b2 + hstep, voffB);
;             PG8_WAIT_V(6); PG8_BAR; PG8_MMA(1, 1, At, B1); PG8_BAR;
;             PG8_LDB(B0, 1, 0); PG8_SCHED; PG8_LDA(At, 1, 0); PG8_STAGE_A(PG8_SA(0, 1), 1, last, k2);
;             PG8_WAIT_L(8); PG8_BAR; PG8_WAIT_L(0); PG8_MMA(0, 0, At, B0); PG8_BAR; PG8_SCHED;
;             PG8_LDB(B1, 1, 1); PG8_STAGE(PG8_SB(1, 0), b3, voffB);
;             PG8_BAR; PG8_WAIT_L(0); PG8_MMA(0, 1, At, B1); PG8_BAR;
;             PG8_LDA(At, 1, 1); PG8_STAGE_A(PG8_SA(1, 0), 0, last, k3);
;             PG8_BAR; PG8_WAIT_L(0); PG8_MMA(1, 0, At, B0); PG8_BAR; PG8_SCHED;
;             PG8_STAGE(PG8_SB(1, 1), b3 + hstep, voffB);
;             PG8_WAIT_V(6); PG8_BAR; PG8_MMA(1, 1, At, B1); PG8_BAR;
;         }
;         E(acc, cur, wr, wc, fr, fq);
;         if (!has_next) break;
; #pragma unroll
;         for (int a_ = 0; a_ < 2; ++a_)
; #pragma unroll
;             for (int b_ = 0; b_ < 2; ++b_)
; #pragma unroll
;                 for (int m = 0; m < 4; ++m)
; #pragma unroll
;                     for (int n = 0; n < 2; ++n) acc[a_][b_][m][n] = (f32x4){0.f, 0.f, 0.f, 0.f};
;         cur = nxt; cB = nB; cA = nA; ++ui;
.LBB0_318:
	s_ashr_i32 s15, s14, 31
	s_lshl_b64 s[24:25], s[14:15], 20
	s_add_u32 s24, s60, s24
	s_addc_u32 s25, s61, s25
	s_and_b64 s[28:29], s[8:9], exec
	s_cselect_b32 s15, s25, s11
	s_cselect_b32 s18, s24, s10
	s_ashr_i32 s17, s16, 31
	s_lshl_b64 s[28:29], s[16:17], 20
	s_add_u32 s28, s62, s28
	s_addc_u32 s29, s63, s29
	s_add_u32 s17, s10, 0x100
	v_mov_b32_e32 v0, 0
	s_addc_u32 s33, s11, 0
	s_waitcnt vmcnt(0)
	v_lshl_add_u64 v[128:129], s[2:3], 0, v[182:183]
	v_lshl_add_u64 v[130:131], s[2:3], 0, v[184:185]
	s_mov_b32 s79, -2
	s_mov_b64 s[10:11], 0
	v_mov_b32_e32 v1, v0
	v_mov_b32_e32 v2, v0
	s_waitcnt lgkmcnt(0)
	v_mov_b32_e32 v3, v0
	v_mov_b32_e32 v4, v0
	v_mov_b32_e32 v5, v0
	v_mov_b32_e32 v6, v0
	v_mov_b32_e32 v7, v0
	s_waitcnt vmcnt(0)
	v_mov_b32_e32 v16, v0
	v_mov_b32_e32 v17, v0
	v_mov_b32_e32 v18, v0
	v_mov_b32_e32 v19, v0
	v_mov_b32_e32 v20, v0
	v_mov_b32_e32 v21, v0
	v_mov_b32_e32 v22, v0
	v_mov_b32_e32 v23, v0
	v_mov_b32_e32 v32, v0
	v_mov_b32_e32 v33, v0
	v_mov_b32_e32 v34, v0
	v_mov_b32_e32 v35, v0
	v_mov_b32_e32 v36, v0
	v_mov_b32_e32 v37, v0
	v_mov_b32_e32 v38, v0
	v_mov_b32_e32 v39, v0
	v_mov_b32_e32 v48, v0
	v_mov_b32_e32 v49, v0
	v_mov_b32_e32 v50, v0
	v_mov_b32_e32 v51, v0
	v_mov_b32_e32 v52, v0
	v_mov_b32_e32 v53, v0
	v_mov_b32_e32 v54, v0
	v_mov_b32_e32 v55, v0
	v_mov_b32_e32 v8, v0
	v_mov_b32_e32 v9, v0
	v_mov_b32_e32 v10, v0
	v_mov_b32_e32 v11, v0
	v_mov_b32_e32 v12, v0
	v_mov_b32_e32 v13, v0
	v_mov_b32_e32 v14, v0
	v_mov_b32_e32 v15, v0
	v_mov_b32_e32 v24, v0
	v_mov_b32_e32 v25, v0
	v_mov_b32_e32 v26, v0
	v_mov_b32_e32 v27, v0
	v_mov_b32_e32 v28, v0
	v_mov_b32_e32 v29, v0
	v_mov_b32_e32 v30, v0
	v_mov_b32_e32 v31, v0
	v_mov_b32_e32 v40, v0
	v_mov_b32_e32 v41, v0
	v_mov_b32_e32 v42, v0
	v_mov_b32_e32 v43, v0
	v_mov_b32_e32 v44, v0
	v_mov_b32_e32 v45, v0
	v_mov_b32_e32 v46, v0
	v_mov_b32_e32 v47, v0
	v_mov_b32_e32 v56, v0
	v_mov_b32_e32 v57, v0
	v_mov_b32_e32 v58, v0
	v_mov_b32_e32 v59, v0
	v_mov_b32_e32 v60, v0
	v_mov_b32_e32 v61, v0
	v_mov_b32_e32 v62, v0
	v_mov_b32_e32 v63, v0
	v_mov_b32_e32 v64, v0
	v_mov_b32_e32 v65, v0
	v_mov_b32_e32 v66, v0
	v_mov_b32_e32 v67, v0
	v_mov_b32_e32 v68, v0
	v_mov_b32_e32 v69, v0
	v_mov_b32_e32 v70, v0
	v_mov_b32_e32 v71, v0
	v_mov_b32_e32 v80, v0
	v_mov_b32_e32 v81, v0
	v_mov_b32_e32 v82, v0
	v_mov_b32_e32 v83, v0
	v_mov_b32_e32 v84, v0
	v_mov_b32_e32 v85, v0
	v_mov_b32_e32 v86, v0
	v_mov_b32_e32 v87, v0
	v_mov_b32_e32 v96, v0
	v_mov_b32_e32 v97, v0
	v_mov_b32_e32 v98, v0
	v_mov_b32_e32 v99, v0
	v_mov_b32_e32 v100, v0
	v_mov_b32_e32 v101, v0
	v_mov_b32_e32 v102, v0
	v_mov_b32_e32 v103, v0
	v_mov_b32_e32 v112, v0
	v_mov_b32_e32 v113, v0
	v_mov_b32_e32 v114, v0
	v_mov_b32_e32 v115, v0
	v_mov_b32_e32 v116, v0
	v_mov_b32_e32 v117, v0
	v_mov_b32_e32 v118, v0
	v_mov_b32_e32 v119, v0
	v_mov_b32_e32 v72, v0
	v_mov_b32_e32 v73, v0
	v_mov_b32_e32 v74, v0
	v_mov_b32_e32 v75, v0
	v_mov_b32_e32 v76, v0
	v_mov_b32_e32 v77, v0
	v_mov_b32_e32 v78, v0
	v_mov_b32_e32 v79, v0
	v_mov_b32_e32 v88, v0
	v_mov_b32_e32 v89, v0
	v_mov_b32_e32 v90, v0
	v_mov_b32_e32 v91, v0
	v_mov_b32_e32 v92, v0
	v_mov_b32_e32 v93, v0
	v_mov_b32_e32 v94, v0
	v_mov_b32_e32 v95, v0
	v_mov_b32_e32 v104, v0
	v_mov_b32_e32 v105, v0
	v_mov_b32_e32 v106, v0
	v_mov_b32_e32 v107, v0
	v_mov_b32_e32 v108, v0
	v_mov_b32_e32 v109, v0
	v_mov_b32_e32 v110, v0
	v_mov_b32_e32 v111, v0
	v_mov_b32_e32 v120, v0
	v_mov_b32_e32 v121, v0
	v_mov_b32_e32 v122, v0
	v_mov_b32_e32 v123, v0
	v_mov_b32_e32 v124, v0
	v_mov_b32_e32 v125, v0
	v_mov_b32_e32 v126, v0
	v_mov_b32_e32 v127, v0
	s_bitcmp1_b32 s92, 8
	s_cbranch_scc0 .Lmy_ph_0
	s_barrier
.Lmy_ph_0:
.LBB0_319:
	s_add_u32 s42, s10, 0x100
	ds_read_b128 v[132:135], v208
	ds_read_b128 v[136:139], v208 offset:1024
	ds_read_b128 v[140:143], v208 offset:2048
	ds_read_b128 v[144:147], v208 offset:3072
	s_addc_u32 s43, s11, 0
	s_add_u32 s82, s17, s10
	s_addc_u32 s83, s33, s11
	s_cmp_eq_u32 s79, 28
	s_cselect_b64 s[80:81], -1, 0
	s_and_b64 s[54:55], s[80:81], exec
	s_cselect_b32 s84, 0, s42
	s_cselect_b32 s55, s15, s83
	s_cselect_b32 s54, s18, s82
	v_lshl_add_u64 v[218:219], v[128:129], 0, s[10:11]
	s_add_i32 m0, s65, 0xc000
	ds_read_b128 v[148:151], v209
	ds_read_b128 v[152:155], v209 offset:1024
	ds_read_b128 v[156:159], v209 offset:2048
	ds_read_b128 v[192:195], v209 offset:3072
	ds_read_b128 v[196:199], v209 offset:4096
	ds_read_b128 v[200:203], v209 offset:5120
	ds_read_b128 v[204:207], v209 offset:6144
	ds_read_b128 v[214:217], v209 offset:7168
	global_load_lds_dwordx4 v[218:219], off
	v_lshl_add_u64 v[218:219], v[130:131], 0, s[10:11]
	s_add_i32 m0, s65, 0xe000
	s_nop 0
	global_load_lds_dwordx4 v[218:219], off
	s_waitcnt lgkmcnt(8)
	s_barrier
	s_waitcnt lgkmcnt(0)
	s_setprio 1
	s_waitcnt lgkmcnt(0)
	v_mfma_f32_16x16x32_bf16 v[124:127], v[132:135], v[148:151], v[124:127]
	v_mfma_f32_16x16x32_bf16 v[120:123], v[140:143], v[148:151], v[120:123]
	v_mfma_f32_16x16x32_bf16 v[108:111], v[132:135], v[156:159], v[108:111]
	v_mfma_f32_16x16x32_bf16 v[104:107], v[140:143], v[156:159], v[104:107]
	v_mfma_f32_16x16x32_bf16 v[92:95], v[132:135], v[196:199], v[92:95]
	v_mfma_f32_16x16x32_bf16 v[88:91], v[140:143], v[196:199], v[88:91]
	v_mfma_f32_16x16x32_bf16 v[76:79], v[132:135], v[204:207], v[76:79]
	v_mfma_f32_16x16x32_bf16 v[72:75], v[140:143], v[204:207], v[72:75]
	v_mfma_f32_16x16x32_bf16 v[124:127], v[136:139], v[152:155], v[124:127]
	v_mfma_f32_16x16x32_bf16 v[120:123], v[144:147], v[152:155], v[120:123]
	v_mfma_f32_16x16x32_bf16 v[108:111], v[136:139], v[192:195], v[108:111]
	v_mfma_f32_16x16x32_bf16 v[104:107], v[144:147], v[192:195], v[104:107]
	v_mfma_f32_16x16x32_bf16 v[92:95], v[136:139], v[200:203], v[92:95]
	v_mfma_f32_16x16x32_bf16 v[88:91], v[144:147], v[200:203], v[88:91]
	v_mfma_f32_16x16x32_bf16 v[76:79], v[136:139], v[214:217], v[76:79]
	v_mfma_f32_16x16x32_bf16 v[72:75], v[144:147], v[214:217], v[72:75]
	s_setprio 0
	s_barrier
; #define PG8_STAGE(bufoff, gbase, voff) do { _Pragma("unroll") for (int _i = 0; _i < 2; ++_i) \
;         __builtin_amdgcn_global_load_lds((const unsigned*)((const char*)(gbase) + (voff)[_i]), (LAS unsigned*)(lds + (bufoff) + ldsw + _i * 8192), 16, 0, 0); } while (0)
; #define PG8_LDA(dst, b, h) do { _Pragma("unroll") for (int m = 0; m < 4; ++m) _Pragma("unroll") for (int k = 0; k < 2; ++k) dst[m][k] = *(const LAS bf16x8*)(lds + PG8_SA(b, h) + aoff + m * 2048 + k * 1024); } while (0)
; #define PG8_LDB(dst, b, h) do { _Pragma("unroll") for (int n = 0; n < 2; ++n) _Pragma("unroll") for (int k = 0; k < 2; ++k) dst[n][k] = *(const LAS bf16x8*)(lds + PG8_SB(b, h) + boff + n * 2048 + k * 1024); } while (0)
; #define PG8_WAIT_V(n) asm volatile("s_waitcnt vmcnt(" #n ")" ::: "memory")
; #define PG8_WAIT_L(n) asm volatile("s_waitcnt lgkmcnt(" #n ")" ::: "memory")
; #define PG8_BAR __builtin_amdgcn_s_barrier()
; #define PG8_SCHED __builtin_amdgcn_sched_barrier(0)
; template <class Epi, class Sched>
; __device__ __forceinline__ void gemm_phase(LAS unsigned char* lds, const bf16_t* A, const int K, const Sched& S, const Epi& E, const int wv) {
;     ...
;             PG8_LDB(B0, 0, 0); PG8_SCHED; PG8_LDA(At, 0, 0); PG8_STAGE_A(PG8_SA(1, 1), 1, false, k1);
;             PG8_WAIT_L(8); PG8_BAR; PG8_WAIT_L(0); PG8_MMA(0, 0, At, B0); PG8_BAR; PG8_SCHED;
;             PG8_LDB(B1, 0, 1); PG8_STAGE(PG8_SB(0, 0), b2, voffB);
;             PG8_BAR; PG8_WAIT_L(0); PG8_MMA(0, 1, At, B1); PG8_BAR;
;             PG8_LDA(At, 0, 1); PG8_STAGE_A(PG8_SA(0, 0), 0, last, k2);
;             PG8_BAR; PG8_WAIT_L(0); PG8_MMA(1, 0, At, B0); PG8_BAR; PG8_SCHED;
;             PG8_STAGE(PG8_SB(0, 1), b2 + hstep, voffB);
;             PG8_WAIT_V(6); PG8_BAR; PG8_MMA(1, 1, At, B1); PG8_BAR;
;             PG8_LDB(B0, 1, 0); PG8_SCHED; PG8_LDA(At, 1, 0); PG8_STAGE_A(PG8_SA(0, 1), 1, last, k2);
;             PG8_WAIT_L(8); PG8_BAR; PG8_WAIT_L(0); PG8_MMA(0, 0, At, B0); PG8_BAR; PG8_SCHED;
;             PG8_LDB(B1, 1, 1); PG8_STAGE(PG8_SB(1, 0), b3, voffB);
;             PG8_BAR; PG8_WAIT_L(0); PG8_MMA(0, 1, At, B1); PG8_BAR;
;             PG8_LDA(At, 1, 1); PG8_STAGE_A(PG8_SA(1, 0), 0, last, k3);
;             PG8_BAR; PG8_WAIT_L(0); PG8_MMA(1, 0, At, B0); PG8_BAR; PG8_SCHED;
;             PG8_STAGE(PG8_SB(1, 1), b3 + hstep, voffB);
;             PG8_WAIT_V(6); PG8_BAR; PG8_MMA(1, 1, At, B1); PG8_BAR;
	s_add_i32 s10, s74, s64
	v_lshl_add_u64 v[234:235], s[54:55], 0, v[162:163]
	s_mov_b32 m0, s10
	ds_read_b128 v[218:221], v210
	ds_read_b128 v[222:225], v210 offset:1024
	ds_read_b128 v[226:229], v210 offset:2048
	ds_read_b128 v[230:233], v210 offset:3072
	global_load_lds_dwordx4 v[234:235], off
	v_lshl_add_u64 v[236:237], s[54:55], 0, v[166:167]
	s_add_i32 m0, s10, 0x2000
	s_nop 0
	global_load_lds_dwordx4 v[236:237], off
	s_barrier
	s_waitcnt lgkmcnt(0)
	s_setprio 1
	s_waitcnt lgkmcnt(0)
	v_mfma_f32_16x16x32_bf16 v[116:119], v[218:221], v[148:151], v[116:119]
	v_mfma_f32_16x16x32_bf16 v[112:115], v[226:229], v[148:151], v[112:115]
	v_mfma_f32_16x16x32_bf16 v[100:103], v[218:221], v[156:159], v[100:103]
	v_mfma_f32_16x16x32_bf16 v[96:99], v[226:229], v[156:159], v[96:99]
	v_mfma_f32_16x16x32_bf16 v[84:87], v[218:221], v[196:199], v[84:87]
	v_mfma_f32_16x16x32_bf16 v[80:83], v[226:229], v[196:199], v[80:83]
	v_mfma_f32_16x16x32_bf16 v[68:71], v[218:221], v[204:207], v[68:71]
	v_mfma_f32_16x16x32_bf16 v[64:67], v[226:229], v[204:207], v[64:67]
	v_mfma_f32_16x16x32_bf16 v[116:119], v[222:225], v[152:155], v[116:119]
	v_mfma_f32_16x16x32_bf16 v[112:115], v[230:233], v[152:155], v[112:115]
	v_mfma_f32_16x16x32_bf16 v[100:103], v[222:225], v[192:195], v[100:103]
	v_mfma_f32_16x16x32_bf16 v[96:99], v[230:233], v[192:195], v[96:99]
	v_mfma_f32_16x16x32_bf16 v[84:87], v[222:225], v[200:203], v[84:87]
	v_mfma_f32_16x16x32_bf16 v[80:83], v[230:233], v[200:203], v[80:83]
	v_mfma_f32_16x16x32_bf16 v[68:71], v[222:225], v[214:217], v[68:71]
	v_mfma_f32_16x16x32_bf16 v[64:67], v[230:233], v[214:217], v[64:67]
	s_setprio 0
	s_and_b64 s[10:11], s[8:9], s[80:81]
	s_and_b64 s[10:11], s[10:11], exec
	s_cselect_b32 s10, s28, s2
	s_cselect_b32 s11, s29, s3
	s_add_u32 s10, s10, s84
	s_addc_u32 s11, s11, 0
	s_mov_b32 m0, s65
	v_lshl_add_u64 v[238:239], s[10:11], 0, v[160:161]
	s_barrier
	ds_read_b128 v[148:151], v209 offset:16384
	ds_read_b128 v[152:155], v209 offset:17408
	ds_read_b128 v[156:159], v209 offset:18432
	ds_read_b128 v[192:195], v209 offset:19456
	ds_read_b128 v[196:199], v209 offset:20480
	ds_read_b128 v[200:203], v209 offset:21504
	ds_read_b128 v[204:207], v209 offset:22528
	ds_read_b128 v[214:217], v209 offset:23552
	global_load_lds_dwordx4 v[238:239], off
	v_lshl_add_u64 v[240:241], s[10:11], 0, v[164:165]
	s_mov_b32 m0, s66
	s_nop 0
	global_load_lds_dwordx4 v[240:241], off
	s_barrier
	s_waitcnt lgkmcnt(0)
	s_setprio 1
	s_waitcnt lgkmcnt(0)
	v_mfma_f32_16x16x32_bf16 v[60:63], v[132:135], v[148:151], v[60:63]
	v_mfma_f32_16x16x32_bf16 v[56:59], v[140:143], v[148:151], v[56:59]
	v_mfma_f32_16x16x32_bf16 v[44:47], v[132:135], v[156:159], v[44:47]
	v_mfma_f32_16x16x32_bf16 v[40:43], v[140:143], v[156:159], v[40:43]
	v_mfma_f32_16x16x32_bf16 v[28:31], v[132:135], v[196:199], v[28:31]
	v_mfma_f32_16x16x32_bf16 v[24:27], v[140:143], v[196:199], v[24:27]
	v_mfma_f32_16x16x32_bf16 v[12:15], v[132:135], v[204:207], v[12:15]
	v_mfma_f32_16x16x32_bf16 v[8:11], v[140:143], v[204:207], v[8:11]
	v_mfma_f32_16x16x32_bf16 v[60:63], v[136:139], v[152:155], v[60:63]
	v_mfma_f32_16x16x32_bf16 v[56:59], v[144:147], v[152:155], v[56:59]
	v_mfma_f32_16x16x32_bf16 v[44:47], v[136:139], v[192:195], v[44:47]
	v_mfma_f32_16x16x32_bf16 v[40:43], v[144:147], v[192:195], v[40:43]
	v_mfma_f32_16x16x32_bf16 v[28:31], v[136:139], v[200:203], v[28:31]
	v_mfma_f32_16x16x32_bf16 v[24:27], v[144:147], v[200:203], v[24:27]
	v_mfma_f32_16x16x32_bf16 v[12:15], v[136:139], v[214:217], v[12:15]
	v_mfma_f32_16x16x32_bf16 v[8:11], v[144:147], v[214:217], v[8:11]
	s_setprio 0
	s_barrier
	s_add_u32 s80, s54, 0x80000
	s_addc_u32 s81, s55, 0
	s_add_i32 s82, s75, s64
	v_lshl_add_u64 v[132:133], s[80:81], 0, v[162:163]
	s_mov_b32 m0, s82
	s_nop 0
	global_load_lds_dwordx4 v[132:133], off
	v_lshl_add_u64 v[132:133], s[80:81], 0, v[166:167]
	s_add_i32 m0, s82, 0x2000
	s_nop 0
	global_load_lds_dwordx4 v[132:133], off
	s_waitcnt vmcnt(6)
	s_barrier
	s_setprio 1
	v_mfma_f32_16x16x32_bf16 v[52:55], v[218:221], v[148:151], v[52:55]
	v_mfma_f32_16x16x32_bf16 v[48:51], v[226:229], v[148:151], v[48:51]
	v_mfma_f32_16x16x32_bf16 v[36:39], v[218:221], v[156:159], v[36:39]
	v_mfma_f32_16x16x32_bf16 v[32:35], v[226:229], v[156:159], v[32:35]
	v_mfma_f32_16x16x32_bf16 v[20:23], v[218:221], v[196:199], v[20:23]
	v_mfma_f32_16x16x32_bf16 v[16:19], v[226:229], v[196:199], v[16:19]
	v_mfma_f32_16x16x32_bf16 v[4:7], v[218:221], v[204:207], v[4:7]
	v_mfma_f32_16x16x32_bf16 v[0:3], v[226:229], v[204:207], v[0:3]
	v_mfma_f32_16x16x32_bf16 v[52:55], v[222:225], v[152:155], v[52:55]
	v_mfma_f32_16x16x32_bf16 v[48:51], v[230:233], v[152:155], v[48:51]
	v_mfma_f32_16x16x32_bf16 v[36:39], v[222:225], v[192:195], v[36:39]
	v_mfma_f32_16x16x32_bf16 v[32:35], v[230:233], v[192:195], v[32:35]
	v_mfma_f32_16x16x32_bf16 v[20:23], v[222:225], v[200:203], v[20:23]
	v_mfma_f32_16x16x32_bf16 v[16:19], v[230:233], v[200:203], v[16:19]
	v_mfma_f32_16x16x32_bf16 v[4:7], v[222:225], v[214:217], v[4:7]
	v_mfma_f32_16x16x32_bf16 v[0:3], v[230:233], v[214:217], v[0:3]
	s_setprio 0
	s_add_i32 s80, 0, 0x18000
	v_add_u32_e32 v144, s80, v173
	s_barrier
	ds_read_b128 v[132:135], v144
	ds_read_b128 v[136:139], v144 offset:1024
	ds_read_b128 v[140:143], v144 offset:2048
	ds_read_b128 v[144:147], v144 offset:3072
	s_add_u32 s10, s10, 0x80000
	s_addc_u32 s11, s11, 0
	s_mov_b32 m0, s67
	v_lshl_add_u64 v[218:219], s[10:11], 0, v[160:161]
	ds_read_b128 v[148:151], v209 offset:32768
	ds_read_b128 v[152:155], v209 offset:33792
	ds_read_b128 v[156:159], v209 offset:34816
	ds_read_b128 v[192:195], v209 offset:35840
	ds_read_b128 v[196:199], v209 offset:36864
	ds_read_b128 v[200:203], v209 offset:37888
	ds_read_b128 v[204:207], v209 offset:38912
	ds_read_b128 v[214:217], v209 offset:39936
	global_load_lds_dwordx4 v[218:219], off
	v_lshl_add_u64 v[218:219], s[10:11], 0, v[164:165]
	s_mov_b32 m0, s68
	s_nop 0
	global_load_lds_dwordx4 v[218:219], off
	s_waitcnt lgkmcnt(8)
	s_barrier
; #define PG8_STAGE(bufoff, gbase, voff) do { _Pragma("unroll") for (int _i = 0; _i < 2; ++_i) \
;         __builtin_amdgcn_global_load_lds((const unsigned*)((const char*)(gbase) + (voff)[_i]), (LAS unsigned*)(lds + (bufoff) + ldsw + _i * 8192), 16, 0, 0); } while (0)
; #define PG8_LDA(dst, b, h) do { _Pragma("unroll") for (int m = 0; m < 4; ++m) _Pragma("unroll") for (int k = 0; k < 2; ++k) dst[m][k] = *(const LAS bf16x8*)(lds + PG8_SA(b, h) + aoff + m * 2048 + k * 1024); } while (0)
; #define PG8_LDB(dst, b, h) do { _Pragma("unroll") for (int n = 0; n < 2; ++n) _Pragma("unroll") for (int k = 0; k < 2; ++k) dst[n][k] = *(const LAS bf16x8*)(lds + PG8_SB(b, h) + boff + n * 2048 + k * 1024); } while (0)
; #define PG8_MMA(ai, bj, At, Bt) do { __builtin_amdgcn_s_setprio(1); _Pragma("unroll") for (int m = 0; m < 4; ++m) _Pragma("unroll") for (int n = 0; n < 2; ++n) _Pragma("unroll") for (int k = 0; k < 2; ++k) \
;         acc[ai][bj][m][n] = __builtin_amdgcn_mfma_f32_16x16x32_bf16(Bt[n][k], At[m][k], acc[ai][bj][m][n], 0, 0, 0); __builtin_amdgcn_s_setprio(0); } while (0)
; #define PG8_WAIT_V(n) asm volatile("s_waitcnt vmcnt(" #n ")" ::: "memory")
; #define PG8_WAIT_L(n) asm volatile("s_waitcnt lgkmcnt(" #n ")" ::: "memory")
; #define PG8_BAR __builtin_amdgcn_s_barrier()
; #define PG8_SCHED __builtin_amdgcn_sched_barrier(0)
; template <class Epi, class Sched>
; __device__ __forceinline__ void gemm_phase(LAS unsigned char* lds, const bf16_t* A, const int K, const Sched& S, const Epi& E, const int wv) {
;     ...
;             PG8_LDB(B0, 1, 0); PG8_SCHED; PG8_LDA(At, 1, 0); PG8_STAGE_A(PG8_SA(0, 1), 1, last, k2);
;             PG8_WAIT_L(8); PG8_BAR; PG8_WAIT_L(0); PG8_MMA(0, 0, At, B0); PG8_BAR; PG8_SCHED;
;             PG8_LDB(B1, 1, 1); PG8_STAGE(PG8_SB(1, 0), b3, voffB);
;             PG8_BAR; PG8_WAIT_L(0); PG8_MMA(0, 1, At, B1); PG8_BAR;
;             PG8_LDA(At, 1, 1); PG8_STAGE_A(PG8_SA(1, 0), 0, last, k3);
;             PG8_BAR; PG8_WAIT_L(0); PG8_MMA(1, 0, At, B0); PG8_BAR; PG8_SCHED;
;             PG8_STAGE(PG8_SB(1, 1), b3 + hstep, voffB);
;             PG8_WAIT_V(6); PG8_BAR; PG8_MMA(1, 1, At, B1); PG8_BAR;
;         }
	s_waitcnt lgkmcnt(0)
	s_setprio 1
	s_waitcnt lgkmcnt(0)
	v_mfma_f32_16x16x32_bf16 v[124:127], v[132:135], v[148:151], v[124:127]
	v_mfma_f32_16x16x32_bf16 v[120:123], v[140:143], v[148:151], v[120:123]
	v_mfma_f32_16x16x32_bf16 v[108:111], v[132:135], v[156:159], v[108:111]
	v_mfma_f32_16x16x32_bf16 v[104:107], v[140:143], v[156:159], v[104:107]
	v_mfma_f32_16x16x32_bf16 v[92:95], v[132:135], v[196:199], v[92:95]
	v_mfma_f32_16x16x32_bf16 v[88:91], v[140:143], v[196:199], v[88:91]
	v_mfma_f32_16x16x32_bf16 v[76:79], v[132:135], v[204:207], v[76:79]
	v_mfma_f32_16x16x32_bf16 v[72:75], v[140:143], v[204:207], v[72:75]
	v_mfma_f32_16x16x32_bf16 v[124:127], v[136:139], v[152:155], v[124:127]
	v_mfma_f32_16x16x32_bf16 v[120:123], v[144:147], v[152:155], v[120:123]
	v_mfma_f32_16x16x32_bf16 v[108:111], v[136:139], v[192:195], v[108:111]
	v_mfma_f32_16x16x32_bf16 v[104:107], v[144:147], v[192:195], v[104:107]
	v_mfma_f32_16x16x32_bf16 v[92:95], v[136:139], v[200:203], v[92:95]
	v_mfma_f32_16x16x32_bf16 v[88:91], v[144:147], v[200:203], v[88:91]
	v_mfma_f32_16x16x32_bf16 v[76:79], v[136:139], v[214:217], v[76:79]
	v_mfma_f32_16x16x32_bf16 v[72:75], v[144:147], v[214:217], v[72:75]
	s_setprio 0
	s_barrier
	s_add_i32 s81, 0, 0x1c000
	s_add_i32 s10, s80, s64
	v_add_u32_e32 v168, s81, v173
	v_lshl_add_u64 v[234:235], v[234:235], 0, s[26:27]
	s_mov_b32 m0, s10
	ds_read_b128 v[218:221], v168
	ds_read_b128 v[222:225], v168 offset:1024
	ds_read_b128 v[226:229], v168 offset:2048
	ds_read_b128 v[230:233], v168 offset:3072
	global_load_lds_dwordx4 v[234:235], off
	v_lshl_add_u64 v[234:235], v[236:237], 0, s[26:27]
	s_add_i32 m0, s10, 0x2000
	s_nop 0
	global_load_lds_dwordx4 v[234:235], off
	s_barrier
	s_waitcnt lgkmcnt(0)
	s_setprio 1
	s_waitcnt lgkmcnt(0)
	v_mfma_f32_16x16x32_bf16 v[116:119], v[218:221], v[148:151], v[116:119]
	v_mfma_f32_16x16x32_bf16 v[112:115], v[226:229], v[148:151], v[112:115]
	v_mfma_f32_16x16x32_bf16 v[100:103], v[218:221], v[156:159], v[100:103]
	v_mfma_f32_16x16x32_bf16 v[96:99], v[226:229], v[156:159], v[96:99]
	v_mfma_f32_16x16x32_bf16 v[84:87], v[218:221], v[196:199], v[84:87]
	v_mfma_f32_16x16x32_bf16 v[80:83], v[226:229], v[196:199], v[80:83]
	v_mfma_f32_16x16x32_bf16 v[68:71], v[218:221], v[204:207], v[68:71]
	v_mfma_f32_16x16x32_bf16 v[64:67], v[226:229], v[204:207], v[64:67]
	v_mfma_f32_16x16x32_bf16 v[116:119], v[222:225], v[152:155], v[116:119]
	v_mfma_f32_16x16x32_bf16 v[112:115], v[230:233], v[152:155], v[112:115]
	v_mfma_f32_16x16x32_bf16 v[100:103], v[222:225], v[192:195], v[100:103]
	v_mfma_f32_16x16x32_bf16 v[96:99], v[230:233], v[192:195], v[96:99]
	v_mfma_f32_16x16x32_bf16 v[84:87], v[222:225], v[200:203], v[84:87]
	v_mfma_f32_16x16x32_bf16 v[80:83], v[230:233], v[200:203], v[80:83]
	v_mfma_f32_16x16x32_bf16 v[68:71], v[222:225], v[214:217], v[68:71]
	v_mfma_f32_16x16x32_bf16 v[64:67], v[230:233], v[214:217], v[64:67]
	s_setprio 0
	s_mov_b32 m0, s70
	v_lshl_add_u64 v[234:235], v[238:239], 0, s[26:27]
	s_barrier
	ds_read_b128 v[148:151], v209 offset:49152
	ds_read_b128 v[152:155], v209 offset:50176
	ds_read_b128 v[156:159], v209 offset:51200
	ds_read_b128 v[192:195], v209 offset:52224
	ds_read_b128 v[196:199], v209 offset:53248
	ds_read_b128 v[200:203], v209 offset:54272
	ds_read_b128 v[204:207], v209 offset:55296
	ds_read_b128 v[214:217], v209 offset:56320
	global_load_lds_dwordx4 v[234:235], off
	v_lshl_add_u64 v[234:235], v[240:241], 0, s[26:27]
	s_mov_b32 m0, s71
	s_nop 0
	global_load_lds_dwordx4 v[234:235], off
	s_barrier
	s_waitcnt lgkmcnt(0)
	s_setprio 1
	s_waitcnt lgkmcnt(0)
	v_mfma_f32_16x16x32_bf16 v[60:63], v[132:135], v[148:151], v[60:63]
	v_mfma_f32_16x16x32_bf16 v[56:59], v[140:143], v[148:151], v[56:59]
	v_mfma_f32_16x16x32_bf16 v[44:47], v[132:135], v[156:159], v[44:47]
	v_mfma_f32_16x16x32_bf16 v[40:43], v[140:143], v[156:159], v[40:43]
	v_mfma_f32_16x16x32_bf16 v[28:31], v[132:135], v[196:199], v[28:31]
	v_mfma_f32_16x16x32_bf16 v[24:27], v[140:143], v[196:199], v[24:27]
	v_mfma_f32_16x16x32_bf16 v[12:15], v[132:135], v[204:207], v[12:15]
	v_mfma_f32_16x16x32_bf16 v[8:11], v[140:143], v[204:207], v[8:11]
	v_mfma_f32_16x16x32_bf16 v[60:63], v[136:139], v[152:155], v[60:63]
	v_mfma_f32_16x16x32_bf16 v[56:59], v[144:147], v[152:155], v[56:59]
	v_mfma_f32_16x16x32_bf16 v[44:47], v[136:139], v[192:195], v[44:47]
	v_mfma_f32_16x16x32_bf16 v[40:43], v[144:147], v[192:195], v[40:43]
	v_mfma_f32_16x16x32_bf16 v[28:31], v[136:139], v[200:203], v[28:31]
	v_mfma_f32_16x16x32_bf16 v[24:27], v[144:147], v[200:203], v[24:27]
	v_mfma_f32_16x16x32_bf16 v[12:15], v[136:139], v[214:217], v[12:15]
	v_mfma_f32_16x16x32_bf16 v[8:11], v[144:147], v[214:217], v[8:11]
	s_setprio 0
	s_barrier
	s_add_u32 s10, s54, 0x80080
	s_addc_u32 s11, s55, 0
	s_add_i32 s54, s81, s64
	v_lshl_add_u64 v[132:133], s[10:11], 0, v[162:163]
	s_mov_b32 m0, s54
	s_nop 0
	global_load_lds_dwordx4 v[132:133], off
	v_lshl_add_u64 v[132:133], s[10:11], 0, v[166:167]
	s_add_i32 m0, s54, 0x2000
	s_nop 0
	global_load_lds_dwordx4 v[132:133], off
	s_waitcnt vmcnt(6)
	s_barrier
	s_setprio 1
	v_mfma_f32_16x16x32_bf16 v[52:55], v[218:221], v[148:151], v[52:55]
	v_mfma_f32_16x16x32_bf16 v[48:51], v[226:229], v[148:151], v[48:51]
	v_mfma_f32_16x16x32_bf16 v[36:39], v[218:221], v[156:159], v[36:39]
	v_mfma_f32_16x16x32_bf16 v[32:35], v[226:229], v[156:159], v[32:35]
	v_mfma_f32_16x16x32_bf16 v[20:23], v[218:221], v[196:199], v[20:23]
	v_mfma_f32_16x16x32_bf16 v[16:19], v[226:229], v[196:199], v[16:19]
	v_mfma_f32_16x16x32_bf16 v[4:7], v[218:221], v[204:207], v[4:7]
	v_mfma_f32_16x16x32_bf16 v[0:3], v[226:229], v[204:207], v[0:3]
	v_mfma_f32_16x16x32_bf16 v[52:55], v[222:225], v[152:155], v[52:55]
	v_mfma_f32_16x16x32_bf16 v[48:51], v[230:233], v[152:155], v[48:51]
	v_mfma_f32_16x16x32_bf16 v[36:39], v[222:225], v[192:195], v[36:39]
	v_mfma_f32_16x16x32_bf16 v[32:35], v[230:233], v[192:195], v[32:35]
	v_mfma_f32_16x16x32_bf16 v[20:23], v[222:225], v[200:203], v[20:23]
	v_mfma_f32_16x16x32_bf16 v[16:19], v[230:233], v[200:203], v[16:19]
	v_mfma_f32_16x16x32_bf16 v[4:7], v[222:225], v[214:217], v[4:7]
	v_mfma_f32_16x16x32_bf16 v[0:3], v[230:233], v[214:217], v[0:3]
	s_setprio 0
	s_add_i32 s79, s79, 2
	s_cmp_gt_u32 s79, 29
	s_mov_b64 s[10:11], s[42:43]
	s_cbranch_scc1 .Lmy_kx_0
	s_barrier
	s_branch .LBB0_319
; __device__ __forceinline__ unsigned cvt_pk_bf16(float lo, float hi) { const bf16x2_t r = __builtin_convertvector((f32x2_t){lo, hi}, bf16x2_t); return __builtin_bit_cast(unsigned, r); }
; __device__ __forceinline__ float silu_fast(float x) { return x * __builtin_amdgcn_rcpf(1.0f + __builtin_amdgcn_exp2f(-x * 1.4426950408889634f)); }
;     __device__ __forceinline__ void operator()(const f32x4 (&acc)[2][2][4][2], const Unit& u, int wr, int wc, int fr, int fq) const {
;         const int row0 = u.pm * BM + wr * 64 + fr;
;         const int lc = wc * 32 + 8 * fq;
;         if (u.pn < 8) {
;     ...
;         } else {
;             const bool isog = u.pn >= 20;
;             size_t woff; int cb;
;             if (u.pn < 20) { woff = WS_VG; cb = (u.pn - 16) * 256; }
;             else { woff = WS_OG; cb = (u.pn - 20) * 256; }
;             bf16_t* dst = (bf16_t*)(ws + woff);
; #pragma unroll
;             for (int ai = 0; ai < 2; ++ai)
; #pragma unroll
;                 for (int m = 0; m < 4; ++m) {
;                     const int r = row0 + ai * HALF + m * 16;
; #pragma unroll
;                     for (int bj = 0; bj < 2; ++bj) {
;                         f32x4 v0 = acc[ai][bj][m][0], v1 = acc[ai][bj][m][1];
;                         if (isog) {
; #pragma unroll
;                             for (int i = 0; i < 4; ++i) { v0[i] = silu_fast(v0[i]); v1[i] = silu_fast(v1[i]); }
;                         }
;                         u32x4 o; o[0] = cvt_pk_bf16(v0[0], v0[1]); o[1] = cvt_pk_bf16(v0[2], v0[3]); o[2] = cvt_pk_bf16(v1[0], v1[1]); o[3] = cvt_pk_bf16(v1[2], v1[3]);
;                         __builtin_nontemporal_store(o, (u32x4*)(dst + ((size_t)((r >> 11) * 4 + (cb >> 8)) * SEQ + (r & (SEQ - 1))) * 256 + bj * HALF + lc));
.Lmy_kx_0:
	s_bitcmp1_b32 s92, 8
	s_cbranch_scc1 .Lmy_kxb_0
	s_barrier
.Lmy_kxb_0:
	s_lshl_b32 s15, s77, 8
	s_add_i32 s15, s15, s69
	v_or_b32_e32 v192, s15, v171
	s_cmp_gt_i32 s78, 7
	s_mov_b64 s[2:3], -1
	s_cbranch_scc0 .LBB0_425
	s_cmp_gt_u32 s78, 11
	s_cbranch_scc0 .LBB0_422
	s_cmp_gt_u32 s78, 15
	s_cbranch_scc0 .LBB0_356
	s_cmp_gt_u32 s78, 19
	v_mov_b64_e32 v[130:131], v[126:127]
	v_mov_b64_e32 v[134:135], v[122:123]
	s_cselect_b64 s[2:3], -1, 0
	s_cmp_lt_u32 s78, 20
	v_mov_b64_e32 v[128:129], v[124:125]
	v_mov_b64_e32 v[132:133], v[120:121]
	s_cbranch_scc1 .LBB0_325
	v_mul_f32_e32 v129, 0xbfb8aa3b, v120
	v_mul_f32_e32 v130, 0xbfb8aa3b, v125
	v_exp_f32_e32 v129, v129
	v_exp_f32_e32 v130, v130
	v_mul_f32_e32 v131, 0xbfb8aa3b, v126
	v_mul_f32_e32 v133, 0xbfb8aa3b, v122
	v_add_f32_e32 v129, 1.0, v129
	v_rcp_f32_e32 v132, v129
	v_add_f32_e32 v129, 1.0, v130
	v_mul_f32_e32 v130, 0xbfb8aa3b, v121
	v_exp_f32_e32 v130, v130
	v_exp_f32_e32 v131, v131
	v_exp_f32_e32 v133, v133
	v_mul_f32_e32 v128, 0xbfb8aa3b, v124
	v_add_f32_e32 v136, 1.0, v130
	v_add_f32_e32 v130, 1.0, v131
	v_add_f32_e32 v131, 1.0, v133
	v_mul_f32_e32 v133, 0xbfb8aa3b, v127
	v_mul_f32_e32 v134, 0xbfb8aa3b, v123
	v_exp_f32_e32 v128, v128
	v_exp_f32_e32 v133, v133
	v_exp_f32_e32 v135, v134
	v_rcp_f32_e32 v134, v131
	v_add_f32_e32 v128, 1.0, v128
	v_add_f32_e32 v131, 1.0, v133
	v_add_f32_e32 v133, 1.0, v135
	v_rcp_f32_e32 v128, v128
	v_rcp_f32_e32 v129, v129
	v_rcp_f32_e32 v130, v130
	v_rcp_f32_e32 v131, v131
	v_rcp_f32_e32 v135, v133
	v_rcp_f32_e32 v133, v136
	v_pk_mul_f32 v[128:129], v[124:125], v[128:129]
	v_pk_mul_f32 v[130:131], v[126:127], v[130:131]
	v_pk_mul_f32 v[134:135], v[122:123], v[134:135]
	v_pk_mul_f32 v[132:133], v[120:121], v[132:133]

; #define PG8_WAIT_V(n) asm volatile("s_waitcnt vmcnt(" #n ")" ::: "memory")
; #define PG8_BAR __builtin_amdgcn_s_barrier()
; template <class Epi, class Sched>
; __device__ __forceinline__ void gemm_phase(LAS unsigned char* lds, const bf16_t* A, const int K, const Sched& S, const Epi& E, const int wv) {
;     ...
;     PG8_WAIT_V(0);
;     if (wr == 0) PG8_BAR;
;     PG8_BAR;
.LBB0_572:
	s_waitcnt vmcnt(0)
	v_readlane_b32 s84, v252, 20
	s_cmpk_gt_u32 s35, 0xff
	v_readlane_b32 s85, v252, 21
	v_readlane_b32 s86, v252, 22
	v_readlane_b32 s87, v252, 23
	v_readlane_b32 s88, v252, 24
	v_readlane_b32 s89, v252, 25
	v_readlane_b32 s90, v252, 26
	v_readlane_b32 s91, v252, 27
	s_cbranch_scc1 .LBB0_574
.LBB0_574:
	v_readlane_b32 s76, v252, 28
	v_readlane_b32 s77, v252, 29
	v_readlane_b32 s78, v252, 30
	v_readlane_b32 s79, v252, 31
	s_barrier

;     __device__ __forceinline__ unsigned arow(const Unit& u, int r) const { return (unsigned)(u.pm * 256 + r); }
; template <class Epi, class Sched>
; __device__ __forceinline__ void gemm_phase(LAS unsigned char* lds, const bf16_t* A, const int K, const Sched& S, const Epi& E, const int wv) {
;     ...
;     const int wid = __builtin_amdgcn_readfirstlane(tid >> 6), lane = tid & 63, wr = wid >> 2, wc = wid & 3, fr = lane & 15, fq = lane >> 4;
;     const int nt = K / BK;
;     unsigned voffA[2], voffB[2];
; #pragma unroll
;     for (int i = 0; i < 2; ++i) { int R, C; stage_rc(tid * 16 + i * 8192, R, C); const int Rb = Epi::PERM ? ((R & ~31) + perm32(R & 31)) : R;
;         voffA[i] = (unsigned)(R * K + C) * 2u; voffB[i] = (unsigned)(Rb * K + C) * 2u; }
;     const size_t kstep = (size_t)(BK * 2);
;     const size_t hstep = (size_t)HALF * K * 2;
;     const size_t tstep = 2 * hstep;
;     const unsigned ldsw = (unsigned)wid * 1024u;
;     const int aoff = lds_byte(wr * 64 + fr, fq * 8), boff = lds_byte(wc * 32 + fr, fq * 8);
;     Unit cur, nxt; int ui = 0;
;     if (!S.next(0, cur)) return;
;     f32x4 acc[2][2][4][2];
; #pragma unroll
;     for (int a_ = 0; a_ < 2; ++a_)
; #pragma unroll
;         for (int b_ = 0; b_ < 2; ++b_)
; #pragma unroll
;             for (int m = 0; m < 4; ++m)
; #pragma unroll
;                 for (int n = 0; n < 2; ++n) acc[a_][b_][m][n] = (f32x4){0.f, 0.f, 0.f, 0.f};
;     bf16x8 At[4][2], B0[2][2], B1[2][2];
;     unsigned ao0[2] = {0u, 0u}, ao1[2] = {0u, 0u}, no0[2] = {0u, 0u}, no1[2] = {0u, 0u};
;     const char* Ab = (const char*)A;
;     const char* cA = Ab; const char* nA = Ab;
;     if constexpr (Sched::GATHER) {
; #pragma unroll
;         for (int i = 0; i < 2; ++i) { int R, C; stage_rc(tid * 16 + i * 8192, R, C);
;             ao0[i] = (S.arow(cur, R) * (unsigned)K + (unsigned)C) * 2u; ao1[i] = (S.arow(cur, HALF + R) * (unsigned)K + (unsigned)C) * 2u; }
;     } else cA = Ab + (size_t)cur.pm * tstep;
;     const char* cB = S.bptr(cur);
;     PG8_STAGE(PG8_SB(0, 0), cB, voffB); PG8_STAGE_A(PG8_SA(0, 0), 0, false, 0); PG8_STAGE(PG8_SB(0, 1), cB + hstep, voffB); PG8_STAGE_A(PG8_SA(0, 1), 1, false, 0);
;     if (wr == 1) PG8_BAR;
;     PG8_WAIT_V(4); PG8_BAR;
;     PG8_STAGE(PG8_SB(1, 0), cB + kstep, voffB); PG8_STAGE_A(PG8_SA(1, 0), 0, false, kstep); PG8_STAGE(PG8_SB(1, 1), cB + hstep + kstep, voffB);
;     PG8_WAIT_V(6); PG8_BAR;
.LBB0_823:
	v_ashrrev_i32_e32 v1, 31, v8
	v_lshrrev_b32_e32 v1, 26, v1
	v_add_u32_e32 v1, v8, v1
	v_ashrrev_i32_e32 v9, 6, v1
	v_bfe_i32 v1, v8, 27, 1
	v_lshlrev_b32_e32 v0, 4, v8
	v_lshrrev_b32_e32 v1, 22, v1
	v_add_u32_e32 v1, v0, v1
	v_and_b32_e32 v1, 0xfffffc00, v1
	v_sub_u32_e32 v1, v0, v1
	v_lshrrev_b32_e32 v2, 4, v1
	v_bitop3_b32 v1, v2, v1, 32 bitop3:0x6c
	s_waitcnt lgkmcnt(0)
	v_ashrrev_i32_e32 v3, 31, v1
	s_ashr_i32 s0, s4, 3
	v_lshrrev_b32_e32 v3, 26, v3
	s_add_u32 s37, s76, 0x3188000
	v_add_u32_e32 v3, v1, v3
	s_addc_u32 s38, s77, 0
	v_ashrrev_i32_e32 v10, 6, v3
	v_and_b32_e32 v3, 0xc0, v3
	s_add_u32 s39, s76, 0x4e188000
	v_sub_u32_e32 v1, v1, v3
	v_mov_b32_e32 v3, 1
	s_addc_u32 s40, s77, 0
	v_lshlrev_b32_e32 v2, 3, v9
	v_lshlrev_b32_e32 v4, 5, v9
	v_ashrrev_i16_sdwa v1, v3, sext(v1) dst_sel:DWORD dst_unused:UNUSED_PAD src0_sel:DWORD src1_sel:BYTE_0
	s_add_i32 s0, s5, s0
	v_and_b32_e32 v2, 0xffff0, v2
	v_and_b32_e32 v4, 32, v4
	v_bfe_i32 v11, v1, 0, 16
	s_ashr_i32 s5, s0, 31
	v_add_u32_e32 v1, v4, v11
	v_add_lshl_u32 v2, v10, v2, 12
	v_add_u32_e32 v0, 0x2000, v0
	s_lshr_b32 s5, s5, 26
	v_lshl_add_u32 v144, v1, 1, v2
	v_ashrrev_i32_e32 v1, 31, v0
	s_add_i32 s5, s0, s5
	v_lshrrev_b32_e32 v1, 22, v1
	s_ashr_i32 s6, s5, 6
	s_andn2_b32 s5, s5, 63
	v_add_u32_e32 v1, v0, v1
	s_sub_i32 s5, s0, s5
	v_ashrrev_i32_e32 v12, 10, v1
	s_bfe_i32 s0, s5, 0x80000
	v_mul_i32_i24_e32 v1, 0x400, v12
	s_bfe_u32 s0, s0, 0x3000c
	v_sub_u32_e32 v0, v0, v1
	s_add_i32 s7, s5, s0
	v_lshrrev_b32_e32 v1, 4, v0
	s_bfe_i32 s0, s7, 0x80000
	s_and_b32 s7, s7, 0xf8
	v_bitop3_b32 v0, v1, v0, 32 bitop3:0x6c
	s_sub_i32 s5, s5, s7
	v_ashrrev_i32_e32 v2, 31, v0
	s_lshl_b32 s6, s6, 3
	s_sext_i32_i16 s0, s0
	s_sext_i32_i8 s5, s5
	s_ashr_i32 s1, s33, 8
	v_lshrrev_b32_e32 v2, 26, v2
	s_lshr_b32 s0, s0, 3
	s_add_i32 s24, s6, s5
	v_add_u32_e32 v2, v0, v2
	s_ashr_i32 s4, s33, 6
	s_ashr_i32 s25, s24, 31
	s_bfe_i64 s[8:9], s[0:1], 0x100000
	v_ashrrev_i32_e32 v13, 6, v2
	v_and_b32_e32 v2, 0xc0, v2
	s_lshl_b32 s41, s4, 10
	s_lshl_b64 s[6:7], s[24:25], 20
	s_lshl_b64 s[8:9], s[8:9], 20
	v_sub_u32_e32 v0, v0, v2
	s_add_u32 s28, s37, s8
	v_lshlrev_b32_e32 v1, 3, v12
	v_lshlrev_b32_e32 v4, 5, v12
	v_ashrrev_i16_sdwa v0, v3, sext(v0) dst_sel:DWORD dst_unused:UNUSED_PAD src0_sel:DWORD src1_sel:BYTE_0
	s_addc_u32 s29, s38, s9
	s_add_i32 s25, s41, 0
	v_and_b32_e32 v1, 0xffff0, v1
	v_and_b32_e32 v4, 32, v4
	v_bfe_i32 v14, v0, 0, 16
	s_add_i32 m0, s25, 0x10000
	v_add_u32_e32 v0, v4, v14
	v_add_lshl_u32 v1, v13, v1, 12
	global_load_lds_dwordx4 v144, s[28:29]
	s_add_i32 m0, s25, 0x12000
	v_lshl_add_u32 v146, v0, 1, v1
	s_add_u32 s26, s39, s6
	global_load_lds_dwordx4 v146, s[28:29]
	s_addc_u32 s27, s40, s7
	s_mov_b32 m0, s25
	s_add_i32 s42, s25, 0x2000
	global_load_lds_dwordx4 v144, s[26:27]
	s_mov_b32 m0, s42
	s_add_u32 s6, s28, 0x80000
	global_load_lds_dwordx4 v146, s[26:27]
	s_addc_u32 s7, s29, 0
	s_add_i32 m0, s25, 0x14000
	v_mov_b32_e32 v145, 0
	global_load_lds_dwordx4 v144, s[6:7]
	s_add_i32 m0, s25, 0x16000
	v_mov_b32_e32 v147, v145
	global_load_lds_dwordx4 v146, s[6:7]
	s_add_u32 s6, s26, 0x80000
	s_addc_u32 s7, s27, 0
	s_add_i32 s43, s25, 0x4000
	s_mov_b32 m0, s43
	s_add_i32 s50, s25, 0x6000
	global_load_lds_dwordx4 v144, s[6:7]
	s_mov_b32 m0, s50
	s_mov_b32 s51, 0
	global_load_lds_dwordx4 v146, s[6:7]
	v_lshl_add_u64 v[6:7], s[28:29], 0, v[144:145]
	v_lshl_add_u64 v[4:5], s[28:29], 0, v[146:147]
	v_lshl_add_u64 v[2:3], s[26:27], 0, v[144:145]
	s_cmp_lg_u32 s1, 1
	v_lshl_add_u64 v[0:1], s[26:27], 0, v[146:147]
	s_cbranch_scc1 .LBB0_825
.LBB0_825:
	s_add_u32 s6, s76, 0x34188000
	s_addc_u32 s7, s77, 0
	s_add_u32 s54, s76, 0xc000
	s_addc_u32 s55, s77, 0
	s_lshl_b32 s4, s4, 5
	s_mov_b64 s[8:9], 0x80
	s_and_b32 s11, s4, 0x60
	s_add_i32 m0, s25, 0x18000
	v_lshl_add_u64 v[6:7], v[6:7], 0, s[8:9]
	s_lshl_b32 s10, s1, 13
	s_lshl_b32 s12, s11, 7
	s_waitcnt vmcnt(4)
	s_barrier
	global_load_lds_dwordx4 v[6:7], off
	v_lshl_add_u64 v[4:5], v[4:5], 0, s[8:9]
	s_add_i32 m0, s25, 0x1a000
	s_add_i32 s60, s25, 0x8000
	s_add_i32 s61, s25, 0xa000
	global_load_lds_dwordx4 v[4:5], off
	v_lshl_add_u64 v[2:3], v[2:3], 0, s[8:9]
	s_mov_b32 m0, s60
	s_add_u32 s4, s28, 0x80080
	global_load_lds_dwordx4 v[2:3], off
	v_lshl_add_u64 v[0:1], v[0:1], 0, s[8:9]
	s_mov_b32 m0, s61
	s_addc_u32 s5, s29, 0
	global_load_lds_dwordx4 v[0:1], off
	s_add_i32 m0, s25, 0x1c000
	v_lshl_add_u64 v[0:1], s[4:5], 0, v[144:145]
	global_load_lds_dwordx4 v[0:1], off
	v_lshl_add_u64 v[0:1], s[4:5], 0, v[146:147]
	s_add_i32 m0, s25, 0x1e000
	s_sext_i32_i8 s65, s0
	global_load_lds_dwordx4 v[0:1], off
	v_bfe_u32 v1, v8, 4, 2
	v_and_b32_e32 v0, 15, v8
	v_lshlrev_b32_e32 v2, 4, v1
	v_lshl_or_b32 v162, s1, 6, v0
	v_lshl_or_b32 v0, v0, 6, v2
	v_lshlrev_b32_e32 v2, 2, v8
	v_and_b32_e32 v2, 32, v2
	v_bitop3_b32 v3, v0, s10, v2 bitop3:0xde
	v_bitop3_b32 v163, v0, s12, v2 bitop3:0xde
	v_lshlrev_b32_e32 v0, 15, v9
	v_and_b32_e32 v0, 0xffff0000, v0
	v_lshl_or_b32 v164, v1, 2, s11
	v_lshl_add_u32 v0, v10, 12, v0
	v_and_b32_e32 v1, 1, v9
	v_lshl_or_b32 v0, v1, 6, v0
	s_mov_b64 s[0:1], 0x80080
	v_lshl_add_u32 v0, v11, 1, v0
	v_mov_b32_e32 v1, v145
	v_lshl_add_u64 v[148:149], v[0:1], 0, s[0:1]
	v_lshlrev_b32_e32 v0, 15, v12
	v_and_b32_e32 v0, 0xffff0000, v0
	v_lshl_add_u32 v0, v13, 12, v0
	v_and_b32_e32 v1, 1, v12
	s_waitcnt vmcnt(6)
	v_lshl_or_b32 v0, v1, 6, v0
	v_lshl_add_u32 v0, v14, 1, v0
	v_mov_b32_e32 v1, v145
	s_add_i32 s63, 0, 0x10000
	s_add_i32 s64, 0, 0x14000
	s_ashr_i32 s62, s93, 31
	v_lshl_add_u64 v[150:151], v[0:1], 0, s[0:1]
	v_mov_b64_e32 v[152:153], 0x200
	v_mov_b64_e32 v[154:155], 0x1ff
	v_add_u32_e32 v165, s63, v163
	v_add_u32_e32 v166, 0, v3
	v_add_u32_e32 v167, s64, v163
	s_mov_b64 s[10:11], 0x120000
	s_mov_b64 s[12:13], 0x140000
	s_mov_b64 s[14:15], 0x160000
	s_barrier

; #define PG8_LDA(dst, b, h) do { _Pragma("unroll") for (int m = 0; m < 4; ++m) _Pragma("unroll") for (int k = 0; k < 2; ++k) dst[m][k] = *(const LAS bf16x8*)(lds + PG8_SA(b, h) + aoff + m * 2048 + k * 1024); } while (0)
; #define PG8_LDB(dst, b, h) do { _Pragma("unroll") for (int n = 0; n < 2; ++n) _Pragma("unroll") for (int k = 0; k < 2; ++k) dst[n][k] = *(const LAS bf16x8*)(lds + PG8_SB(b, h) + boff + n * 2048 + k * 1024); } while (0)
; #define PG8_MMA(ai, bj, At, Bt) do { __builtin_amdgcn_s_setprio(1); _Pragma("unroll") for (int m = 0; m < 4; ++m) _Pragma("unroll") for (int n = 0; n < 2; ++n) _Pragma("unroll") for (int k = 0; k < 2; ++k) \
;         acc[ai][bj][m][n] = __builtin_amdgcn_mfma_f32_16x16x32_bf16(Bt[n][k], At[m][k], acc[ai][bj][m][n], 0, 0, 0); __builtin_amdgcn_s_setprio(0); } while (0)
; #define PG8_WAIT_L(n) asm volatile("s_waitcnt lgkmcnt(" #n ")" ::: "memory")
; #define PG8_BAR __builtin_amdgcn_s_barrier()
; #define PG8_SCHED __builtin_amdgcn_sched_barrier(0)
; template <class Epi, class Sched>
; __device__ __forceinline__ void gemm_phase(LAS unsigned char* lds, const bf16_t* A, const int K, const Sched& S, const Epi& E, const int wv) {
;     ...
;         for (int t = 0; t < nt; t += 2) {
;             const bool last = (t == nt - 2);
;             const size_t k1 = (size_t)(t + 1) * kstep;
;             const size_t k2 = last ? 0 : (size_t)(t + 2) * kstep, k3 = k2 + kstep;
;             const char* b2 = last ? nB : cB + (size_t)(t + 2) * kstep; const char* b3 = b2 + kstep;
;             PG8_LDB(B0, 0, 0); PG8_SCHED; PG8_LDA(At, 0, 0); PG8_STAGE_A(PG8_SA(1, 1), 1, false, k1);
;             PG8_WAIT_L(8); PG8_BAR; PG8_WAIT_L(0); PG8_MMA(0, 0, At, B0); PG8_BAR; PG8_SCHED;
;     ...
; #pragma unroll
;         for (int a_ = 0; a_ < 2; ++a_)
; #pragma unroll
;             for (int b_ = 0; b_ < 2; ++b_)
; #pragma unroll
;                 for (int m = 0; m < 4; ++m)
; #pragma unroll
;                     for (int n = 0; n < 2; ++n) acc[a_][b_][m][n] = (f32x4){0.f, 0.f, 0.f, 0.f};
;         cur = nxt; cB = nB; cA = nA; ++ui;
.LBB0_832:
	s_ashr_i32 s17, s16, 31
	s_lshl_b64 s[20:21], s[16:17], 20
	s_add_u32 s20, s37, s20
	s_addc_u32 s21, s38, s21
	s_and_b64 s[22:23], s[4:5], exec
	s_cselect_b32 s17, s21, s29
	s_cselect_b32 s66, s20, s28
	s_ashr_i32 s19, s18, 31
	s_lshl_b64 s[22:23], s[18:19], 20
	s_add_u32 s22, s39, s22
	s_addc_u32 s23, s40, s23
	s_add_u32 s19, s28, 0x100
	v_mov_b32_e32 v0, 0
	s_addc_u32 s67, s29, 0
	v_lshl_add_u64 v[128:129], s[26:27], 0, v[148:149]
	v_lshl_add_u64 v[130:131], s[26:27], 0, v[150:151]
	s_mov_b32 s68, -2
	s_mov_b64 s[28:29], 0
	v_mov_b32_e32 v1, v0
	v_mov_b32_e32 v2, v0
	v_mov_b32_e32 v3, v0
	v_mov_b32_e32 v4, v0
	v_mov_b32_e32 v5, v0
	v_mov_b32_e32 v6, v0
	v_mov_b32_e32 v7, v0
	v_mov_b32_e32 v12, v0
	v_mov_b32_e32 v13, v0
	v_mov_b32_e32 v14, v0
	v_mov_b32_e32 v15, v0
	v_mov_b32_e32 v20, v0
	v_mov_b32_e32 v21, v0
	v_mov_b32_e32 v22, v0
	v_mov_b32_e32 v23, v0
	v_mov_b32_e32 v24, v0
	v_mov_b32_e32 v25, v0
	v_mov_b32_e32 v26, v0
	v_mov_b32_e32 v27, v0
	v_mov_b32_e32 v28, v0
	v_mov_b32_e32 v29, v0
	v_mov_b32_e32 v30, v0
	v_mov_b32_e32 v31, v0
	v_mov_b32_e32 v36, v0
	v_mov_b32_e32 v37, v0
	v_mov_b32_e32 v38, v0
	v_mov_b32_e32 v39, v0
	v_mov_b32_e32 v40, v0
	v_mov_b32_e32 v41, v0
	v_mov_b32_e32 v42, v0
	v_mov_b32_e32 v43, v0
	v_mov_b32_e32 v8, v0
	v_mov_b32_e32 v9, v0
	v_mov_b32_e32 v10, v0
	v_mov_b32_e32 v11, v0
	v_mov_b32_e32 v16, v0
	v_mov_b32_e32 v17, v0
	v_mov_b32_e32 v18, v0
	v_mov_b32_e32 v19, v0
	v_mov_b32_e32 v32, v0
	v_mov_b32_e32 v33, v0
	v_mov_b32_e32 v34, v0
	v_mov_b32_e32 v35, v0
	v_mov_b32_e32 v44, v0
	v_mov_b32_e32 v45, v0
	v_mov_b32_e32 v46, v0
	v_mov_b32_e32 v47, v0
	v_mov_b32_e32 v48, v0
	v_mov_b32_e32 v49, v0
	v_mov_b32_e32 v50, v0
	v_mov_b32_e32 v51, v0
	v_mov_b32_e32 v52, v0
	v_mov_b32_e32 v53, v0
	v_mov_b32_e32 v54, v0
	v_mov_b32_e32 v55, v0
	v_mov_b32_e32 v56, v0
	v_mov_b32_e32 v57, v0
	v_mov_b32_e32 v58, v0
	v_mov_b32_e32 v59, v0
	v_mov_b32_e32 v60, v0
	v_mov_b32_e32 v61, v0
	v_mov_b32_e32 v62, v0
	v_mov_b32_e32 v63, v0
	v_mov_b32_e32 v64, v0
	v_mov_b32_e32 v65, v0
	v_mov_b32_e32 v66, v0
	v_mov_b32_e32 v67, v0
	v_mov_b32_e32 v68, v0
	v_mov_b32_e32 v69, v0
	v_mov_b32_e32 v70, v0
	v_mov_b32_e32 v71, v0
	v_mov_b32_e32 v76, v0
	v_mov_b32_e32 v77, v0
	v_mov_b32_e32 v78, v0
	v_mov_b32_e32 v79, v0
	v_mov_b32_e32 v84, v0
	v_mov_b32_e32 v85, v0
	v_mov_b32_e32 v86, v0
	v_mov_b32_e32 v87, v0
	v_mov_b32_e32 v88, v0
	v_mov_b32_e32 v89, v0
	v_mov_b32_e32 v90, v0
	v_mov_b32_e32 v91, v0
	v_mov_b32_e32 v92, v0
	v_mov_b32_e32 v93, v0
	v_mov_b32_e32 v94, v0
	v_mov_b32_e32 v95, v0
	v_mov_b32_e32 v100, v0
	v_mov_b32_e32 v101, v0
	v_mov_b32_e32 v102, v0
	v_mov_b32_e32 v103, v0
	v_mov_b32_e32 v104, v0
	v_mov_b32_e32 v105, v0
	v_mov_b32_e32 v106, v0
	v_mov_b32_e32 v107, v0
	v_mov_b32_e32 v72, v0
	v_mov_b32_e32 v73, v0
	v_mov_b32_e32 v74, v0
	v_mov_b32_e32 v75, v0
	v_mov_b32_e32 v80, v0
	v_mov_b32_e32 v81, v0
	v_mov_b32_e32 v82, v0
	v_mov_b32_e32 v83, v0
	v_mov_b32_e32 v96, v0
	v_mov_b32_e32 v97, v0
	v_mov_b32_e32 v98, v0
	v_mov_b32_e32 v99, v0
	v_mov_b32_e32 v108, v0
	v_mov_b32_e32 v109, v0
	v_mov_b32_e32 v110, v0
	v_mov_b32_e32 v111, v0
	v_mov_b32_e32 v112, v0
	v_mov_b32_e32 v113, v0
	v_mov_b32_e32 v114, v0
	v_mov_b32_e32 v115, v0
	v_mov_b32_e32 v116, v0
	v_mov_b32_e32 v117, v0
	v_mov_b32_e32 v118, v0
	v_mov_b32_e32 v119, v0
	v_mov_b32_e32 v120, v0
	v_mov_b32_e32 v121, v0
	v_mov_b32_e32 v122, v0
	v_mov_b32_e32 v123, v0
	v_mov_b32_e32 v124, v0
	v_mov_b32_e32 v125, v0
	v_mov_b32_e32 v126, v0
	v_mov_b32_e32 v127, v0
	s_bitcmp1_b32 s92, 8
	s_cbranch_scc0 .Lmy_ph_1
	s_barrier
.Lmy_ph_1:
.LBB0_833:
	s_add_u32 s30, s28, 0x100
	ds_read_b128 v[132:135], v165
	ds_read_b128 v[136:139], v165 offset:1024
	ds_read_b128 v[140:143], v165 offset:2048
	ds_read_b128 v[156:159], v165 offset:3072
	s_addc_u32 s31, s29, 0
	s_add_u32 s69, s19, s28
	s_addc_u32 s72, s67, s29
	s_cmp_eq_u32 s68, 28
	s_cselect_b64 s[70:71], -1, 0
	s_and_b64 s[34:35], s[70:71], exec
	s_cselect_b32 s73, 0, s30
	s_cselect_b32 s35, s17, s72
	s_cselect_b32 s34, s66, s69
	v_lshl_add_u64 v[160:161], v[128:129], 0, s[28:29]
	s_add_i32 m0, s25, 0xc000
	ds_read_b128 v[168:171], v166
	ds_read_b128 v[172:175], v166 offset:1024
	ds_read_b128 v[176:179], v166 offset:2048
	ds_read_b128 v[180:183], v166 offset:3072
	ds_read_b128 v[184:187], v166 offset:4096
	ds_read_b128 v[188:191], v166 offset:5120
	ds_read_b128 v[192:195], v166 offset:6144
	ds_read_b128 v[196:199], v166 offset:7168
	global_load_lds_dwordx4 v[160:161], off
	v_lshl_add_u64 v[160:161], v[130:131], 0, s[28:29]
	s_add_i32 m0, s25, 0xe000
	s_nop 0
	global_load_lds_dwordx4 v[160:161], off
	s_waitcnt lgkmcnt(8)
	s_barrier
	s_waitcnt lgkmcnt(0)
	s_setprio 1
	s_waitcnt lgkmcnt(0)
	v_mfma_f32_16x16x32_bf16 v[124:127], v[132:135], v[168:171], v[124:127]
	v_mfma_f32_16x16x32_bf16 v[120:123], v[140:143], v[168:171], v[120:123]
	v_mfma_f32_16x16x32_bf16 v[116:119], v[132:135], v[176:179], v[116:119]
	v_mfma_f32_16x16x32_bf16 v[112:115], v[140:143], v[176:179], v[112:115]
	v_mfma_f32_16x16x32_bf16 v[108:111], v[132:135], v[184:187], v[108:111]
	v_mfma_f32_16x16x32_bf16 v[96:99], v[140:143], v[184:187], v[96:99]
	v_mfma_f32_16x16x32_bf16 v[80:83], v[132:135], v[192:195], v[80:83]
	v_mfma_f32_16x16x32_bf16 v[72:75], v[140:143], v[192:195], v[72:75]
	v_mfma_f32_16x16x32_bf16 v[124:127], v[136:139], v[172:175], v[124:127]
	v_mfma_f32_16x16x32_bf16 v[120:123], v[156:159], v[172:175], v[120:123]
	v_mfma_f32_16x16x32_bf16 v[116:119], v[136:139], v[180:183], v[116:119]
	v_mfma_f32_16x16x32_bf16 v[112:115], v[156:159], v[180:183], v[112:115]
	v_mfma_f32_16x16x32_bf16 v[108:111], v[136:139], v[188:191], v[108:111]
	v_mfma_f32_16x16x32_bf16 v[96:99], v[156:159], v[188:191], v[96:99]
	v_mfma_f32_16x16x32_bf16 v[80:83], v[136:139], v[196:199], v[80:83]
	v_mfma_f32_16x16x32_bf16 v[72:75], v[156:159], v[196:199], v[72:75]
	s_setprio 0
	s_barrier
; #define PG8_STAGE(bufoff, gbase, voff) do { _Pragma("unroll") for (int _i = 0; _i < 2; ++_i) \
;         __builtin_amdgcn_global_load_lds((const unsigned*)((const char*)(gbase) + (voff)[_i]), (LAS unsigned*)(lds + (bufoff) + ldsw + _i * 8192), 16, 0, 0); } while (0)
; #define PG8_LDA(dst, b, h) do { _Pragma("unroll") for (int m = 0; m < 4; ++m) _Pragma("unroll") for (int k = 0; k < 2; ++k) dst[m][k] = *(const LAS bf16x8*)(lds + PG8_SA(b, h) + aoff + m * 2048 + k * 1024); } while (0)
; #define PG8_LDB(dst, b, h) do { _Pragma("unroll") for (int n = 0; n < 2; ++n) _Pragma("unroll") for (int k = 0; k < 2; ++k) dst[n][k] = *(const LAS bf16x8*)(lds + PG8_SB(b, h) + boff + n * 2048 + k * 1024); } while (0)
; #define PG8_MMA(ai, bj, At, Bt) do { __builtin_amdgcn_s_setprio(1); _Pragma("unroll") for (int m = 0; m < 4; ++m) _Pragma("unroll") for (int n = 0; n < 2; ++n) _Pragma("unroll") for (int k = 0; k < 2; ++k) \
;         acc[ai][bj][m][n] = __builtin_amdgcn_mfma_f32_16x16x32_bf16(Bt[n][k], At[m][k], acc[ai][bj][m][n], 0, 0, 0); __builtin_amdgcn_s_setprio(0); } while (0)
; #define PG8_WAIT_V(n) asm volatile("s_waitcnt vmcnt(" #n ")" ::: "memory")
; #define PG8_WAIT_L(n) asm volatile("s_waitcnt lgkmcnt(" #n ")" ::: "memory")
; template <class Epi, class Sched>
; __device__ __forceinline__ void gemm_phase(LAS unsigned char* lds, const bf16_t* A, const int K, const Sched& S, const Epi& E, const int wv) {
;     ...
;             PG8_LDB(B1, 0, 1); PG8_STAGE(PG8_SB(0, 0), b2, voffB);
;             PG8_BAR; PG8_WAIT_L(0); PG8_MMA(0, 1, At, B1); PG8_BAR;
;             PG8_LDA(At, 0, 1); PG8_STAGE_A(PG8_SA(0, 0), 0, last, k2);
;             PG8_BAR; PG8_WAIT_L(0); PG8_MMA(1, 0, At, B0); PG8_BAR; PG8_SCHED;
;             PG8_STAGE(PG8_SB(0, 1), b2 + hstep, voffB);
;             PG8_WAIT_V(6); PG8_BAR; PG8_MMA(1, 1, At, B1); PG8_BAR;
;             PG8_LDB(B0, 1, 0); PG8_SCHED; PG8_LDA(At, 1, 0); PG8_STAGE_A(PG8_SA(0, 1), 1, last, k2);
;             PG8_WAIT_L(8); PG8_BAR; PG8_WAIT_L(0); PG8_MMA(0, 0, At, B0); PG8_BAR; PG8_SCHED;
;             PG8_LDB(B1, 1, 1); PG8_STAGE(PG8_SB(1, 0), b3, voffB);
;             PG8_BAR; PG8_WAIT_L(0); PG8_MMA(0, 1, At, B1); PG8_BAR;
;             PG8_LDA(At, 1, 1); PG8_STAGE_A(PG8_SA(1, 0), 0, last, k3);
;             PG8_BAR; PG8_WAIT_L(0); PG8_MMA(1, 0, At, B0); PG8_BAR; PG8_SCHED;
;             PG8_STAGE(PG8_SB(1, 1), b3 + hstep, voffB);
	s_add_i32 s28, s63, s41
	v_lshl_add_u64 v[160:161], s[34:35], 0, v[144:145]
	s_mov_b32 m0, s28
	ds_read_b128 v[200:203], v167
	ds_read_b128 v[204:207], v167 offset:1024
	ds_read_b128 v[208:211], v167 offset:2048
	ds_read_b128 v[212:215], v167 offset:3072
	global_load_lds_dwordx4 v[160:161], off
	v_lshl_add_u64 v[216:217], s[34:35], 0, v[146:147]
	s_add_i32 m0, s28, 0x2000
	s_nop 0
	global_load_lds_dwordx4 v[216:217], off
	s_barrier
	s_waitcnt lgkmcnt(0)
	s_setprio 1
	s_waitcnt lgkmcnt(0)
	v_mfma_f32_16x16x32_bf16 v[104:107], v[200:203], v[168:171], v[104:107]
	v_mfma_f32_16x16x32_bf16 v[100:103], v[208:211], v[168:171], v[100:103]
	v_mfma_f32_16x16x32_bf16 v[92:95], v[200:203], v[176:179], v[92:95]
	v_mfma_f32_16x16x32_bf16 v[88:91], v[208:211], v[176:179], v[88:91]
	v_mfma_f32_16x16x32_bf16 v[84:87], v[200:203], v[184:187], v[84:87]
	v_mfma_f32_16x16x32_bf16 v[76:79], v[208:211], v[184:187], v[76:79]
	v_mfma_f32_16x16x32_bf16 v[68:71], v[200:203], v[192:195], v[68:71]
	v_mfma_f32_16x16x32_bf16 v[64:67], v[208:211], v[192:195], v[64:67]
	v_mfma_f32_16x16x32_bf16 v[104:107], v[204:207], v[172:175], v[104:107]
	v_mfma_f32_16x16x32_bf16 v[100:103], v[212:215], v[172:175], v[100:103]
	v_mfma_f32_16x16x32_bf16 v[92:95], v[204:207], v[180:183], v[92:95]
	v_mfma_f32_16x16x32_bf16 v[88:91], v[212:215], v[180:183], v[88:91]
	v_mfma_f32_16x16x32_bf16 v[84:87], v[204:207], v[188:191], v[84:87]
	v_mfma_f32_16x16x32_bf16 v[76:79], v[212:215], v[188:191], v[76:79]
	v_mfma_f32_16x16x32_bf16 v[68:71], v[204:207], v[196:199], v[68:71]
	v_mfma_f32_16x16x32_bf16 v[64:67], v[212:215], v[196:199], v[64:67]
	s_setprio 0
	s_and_b64 s[28:29], s[4:5], s[70:71]
	s_and_b64 s[28:29], s[28:29], exec
	s_cselect_b32 s28, s22, s26
	s_cselect_b32 s29, s23, s27
	s_add_u32 s28, s28, s73
	s_addc_u32 s29, s29, 0
	s_mov_b32 m0, s25
	v_lshl_add_u64 v[218:219], s[28:29], 0, v[144:145]
	s_barrier
	ds_read_b128 v[168:171], v166 offset:16384
	ds_read_b128 v[172:175], v166 offset:17408
	ds_read_b128 v[176:179], v166 offset:18432
	ds_read_b128 v[180:183], v166 offset:19456
	ds_read_b128 v[184:187], v166 offset:20480
	ds_read_b128 v[188:191], v166 offset:21504
	ds_read_b128 v[192:195], v166 offset:22528
	ds_read_b128 v[196:199], v166 offset:23552
	global_load_lds_dwordx4 v[218:219], off
	v_lshl_add_u64 v[220:221], s[28:29], 0, v[146:147]
	s_mov_b32 m0, s42
	s_nop 0
	global_load_lds_dwordx4 v[220:221], off
	s_barrier
	s_waitcnt lgkmcnt(0)
	s_setprio 1
	s_waitcnt lgkmcnt(0)
	v_mfma_f32_16x16x32_bf16 v[60:63], v[132:135], v[168:171], v[60:63]
	v_mfma_f32_16x16x32_bf16 v[56:59], v[140:143], v[168:171], v[56:59]
	v_mfma_f32_16x16x32_bf16 v[52:55], v[132:135], v[176:179], v[52:55]
	v_mfma_f32_16x16x32_bf16 v[48:51], v[140:143], v[176:179], v[48:51]
	v_mfma_f32_16x16x32_bf16 v[44:47], v[132:135], v[184:187], v[44:47]
	v_mfma_f32_16x16x32_bf16 v[32:35], v[140:143], v[184:187], v[32:35]
	v_mfma_f32_16x16x32_bf16 v[16:19], v[132:135], v[192:195], v[16:19]
	v_mfma_f32_16x16x32_bf16 v[8:11], v[140:143], v[192:195], v[8:11]
	v_mfma_f32_16x16x32_bf16 v[60:63], v[136:139], v[172:175], v[60:63]
	v_mfma_f32_16x16x32_bf16 v[56:59], v[156:159], v[172:175], v[56:59]
	v_mfma_f32_16x16x32_bf16 v[52:55], v[136:139], v[180:183], v[52:55]
	v_mfma_f32_16x16x32_bf16 v[48:51], v[156:159], v[180:183], v[48:51]
	v_mfma_f32_16x16x32_bf16 v[44:47], v[136:139], v[188:191], v[44:47]
	v_mfma_f32_16x16x32_bf16 v[32:35], v[156:159], v[188:191], v[32:35]
	v_mfma_f32_16x16x32_bf16 v[16:19], v[136:139], v[196:199], v[16:19]
	v_mfma_f32_16x16x32_bf16 v[8:11], v[156:159], v[196:199], v[8:11]
	s_setprio 0
	s_barrier
	s_add_u32 s70, s34, 0x80000
	s_addc_u32 s71, s35, 0
	s_add_i32 s69, s64, s41
	v_lshl_add_u64 v[132:133], s[70:71], 0, v[144:145]
	s_mov_b32 m0, s69
	s_nop 0
	global_load_lds_dwordx4 v[132:133], off
	v_lshl_add_u64 v[132:133], s[70:71], 0, v[146:147]
	s_add_i32 m0, s69, 0x2000
	s_nop 0
	global_load_lds_dwordx4 v[132:133], off
	s_waitcnt vmcnt(6)
	s_barrier
	s_setprio 1
	v_mfma_f32_16x16x32_bf16 v[40:43], v[200:203], v[168:171], v[40:43]
	v_mfma_f32_16x16x32_bf16 v[36:39], v[208:211], v[168:171], v[36:39]
	v_mfma_f32_16x16x32_bf16 v[28:31], v[200:203], v[176:179], v[28:31]
	v_mfma_f32_16x16x32_bf16 v[24:27], v[208:211], v[176:179], v[24:27]
	v_mfma_f32_16x16x32_bf16 v[20:23], v[200:203], v[184:187], v[20:23]
	v_mfma_f32_16x16x32_bf16 v[12:15], v[208:211], v[184:187], v[12:15]
	v_mfma_f32_16x16x32_bf16 v[4:7], v[200:203], v[192:195], v[4:7]
	v_mfma_f32_16x16x32_bf16 v[0:3], v[208:211], v[192:195], v[0:3]
	v_mfma_f32_16x16x32_bf16 v[40:43], v[204:207], v[172:175], v[40:43]
	v_mfma_f32_16x16x32_bf16 v[36:39], v[212:215], v[172:175], v[36:39]
	v_mfma_f32_16x16x32_bf16 v[28:31], v[204:207], v[180:183], v[28:31]
	v_mfma_f32_16x16x32_bf16 v[24:27], v[212:215], v[180:183], v[24:27]
	v_mfma_f32_16x16x32_bf16 v[20:23], v[204:207], v[188:191], v[20:23]
	v_mfma_f32_16x16x32_bf16 v[12:15], v[212:215], v[188:191], v[12:15]
	v_mfma_f32_16x16x32_bf16 v[4:7], v[204:207], v[196:199], v[4:7]
	v_mfma_f32_16x16x32_bf16 v[0:3], v[212:215], v[196:199], v[0:3]
	s_setprio 0
	s_add_i32 s69, 0, 0x18000
	v_add_u32_e32 v156, s69, v163
	s_barrier
	ds_read_b128 v[132:135], v156
	ds_read_b128 v[136:139], v156 offset:1024
	ds_read_b128 v[140:143], v156 offset:2048
	ds_read_b128 v[156:159], v156 offset:3072
	s_add_u32 s28, s28, 0x80000
	s_addc_u32 s29, s29, 0
	s_mov_b32 m0, s43
	v_lshl_add_u64 v[200:201], s[28:29], 0, v[144:145]
	ds_read_b128 v[168:171], v166 offset:32768
	ds_read_b128 v[172:175], v166 offset:33792
	ds_read_b128 v[176:179], v166 offset:34816
	ds_read_b128 v[180:183], v166 offset:35840
	ds_read_b128 v[184:187], v166 offset:36864
	ds_read_b128 v[188:191], v166 offset:37888
	ds_read_b128 v[192:195], v166 offset:38912
	ds_read_b128 v[196:199], v166 offset:39936
	global_load_lds_dwordx4 v[200:201], off
	v_lshl_add_u64 v[200:201], s[28:29], 0, v[146:147]
	s_mov_b32 m0, s50
	s_nop 0
	global_load_lds_dwordx4 v[200:201], off
	s_waitcnt lgkmcnt(8)
	s_barrier
; #define PG8_STAGE(bufoff, gbase, voff) do { _Pragma("unroll") for (int _i = 0; _i < 2; ++_i) \
;         __builtin_amdgcn_global_load_lds((const unsigned*)((const char*)(gbase) + (voff)[_i]), (LAS unsigned*)(lds + (bufoff) + ldsw + _i * 8192), 16, 0, 0); } while (0)
; #define PG8_LDA(dst, b, h) do { _Pragma("unroll") for (int m = 0; m < 4; ++m) _Pragma("unroll") for (int k = 0; k < 2; ++k) dst[m][k] = *(const LAS bf16x8*)(lds + PG8_SA(b, h) + aoff + m * 2048 + k * 1024); } while (0)
; #define PG8_LDB(dst, b, h) do { _Pragma("unroll") for (int n = 0; n < 2; ++n) _Pragma("unroll") for (int k = 0; k < 2; ++k) dst[n][k] = *(const LAS bf16x8*)(lds + PG8_SB(b, h) + boff + n * 2048 + k * 1024); } while (0)
; #define PG8_MMA(ai, bj, At, Bt) do { __builtin_amdgcn_s_setprio(1); _Pragma("unroll") for (int m = 0; m < 4; ++m) _Pragma("unroll") for (int n = 0; n < 2; ++n) _Pragma("unroll") for (int k = 0; k < 2; ++k) \
;         acc[ai][bj][m][n] = __builtin_amdgcn_mfma_f32_16x16x32_bf16(Bt[n][k], At[m][k], acc[ai][bj][m][n], 0, 0, 0); __builtin_amdgcn_s_setprio(0); } while (0)
; #define PG8_WAIT_V(n) asm volatile("s_waitcnt vmcnt(" #n ")" ::: "memory")
; #define PG8_WAIT_L(n) asm volatile("s_waitcnt lgkmcnt(" #n ")" ::: "memory")
; #define PG8_BAR __builtin_amdgcn_s_barrier()
; #define PG8_SCHED __builtin_amdgcn_sched_barrier(0)
; template <class Epi, class Sched>
; __device__ __forceinline__ void gemm_phase(LAS unsigned char* lds, const bf16_t* A, const int K, const Sched& S, const Epi& E, const int wv) {
;     ...
;             PG8_LDB(B0, 1, 0); PG8_SCHED; PG8_LDA(At, 1, 0); PG8_STAGE_A(PG8_SA(0, 1), 1, last, k2);
;             PG8_WAIT_L(8); PG8_BAR; PG8_WAIT_L(0); PG8_MMA(0, 0, At, B0); PG8_BAR; PG8_SCHED;
;             PG8_LDB(B1, 1, 1); PG8_STAGE(PG8_SB(1, 0), b3, voffB);
;             PG8_BAR; PG8_WAIT_L(0); PG8_MMA(0, 1, At, B1); PG8_BAR;
;             PG8_LDA(At, 1, 1); PG8_STAGE_A(PG8_SA(1, 0), 0, last, k3);
;             PG8_BAR; PG8_WAIT_L(0); PG8_MMA(1, 0, At, B0); PG8_BAR; PG8_SCHED;
;             PG8_STAGE(PG8_SB(1, 1), b3 + hstep, voffB);
;             PG8_WAIT_V(6); PG8_BAR; PG8_MMA(1, 1, At, B1); PG8_BAR;
;         }
	s_waitcnt lgkmcnt(0)
	s_setprio 1
	s_waitcnt lgkmcnt(0)
	v_mfma_f32_16x16x32_bf16 v[124:127], v[132:135], v[168:171], v[124:127]
	v_mfma_f32_16x16x32_bf16 v[120:123], v[140:143], v[168:171], v[120:123]
	v_mfma_f32_16x16x32_bf16 v[116:119], v[132:135], v[176:179], v[116:119]
	v_mfma_f32_16x16x32_bf16 v[112:115], v[140:143], v[176:179], v[112:115]
	v_mfma_f32_16x16x32_bf16 v[108:111], v[132:135], v[184:187], v[108:111]
	v_mfma_f32_16x16x32_bf16 v[96:99], v[140:143], v[184:187], v[96:99]
	v_mfma_f32_16x16x32_bf16 v[80:83], v[132:135], v[192:195], v[80:83]
	v_mfma_f32_16x16x32_bf16 v[72:75], v[140:143], v[192:195], v[72:75]
	v_mfma_f32_16x16x32_bf16 v[124:127], v[136:139], v[172:175], v[124:127]
	v_mfma_f32_16x16x32_bf16 v[120:123], v[156:159], v[172:175], v[120:123]
	v_mfma_f32_16x16x32_bf16 v[116:119], v[136:139], v[180:183], v[116:119]
	v_mfma_f32_16x16x32_bf16 v[112:115], v[156:159], v[180:183], v[112:115]
	v_mfma_f32_16x16x32_bf16 v[108:111], v[136:139], v[188:191], v[108:111]
	v_mfma_f32_16x16x32_bf16 v[96:99], v[156:159], v[188:191], v[96:99]
	v_mfma_f32_16x16x32_bf16 v[80:83], v[136:139], v[196:199], v[80:83]
	v_mfma_f32_16x16x32_bf16 v[72:75], v[156:159], v[196:199], v[72:75]
	s_setprio 0
	s_barrier
	s_add_i32 s70, 0, 0x1c000
	s_add_i32 s28, s69, s41
	v_add_u32_e32 v212, s70, v163
	v_lshl_add_u64 v[160:161], v[160:161], 0, s[8:9]
	s_mov_b32 m0, s28
	ds_read_b128 v[200:203], v212
	ds_read_b128 v[204:207], v212 offset:1024
	ds_read_b128 v[208:211], v212 offset:2048
	ds_read_b128 v[212:215], v212 offset:3072
	global_load_lds_dwordx4 v[160:161], off
	v_lshl_add_u64 v[160:161], v[216:217], 0, s[8:9]
	s_add_i32 m0, s28, 0x2000
	s_nop 0
	global_load_lds_dwordx4 v[160:161], off
	s_barrier
	s_waitcnt lgkmcnt(0)
	s_setprio 1
	s_waitcnt lgkmcnt(0)
	v_mfma_f32_16x16x32_bf16 v[104:107], v[200:203], v[168:171], v[104:107]
	v_mfma_f32_16x16x32_bf16 v[100:103], v[208:211], v[168:171], v[100:103]
	v_mfma_f32_16x16x32_bf16 v[92:95], v[200:203], v[176:179], v[92:95]
	v_mfma_f32_16x16x32_bf16 v[88:91], v[208:211], v[176:179], v[88:91]
	v_mfma_f32_16x16x32_bf16 v[84:87], v[200:203], v[184:187], v[84:87]
	v_mfma_f32_16x16x32_bf16 v[76:79], v[208:211], v[184:187], v[76:79]
	v_mfma_f32_16x16x32_bf16 v[68:71], v[200:203], v[192:195], v[68:71]
	v_mfma_f32_16x16x32_bf16 v[64:67], v[208:211], v[192:195], v[64:67]
	v_mfma_f32_16x16x32_bf16 v[104:107], v[204:207], v[172:175], v[104:107]
	v_mfma_f32_16x16x32_bf16 v[100:103], v[212:215], v[172:175], v[100:103]
	v_mfma_f32_16x16x32_bf16 v[92:95], v[204:207], v[180:183], v[92:95]
	v_mfma_f32_16x16x32_bf16 v[88:91], v[212:215], v[180:183], v[88:91]
	v_mfma_f32_16x16x32_bf16 v[84:87], v[204:207], v[188:191], v[84:87]
	v_mfma_f32_16x16x32_bf16 v[76:79], v[212:215], v[188:191], v[76:79]
	v_mfma_f32_16x16x32_bf16 v[68:71], v[204:207], v[196:199], v[68:71]
	v_mfma_f32_16x16x32_bf16 v[64:67], v[212:215], v[196:199], v[64:67]
	s_setprio 0
	s_mov_b32 m0, s60
	v_lshl_add_u64 v[160:161], v[218:219], 0, s[8:9]
	s_barrier
	ds_read_b128 v[168:171], v166 offset:49152
	ds_read_b128 v[172:175], v166 offset:50176
	ds_read_b128 v[176:179], v166 offset:51200
	ds_read_b128 v[180:183], v166 offset:52224
	ds_read_b128 v[184:187], v166 offset:53248
	ds_read_b128 v[188:191], v166 offset:54272
	ds_read_b128 v[192:195], v166 offset:55296
	ds_read_b128 v[196:199], v166 offset:56320
	global_load_lds_dwordx4 v[160:161], off
	v_lshl_add_u64 v[160:161], v[220:221], 0, s[8:9]
	s_mov_b32 m0, s61
	s_nop 0
	global_load_lds_dwordx4 v[160:161], off
	s_barrier
	s_waitcnt lgkmcnt(0)
	s_setprio 1
	s_waitcnt lgkmcnt(0)
	v_mfma_f32_16x16x32_bf16 v[60:63], v[132:135], v[168:171], v[60:63]
	v_mfma_f32_16x16x32_bf16 v[56:59], v[140:143], v[168:171], v[56:59]
	v_mfma_f32_16x16x32_bf16 v[52:55], v[132:135], v[176:179], v[52:55]
	v_mfma_f32_16x16x32_bf16 v[48:51], v[140:143], v[176:179], v[48:51]
	v_mfma_f32_16x16x32_bf16 v[44:47], v[132:135], v[184:187], v[44:47]
	v_mfma_f32_16x16x32_bf16 v[32:35], v[140:143], v[184:187], v[32:35]
	v_mfma_f32_16x16x32_bf16 v[16:19], v[132:135], v[192:195], v[16:19]
	v_mfma_f32_16x16x32_bf16 v[8:11], v[140:143], v[192:195], v[8:11]
	v_mfma_f32_16x16x32_bf16 v[60:63], v[136:139], v[172:175], v[60:63]
	v_mfma_f32_16x16x32_bf16 v[56:59], v[156:159], v[172:175], v[56:59]
	v_mfma_f32_16x16x32_bf16 v[52:55], v[136:139], v[180:183], v[52:55]
	v_mfma_f32_16x16x32_bf16 v[48:51], v[156:159], v[180:183], v[48:51]
	v_mfma_f32_16x16x32_bf16 v[44:47], v[136:139], v[188:191], v[44:47]
	v_mfma_f32_16x16x32_bf16 v[32:35], v[156:159], v[188:191], v[32:35]
	v_mfma_f32_16x16x32_bf16 v[16:19], v[136:139], v[196:199], v[16:19]
	v_mfma_f32_16x16x32_bf16 v[8:11], v[156:159], v[196:199], v[8:11]
	s_setprio 0
	s_barrier
	s_add_u32 s28, s34, 0x80080
	s_addc_u32 s29, s35, 0
	s_add_i32 s34, s70, s41
	v_lshl_add_u64 v[132:133], s[28:29], 0, v[144:145]
	s_mov_b32 m0, s34
	s_nop 0
	global_load_lds_dwordx4 v[132:133], off
	v_lshl_add_u64 v[132:133], s[28:29], 0, v[146:147]
	s_add_i32 m0, s34, 0x2000
	s_nop 0
	global_load_lds_dwordx4 v[132:133], off
	s_waitcnt vmcnt(6)
	s_barrier
	s_setprio 1
	v_mfma_f32_16x16x32_bf16 v[40:43], v[200:203], v[168:171], v[40:43]
	v_mfma_f32_16x16x32_bf16 v[36:39], v[208:211], v[168:171], v[36:39]
	v_mfma_f32_16x16x32_bf16 v[28:31], v[200:203], v[176:179], v[28:31]
	v_mfma_f32_16x16x32_bf16 v[24:27], v[208:211], v[176:179], v[24:27]
	v_mfma_f32_16x16x32_bf16 v[20:23], v[200:203], v[184:187], v[20:23]
	v_mfma_f32_16x16x32_bf16 v[12:15], v[208:211], v[184:187], v[12:15]
	v_mfma_f32_16x16x32_bf16 v[4:7], v[200:203], v[192:195], v[4:7]
	v_mfma_f32_16x16x32_bf16 v[0:3], v[208:211], v[192:195], v[0:3]
	v_mfma_f32_16x16x32_bf16 v[40:43], v[204:207], v[172:175], v[40:43]
	v_mfma_f32_16x16x32_bf16 v[36:39], v[212:215], v[172:175], v[36:39]
	v_mfma_f32_16x16x32_bf16 v[28:31], v[204:207], v[180:183], v[28:31]
	v_mfma_f32_16x16x32_bf16 v[24:27], v[212:215], v[180:183], v[24:27]
	v_mfma_f32_16x16x32_bf16 v[20:23], v[204:207], v[188:191], v[20:23]
	v_mfma_f32_16x16x32_bf16 v[12:15], v[212:215], v[188:191], v[12:15]
	v_mfma_f32_16x16x32_bf16 v[4:7], v[204:207], v[196:199], v[4:7]
	v_mfma_f32_16x16x32_bf16 v[0:3], v[212:215], v[196:199], v[0:3]
	s_setprio 0
	s_add_i32 s68, s68, 2
	s_cmp_gt_u32 s68, 29
	s_mov_b64 s[28:29], s[30:31]
	s_cbranch_scc1 .Lmy_kx_1
	s_barrier
	s_branch .LBB0_833

;     __device__ __forceinline__ void operator()(const f32x4 (&acc)[2][2][4][2], const Unit& u, int wr, int wc, int fr, int fq) const {
;         const int row0 = u.pm * BM + wr * 64 + fr, col0 = u.pn * BM + wc * 32 + 4 * fq;
;         const int b = u.pm >> 3;
;         f32x4 gv[2][2];
; #pragma unroll
;         for (int bj = 0; bj < 2; ++bj)
; #pragma unroll
;             for (int n = 0; n < 2; ++n) gv[bj][n] = *(const f32x4*)(gate + (size_t)b * (6 * DM) + col0 + bj * HALF + n * 16);
; #pragma unroll
;         for (int ai = 0; ai < 2; ++ai) {
;             f32x4 rv[4][2][2];
; #pragma unroll
;             for (int m = 0; m < 4; ++m) { const size_t off = (size_t)(row0 + ai * HALF + m * 16) * DM + col0;
; #pragma unroll
;                 for (int bj = 0; bj < 2; ++bj)
; #pragma unroll
;                     for (int n = 0; n < 2; ++n) rv[m][bj][n] = *(const f32x4*)(res + off + bj * HALF + n * 16); }
; #pragma unroll
;             for (int m = 0; m < 4; ++m) { const size_t off = (size_t)(row0 + ai * HALF + m * 16) * DM + col0;
; #pragma unroll
;                 for (int bj = 0; bj < 2; ++bj)
; #pragma unroll
;                     for (int n = 0; n < 2; ++n) *(f32x4*)(out + off + bj * HALF + n * 16) = rv[m][bj][n] + gv[bj][n] * acc[ai][bj][m][n]; }
.Lmy_kxb_1:
	v_lshl_or_b32 v128, s65, 8, v164
	s_ashr_i32 s4, s24, 3
	v_lshl_add_u32 v216, s24, 8, v162
	s_mul_hi_i32 s5, s4, 0xc000
	s_mul_i32 s4, s4, 0xc000
	v_ashrrev_i32_e32 v129, 31, v128
	v_readlane_b32 s68, v252, 2
	v_or_b32_e32 v184, 16, v216
	v_or_b32_e32 v200, 32, v216
	s_add_u32 s4, s54, s4
	v_lshlrev_b64 v[156:157], 2, v[128:129]
	v_readlane_b32 s69, v252, 3
	v_ashrrev_i32_e32 v217, 31, v216
	v_ashrrev_i32_e32 v185, 31, v184
	v_ashrrev_i32_e32 v201, 31, v200
	s_addc_u32 s5, s55, s5
	v_lshl_add_u64 v[158:159], s[68:69], 0, v[156:157]
	v_lshlrev_b64 v[160:161], 13, v[216:217]
	v_lshlrev_b64 v[232:233], 13, v[184:185]
	v_lshlrev_b64 v[234:235], 13, v[200:201]
	v_or_b32_e32 v216, 48, v216
	v_lshl_add_u64 v[128:129], s[4:5], 0, v[156:157]
	v_lshl_add_u64 v[180:181], v[158:159], 0, v[160:161]
	v_lshl_add_u64 v[196:197], v[158:159], 0, v[232:233]
	v_lshl_add_u64 v[212:213], v[158:159], 0, v[234:235]
	v_ashrrev_i32_e32 v217, 31, v216
	global_load_dwordx4 v[140:143], v[128:129], off
	global_load_dwordx4 v[136:139], v[128:129], off offset:64
	global_load_dwordx4 v[132:135], v[128:129], off offset:512
	s_nop 0
	global_load_dwordx4 v[128:131], v[128:129], off offset:576
	s_nop 0
	global_load_dwordx4 v[168:171], v[180:181], off
	global_load_dwordx4 v[172:175], v[180:181], off offset:64
	global_load_dwordx4 v[176:179], v[180:181], off offset:512
	s_nop 0
	global_load_dwordx4 v[180:183], v[180:181], off offset:576
	s_nop 0
	global_load_dwordx4 v[184:187], v[196:197], off
	global_load_dwordx4 v[188:191], v[196:197], off offset:64
	global_load_dwordx4 v[192:195], v[196:197], off offset:512
	s_nop 0
	global_load_dwordx4 v[196:199], v[196:197], off offset:576
	s_nop 0
	global_load_dwordx4 v[200:203], v[212:213], off
	global_load_dwordx4 v[204:207], v[212:213], off offset:64
	global_load_dwordx4 v[208:211], v[212:213], off offset:512
	s_nop 0
	global_load_dwordx4 v[212:215], v[212:213], off offset:576
	v_lshlrev_b64 v[236:237], 13, v[216:217]
	v_lshl_add_u64 v[228:229], v[158:159], 0, v[236:237]
	global_load_dwordx4 v[216:219], v[228:229], off
	global_load_dwordx4 v[220:223], v[228:229], off offset:64
	global_load_dwordx4 v[224:227], v[228:229], off offset:512
	s_nop 0
	global_load_dwordx4 v[228:231], v[228:229], off offset:576
	v_lshl_add_u64 v[238:239], s[6:7], 0, v[160:161]
	v_lshl_add_u64 v[238:239], v[238:239], 0, v[156:157]
	v_lshl_add_u64 v[232:233], s[6:7], 0, v[232:233]
	v_lshl_add_u64 v[234:235], s[6:7], 0, v[234:235]
	v_lshl_add_u64 v[232:233], v[232:233], 0, v[156:157]
	v_lshl_add_u64 v[234:235], v[234:235], 0, v[156:157]
	s_mov_b64 s[4:5], 0x100000
	v_readlane_b32 s76, v252, 10
	v_readlane_b32 s77, v252, 11
	v_readlane_b32 s78, v252, 12
	v_readlane_b32 s79, v252, 13
	v_readlane_b32 s76, v252, 28
	s_and_b64 vcc, exec, s[0:1]
	s_mov_b32 s65, s16
	s_mov_b32 s24, s18
	s_mov_b64 s[28:29], s[20:21]
	s_mov_b64 s[26:27], s[22:23]
	v_readlane_b32 s77, v252, 29
	v_readlane_b32 s78, v252, 30
	v_readlane_b32 s79, v252, 31
	v_readlane_b32 s70, v252, 4
	v_readlane_b32 s71, v252, 5
	v_readlane_b32 s72, v252, 6
	v_readlane_b32 s73, v252, 7
	v_readlane_b32 s74, v252, 8
	v_readlane_b32 s75, v252, 9
	v_readlane_b32 s80, v252, 14
	v_readlane_b32 s81, v252, 15
	v_readlane_b32 s82, v252, 16
	v_readlane_b32 s83, v252, 17
	s_waitcnt vmcnt(0)
	v_pk_fma_f32 v[126:127], v[126:127], v[142:143], v[170:171]
	v_pk_fma_f32 v[124:125], v[124:125], v[140:141], v[168:169]
	v_pk_fma_f32 v[122:123], v[122:123], v[138:139], v[174:175]
	v_pk_fma_f32 v[120:121], v[120:121], v[136:137], v[172:173]
	v_pk_fma_f32 v[106:107], v[106:107], v[134:135], v[178:179]
	v_pk_fma_f32 v[76:77], v[76:77], v[128:129], v[212:213]
	v_pk_fma_f32 v[104:105], v[104:105], v[132:133], v[176:177]
	v_pk_fma_f32 v[102:103], v[102:103], v[130:131], v[182:183]
	v_pk_fma_f32 v[100:101], v[100:101], v[128:129], v[180:181]
	v_pk_fma_f32 v[118:119], v[118:119], v[142:143], v[186:187]
	v_pk_fma_f32 v[116:117], v[116:117], v[140:141], v[184:185]
	v_pk_fma_f32 v[114:115], v[114:115], v[138:139], v[190:191]
	v_pk_fma_f32 v[112:113], v[112:113], v[136:137], v[188:189]
	v_pk_fma_f32 v[94:95], v[94:95], v[134:135], v[194:195]
	v_pk_fma_f32 v[92:93], v[92:93], v[132:133], v[192:193]
	v_pk_fma_f32 v[90:91], v[90:91], v[130:131], v[198:199]
	v_pk_fma_f32 v[88:89], v[88:89], v[128:129], v[196:197]
	v_pk_fma_f32 v[110:111], v[110:111], v[142:143], v[202:203]
	v_pk_fma_f32 v[108:109], v[108:109], v[140:141], v[200:201]
	v_pk_fma_f32 v[98:99], v[98:99], v[138:139], v[206:207]
	v_pk_fma_f32 v[96:97], v[96:97], v[136:137], v[204:205]
	v_pk_fma_f32 v[86:87], v[86:87], v[134:135], v[210:211]
	v_pk_fma_f32 v[84:85], v[84:85], v[132:133], v[208:209]
	v_pk_fma_f32 v[78:79], v[78:79], v[130:131], v[214:215]
	global_store_dwordx4 v[238:239], v[124:127], off
	global_store_dwordx4 v[238:239], v[120:123], off offset:64
	global_store_dwordx4 v[238:239], v[104:107], off offset:512
	global_store_dwordx4 v[238:239], v[100:103], off offset:576
	global_store_dwordx4 v[232:233], v[116:119], off
	global_store_dwordx4 v[232:233], v[112:115], off offset:64
	global_store_dwordx4 v[232:233], v[92:95], off offset:512
	global_store_dwordx4 v[232:233], v[88:91], off offset:576
	global_store_dwordx4 v[234:235], v[108:111], off
	global_store_dwordx4 v[234:235], v[96:99], off offset:64
	global_store_dwordx4 v[234:235], v[84:87], off offset:512
; #define PG8_WAIT_V(n) asm volatile("s_waitcnt vmcnt(" #n ")" ::: "memory")
; #define PG8_BAR __builtin_amdgcn_s_barrier()
; template <class Epi, class Sched>
; __device__ __forceinline__ void gemm_phase(LAS unsigned char* lds, const bf16_t* A, const int K, const Sched& S, const Epi& E, const int wv) {
;     ...
;     PG8_WAIT_V(0);
;     if (wr == 0) PG8_BAR;
;     PG8_BAR;
;     __device__ __forceinline__ void operator()(const f32x4 (&acc)[2][2][4][2], const Unit& u, int wr, int wc, int fr, int fq) const {
;     ...
;             for (int m = 0; m < 4; ++m) { const size_t off = (size_t)(row0 + ai * HALF + m * 16) * DM + col0;
; #pragma unroll
;                 for (int bj = 0; bj < 2; ++bj)
; #pragma unroll
;                     for (int n = 0; n < 2; ++n) rv[m][bj][n] = *(const f32x4*)(res + off + bj * HALF + n * 16); }
; #pragma unroll
;             for (int m = 0; m < 4; ++m) { const size_t off = (size_t)(row0 + ai * HALF + m * 16) * DM + col0;
; #pragma unroll
;                 for (int bj = 0; bj < 2; ++bj)
; #pragma unroll
;                     for (int n = 0; n < 2; ++n) *(f32x4*)(out + off + bj * HALF + n * 16) = rv[m][bj][n] + gv[bj][n] * acc[ai][bj][m][n]; }
;             asm volatile("" ::: "memory");
	global_store_dwordx4 v[234:235], v[76:79], off offset:576
	v_pk_fma_f32 v[74:75], v[74:75], v[138:139], v[222:223]
	v_pk_fma_f32 v[72:73], v[72:73], v[136:137], v[220:221]
	v_pk_fma_f32 v[76:77], v[80:81], v[140:141], v[216:217]
	v_lshl_add_u64 v[80:81], s[6:7], 0, v[236:237]
	v_pk_fma_f32 v[78:79], v[82:83], v[142:143], v[218:219]
	v_lshl_add_u64 v[80:81], v[80:81], 0, v[156:157]
	v_pk_fma_f32 v[70:71], v[70:71], v[134:135], v[226:227]
	v_pk_fma_f32 v[68:69], v[68:69], v[132:133], v[224:225]
	v_pk_fma_f32 v[66:67], v[66:67], v[130:131], v[230:231]
	v_pk_fma_f32 v[64:65], v[64:65], v[128:129], v[228:229]
	global_store_dwordx4 v[80:81], v[76:79], off
	global_store_dwordx4 v[80:81], v[72:75], off offset:64
	global_store_dwordx4 v[80:81], v[68:71], off offset:512
	global_store_dwordx4 v[80:81], v[64:67], off offset:576
	v_lshl_add_u64 v[168:169], v[160:161], 0, s[4:5]
	v_lshl_add_u64 v[170:171], v[160:161], 0, s[10:11]
	v_lshl_add_u64 v[172:173], v[160:161], 0, s[12:13]
	v_lshl_add_u64 v[76:77], v[158:159], 0, v[168:169]
	v_lshl_add_u64 v[92:93], v[158:159], 0, v[170:171]
	v_lshl_add_u64 v[108:109], v[158:159], 0, v[172:173]
	global_load_dwordx4 v[64:67], v[76:77], off
	global_load_dwordx4 v[68:71], v[76:77], off offset:64
	global_load_dwordx4 v[72:75], v[76:77], off offset:512
	s_nop 0
	global_load_dwordx4 v[76:79], v[76:77], off offset:576
	s_nop 0
	global_load_dwordx4 v[80:83], v[92:93], off
	global_load_dwordx4 v[84:87], v[92:93], off offset:64
	global_load_dwordx4 v[88:91], v[92:93], off offset:512
	s_nop 0
	global_load_dwordx4 v[92:95], v[92:93], off offset:576
	s_nop 0
	global_load_dwordx4 v[96:99], v[108:109], off
	global_load_dwordx4 v[100:103], v[108:109], off offset:64
	global_load_dwordx4 v[104:107], v[108:109], off offset:512
	s_nop 0
	global_load_dwordx4 v[108:111], v[108:109], off offset:576
	v_lshl_add_u64 v[160:161], v[160:161], 0, s[14:15]
	v_lshl_add_u64 v[124:125], v[158:159], 0, v[160:161]
	global_load_dwordx4 v[112:115], v[124:125], off
	global_load_dwordx4 v[116:119], v[124:125], off offset:64
	global_load_dwordx4 v[120:123], v[124:125], off offset:512
	s_nop 0
	global_load_dwordx4 v[124:127], v[124:125], off offset:576
	v_lshl_add_u64 v[158:159], s[6:7], 0, v[168:169]
	v_lshl_add_u64 v[168:169], s[6:7], 0, v[170:171]
	v_lshl_add_u64 v[170:171], s[6:7], 0, v[172:173]
	v_lshl_add_u64 v[158:159], v[158:159], 0, v[156:157]
	v_lshl_add_u64 v[168:169], v[168:169], 0, v[156:157]
	v_lshl_add_u64 v[170:171], v[170:171], 0, v[156:157]
	s_waitcnt vmcnt(0)
	v_pk_fma_f32 v[62:63], v[62:63], v[142:143], v[66:67]
	v_pk_fma_f32 v[60:61], v[60:61], v[140:141], v[64:65]
	v_pk_fma_f32 v[58:59], v[58:59], v[138:139], v[70:71]
	v_pk_fma_f32 v[56:57], v[56:57], v[136:137], v[68:69]
	v_pk_fma_f32 v[42:43], v[42:43], v[134:135], v[74:75]
	v_pk_fma_f32 v[12:13], v[12:13], v[128:129], v[108:109]
	v_pk_fma_f32 v[40:41], v[40:41], v[132:133], v[72:73]
	v_pk_fma_f32 v[38:39], v[38:39], v[130:131], v[78:79]
	v_pk_fma_f32 v[36:37], v[36:37], v[128:129], v[76:77]
	v_pk_fma_f32 v[54:55], v[54:55], v[142:143], v[82:83]
	v_pk_fma_f32 v[52:53], v[52:53], v[140:141], v[80:81]
	v_pk_fma_f32 v[50:51], v[50:51], v[138:139], v[86:87]
	v_pk_fma_f32 v[48:49], v[48:49], v[136:137], v[84:85]
	v_pk_fma_f32 v[30:31], v[30:31], v[134:135], v[90:91]
	v_pk_fma_f32 v[28:29], v[28:29], v[132:133], v[88:89]
	v_pk_fma_f32 v[26:27], v[26:27], v[130:131], v[94:95]
	v_pk_fma_f32 v[24:25], v[24:25], v[128:129], v[92:93]
	v_pk_fma_f32 v[46:47], v[46:47], v[142:143], v[98:99]
	v_pk_fma_f32 v[44:45], v[44:45], v[140:141], v[96:97]
	v_pk_fma_f32 v[34:35], v[34:35], v[138:139], v[102:103]
	v_pk_fma_f32 v[32:33], v[32:33], v[136:137], v[100:101]
	v_pk_fma_f32 v[22:23], v[22:23], v[134:135], v[106:107]
	v_pk_fma_f32 v[20:21], v[20:21], v[132:133], v[104:105]
	v_pk_fma_f32 v[14:15], v[14:15], v[130:131], v[110:111]
	global_store_dwordx4 v[158:159], v[60:63], off
	global_store_dwordx4 v[158:159], v[56:59], off offset:64
	global_store_dwordx4 v[158:159], v[40:43], off offset:512
	global_store_dwordx4 v[158:159], v[36:39], off offset:576
	global_store_dwordx4 v[168:169], v[52:55], off
	global_store_dwordx4 v[168:169], v[48:51], off offset:64
	global_store_dwordx4 v[168:169], v[28:31], off offset:512
	global_store_dwordx4 v[168:169], v[24:27], off offset:576
	global_store_dwordx4 v[170:171], v[44:47], off
	global_store_dwordx4 v[170:171], v[32:35], off offset:64
	global_store_dwordx4 v[170:171], v[20:23], off offset:512
	global_store_dwordx4 v[170:171], v[12:15], off offset:576
	v_pk_fma_f32 v[18:19], v[18:19], v[142:143], v[114:115]
	v_pk_fma_f32 v[16:17], v[16:17], v[140:141], v[112:113]
	v_lshl_add_u64 v[12:13], s[6:7], 0, v[160:161]
	v_lshl_add_u64 v[12:13], v[12:13], 0, v[156:157]
	v_pk_fma_f32 v[10:11], v[10:11], v[138:139], v[118:119]
	v_pk_fma_f32 v[8:9], v[8:9], v[136:137], v[116:117]
	v_pk_fma_f32 v[6:7], v[6:7], v[134:135], v[122:123]
	v_pk_fma_f32 v[4:5], v[4:5], v[132:133], v[120:121]
	v_pk_fma_f32 v[2:3], v[2:3], v[130:131], v[126:127]
	v_pk_fma_f32 v[0:1], v[0:1], v[128:129], v[124:125]
	global_store_dwordx4 v[12:13], v[16:19], off
	global_store_dwordx4 v[12:13], v[8:11], off offset:64
	global_store_dwordx4 v[12:13], v[4:7], off offset:512
	global_store_dwordx4 v[12:13], v[0:3], off offset:576
	s_cbranch_vccz .LBB0_826
	s_waitcnt vmcnt(0)
	s_cmpk_gt_u32 s33, 0xff
	s_cbranch_scc1 .LBB0_837

;     __device__ __forceinline__ unsigned arow(const Unit& u, int r) const { return (unsigned)(u.pm * 256 + r); }
; template <class Epi, class Sched>
; __device__ __forceinline__ void gemm_phase(LAS unsigned char* lds, const bf16_t* A, const int K, const Sched& S, const Epi& E, const int wv) {
;     ...
;     const int wid = __builtin_amdgcn_readfirstlane(tid >> 6), lane = tid & 63, wr = wid >> 2, wc = wid & 3, fr = lane & 15, fq = lane >> 4;
;     const int nt = K / BK;
;     unsigned voffA[2], voffB[2];
; #pragma unroll
;     for (int i = 0; i < 2; ++i) { int R, C; stage_rc(tid * 16 + i * 8192, R, C); const int Rb = Epi::PERM ? ((R & ~31) + perm32(R & 31)) : R;
;         voffA[i] = (unsigned)(R * K + C) * 2u; voffB[i] = (unsigned)(Rb * K + C) * 2u; }
;     const size_t kstep = (size_t)(BK * 2);
;     const size_t hstep = (size_t)HALF * K * 2;
;     const size_t tstep = 2 * hstep;
;     const unsigned ldsw = (unsigned)wid * 1024u;
;     const int aoff = lds_byte(wr * 64 + fr, fq * 8), boff = lds_byte(wc * 32 + fr, fq * 8);
;     Unit cur, nxt; int ui = 0;
;     if (!S.next(0, cur)) return;
;     f32x4 acc[2][2][4][2];
; #pragma unroll
;     for (int a_ = 0; a_ < 2; ++a_)
; #pragma unroll
;         for (int b_ = 0; b_ < 2; ++b_)
; #pragma unroll
;             for (int m = 0; m < 4; ++m)
; #pragma unroll
;                 for (int n = 0; n < 2; ++n) acc[a_][b_][m][n] = (f32x4){0.f, 0.f, 0.f, 0.f};
;     bf16x8 At[4][2], B0[2][2], B1[2][2];
;     unsigned ao0[2] = {0u, 0u}, ao1[2] = {0u, 0u}, no0[2] = {0u, 0u}, no1[2] = {0u, 0u};
;     const char* Ab = (const char*)A;
;     const char* cA = Ab; const char* nA = Ab;
;     if constexpr (Sched::GATHER) {
; #pragma unroll
;         for (int i = 0; i < 2; ++i) { int R, C; stage_rc(tid * 16 + i * 8192, R, C);
;             ao0[i] = (S.arow(cur, R) * (unsigned)K + (unsigned)C) * 2u; ao1[i] = (S.arow(cur, HALF + R) * (unsigned)K + (unsigned)C) * 2u; }
;     } else cA = Ab + (size_t)cur.pm * tstep;
;     const char* cB = S.bptr(cur);
;     PG8_STAGE(PG8_SB(0, 0), cB, voffB); PG8_STAGE_A(PG8_SA(0, 0), 0, false, 0); PG8_STAGE(PG8_SB(0, 1), cB + hstep, voffB); PG8_STAGE_A(PG8_SA(0, 1), 1, false, 0);
;     if (wr == 1) PG8_BAR;
;     PG8_WAIT_V(4); PG8_BAR;
;     PG8_STAGE(PG8_SB(1, 0), cB + kstep, voffB); PG8_STAGE_A(PG8_SA(1, 0), 0, false, kstep); PG8_STAGE(PG8_SB(1, 1), cB + hstep + kstep, voffB);
;     PG8_WAIT_V(6); PG8_BAR;
.LBB0_997:
	v_bfe_i32 v2, v4, 27, 1
	v_lshlrev_b32_e32 v0, 4, v4
	v_lshrrev_b32_e32 v2, 22, v2
	v_add_u32_e32 v2, v0, v2
	v_and_b32_e32 v2, 0xfffffc00, v2
	v_sub_u32_e32 v2, v0, v2
	v_ashrrev_i32_e32 v1, 31, v4
	v_lshrrev_b32_e32 v3, 4, v2
	v_lshrrev_b32_e32 v1, 26, v1
	v_bitop3_b32 v2, v3, v2, 32 bitop3:0x6c
	v_add_u32_e32 v1, v4, v1
	v_ashrrev_i32_e32 v5, 31, v2
	v_ashrrev_i32_e32 v1, 6, v1
	v_lshrrev_b32_e32 v5, 26, v5
	v_lshlrev_b32_e32 v3, 3, v1
	v_add_u32_e32 v5, v2, v5
	v_and_b32_e32 v3, -16, v3
	v_ashrrev_i32_e32 v6, 6, v5
	v_add_u32_e32 v144, v6, v3
	v_and_b32_e32 v3, 0xc0, v5
	v_sub_u32_e32 v2, v2, v3
	v_mov_b32_e32 v3, 1
	v_lshlrev_b32_e32 v1, 5, v1
	v_ashrrev_i16_sdwa v2, v3, sext(v2) dst_sel:DWORD dst_unused:UNUSED_PAD src0_sel:DWORD src1_sel:BYTE_0
	v_and_b32_e32 v1, 32, v1
	v_bfe_i32 v2, v2, 0, 16
	v_add_u32_e32 v0, 0x2000, v0
	v_add_lshl_u32 v145, v1, v2, 1
	v_ashrrev_i32_e32 v1, 31, v0
	v_lshrrev_b32_e32 v1, 22, v1
	v_add_u32_e32 v1, v0, v1
	v_ashrrev_i32_e32 v1, 10, v1
	v_mul_i32_i24_e32 v2, 0x400, v1
	v_lshlrev_b32_e32 v5, 1, v144
	v_lshrrev_b32_e32 v7, 2, v144
	v_and_b32_e32 v6, 3, v6
	s_mov_b32 s1, 0xfffe0
	v_sub_u32_e32 v0, v0, v2
	v_and_b32_e32 v5, 24, v5
	v_and_b32_e32 v7, 4, v7
	v_and_or_b32 v6, v144, s1, v6
	v_lshrrev_b32_e32 v2, 4, v0
	v_or3_b32 v5, v6, v7, v5
	v_bitop3_b32 v0, v2, v0, 32 bitop3:0x6c
	v_lshl_add_u32 v128, v5, 12, v145
	v_ashrrev_i32_e32 v5, 31, v0
	v_lshrrev_b32_e32 v5, 26, v5
	v_lshlrev_b32_e32 v2, 3, v1
	v_add_u32_e32 v5, v0, v5
	v_and_b32_e32 v2, -16, v2
	v_ashrrev_i32_e32 v6, 6, v5
	v_lshlrev_b32_e32 v1, 5, v1
	v_add_u32_e32 v146, v6, v2
	v_and_b32_e32 v2, 32, v1
	v_and_b32_e32 v1, 0xc0, v5
	v_sub_u32_e32 v0, v0, v1
	v_ashrrev_i16_sdwa v0, v3, sext(v0) dst_sel:DWORD dst_unused:UNUSED_PAD src0_sel:DWORD src1_sel:BYTE_0
	s_add_u32 s2, s76, 0x3c188000
	v_bfe_i32 v3, v0, 0, 16
	v_lshlrev_b32_e32 v0, 1, v146
	v_lshrrev_b32_e32 v1, 2, v146
	v_and_b32_e32 v5, 3, v6
	s_addc_u32 s3, s77, 0
	v_and_b32_e32 v0, 24, v0
	v_and_b32_e32 v1, 4, v1
	v_and_or_b32 v5, v146, s1, v5
	s_add_i32 s12, 0, 0x20800
	v_or3_b32 v5, v5, v1, v0
	v_lshl_add_u32 v0, v144, 2, s12
	ds_read2st64_b32 v[0:1], v0 offset1:2
	s_ashr_i32 s8, s28, 6
	s_ashr_i32 s21, s20, 31
	s_ashr_i32 s0, s28, 8
	v_add_lshl_u32 v147, v2, v3, 1
	s_lshl_b32 s1, s8, 10
	v_lshl_add_u32 v2, v146, 2, s12
	s_lshl_b64 s[10:11], s[20:21], 20
	ds_read2st64_b32 v[2:3], v2 offset1:2
	s_add_u32 s9, s26, s10
	s_waitcnt lgkmcnt(1)
	v_lshlrev_b32_e32 v0, 11, v0
	s_addc_u32 s10, s27, s11
	v_and_b32_e32 v0, 0xfffff000, v0
	s_add_u32 s22, s9, s6
	v_add_u32_e32 v132, v0, v145
	v_lshlrev_b32_e32 v0, 11, v1
	s_addc_u32 s23, s10, s7
	s_add_i32 s21, s1, 0
	v_and_b32_e32 v0, 0xfffff000, v0
	s_add_i32 m0, s21, 0x10000
	v_lshl_add_u32 v130, v5, 12, v147
	v_add_u32_e32 v134, v0, v145
	s_waitcnt lgkmcnt(0)
	v_lshlrev_b32_e32 v0, 11, v2
	global_load_lds_dwordx4 v128, s[22:23]
	s_add_i32 m0, s21, 0x12000
	v_and_b32_e32 v0, 0xfffff000, v0
	global_load_lds_dwordx4 v130, s[22:23]
	s_mov_b32 m0, s21
	s_add_i32 s29, s21, 0x2000
	v_add_u32_e32 v136, v0, v147
	global_load_lds_dwordx4 v132, s[2:3]
	s_mov_b32 m0, s29
	s_add_u32 s6, s22, 0x80000
	global_load_lds_dwordx4 v136, s[2:3]
	s_addc_u32 s7, s23, 0
	s_add_i32 m0, s21, 0x14000
	v_lshlrev_b32_e32 v0, 11, v3
	global_load_lds_dwordx4 v128, s[6:7]
	s_add_i32 m0, s21, 0x16000
	s_add_i32 s30, s21, 0x4000
	v_and_b32_e32 v0, 0xfffff000, v0
	global_load_lds_dwordx4 v130, s[6:7]
	s_mov_b32 m0, s30
	s_add_i32 s31, s21, 0x6000
	v_add_u32_e32 v138, v0, v147
	global_load_lds_dwordx4 v134, s[2:3]
	s_mov_b32 m0, s31
	v_mov_b32_e32 v133, 0
	global_load_lds_dwordx4 v138, s[2:3]
	v_mov_b32_e32 v129, v133
	v_mov_b32_e32 v131, v133
	s_mov_b32 s38, 0
	v_lshl_add_u64 v[2:3], s[22:23], 0, v[128:129]
	v_lshl_add_u64 v[0:1], s[22:23], 0, v[130:131]
	s_cmp_lg_u32 s0, 1
	v_mov_b32_e32 v137, v133
	s_cbranch_scc1 .LBB0_999
.LBB0_999:
	s_add_u32 s6, s76, 0x52188000
	s_addc_u32 s7, s77, 0
	s_lshl_b32 s8, s8, 5
	s_and_b32 s16, s8, 0x60
	s_mov_b64 s[8:9], 0x80
	s_add_i32 m0, s21, 0x18000
	v_lshl_add_u64 v[2:3], v[2:3], 0, s[8:9]
	s_lshl_b32 s13, s0, 13
	s_lshl_b32 s17, s16, 7
	s_waitcnt vmcnt(4)
	s_barrier
	global_load_lds_dwordx4 v[2:3], off
	s_add_i32 m0, s21, 0x1a000
	s_add_u32 s10, s76, 0x3c188080
	v_lshl_add_u64 v[0:1], v[0:1], 0, s[8:9]
	s_addc_u32 s11, s77, 0
	s_add_i32 s33, s21, 0x8000
	s_add_i32 s34, s21, 0xa000
	global_load_lds_dwordx4 v[0:1], off
	v_lshl_add_u64 v[0:1], s[10:11], 0, v[132:133]
	s_mov_b32 m0, s33
	s_add_u32 s14, s22, 0x80080
	global_load_lds_dwordx4 v[0:1], off
	v_lshl_add_u64 v[0:1], s[10:11], 0, v[136:137]
	s_mov_b32 m0, s34
	s_addc_u32 s15, s23, 0
	global_load_lds_dwordx4 v[0:1], off
	s_add_i32 m0, s21, 0x1c000
	v_lshl_add_u64 v[0:1], s[14:15], 0, v[128:129]
	global_load_lds_dwordx4 v[0:1], off
	v_lshl_add_u64 v[0:1], s[14:15], 0, v[130:131]
	s_add_i32 m0, s21, 0x1e000
	s_add_i32 s64, 0, 0x10000
	global_load_lds_dwordx4 v[0:1], off
	v_lshrrev_b32_e32 v1, 1, v4
	v_and_b32_e32 v0, 15, v4
	v_and_b32_e32 v1, 24, v1
	v_lshl_or_b32 v137, s0, 6, v0
	v_lshlrev_b32_e32 v2, 1, v1
	v_lshl_or_b32 v0, v0, 6, v2
	v_lshlrev_b32_e32 v2, 2, v137
	v_and_b32_e32 v3, 32, v2
	v_lshlrev_b32_e32 v4, 2, v4
	s_waitcnt vmcnt(6)
	s_add_i32 s65, 0, 0x14000
	s_add_i32 s72, 0, 0x18000
	s_add_i32 s73, 0, 0x1c000
	v_bitop3_b32 v3, v0, s13, v3 bitop3:0xde
	v_and_b32_e32 v4, 32, v4
	v_or_b32_e32 v151, 16, v137
	v_or_b32_e32 v152, 32, v137
	v_or_b32_e32 v153, 48, v137
	v_add_u32_e32 v154, 0x80, v137
	v_add_u32_e32 v155, 0x90, v137
	v_add_u32_e32 v156, 0xa0, v137
	v_add_u32_e32 v157, 0xb0, v137
	s_add_i32 s0, 0, 0x20480
	s_add_i32 s68, s64, s1
	s_add_i32 s70, s65, s1
	s_add_i32 s74, s72, s1
	s_add_i32 s76, s73, s1
	v_bitop3_b32 v149, v0, s17, v4 bitop3:0xde
	v_add_u32_e32 v150, s12, v2
	v_or_b32_e32 v158, s16, v1
	v_lshl_add_u32 v159, v151, 2, s12
	v_lshl_add_u32 v160, v152, 2, s12
	v_lshl_add_u32 v161, v153, 2, s12
	v_lshl_add_u32 v162, v154, 2, s12
	v_lshl_add_u32 v163, v155, 2, s12
	v_lshl_add_u32 v164, v156, 2, s12
	v_lshl_add_u32 v165, v157, 2, s12
	v_mov_b32_e32 v166, s0
	s_add_i32 s35, 0, 0x20404
	s_add_i32 s36, 0, 0x2040c
	s_add_i32 s37, 0, 0x20414
	s_add_i32 s39, 0, 0x2041c
	s_add_i32 s40, 0, 0x20424
	s_add_i32 s41, 0, 0x2042c
	s_add_i32 s42, 0, 0x20434
	s_add_i32 s43, 0, 0x2043c
	s_add_i32 s50, 0, 0x20444
	s_add_i32 s51, 0, 0x2044c
	s_add_i32 s54, 0, 0x20454
	s_add_i32 s55, 0, 0x2045c
	s_add_i32 s60, 0, 0x20464
	s_add_i32 s61, 0, 0x2046c
	s_add_i32 s62, 0, 0x20474
	s_add_i32 s63, 0, 0x2047c
	v_add_u32_e32 v167, 0, v3
	s_add_i32 s66, s21, 0xc000
	s_add_i32 s67, s21, 0xe000
	s_add_i32 s69, s68, 0x2000
	s_add_i32 s71, s70, 0x2000
	s_add_i32 s75, s74, 0x2000
	s_add_i32 s77, s76, 0x2000
	v_mov_b32_e32 v173, v132
	s_mov_b32 s78, 0
	s_barrier
	s_branch .LBB0_1001

; #define PG8_LDA(dst, b, h) do { _Pragma("unroll") for (int m = 0; m < 4; ++m) _Pragma("unroll") for (int k = 0; k < 2; ++k) dst[m][k] = *(const LAS bf16x8*)(lds + PG8_SA(b, h) + aoff + m * 2048 + k * 1024); } while (0)
; #define PG8_LDB(dst, b, h) do { _Pragma("unroll") for (int n = 0; n < 2; ++n) _Pragma("unroll") for (int k = 0; k < 2; ++k) dst[n][k] = *(const LAS bf16x8*)(lds + PG8_SB(b, h) + boff + n * 2048 + k * 1024); } while (0)
; #define PG8_MMA(ai, bj, At, Bt) do { __builtin_amdgcn_s_setprio(1); _Pragma("unroll") for (int m = 0; m < 4; ++m) _Pragma("unroll") for (int n = 0; n < 2; ++n) _Pragma("unroll") for (int k = 0; k < 2; ++k) \
;         acc[ai][bj][m][n] = __builtin_amdgcn_mfma_f32_16x16x32_bf16(Bt[n][k], At[m][k], acc[ai][bj][m][n], 0, 0, 0); __builtin_amdgcn_s_setprio(0); } while (0)
; #define PG8_WAIT_L(n) asm volatile("s_waitcnt lgkmcnt(" #n ")" ::: "memory")
; #define PG8_BAR __builtin_amdgcn_s_barrier()
; #define PG8_SCHED __builtin_amdgcn_sched_barrier(0)
; template <class Epi, class Sched>
; __device__ __forceinline__ void gemm_phase(LAS unsigned char* lds, const bf16_t* A, const int K, const Sched& S, const Epi& E, const int wv) {
;     ...
;         for (int t = 0; t < nt; t += 2) {
;             const bool last = (t == nt - 2);
;             const size_t k1 = (size_t)(t + 1) * kstep;
;             const size_t k2 = last ? 0 : (size_t)(t + 2) * kstep, k3 = k2 + kstep;
;             const char* b2 = last ? nB : cB + (size_t)(t + 2) * kstep; const char* b3 = b2 + kstep;
;             PG8_LDB(B0, 0, 0); PG8_SCHED; PG8_LDA(At, 0, 0); PG8_STAGE_A(PG8_SA(1, 1), 1, false, k1);
;             PG8_WAIT_L(8); PG8_BAR; PG8_WAIT_L(0); PG8_MMA(0, 0, At, B0); PG8_BAR; PG8_SCHED;
;     ...
; #pragma unroll
;         for (int a_ = 0; a_ < 2; ++a_)
; #pragma unroll
;             for (int b_ = 0; b_ < 2; ++b_)
; #pragma unroll
;                 for (int m = 0; m < 4; ++m)
; #pragma unroll
;                     for (int n = 0; n < 2; ++n) acc[a_][b_][m][n] = (f32x4){0.f, 0.f, 0.f, 0.f};
;         cur = nxt; cB = nB; cA = nA; ++ui;
; #pragma unroll
;         for (int i = 0; i < 2; ++i) { ao0[i] = no0[i]; ao1[i] = no1[i]; }
.LBB0_1007:
	s_waitcnt lgkmcnt(0)
	v_mov_b32_e32 v135, v133
	v_mov_b32_e32 v139, v133
	s_add_u32 s15, s22, 0x100
	v_mov_b32_e32 v36, 0
	s_addc_u32 s17, s23, 0
	v_lshl_add_u64 v[140:141], s[10:11], 0, v[138:139]
	v_lshl_add_u64 v[142:143], s[10:11], 0, v[134:135]
	s_mov_b32 s80, -2
	s_mov_b64 s[0:1], 0
	v_mov_b32_e32 v37, v36
	v_mov_b32_e32 v38, v36
	v_mov_b32_e32 v39, v36
	v_mov_b32_e32 v52, v36
	v_mov_b32_e32 v53, v36
	v_mov_b32_e32 v54, v36
	v_mov_b32_e32 v55, v36
	v_mov_b32_e32 v64, v36
	v_mov_b32_e32 v65, v36
	v_mov_b32_e32 v66, v36
	v_mov_b32_e32 v67, v36
	v_mov_b32_e32 v68, v36
	v_mov_b32_e32 v69, v36
	v_mov_b32_e32 v70, v36
	v_mov_b32_e32 v71, v36
	v_mov_b32_e32 v80, v36
	v_mov_b32_e32 v81, v36
	v_mov_b32_e32 v82, v36
	v_mov_b32_e32 v83, v36
	v_mov_b32_e32 v84, v36
	v_mov_b32_e32 v85, v36
	v_mov_b32_e32 v86, v36
	v_mov_b32_e32 v87, v36
	v_mov_b32_e32 v96, v36
	v_mov_b32_e32 v97, v36
	v_mov_b32_e32 v98, v36
	v_mov_b32_e32 v99, v36
	v_mov_b32_e32 v100, v36
	v_mov_b32_e32 v101, v36
	v_mov_b32_e32 v102, v36
	v_mov_b32_e32 v103, v36
	v_mov_b32_e32 v112, v36
	v_mov_b32_e32 v113, v36
	v_mov_b32_e32 v114, v36
	v_mov_b32_e32 v115, v36
	v_mov_b32_e32 v116, v36
	v_mov_b32_e32 v117, v36
	v_mov_b32_e32 v118, v36
	v_mov_b32_e32 v119, v36
	v_mov_b32_e32 v72, v36
	v_mov_b32_e32 v73, v36
	v_mov_b32_e32 v74, v36
	v_mov_b32_e32 v75, v36
	v_mov_b32_e32 v76, v36
	v_mov_b32_e32 v77, v36
	v_mov_b32_e32 v78, v36
	v_mov_b32_e32 v79, v36
	v_mov_b32_e32 v88, v36
	v_mov_b32_e32 v89, v36
	v_mov_b32_e32 v90, v36
	v_mov_b32_e32 v91, v36
	v_mov_b32_e32 v92, v36
	v_mov_b32_e32 v93, v36
	v_mov_b32_e32 v94, v36
	v_mov_b32_e32 v95, v36
	v_mov_b32_e32 v104, v36
	v_mov_b32_e32 v105, v36
	v_mov_b32_e32 v106, v36
	v_mov_b32_e32 v107, v36
	v_mov_b32_e32 v108, v36
	v_mov_b32_e32 v109, v36
	v_mov_b32_e32 v110, v36
	v_mov_b32_e32 v111, v36
	v_mov_b32_e32 v120, v36
	v_mov_b32_e32 v121, v36
	v_mov_b32_e32 v122, v36
	v_mov_b32_e32 v123, v36
	v_mov_b32_e32 v124, v36
	v_mov_b32_e32 v125, v36
	v_mov_b32_e32 v126, v36
	v_mov_b32_e32 v127, v36
	v_mov_b32_e32 v40, v36
	v_mov_b32_e32 v41, v36
	v_mov_b32_e32 v42, v36
	v_mov_b32_e32 v43, v36
	v_mov_b32_e32 v32, v36
	v_mov_b32_e32 v33, v36
	v_mov_b32_e32 v34, v36
	v_mov_b32_e32 v35, v36
	v_mov_b32_e32 v20, v36
	v_mov_b32_e32 v21, v36
	v_mov_b32_e32 v22, v36
	v_mov_b32_e32 v23, v36
	v_mov_b32_e32 v16, v36
	v_mov_b32_e32 v17, v36
	v_mov_b32_e32 v18, v36
	v_mov_b32_e32 v19, v36
	v_mov_b32_e32 v4, v36
	v_mov_b32_e32 v5, v36
	v_mov_b32_e32 v6, v36
	v_mov_b32_e32 v7, v36
	v_mov_b32_e32 v0, v36
	v_mov_b32_e32 v1, v36
	v_mov_b32_e32 v2, v36
	v_mov_b32_e32 v3, v36
	v_mov_b32_e32 v60, v36
	v_mov_b32_e32 v61, v36
	v_mov_b32_e32 v62, v36
	v_mov_b32_e32 v63, v36
	v_mov_b32_e32 v56, v36
	v_mov_b32_e32 v57, v36
	v_mov_b32_e32 v58, v36
	v_mov_b32_e32 v59, v36
	v_mov_b32_e32 v48, v36
	v_mov_b32_e32 v49, v36
	v_mov_b32_e32 v50, v36
	v_mov_b32_e32 v51, v36
	v_mov_b32_e32 v44, v36
	v_mov_b32_e32 v45, v36
	v_mov_b32_e32 v46, v36
	v_mov_b32_e32 v47, v36
	v_mov_b32_e32 v28, v36
	v_mov_b32_e32 v29, v36
	v_mov_b32_e32 v30, v36
	v_mov_b32_e32 v31, v36
	v_mov_b32_e32 v24, v36
	v_mov_b32_e32 v25, v36
	v_mov_b32_e32 v26, v36
	v_mov_b32_e32 v27, v36
	v_mov_b32_e32 v12, v36
	v_mov_b32_e32 v13, v36
	v_mov_b32_e32 v14, v36
	v_mov_b32_e32 v15, v36
	v_mov_b32_e32 v8, v36
	v_mov_b32_e32 v9, v36
	v_mov_b32_e32 v10, v36
	v_mov_b32_e32 v11, v36
	s_bitcmp1_b32 s92, 8
	s_cbranch_scc0 .Lmy_ph_2
	s_barrier
.Lmy_ph_2:
.LBB0_1008:
	v_add_u32_e32 v132, s64, v149
	s_add_u32 s22, s0, 0x100
	ds_read_b128 v[174:177], v132
	ds_read_b128 v[178:181], v132 offset:1024
	ds_read_b128 v[182:185], v132 offset:2048
	ds_read_b128 v[186:189], v132 offset:3072
	s_addc_u32 s23, s1, 0
	s_add_u32 s81, s15, s0
	s_addc_u32 s82, s17, s1
	s_cmpk_eq_i32 s0, 0xf00
	s_cselect_b64 vcc, -1, 0
	s_and_b64 s[24:25], vcc, exec
	s_cselect_b32 s83, 0, s22
	s_cselect_b32 s25, s19, s82
	s_cselect_b32 s24, s18, s81
	s_mov_b32 m0, s66
	v_lshl_add_u64 v[222:223], v[142:143], 0, s[0:1]
	ds_read_b128 v[190:193], v167
	ds_read_b128 v[194:197], v167 offset:1024
	ds_read_b128 v[198:201], v167 offset:2048
	ds_read_b128 v[202:205], v167 offset:3072
	ds_read_b128 v[206:209], v167 offset:4096
	ds_read_b128 v[210:213], v167 offset:5120
	ds_read_b128 v[214:217], v167 offset:6144
	ds_read_b128 v[218:221], v167 offset:7168
	global_load_lds_dwordx4 v[222:223], off
	v_lshl_add_u64 v[222:223], v[140:141], 0, s[0:1]
	s_mov_b32 m0, s67
	s_nop 0
	global_load_lds_dwordx4 v[222:223], off
	s_waitcnt lgkmcnt(8)
	s_barrier
	s_waitcnt lgkmcnt(0)
	s_setprio 1
	s_waitcnt lgkmcnt(0)
	v_mfma_f32_16x16x32_bf16 v[124:127], v[174:177], v[190:193], v[124:127]
	v_mfma_f32_16x16x32_bf16 v[120:123], v[182:185], v[190:193], v[120:123]
	v_mfma_f32_16x16x32_bf16 v[108:111], v[174:177], v[198:201], v[108:111]
	v_mfma_f32_16x16x32_bf16 v[104:107], v[182:185], v[198:201], v[104:107]
	v_mfma_f32_16x16x32_bf16 v[92:95], v[174:177], v[206:209], v[92:95]
	v_mfma_f32_16x16x32_bf16 v[88:91], v[182:185], v[206:209], v[88:91]
	v_mfma_f32_16x16x32_bf16 v[76:79], v[174:177], v[214:217], v[76:79]
	v_mfma_f32_16x16x32_bf16 v[72:75], v[182:185], v[214:217], v[72:75]
	v_mfma_f32_16x16x32_bf16 v[124:127], v[178:181], v[194:197], v[124:127]
	v_mfma_f32_16x16x32_bf16 v[120:123], v[186:189], v[194:197], v[120:123]
	v_mfma_f32_16x16x32_bf16 v[108:111], v[178:181], v[202:205], v[108:111]
	v_mfma_f32_16x16x32_bf16 v[104:107], v[186:189], v[202:205], v[104:107]
	v_mfma_f32_16x16x32_bf16 v[92:95], v[178:181], v[210:213], v[92:95]
	v_mfma_f32_16x16x32_bf16 v[88:91], v[186:189], v[210:213], v[88:91]
	v_mfma_f32_16x16x32_bf16 v[76:79], v[178:181], v[218:221], v[76:79]
	v_mfma_f32_16x16x32_bf16 v[72:75], v[186:189], v[218:221], v[72:75]
	s_setprio 0
	s_barrier
; #define PG8_STAGE(bufoff, gbase, voff) do { _Pragma("unroll") for (int _i = 0; _i < 2; ++_i) \
;         __builtin_amdgcn_global_load_lds((const unsigned*)((const char*)(gbase) + (voff)[_i]), (LAS unsigned*)(lds + (bufoff) + ldsw + _i * 8192), 16, 0, 0); } while (0)
; #define PG8_LDA(dst, b, h) do { _Pragma("unroll") for (int m = 0; m < 4; ++m) _Pragma("unroll") for (int k = 0; k < 2; ++k) dst[m][k] = *(const LAS bf16x8*)(lds + PG8_SA(b, h) + aoff + m * 2048 + k * 1024); } while (0)
; #define PG8_LDB(dst, b, h) do { _Pragma("unroll") for (int n = 0; n < 2; ++n) _Pragma("unroll") for (int k = 0; k < 2; ++k) dst[n][k] = *(const LAS bf16x8*)(lds + PG8_SB(b, h) + boff + n * 2048 + k * 1024); } while (0)
; #define PG8_MMA(ai, bj, At, Bt) do { __builtin_amdgcn_s_setprio(1); _Pragma("unroll") for (int m = 0; m < 4; ++m) _Pragma("unroll") for (int n = 0; n < 2; ++n) _Pragma("unroll") for (int k = 0; k < 2; ++k) \
;         acc[ai][bj][m][n] = __builtin_amdgcn_mfma_f32_16x16x32_bf16(Bt[n][k], At[m][k], acc[ai][bj][m][n], 0, 0, 0); __builtin_amdgcn_s_setprio(0); } while (0)
; #define PG8_WAIT_V(n) asm volatile("s_waitcnt vmcnt(" #n ")" ::: "memory")
; #define PG8_WAIT_L(n) asm volatile("s_waitcnt lgkmcnt(" #n ")" ::: "memory")
; template <class Epi, class Sched>
; __device__ __forceinline__ void gemm_phase(LAS unsigned char* lds, const bf16_t* A, const int K, const Sched& S, const Epi& E, const int wv) {
;     ...
;             PG8_LDB(B1, 0, 1); PG8_STAGE(PG8_SB(0, 0), b2, voffB);
;             PG8_BAR; PG8_WAIT_L(0); PG8_MMA(0, 1, At, B1); PG8_BAR;
;             PG8_LDA(At, 0, 1); PG8_STAGE_A(PG8_SA(0, 0), 0, last, k2);
;             PG8_BAR; PG8_WAIT_L(0); PG8_MMA(1, 0, At, B0); PG8_BAR; PG8_SCHED;
;             PG8_STAGE(PG8_SB(0, 1), b2 + hstep, voffB);
;             PG8_WAIT_V(6); PG8_BAR; PG8_MMA(1, 1, At, B1); PG8_BAR;
;             PG8_LDB(B0, 1, 0); PG8_SCHED; PG8_LDA(At, 1, 0); PG8_STAGE_A(PG8_SA(0, 1), 1, last, k2);
;             PG8_WAIT_L(8); PG8_BAR; PG8_WAIT_L(0); PG8_MMA(0, 0, At, B0); PG8_BAR; PG8_SCHED;
;             PG8_LDB(B1, 1, 1); PG8_STAGE(PG8_SB(1, 0), b3, voffB);
;             PG8_BAR; PG8_WAIT_L(0); PG8_MMA(0, 1, At, B1); PG8_BAR;
;             PG8_LDA(At, 1, 1); PG8_STAGE_A(PG8_SA(1, 0), 0, last, k3);
;             PG8_BAR; PG8_WAIT_L(0); PG8_MMA(1, 0, At, B0); PG8_BAR; PG8_SCHED;
;             PG8_STAGE(PG8_SB(1, 1), b3 + hstep, voffB);
	s_mov_b32 m0, s68
	v_add_u32_e32 v132, s65, v149
	v_lshl_add_u64 v[238:239], s[24:25], 0, v[128:129]
	ds_read_b128 v[222:225], v132
	ds_read_b128 v[226:229], v132 offset:1024
	ds_read_b128 v[230:233], v132 offset:2048
	ds_read_b128 v[234:237], v132 offset:3072
	global_load_lds_dwordx4 v[238:239], off
	v_lshl_add_u64 v[240:241], s[24:25], 0, v[130:131]
	s_mov_b32 m0, s69
	s_nop 0
	global_load_lds_dwordx4 v[240:241], off
	s_barrier
	s_waitcnt lgkmcnt(0)
	s_setprio 1
	s_waitcnt lgkmcnt(0)
	v_mfma_f32_16x16x32_bf16 v[116:119], v[222:225], v[190:193], v[116:119]
	v_mfma_f32_16x16x32_bf16 v[112:115], v[230:233], v[190:193], v[112:115]
	v_mfma_f32_16x16x32_bf16 v[100:103], v[222:225], v[198:201], v[100:103]
	v_mfma_f32_16x16x32_bf16 v[96:99], v[230:233], v[198:201], v[96:99]
	v_mfma_f32_16x16x32_bf16 v[84:87], v[222:225], v[206:209], v[84:87]
	v_mfma_f32_16x16x32_bf16 v[80:83], v[230:233], v[206:209], v[80:83]
	v_mfma_f32_16x16x32_bf16 v[68:71], v[222:225], v[214:217], v[68:71]
	v_mfma_f32_16x16x32_bf16 v[64:67], v[230:233], v[214:217], v[64:67]
	v_mfma_f32_16x16x32_bf16 v[116:119], v[226:229], v[194:197], v[116:119]
	v_mfma_f32_16x16x32_bf16 v[112:115], v[234:237], v[194:197], v[112:115]
	v_mfma_f32_16x16x32_bf16 v[100:103], v[226:229], v[202:205], v[100:103]
	v_mfma_f32_16x16x32_bf16 v[96:99], v[234:237], v[202:205], v[96:99]
	v_mfma_f32_16x16x32_bf16 v[84:87], v[226:229], v[210:213], v[84:87]
	v_mfma_f32_16x16x32_bf16 v[80:83], v[234:237], v[210:213], v[80:83]
	v_mfma_f32_16x16x32_bf16 v[68:71], v[226:229], v[218:221], v[68:71]
	v_mfma_f32_16x16x32_bf16 v[64:67], v[234:237], v[218:221], v[64:67]
	s_setprio 0
	s_add_u32 s0, s2, s83
	s_mov_b32 m0, s21
	s_addc_u32 s1, s3, 0
	v_cndmask_b32_e32 v132, v173, v169, vcc
	s_barrier
	ds_read_b128 v[190:193], v167 offset:16384
	ds_read_b128 v[194:197], v167 offset:17408
	ds_read_b128 v[198:201], v167 offset:18432
	ds_read_b128 v[202:205], v167 offset:19456
	ds_read_b128 v[206:209], v167 offset:20480
	ds_read_b128 v[210:213], v167 offset:21504
	ds_read_b128 v[214:217], v167 offset:22528
	ds_read_b128 v[218:221], v167 offset:23552
	v_cndmask_b32_e32 v242, v136, v171, vcc
	global_load_lds_dwordx4 v132, s[0:1]
	s_mov_b32 m0, s29
	v_mov_b32_e32 v243, v133
	global_load_lds_dwordx4 v242, s[0:1]
	s_barrier
	s_waitcnt lgkmcnt(0)
	v_lshl_add_u64 v[244:245], s[0:1], 0, v[132:133]
	v_lshl_add_u64 v[242:243], s[0:1], 0, v[242:243]
	s_setprio 1
	s_waitcnt lgkmcnt(0)
	v_mfma_f32_16x16x32_bf16 v[52:55], v[174:177], v[190:193], v[52:55]
	v_mfma_f32_16x16x32_bf16 v[36:39], v[182:185], v[190:193], v[36:39]
	v_mfma_f32_16x16x32_bf16 v[40:43], v[174:177], v[198:201], v[40:43]
	v_mfma_f32_16x16x32_bf16 v[32:35], v[182:185], v[198:201], v[32:35]
	v_mfma_f32_16x16x32_bf16 v[20:23], v[174:177], v[206:209], v[20:23]
	v_mfma_f32_16x16x32_bf16 v[16:19], v[182:185], v[206:209], v[16:19]
	v_mfma_f32_16x16x32_bf16 v[4:7], v[174:177], v[214:217], v[4:7]
	v_mfma_f32_16x16x32_bf16 v[0:3], v[182:185], v[214:217], v[0:3]
	v_mfma_f32_16x16x32_bf16 v[52:55], v[178:181], v[194:197], v[52:55]
	v_mfma_f32_16x16x32_bf16 v[36:39], v[186:189], v[194:197], v[36:39]
	v_mfma_f32_16x16x32_bf16 v[40:43], v[178:181], v[202:205], v[40:43]
	v_mfma_f32_16x16x32_bf16 v[32:35], v[186:189], v[202:205], v[32:35]
	v_mfma_f32_16x16x32_bf16 v[20:23], v[178:181], v[210:213], v[20:23]
	v_mfma_f32_16x16x32_bf16 v[16:19], v[186:189], v[210:213], v[16:19]
	v_mfma_f32_16x16x32_bf16 v[4:7], v[178:181], v[218:221], v[4:7]
	v_mfma_f32_16x16x32_bf16 v[0:3], v[186:189], v[218:221], v[0:3]
	s_setprio 0
	s_barrier
	s_add_u32 s82, s24, 0x80000
	s_addc_u32 s83, s25, 0
	s_mov_b32 m0, s70
	v_lshl_add_u64 v[174:175], s[82:83], 0, v[128:129]
	global_load_lds_dwordx4 v[174:175], off
	v_lshl_add_u64 v[174:175], s[82:83], 0, v[130:131]
	s_mov_b32 m0, s71
	s_nop 0
	global_load_lds_dwordx4 v[174:175], off
	s_waitcnt vmcnt(6)
	s_barrier
	s_setprio 1
	v_mfma_f32_16x16x32_bf16 v[60:63], v[222:225], v[190:193], v[60:63]
	v_mfma_f32_16x16x32_bf16 v[56:59], v[230:233], v[190:193], v[56:59]
	v_mfma_f32_16x16x32_bf16 v[48:51], v[222:225], v[198:201], v[48:51]
	v_mfma_f32_16x16x32_bf16 v[44:47], v[230:233], v[198:201], v[44:47]
	v_mfma_f32_16x16x32_bf16 v[28:31], v[222:225], v[206:209], v[28:31]
	v_mfma_f32_16x16x32_bf16 v[24:27], v[230:233], v[206:209], v[24:27]
	v_mfma_f32_16x16x32_bf16 v[12:15], v[222:225], v[214:217], v[12:15]
	v_mfma_f32_16x16x32_bf16 v[8:11], v[230:233], v[214:217], v[8:11]
	v_mfma_f32_16x16x32_bf16 v[60:63], v[226:229], v[194:197], v[60:63]
	v_mfma_f32_16x16x32_bf16 v[56:59], v[234:237], v[194:197], v[56:59]
	v_mfma_f32_16x16x32_bf16 v[48:51], v[226:229], v[202:205], v[48:51]
	v_mfma_f32_16x16x32_bf16 v[44:47], v[234:237], v[202:205], v[44:47]
	v_mfma_f32_16x16x32_bf16 v[28:31], v[226:229], v[210:213], v[28:31]
	v_mfma_f32_16x16x32_bf16 v[24:27], v[234:237], v[210:213], v[24:27]
	v_mfma_f32_16x16x32_bf16 v[12:15], v[226:229], v[218:221], v[12:15]
	v_mfma_f32_16x16x32_bf16 v[8:11], v[234:237], v[218:221], v[8:11]
	s_setprio 0
	v_add_u32_e32 v132, s72, v149
	s_barrier
	ds_read_b128 v[174:177], v132
	ds_read_b128 v[178:181], v132 offset:1024
	ds_read_b128 v[182:185], v132 offset:2048
	ds_read_b128 v[186:189], v132 offset:3072
	s_mov_b32 m0, s30
	v_cndmask_b32_e32 v132, v134, v170, vcc
	ds_read_b128 v[190:193], v167 offset:32768
	ds_read_b128 v[194:197], v167 offset:33792
	ds_read_b128 v[198:201], v167 offset:34816
	ds_read_b128 v[202:205], v167 offset:35840
	ds_read_b128 v[206:209], v167 offset:36864
	ds_read_b128 v[210:213], v167 offset:37888
	ds_read_b128 v[214:217], v167 offset:38912
	ds_read_b128 v[218:221], v167 offset:39936
	v_cndmask_b32_e32 v135, v138, v172, vcc
	global_load_lds_dwordx4 v132, s[0:1]
	s_mov_b32 m0, s31
	s_nop 0
	global_load_lds_dwordx4 v135, s[0:1]
	s_waitcnt lgkmcnt(8)
	s_barrier
; #define PG8_STAGE(bufoff, gbase, voff) do { _Pragma("unroll") for (int _i = 0; _i < 2; ++_i) \
;         __builtin_amdgcn_global_load_lds((const unsigned*)((const char*)(gbase) + (voff)[_i]), (LAS unsigned*)(lds + (bufoff) + ldsw + _i * 8192), 16, 0, 0); } while (0)
; #define PG8_LDA(dst, b, h) do { _Pragma("unroll") for (int m = 0; m < 4; ++m) _Pragma("unroll") for (int k = 0; k < 2; ++k) dst[m][k] = *(const LAS bf16x8*)(lds + PG8_SA(b, h) + aoff + m * 2048 + k * 1024); } while (0)
; #define PG8_LDB(dst, b, h) do { _Pragma("unroll") for (int n = 0; n < 2; ++n) _Pragma("unroll") for (int k = 0; k < 2; ++k) dst[n][k] = *(const LAS bf16x8*)(lds + PG8_SB(b, h) + boff + n * 2048 + k * 1024); } while (0)
; #define PG8_MMA(ai, bj, At, Bt) do { __builtin_amdgcn_s_setprio(1); _Pragma("unroll") for (int m = 0; m < 4; ++m) _Pragma("unroll") for (int n = 0; n < 2; ++n) _Pragma("unroll") for (int k = 0; k < 2; ++k) \
;         acc[ai][bj][m][n] = __builtin_amdgcn_mfma_f32_16x16x32_bf16(Bt[n][k], At[m][k], acc[ai][bj][m][n], 0, 0, 0); __builtin_amdgcn_s_setprio(0); } while (0)
; #define PG8_WAIT_V(n) asm volatile("s_waitcnt vmcnt(" #n ")" ::: "memory")
; #define PG8_WAIT_L(n) asm volatile("s_waitcnt lgkmcnt(" #n ")" ::: "memory")
; #define PG8_BAR __builtin_amdgcn_s_barrier()
; #define PG8_SCHED __builtin_amdgcn_sched_barrier(0)
; template <class Epi, class Sched>
; __device__ __forceinline__ void gemm_phase(LAS unsigned char* lds, const bf16_t* A, const int K, const Sched& S, const Epi& E, const int wv) {
;     ...
;             PG8_LDB(B0, 1, 0); PG8_SCHED; PG8_LDA(At, 1, 0); PG8_STAGE_A(PG8_SA(0, 1), 1, last, k2);
;             PG8_WAIT_L(8); PG8_BAR; PG8_WAIT_L(0); PG8_MMA(0, 0, At, B0); PG8_BAR; PG8_SCHED;
;             PG8_LDB(B1, 1, 1); PG8_STAGE(PG8_SB(1, 0), b3, voffB);
;             PG8_BAR; PG8_WAIT_L(0); PG8_MMA(0, 1, At, B1); PG8_BAR;
;             PG8_LDA(At, 1, 1); PG8_STAGE_A(PG8_SA(1, 0), 0, last, k3);
;             PG8_BAR; PG8_WAIT_L(0); PG8_MMA(1, 0, At, B0); PG8_BAR; PG8_SCHED;
;             PG8_STAGE(PG8_SB(1, 1), b3 + hstep, voffB);
;             PG8_WAIT_V(6); PG8_BAR; PG8_MMA(1, 1, At, B1); PG8_BAR;
;         }
	s_waitcnt lgkmcnt(0)
	s_setprio 1
	s_waitcnt lgkmcnt(0)
	v_mfma_f32_16x16x32_bf16 v[124:127], v[174:177], v[190:193], v[124:127]
	v_mfma_f32_16x16x32_bf16 v[120:123], v[182:185], v[190:193], v[120:123]
	v_mfma_f32_16x16x32_bf16 v[108:111], v[174:177], v[198:201], v[108:111]
	v_mfma_f32_16x16x32_bf16 v[104:107], v[182:185], v[198:201], v[104:107]
	v_mfma_f32_16x16x32_bf16 v[92:95], v[174:177], v[206:209], v[92:95]
	v_mfma_f32_16x16x32_bf16 v[88:91], v[182:185], v[206:209], v[88:91]
	v_mfma_f32_16x16x32_bf16 v[76:79], v[174:177], v[214:217], v[76:79]
	v_mfma_f32_16x16x32_bf16 v[72:75], v[182:185], v[214:217], v[72:75]
	v_mfma_f32_16x16x32_bf16 v[124:127], v[178:181], v[194:197], v[124:127]
	v_mfma_f32_16x16x32_bf16 v[120:123], v[186:189], v[194:197], v[120:123]
	v_mfma_f32_16x16x32_bf16 v[108:111], v[178:181], v[202:205], v[108:111]
	v_mfma_f32_16x16x32_bf16 v[104:107], v[186:189], v[202:205], v[104:107]
	v_mfma_f32_16x16x32_bf16 v[92:95], v[178:181], v[210:213], v[92:95]
	v_mfma_f32_16x16x32_bf16 v[88:91], v[186:189], v[210:213], v[88:91]
	v_mfma_f32_16x16x32_bf16 v[76:79], v[178:181], v[218:221], v[76:79]
	v_mfma_f32_16x16x32_bf16 v[72:75], v[186:189], v[218:221], v[72:75]
	s_setprio 0
	s_barrier
	s_mov_b32 m0, s74
	v_add_u32_e32 v132, s73, v149
	v_lshl_add_u64 v[238:239], v[238:239], 0, s[8:9]
	ds_read_b128 v[222:225], v132
	ds_read_b128 v[226:229], v132 offset:1024
	ds_read_b128 v[230:233], v132 offset:2048
	ds_read_b128 v[234:237], v132 offset:3072
	global_load_lds_dwordx4 v[238:239], off
	v_lshl_add_u64 v[238:239], v[240:241], 0, s[8:9]
	s_mov_b32 m0, s75
	s_nop 0
	global_load_lds_dwordx4 v[238:239], off
	s_barrier
	s_waitcnt lgkmcnt(0)
	s_setprio 1
	s_waitcnt lgkmcnt(0)
	v_mfma_f32_16x16x32_bf16 v[116:119], v[222:225], v[190:193], v[116:119]
	v_mfma_f32_16x16x32_bf16 v[112:115], v[230:233], v[190:193], v[112:115]
	v_mfma_f32_16x16x32_bf16 v[100:103], v[222:225], v[198:201], v[100:103]
	v_mfma_f32_16x16x32_bf16 v[96:99], v[230:233], v[198:201], v[96:99]
	v_mfma_f32_16x16x32_bf16 v[84:87], v[222:225], v[206:209], v[84:87]
	v_mfma_f32_16x16x32_bf16 v[80:83], v[230:233], v[206:209], v[80:83]
	v_mfma_f32_16x16x32_bf16 v[68:71], v[222:225], v[214:217], v[68:71]
	v_mfma_f32_16x16x32_bf16 v[64:67], v[230:233], v[214:217], v[64:67]
	v_mfma_f32_16x16x32_bf16 v[116:119], v[226:229], v[194:197], v[116:119]
	v_mfma_f32_16x16x32_bf16 v[112:115], v[234:237], v[194:197], v[112:115]
	v_mfma_f32_16x16x32_bf16 v[100:103], v[226:229], v[202:205], v[100:103]
	v_mfma_f32_16x16x32_bf16 v[96:99], v[234:237], v[202:205], v[96:99]
	v_mfma_f32_16x16x32_bf16 v[84:87], v[226:229], v[210:213], v[84:87]
	v_mfma_f32_16x16x32_bf16 v[80:83], v[234:237], v[210:213], v[80:83]
	v_mfma_f32_16x16x32_bf16 v[68:71], v[226:229], v[218:221], v[68:71]
	v_mfma_f32_16x16x32_bf16 v[64:67], v[234:237], v[218:221], v[64:67]
	s_setprio 0
	s_mov_b32 m0, s33
	v_lshl_add_u64 v[238:239], v[244:245], 0, s[8:9]
	s_barrier
	ds_read_b128 v[190:193], v167 offset:49152
	ds_read_b128 v[194:197], v167 offset:50176
	ds_read_b128 v[198:201], v167 offset:51200
	ds_read_b128 v[202:205], v167 offset:52224
	ds_read_b128 v[206:209], v167 offset:53248
	ds_read_b128 v[210:213], v167 offset:54272
	ds_read_b128 v[214:217], v167 offset:55296
	ds_read_b128 v[218:221], v167 offset:56320
	global_load_lds_dwordx4 v[238:239], off
	v_lshl_add_u64 v[238:239], v[242:243], 0, s[8:9]
	s_mov_b32 m0, s34
	s_nop 0
	global_load_lds_dwordx4 v[238:239], off
	s_barrier
	s_waitcnt lgkmcnt(0)
	s_setprio 1
	s_waitcnt lgkmcnt(0)
	v_mfma_f32_16x16x32_bf16 v[52:55], v[174:177], v[190:193], v[52:55]
	v_mfma_f32_16x16x32_bf16 v[36:39], v[182:185], v[190:193], v[36:39]
	v_mfma_f32_16x16x32_bf16 v[40:43], v[174:177], v[198:201], v[40:43]
	v_mfma_f32_16x16x32_bf16 v[32:35], v[182:185], v[198:201], v[32:35]
	v_mfma_f32_16x16x32_bf16 v[20:23], v[174:177], v[206:209], v[20:23]
	v_mfma_f32_16x16x32_bf16 v[16:19], v[182:185], v[206:209], v[16:19]
	v_mfma_f32_16x16x32_bf16 v[4:7], v[174:177], v[214:217], v[4:7]
	v_mfma_f32_16x16x32_bf16 v[0:3], v[182:185], v[214:217], v[0:3]
	v_mfma_f32_16x16x32_bf16 v[52:55], v[178:181], v[194:197], v[52:55]
	v_mfma_f32_16x16x32_bf16 v[36:39], v[186:189], v[194:197], v[36:39]
	v_mfma_f32_16x16x32_bf16 v[40:43], v[178:181], v[202:205], v[40:43]
	v_mfma_f32_16x16x32_bf16 v[32:35], v[186:189], v[202:205], v[32:35]
	v_mfma_f32_16x16x32_bf16 v[20:23], v[178:181], v[210:213], v[20:23]
	v_mfma_f32_16x16x32_bf16 v[16:19], v[186:189], v[210:213], v[16:19]
	v_mfma_f32_16x16x32_bf16 v[4:7], v[178:181], v[218:221], v[4:7]
	v_mfma_f32_16x16x32_bf16 v[0:3], v[186:189], v[218:221], v[0:3]
	s_setprio 0
	s_barrier
	s_add_u32 s0, s24, 0x80080
	s_addc_u32 s1, s25, 0
	s_mov_b32 m0, s76
	v_lshl_add_u64 v[174:175], s[0:1], 0, v[128:129]
	global_load_lds_dwordx4 v[174:175], off
	v_lshl_add_u64 v[174:175], s[0:1], 0, v[130:131]
	s_mov_b32 m0, s77
	s_nop 0
	global_load_lds_dwordx4 v[174:175], off
	s_waitcnt vmcnt(6)
	s_barrier
	s_setprio 1
	v_mfma_f32_16x16x32_bf16 v[60:63], v[222:225], v[190:193], v[60:63]
	v_mfma_f32_16x16x32_bf16 v[56:59], v[230:233], v[190:193], v[56:59]
	v_mfma_f32_16x16x32_bf16 v[48:51], v[222:225], v[198:201], v[48:51]
	v_mfma_f32_16x16x32_bf16 v[44:47], v[230:233], v[198:201], v[44:47]
	v_mfma_f32_16x16x32_bf16 v[28:31], v[222:225], v[206:209], v[28:31]
	v_mfma_f32_16x16x32_bf16 v[24:27], v[230:233], v[206:209], v[24:27]
	v_mfma_f32_16x16x32_bf16 v[12:15], v[222:225], v[214:217], v[12:15]
	v_mfma_f32_16x16x32_bf16 v[8:11], v[230:233], v[214:217], v[8:11]
	v_mfma_f32_16x16x32_bf16 v[60:63], v[226:229], v[194:197], v[60:63]
	v_mfma_f32_16x16x32_bf16 v[56:59], v[234:237], v[194:197], v[56:59]
	v_mfma_f32_16x16x32_bf16 v[48:51], v[226:229], v[202:205], v[48:51]
	v_mfma_f32_16x16x32_bf16 v[44:47], v[234:237], v[202:205], v[44:47]
	v_mfma_f32_16x16x32_bf16 v[28:31], v[226:229], v[210:213], v[28:31]
	v_mfma_f32_16x16x32_bf16 v[24:27], v[234:237], v[210:213], v[24:27]
	v_mfma_f32_16x16x32_bf16 v[12:15], v[226:229], v[218:221], v[12:15]
	v_mfma_f32_16x16x32_bf16 v[8:11], v[234:237], v[218:221], v[8:11]
	s_setprio 0
	s_add_i32 s80, s80, 2
	s_cmp_gt_u32 s80, 29
	s_mov_b64 s[0:1], s[22:23]
	s_cbranch_scc1 .Lmy_kx_2
	s_barrier
	s_branch .LBB0_1008

; __device__ __forceinline__ unsigned cvt_pk_bf16(float lo, float hi) { const bf16x2_t r = __builtin_convertvector((f32x2_t){lo, hi}, bf16x2_t); return __builtin_bit_cast(unsigned, r); }
; __device__ __forceinline__ float silu_fast(float x) { return x * __builtin_amdgcn_rcpf(1.0f + __builtin_amdgcn_exp2f(-x * 1.4426950408889634f)); }
;     __device__ __forceinline__ void operator()(const f32x4 (&acc)[2][2][4][2], const Unit& u, int wr, int wc, int fr, int fq) const {
;         const int lc = u.pn * 128 + wc * 32 + 8 * fq;
; #pragma unroll
;         for (int ai = 0; ai < 2; ++ai)
; #pragma unroll
;             for (int m = 0; m < 4; ++m) {
;                 const int r = ai * HALF + wr * 64 + m * 16 + fr;
;                 if (r < u.rows) {
;                     const int asg = rowtab[u.ui * 256 + r];
;                     float o[8];
; #pragma unroll
;                     for (int n = 0; n < 2; ++n)
; #pragma unroll
;                         for (int j = 0; j < 4; ++j) { const float g = acc[ai][0][m][n][j], up = acc[ai][1][m][n][j]; o[4 * n + j] = silu_fast(g) * up; }
;                     u32x4 w; w[0] = cvt_pk_bf16(o[0], o[1]); w[1] = cvt_pk_bf16(o[2], o[3]); w[2] = cvt_pk_bf16(o[4], o[5]); w[3] = cvt_pk_bf16(o[6], o[7]);
;                     *(u32x4*)(act + (size_t)asg * DEXP + lc) = w;
;                 }
.Lmy_kxb_2:
	v_lshl_or_b32 v134, s20, 7, v158
	v_ashrrev_i32_e32 v135, 31, v134
	v_cmp_lt_i32_e32 vcc, v137, v148
	s_and_saveexec_b64 s[0:1], vcc
	s_cbranch_execz .LBB0_1017
	v_mul_f32_e32 v136, 0xbfb8aa3b, v124
	v_exp_f32_e32 v136, v136
	v_mul_f32_e32 v138, 0xbfb8aa3b, v125
	v_exp_f32_e32 v139, v138
	v_lshl_add_u32 v132, s38, 10, v150
	ds_read_b32 v138, v132
	v_add_f32_e32 v132, 1.0, v136
	v_rcp_f32_e32 v140, v132
	v_add_f32_e32 v132, 1.0, v139
	v_rcp_f32_e32 v141, v132
	v_mul_f32_e32 v132, 0xbfb8aa3b, v126
	v_mul_f32_e32 v136, 0xbfb8aa3b, v127
	v_exp_f32_e32 v132, v132
	v_exp_f32_e32 v136, v136
	v_pk_mul_f32 v[124:125], v[124:125], v[140:141]
	s_waitcnt lgkmcnt(0)
	v_ashrrev_i32_e32 v139, 31, v138
	v_pk_mul_f32 v[116:117], v[124:125], v[116:117]
	v_add_f32_e32 v124, 1.0, v132
	v_add_f32_e32 v125, 1.0, v136
	v_mul_f32_e32 v132, 0xbfb8aa3b, v120
	v_rcp_f32_e32 v124, v124
	v_rcp_f32_e32 v125, v125
	v_exp_f32_e32 v132, v132
	v_mul_f32_e32 v136, 0xbfb8aa3b, v121
	v_exp_f32_e32 v136, v136
	v_pk_mul_f32 v[124:125], v[126:127], v[124:125]
	v_add_f32_e32 v126, 1.0, v132
	v_mul_f32_e32 v132, 0xbfb8aa3b, v122
	v_add_f32_e32 v127, 1.0, v136
	v_exp_f32_e32 v132, v132
	v_mul_f32_e32 v136, 0xbfb8aa3b, v123
	v_exp_f32_e32 v136, v136
	v_rcp_f32_e32 v126, v126
	v_add_f32_e32 v132, 1.0, v132
	v_rcp_f32_e32 v127, v127
	v_rcp_f32_e32 v140, v132
	v_add_f32_e32 v132, 1.0, v136
	v_rcp_f32_e32 v141, v132
	v_pk_mul_f32 v[120:121], v[120:121], v[126:127]
	v_pk_mul_f32 v[118:119], v[124:125], v[118:119]
	v_pk_mul_f32 v[120:121], v[120:121], v[112:113]
	v_pk_mul_f32 v[112:113], v[122:123], v[140:141]
	s_nop 0
	v_pk_mul_f32 v[122:123], v[112:113], v[114:115]
	v_cvt_pk_bf16_f32 v112, v116, v117
	v_lshlrev_b64 v[116:117], 11, v[138:139]
	v_lshl_add_u64 v[116:117], s[6:7], 0, v[116:117]
	v_cvt_pk_bf16_f32 v113, v118, v119
	v_cvt_pk_bf16_f32 v114, v120, v121
	v_cvt_pk_bf16_f32 v115, v122, v123
	v_lshl_add_u64 v[116:117], v[134:135], 1, v[116:117]
	global_store_dwordx4 v[116:117], v[112:115], off
	s_or_b64 exec, exec, s[0:1]
	v_cmp_lt_i32_e32 vcc, v151, v148
	s_and_saveexec_b64 s[0:1], vcc
	s_cbranch_execnz .LBB0_1018

; #define PG8_WAIT_V(n) asm volatile("s_waitcnt vmcnt(" #n ")" ::: "memory")
; #define PG8_BAR __builtin_amdgcn_s_barrier()
; template <class Epi, class Sched>
; __device__ __forceinline__ void gemm_phase(LAS unsigned char* lds, const bf16_t* A, const int K, const Sched& S, const Epi& E, const int wv) {
;     ...
;     PG8_WAIT_V(0);
;     if (wr == 0) PG8_BAR;
;     PG8_BAR;
.LBB0_1025:
	s_waitcnt vmcnt(0)
	v_readlane_b32 s84, v252, 20
	s_cmpk_gt_u32 s28, 0xff
	v_readlane_b32 s85, v252, 21
	v_readlane_b32 s86, v252, 22
	v_readlane_b32 s87, v252, 23
	v_readlane_b32 s88, v252, 24
	v_readlane_b32 s89, v252, 25
	v_readlane_b32 s90, v252, 26
	v_readlane_b32 s91, v252, 27
	s_cbranch_scc1 .LBB0_1027
.LBB0_1027:
	v_readlane_b32 s76, v252, 28
	v_readlane_b32 s77, v252, 29
	v_readlane_b32 s78, v252, 30
	v_readlane_b32 s79, v252, 31
	s_barrier

;     __device__ __forceinline__ unsigned arow(const Unit& u, int r) const { return (unsigned)(u.pm * 256 + r); }
; template <class Epi, class Sched>
; __device__ __forceinline__ void gemm_phase(LAS unsigned char* lds, const bf16_t* A, const int K, const Sched& S, const Epi& E, const int wv) {
;     ...
;     const int wid = __builtin_amdgcn_readfirstlane(tid >> 6), lane = tid & 63, wr = wid >> 2, wc = wid & 3, fr = lane & 15, fq = lane >> 4;
;     const int nt = K / BK;
;     unsigned voffA[2], voffB[2];
; #pragma unroll
;     for (int i = 0; i < 2; ++i) { int R, C; stage_rc(tid * 16 + i * 8192, R, C); const int Rb = Epi::PERM ? ((R & ~31) + perm32(R & 31)) : R;
;         voffA[i] = (unsigned)(R * K + C) * 2u; voffB[i] = (unsigned)(Rb * K + C) * 2u; }
;     const size_t kstep = (size_t)(BK * 2);
;     const size_t hstep = (size_t)HALF * K * 2;
;     const size_t tstep = 2 * hstep;
;     const unsigned ldsw = (unsigned)wid * 1024u;
;     const int aoff = lds_byte(wr * 64 + fr, fq * 8), boff = lds_byte(wc * 32 + fr, fq * 8);
;     Unit cur, nxt; int ui = 0;
;     if (!S.next(0, cur)) return;
;     f32x4 acc[2][2][4][2];
; #pragma unroll
;     for (int a_ = 0; a_ < 2; ++a_)
; #pragma unroll
;         for (int b_ = 0; b_ < 2; ++b_)
; #pragma unroll
;             for (int m = 0; m < 4; ++m)
; #pragma unroll
;                 for (int n = 0; n < 2; ++n) acc[a_][b_][m][n] = (f32x4){0.f, 0.f, 0.f, 0.f};
;     bf16x8 At[4][2], B0[2][2], B1[2][2];
;     unsigned ao0[2] = {0u, 0u}, ao1[2] = {0u, 0u}, no0[2] = {0u, 0u}, no1[2] = {0u, 0u};
;     const char* Ab = (const char*)A;
;     const char* cA = Ab; const char* nA = Ab;
;     if constexpr (Sched::GATHER) {
; #pragma unroll
;         for (int i = 0; i < 2; ++i) { int R, C; stage_rc(tid * 16 + i * 8192, R, C);
;             ao0[i] = (S.arow(cur, R) * (unsigned)K + (unsigned)C) * 2u; ao1[i] = (S.arow(cur, HALF + R) * (unsigned)K + (unsigned)C) * 2u; }
;     } else cA = Ab + (size_t)cur.pm * tstep;
;     const char* cB = S.bptr(cur);
;     PG8_STAGE(PG8_SB(0, 0), cB, voffB); PG8_STAGE_A(PG8_SA(0, 0), 0, false, 0); PG8_STAGE(PG8_SB(0, 1), cB + hstep, voffB); PG8_STAGE_A(PG8_SA(0, 1), 1, false, 0);
;     if (wr == 1) PG8_BAR;
;     PG8_WAIT_V(4); PG8_BAR;
;     PG8_STAGE(PG8_SB(1, 0), cB + kstep, voffB); PG8_STAGE_A(PG8_SA(1, 0), 0, false, kstep); PG8_STAGE(PG8_SB(1, 1), cB + hstep + kstep, voffB);
;     PG8_WAIT_V(6); PG8_BAR;
.LBB0_1159:
	v_bfe_i32 v2, v4, 27, 1
	v_lshlrev_b32_e32 v0, 4, v4
	v_lshrrev_b32_e32 v2, 22, v2
	v_add_u32_e32 v2, v0, v2
	v_and_b32_e32 v2, 0xfffffc00, v2
	v_sub_u32_e32 v2, v0, v2
	v_ashrrev_i32_e32 v1, 31, v4
	v_lshrrev_b32_e32 v3, 4, v2
	v_lshrrev_b32_e32 v1, 26, v1
	v_bitop3_b32 v2, v3, v2, 32 bitop3:0x6c
	v_add_u32_e32 v1, v4, v1
	v_ashrrev_i32_e32 v5, 31, v2
	v_ashrrev_i32_e32 v1, 6, v1
	v_lshrrev_b32_e32 v5, 26, v5
	v_lshlrev_b32_e32 v3, 3, v1
	v_add_u32_e32 v5, v2, v5
	v_and_b32_e32 v3, -16, v3
	v_ashrrev_i32_e32 v6, 6, v5
	v_add_u32_e32 v144, v6, v3
	v_and_b32_e32 v3, 0xc0, v5
	v_sub_u32_e32 v2, v2, v3
	v_mov_b32_e32 v3, 1
	v_lshlrev_b32_e32 v1, 5, v1
	v_ashrrev_i16_sdwa v2, v3, sext(v2) dst_sel:DWORD dst_unused:UNUSED_PAD src0_sel:DWORD src1_sel:BYTE_0
	v_and_b32_e32 v1, 32, v1
	v_bfe_i32 v2, v2, 0, 16
	v_add_u32_e32 v0, 0x2000, v0
	v_add_lshl_u32 v146, v1, v2, 1
	v_ashrrev_i32_e32 v1, 31, v0
	v_lshrrev_b32_e32 v1, 22, v1
	v_add_u32_e32 v1, v0, v1
	v_ashrrev_i32_e32 v1, 10, v1
	v_mul_i32_i24_e32 v2, 0x400, v1
	v_lshlrev_b32_e32 v5, 1, v144
	v_lshrrev_b32_e32 v7, 2, v144
	v_and_b32_e32 v6, 3, v6
	s_mov_b32 s1, 0x1fffe0
	v_sub_u32_e32 v0, v0, v2
	v_and_b32_e32 v5, 24, v5
	v_and_b32_e32 v7, 4, v7
	v_and_or_b32 v6, v144, s1, v6
	v_lshrrev_b32_e32 v2, 4, v0
	v_or3_b32 v5, v6, v7, v5
	v_bitop3_b32 v0, v2, v0, 32 bitop3:0x6c
	v_lshl_add_u32 v128, v5, 11, v146
	v_ashrrev_i32_e32 v5, 31, v0
	v_lshrrev_b32_e32 v5, 26, v5
	v_lshlrev_b32_e32 v2, 3, v1
	v_add_u32_e32 v5, v0, v5
	v_and_b32_e32 v2, -16, v2
	v_ashrrev_i32_e32 v6, 6, v5
	v_add_u32_e32 v147, v6, v2
	v_and_b32_e32 v2, 0xc0, v5
	s_add_u32 s2, s76, 0x52188000
	v_sub_u32_e32 v0, v0, v2
	s_addc_u32 s3, s77, 0
	v_lshlrev_b32_e32 v1, 5, v1
	v_ashrrev_i16_sdwa v0, v3, sext(v0) dst_sel:DWORD dst_unused:UNUSED_PAD src0_sel:DWORD src1_sel:BYTE_0
	v_lshlrev_b32_e32 v2, 1, v147
	v_lshrrev_b32_e32 v3, 2, v147
	v_and_b32_e32 v5, 3, v6
	s_ashr_i32 s8, s28, 6
	s_ashr_i32 s13, s12, 31
	s_ashr_i32 s0, s28, 8
	v_and_b32_e32 v1, 32, v1
	v_bfe_i32 v0, v0, 0, 16
	v_and_b32_e32 v2, 24, v2
	v_and_b32_e32 v3, 4, v3
	v_and_or_b32 v5, v147, s1, v5
	s_add_i32 s14, 0, 0x20800
	s_lshl_b32 s1, s8, 10
	s_lshl_b64 s[10:11], s[12:13], 19
	v_or3_b32 v2, v5, v3, v2
	v_add_lshl_u32 v148, v1, v0, 1
	v_lshl_add_u32 v0, v144, 2, s14
	s_add_u32 s9, s26, s10
	v_lshl_add_u32 v130, v2, 11, v148
	ds_read2st64_b32 v[0:1], v0 offset1:2
	v_lshl_add_u32 v2, v147, 2, s14
	s_addc_u32 s10, s27, s11
	ds_read2st64_b32 v[2:3], v2 offset1:2
	s_add_u32 s22, s9, s6
	s_addc_u32 s23, s10, s7
	s_add_i32 s13, s1, 0
	s_add_i32 m0, s13, 0x10000
	s_waitcnt lgkmcnt(1)
	v_lshl_add_u32 v132, v0, 11, v146
	global_load_lds_dwordx4 v128, s[22:23]
	s_add_i32 m0, s13, 0x12000
	s_add_i32 s29, s13, 0x2000
	global_load_lds_dwordx4 v130, s[22:23]
	s_mov_b32 m0, s13
	s_waitcnt lgkmcnt(0)
	v_lshl_add_u32 v134, v2, 11, v148
	global_load_lds_dwordx4 v132, s[2:3]
	s_mov_b32 m0, s29
	s_add_u32 s6, s22, 0x40000
	global_load_lds_dwordx4 v134, s[2:3]
	s_addc_u32 s7, s23, 0
	s_add_i32 m0, s13, 0x14000
	s_add_i32 s30, s13, 0x4000
	global_load_lds_dwordx4 v128, s[6:7]
	s_add_i32 m0, s13, 0x16000
	v_lshl_add_u32 v136, v1, 11, v146
	global_load_lds_dwordx4 v130, s[6:7]
	s_mov_b32 m0, s30
	s_add_i32 s31, s13, 0x6000
	v_lshl_add_u32 v138, v3, 11, v148
	global_load_lds_dwordx4 v136, s[2:3]
	s_mov_b32 m0, s31
	v_mov_b32_e32 v133, 0
	global_load_lds_dwordx4 v138, s[2:3]
	v_mov_b32_e32 v129, v133
	v_mov_b32_e32 v131, v133
	s_mov_b32 s33, 0
	v_lshl_add_u64 v[2:3], s[22:23], 0, v[128:129]
	v_lshl_add_u64 v[0:1], s[22:23], 0, v[130:131]
	s_cmp_lg_u32 s0, 1
	v_mov_b32_e32 v135, v133
	s_cbranch_scc1 .LBB0_1161
.LBB0_1161:
	s_add_u32 s6, s76, 0x56188000
	s_addc_u32 s7, s77, 0
	s_lshl_b32 s8, s8, 5
	s_and_b32 s18, s8, 0x60
	s_mov_b64 s[8:9], 0x80
	s_add_i32 m0, s13, 0x18000
	v_lshl_add_u64 v[2:3], v[2:3], 0, s[8:9]
	s_lshl_b32 s15, s0, 13
	s_lshl_b32 s19, s18, 7
	s_waitcnt vmcnt(4)
	s_barrier
	global_load_lds_dwordx4 v[2:3], off
	s_add_i32 m0, s13, 0x1a000
	s_add_u32 s10, s76, 0x52188080
	v_lshl_add_u64 v[0:1], v[0:1], 0, s[8:9]
	s_addc_u32 s11, s77, 0
	s_add_i32 s34, s13, 0x8000
	s_add_i32 s35, s13, 0xa000
	global_load_lds_dwordx4 v[0:1], off
	v_lshl_add_u64 v[0:1], s[10:11], 0, v[132:133]
	s_mov_b32 m0, s34
	s_add_u32 s16, s22, 0x40080
	global_load_lds_dwordx4 v[0:1], off
	v_lshl_add_u64 v[0:1], s[10:11], 0, v[134:135]
	s_mov_b32 m0, s35
	s_addc_u32 s17, s23, 0
	global_load_lds_dwordx4 v[0:1], off
	s_add_i32 m0, s13, 0x1c000
	v_lshl_add_u64 v[0:1], s[16:17], 0, v[128:129]
	global_load_lds_dwordx4 v[0:1], off
	v_lshl_add_u64 v[0:1], s[16:17], 0, v[130:131]
	s_add_i32 m0, s13, 0x1e000
	s_add_i32 s64, 0, 0x10000
	global_load_lds_dwordx4 v[0:1], off
	v_lshrrev_b32_e32 v1, 1, v4
	v_and_b32_e32 v0, 15, v4
	v_and_b32_e32 v1, 24, v1
	v_lshl_or_b32 v149, s0, 6, v0
	v_lshlrev_b32_e32 v2, 1, v1
	v_lshl_or_b32 v0, v0, 6, v2
	v_lshlrev_b32_e32 v2, 2, v149
	v_and_b32_e32 v3, 32, v2
	v_lshlrev_b32_e32 v4, 2, v4
	s_waitcnt vmcnt(6)
	s_add_i32 s65, 0, 0x14000
	s_add_i32 s72, 0, 0x18000
	s_add_i32 s73, 0, 0x1c000
	v_bitop3_b32 v3, v0, s15, v3 bitop3:0xde
	v_and_b32_e32 v4, 32, v4
	v_or_b32_e32 v152, 16, v149
	v_or_b32_e32 v153, 32, v149
	v_or_b32_e32 v154, 48, v149
	v_add_u32_e32 v155, 0x80, v149
	v_add_u32_e32 v156, 0x90, v149
	v_add_u32_e32 v157, 0xa0, v149
	v_add_u32_e32 v158, 0xb0, v149
	s_add_i32 s0, 0, 0x20480
	s_add_i32 s68, s64, s1
	s_add_i32 s70, s65, s1
	s_add_i32 s74, s72, s1
	s_add_i32 s76, s73, s1
	v_bitop3_b32 v150, v0, s19, v4 bitop3:0xde
	v_add_u32_e32 v151, s14, v2
	v_or_b32_e32 v159, s18, v1
	v_lshl_add_u32 v160, v152, 2, s14
	v_lshl_add_u32 v161, v153, 2, s14
	v_lshl_add_u32 v162, v154, 2, s14
	v_lshl_add_u32 v163, v155, 2, s14
	v_lshl_add_u32 v164, v156, 2, s14
	v_lshl_add_u32 v165, v157, 2, s14
	v_lshl_add_u32 v166, v158, 2, s14
	v_mov_b32_e32 v167, s0
	s_add_i32 s36, 0, 0x20404
	s_add_i32 s37, 0, 0x2040c
	s_add_i32 s38, 0, 0x20414
	s_add_i32 s39, 0, 0x2041c
	s_add_i32 s40, 0, 0x20424
	s_add_i32 s41, 0, 0x2042c
	s_add_i32 s42, 0, 0x20434
	s_add_i32 s43, 0, 0x2043c
	s_add_i32 s50, 0, 0x20444
	s_add_i32 s51, 0, 0x2044c
	s_add_i32 s54, 0, 0x20454
	s_add_i32 s55, 0, 0x2045c
	s_add_i32 s60, 0, 0x20464
	s_add_i32 s61, 0, 0x2046c
	s_add_i32 s62, 0, 0x20474
	s_add_i32 s63, 0, 0x2047c
	v_add_u32_e32 v168, 0, v3
	s_add_i32 s66, s13, 0xc000
	s_add_i32 s67, s13, 0xe000
	s_add_i32 s69, s68, 0x2000
	s_add_i32 s71, s70, 0x2000
	s_add_i32 s75, s74, 0x2000
	s_add_i32 s77, s76, 0x2000
	v_mov_b32_e32 v135, v132
	s_mov_b32 s78, 0
	s_barrier
	s_branch .LBB0_1163

; #define PG8_LDA(dst, b, h) do { _Pragma("unroll") for (int m = 0; m < 4; ++m) _Pragma("unroll") for (int k = 0; k < 2; ++k) dst[m][k] = *(const LAS bf16x8*)(lds + PG8_SA(b, h) + aoff + m * 2048 + k * 1024); } while (0)
; #define PG8_LDB(dst, b, h) do { _Pragma("unroll") for (int n = 0; n < 2; ++n) _Pragma("unroll") for (int k = 0; k < 2; ++k) dst[n][k] = *(const LAS bf16x8*)(lds + PG8_SB(b, h) + boff + n * 2048 + k * 1024); } while (0)
; #define PG8_MMA(ai, bj, At, Bt) do { __builtin_amdgcn_s_setprio(1); _Pragma("unroll") for (int m = 0; m < 4; ++m) _Pragma("unroll") for (int n = 0; n < 2; ++n) _Pragma("unroll") for (int k = 0; k < 2; ++k) \
;         acc[ai][bj][m][n] = __builtin_amdgcn_mfma_f32_16x16x32_bf16(Bt[n][k], At[m][k], acc[ai][bj][m][n], 0, 0, 0); __builtin_amdgcn_s_setprio(0); } while (0)
; #define PG8_WAIT_L(n) asm volatile("s_waitcnt lgkmcnt(" #n ")" ::: "memory")
; #define PG8_BAR __builtin_amdgcn_s_barrier()
; #define PG8_SCHED __builtin_amdgcn_sched_barrier(0)
; template <class Epi, class Sched>
; __device__ __forceinline__ void gemm_phase(LAS unsigned char* lds, const bf16_t* A, const int K, const Sched& S, const Epi& E, const int wv) {
;     ...
;         for (int t = 0; t < nt; t += 2) {
;             const bool last = (t == nt - 2);
;             const size_t k1 = (size_t)(t + 1) * kstep;
;             const size_t k2 = last ? 0 : (size_t)(t + 2) * kstep, k3 = k2 + kstep;
;             const char* b2 = last ? nB : cB + (size_t)(t + 2) * kstep; const char* b3 = b2 + kstep;
;             PG8_LDB(B0, 0, 0); PG8_SCHED; PG8_LDA(At, 0, 0); PG8_STAGE_A(PG8_SA(1, 1), 1, false, k1);
;             PG8_WAIT_L(8); PG8_BAR; PG8_WAIT_L(0); PG8_MMA(0, 0, At, B0); PG8_BAR; PG8_SCHED;
;     ...
; #pragma unroll
;         for (int a_ = 0; a_ < 2; ++a_)
; #pragma unroll
;             for (int b_ = 0; b_ < 2; ++b_)
; #pragma unroll
;                 for (int m = 0; m < 4; ++m)
; #pragma unroll
;                     for (int n = 0; n < 2; ++n) acc[a_][b_][m][n] = (f32x4){0.f, 0.f, 0.f, 0.f};
;         cur = nxt; cB = nB; cA = nA; ++ui;
; #pragma unroll
;         for (int i = 0; i < 2; ++i) { ao0[i] = no0[i]; ao1[i] = no1[i]; }
.LBB0_1169:
	s_waitcnt lgkmcnt(0)
	v_mov_b32_e32 v137, v133
	v_mov_b32_e32 v139, v133
	s_add_u32 s17, s22, 0x100
	v_mov_b32_e32 v8, 0
	s_addc_u32 s19, s23, 0
	v_lshl_add_u64 v[140:141], s[10:11], 0, v[138:139]
	v_lshl_add_u64 v[142:143], s[10:11], 0, v[136:137]
	s_mov_b32 s80, -2
	s_mov_b64 s[0:1], 0
	v_mov_b32_e32 v9, v8
	v_mov_b32_e32 v10, v8
	v_mov_b32_e32 v11, v8
	v_mov_b32_e32 v20, v8
	v_mov_b32_e32 v21, v8
	v_mov_b32_e32 v22, v8
	v_mov_b32_e32 v23, v8
	v_mov_b32_e32 v48, v8
	v_mov_b32_e32 v49, v8
	v_mov_b32_e32 v50, v8
	v_mov_b32_e32 v51, v8
	v_mov_b32_e32 v52, v8
	v_mov_b32_e32 v53, v8
	v_mov_b32_e32 v54, v8
	v_mov_b32_e32 v55, v8
	v_mov_b32_e32 v72, v8
	v_mov_b32_e32 v73, v8
	v_mov_b32_e32 v74, v8
	v_mov_b32_e32 v75, v8
	v_mov_b32_e32 v80, v8
	v_mov_b32_e32 v81, v8
	v_mov_b32_e32 v82, v8
	v_mov_b32_e32 v83, v8
	v_mov_b32_e32 v88, v8
	v_mov_b32_e32 v89, v8
	v_mov_b32_e32 v90, v8
	v_mov_b32_e32 v91, v8
	v_mov_b32_e32 v96, v8
	v_mov_b32_e32 v97, v8
	v_mov_b32_e32 v98, v8
	v_mov_b32_e32 v99, v8
	v_mov_b32_e32 v104, v8
	v_mov_b32_e32 v105, v8
	v_mov_b32_e32 v106, v8
	v_mov_b32_e32 v107, v8
	v_mov_b32_e32 v112, v8
	v_mov_b32_e32 v113, v8
	v_mov_b32_e32 v114, v8
	v_mov_b32_e32 v115, v8
	v_mov_b32_e32 v76, v8
	v_mov_b32_e32 v77, v8
	v_mov_b32_e32 v78, v8
	v_mov_b32_e32 v79, v8
	v_mov_b32_e32 v84, v8
	v_mov_b32_e32 v85, v8
	v_mov_b32_e32 v86, v8
	v_mov_b32_e32 v87, v8
	v_mov_b32_e32 v92, v8
	v_mov_b32_e32 v93, v8
	v_mov_b32_e32 v94, v8
	v_mov_b32_e32 v95, v8
	v_mov_b32_e32 v100, v8
	v_mov_b32_e32 v101, v8
	v_mov_b32_e32 v102, v8
	v_mov_b32_e32 v103, v8
	v_mov_b32_e32 v108, v8
	v_mov_b32_e32 v109, v8
	v_mov_b32_e32 v110, v8
	v_mov_b32_e32 v111, v8
	v_mov_b32_e32 v116, v8
	v_mov_b32_e32 v117, v8
	v_mov_b32_e32 v118, v8
	v_mov_b32_e32 v119, v8
	v_mov_b32_e32 v120, v8
	v_mov_b32_e32 v121, v8
	v_mov_b32_e32 v122, v8
	v_mov_b32_e32 v123, v8
	v_mov_b32_e32 v124, v8
	v_mov_b32_e32 v125, v8
	v_mov_b32_e32 v126, v8
	v_mov_b32_e32 v127, v8
	v_mov_b32_e32 v40, v8
	v_mov_b32_e32 v41, v8
	v_mov_b32_e32 v42, v8
	v_mov_b32_e32 v43, v8
	v_mov_b32_e32 v44, v8
	v_mov_b32_e32 v45, v8
	v_mov_b32_e32 v46, v8
	v_mov_b32_e32 v47, v8
	v_mov_b32_e32 v24, v8
	v_mov_b32_e32 v25, v8
	v_mov_b32_e32 v26, v8
	v_mov_b32_e32 v27, v8
	v_mov_b32_e32 v28, v8
	v_mov_b32_e32 v29, v8
	v_mov_b32_e32 v30, v8
	v_mov_b32_e32 v31, v8
	v_mov_b32_e32 v0, v8
	v_mov_b32_e32 v1, v8
	v_mov_b32_e32 v2, v8
	v_mov_b32_e32 v3, v8
	v_mov_b32_e32 v4, v8
	v_mov_b32_e32 v5, v8
	v_mov_b32_e32 v6, v8
	v_mov_b32_e32 v7, v8
	v_mov_b32_e32 v64, v8
	v_mov_b32_e32 v65, v8
	v_mov_b32_e32 v66, v8
	v_mov_b32_e32 v67, v8
	v_mov_b32_e32 v68, v8
	v_mov_b32_e32 v69, v8
	v_mov_b32_e32 v70, v8
	v_mov_b32_e32 v71, v8
	v_mov_b32_e32 v56, v8
	v_mov_b32_e32 v57, v8
	v_mov_b32_e32 v58, v8
	v_mov_b32_e32 v59, v8
	v_mov_b32_e32 v60, v8
	v_mov_b32_e32 v61, v8
	v_mov_b32_e32 v62, v8
	v_mov_b32_e32 v63, v8
	v_mov_b32_e32 v32, v8
	v_mov_b32_e32 v33, v8
	v_mov_b32_e32 v34, v8
	v_mov_b32_e32 v35, v8
	v_mov_b32_e32 v36, v8
	v_mov_b32_e32 v37, v8
	v_mov_b32_e32 v38, v8
	v_mov_b32_e32 v39, v8
	v_mov_b32_e32 v12, v8
	v_mov_b32_e32 v13, v8
	v_mov_b32_e32 v14, v8
	v_mov_b32_e32 v15, v8
	v_mov_b32_e32 v16, v8
	v_mov_b32_e32 v17, v8
	v_mov_b32_e32 v18, v8
	v_mov_b32_e32 v19, v8
	s_bitcmp1_b32 s92, 8
	s_cbranch_scc0 .Lmy_ph_3
	s_barrier
.Lmy_ph_3:
.LBB0_1170:
	v_add_u32_e32 v132, s64, v150
	s_add_u32 s22, s0, 0x100
	ds_read_b128 v[174:177], v132
	ds_read_b128 v[178:181], v132 offset:1024
	ds_read_b128 v[182:185], v132 offset:2048
	ds_read_b128 v[186:189], v132 offset:3072
	s_addc_u32 s23, s1, 0
	s_add_u32 s81, s17, s0
	s_addc_u32 s82, s19, s1
	s_cmpk_eq_i32 s0, 0x700
	s_cselect_b64 vcc, -1, 0
	s_and_b64 s[24:25], vcc, exec
	s_cselect_b32 s83, 0, s22
	s_cselect_b32 s25, s21, s82
	s_cselect_b32 s24, s20, s81
	s_mov_b32 m0, s66
	v_lshl_add_u64 v[222:223], v[142:143], 0, s[0:1]
	ds_read_b128 v[190:193], v168
	ds_read_b128 v[194:197], v168 offset:1024
	ds_read_b128 v[198:201], v168 offset:2048
	ds_read_b128 v[202:205], v168 offset:3072
	ds_read_b128 v[206:209], v168 offset:4096
	ds_read_b128 v[210:213], v168 offset:5120
	ds_read_b128 v[214:217], v168 offset:6144
	ds_read_b128 v[218:221], v168 offset:7168
	global_load_lds_dwordx4 v[222:223], off
	v_lshl_add_u64 v[222:223], v[140:141], 0, s[0:1]
	s_mov_b32 m0, s67
	s_nop 0
	global_load_lds_dwordx4 v[222:223], off
	s_waitcnt lgkmcnt(8)
	s_barrier
	s_waitcnt lgkmcnt(0)
	s_setprio 1
	s_waitcnt lgkmcnt(0)
	v_mfma_f32_16x16x32_bf16 v[124:127], v[174:177], v[190:193], v[124:127]
	v_mfma_f32_16x16x32_bf16 v[120:123], v[182:185], v[190:193], v[120:123]
	v_mfma_f32_16x16x32_bf16 v[116:119], v[174:177], v[198:201], v[116:119]
	v_mfma_f32_16x16x32_bf16 v[108:111], v[182:185], v[198:201], v[108:111]
	v_mfma_f32_16x16x32_bf16 v[100:103], v[174:177], v[206:209], v[100:103]
	v_mfma_f32_16x16x32_bf16 v[92:95], v[182:185], v[206:209], v[92:95]
	v_mfma_f32_16x16x32_bf16 v[84:87], v[174:177], v[214:217], v[84:87]
	v_mfma_f32_16x16x32_bf16 v[76:79], v[182:185], v[214:217], v[76:79]
	v_mfma_f32_16x16x32_bf16 v[124:127], v[178:181], v[194:197], v[124:127]
	v_mfma_f32_16x16x32_bf16 v[120:123], v[186:189], v[194:197], v[120:123]
	v_mfma_f32_16x16x32_bf16 v[116:119], v[178:181], v[202:205], v[116:119]
	v_mfma_f32_16x16x32_bf16 v[108:111], v[186:189], v[202:205], v[108:111]
	v_mfma_f32_16x16x32_bf16 v[100:103], v[178:181], v[210:213], v[100:103]
	v_mfma_f32_16x16x32_bf16 v[92:95], v[186:189], v[210:213], v[92:95]
	v_mfma_f32_16x16x32_bf16 v[84:87], v[178:181], v[218:221], v[84:87]
	v_mfma_f32_16x16x32_bf16 v[76:79], v[186:189], v[218:221], v[76:79]
	s_setprio 0
	s_barrier
; #define PG8_STAGE(bufoff, gbase, voff) do { _Pragma("unroll") for (int _i = 0; _i < 2; ++_i) \
;         __builtin_amdgcn_global_load_lds((const unsigned*)((const char*)(gbase) + (voff)[_i]), (LAS unsigned*)(lds + (bufoff) + ldsw + _i * 8192), 16, 0, 0); } while (0)
; #define PG8_LDA(dst, b, h) do { _Pragma("unroll") for (int m = 0; m < 4; ++m) _Pragma("unroll") for (int k = 0; k < 2; ++k) dst[m][k] = *(const LAS bf16x8*)(lds + PG8_SA(b, h) + aoff + m * 2048 + k * 1024); } while (0)
; #define PG8_LDB(dst, b, h) do { _Pragma("unroll") for (int n = 0; n < 2; ++n) _Pragma("unroll") for (int k = 0; k < 2; ++k) dst[n][k] = *(const LAS bf16x8*)(lds + PG8_SB(b, h) + boff + n * 2048 + k * 1024); } while (0)
; #define PG8_MMA(ai, bj, At, Bt) do { __builtin_amdgcn_s_setprio(1); _Pragma("unroll") for (int m = 0; m < 4; ++m) _Pragma("unroll") for (int n = 0; n < 2; ++n) _Pragma("unroll") for (int k = 0; k < 2; ++k) \
;         acc[ai][bj][m][n] = __builtin_amdgcn_mfma_f32_16x16x32_bf16(Bt[n][k], At[m][k], acc[ai][bj][m][n], 0, 0, 0); __builtin_amdgcn_s_setprio(0); } while (0)
; #define PG8_WAIT_V(n) asm volatile("s_waitcnt vmcnt(" #n ")" ::: "memory")
; #define PG8_WAIT_L(n) asm volatile("s_waitcnt lgkmcnt(" #n ")" ::: "memory")
; template <class Epi, class Sched>
; __device__ __forceinline__ void gemm_phase(LAS unsigned char* lds, const bf16_t* A, const int K, const Sched& S, const Epi& E, const int wv) {
;     ...
;             PG8_LDB(B1, 0, 1); PG8_STAGE(PG8_SB(0, 0), b2, voffB);
;             PG8_BAR; PG8_WAIT_L(0); PG8_MMA(0, 1, At, B1); PG8_BAR;
;             PG8_LDA(At, 0, 1); PG8_STAGE_A(PG8_SA(0, 0), 0, last, k2);
;             PG8_BAR; PG8_WAIT_L(0); PG8_MMA(1, 0, At, B0); PG8_BAR; PG8_SCHED;
;             PG8_STAGE(PG8_SB(0, 1), b2 + hstep, voffB);
;             PG8_WAIT_V(6); PG8_BAR; PG8_MMA(1, 1, At, B1); PG8_BAR;
;             PG8_LDB(B0, 1, 0); PG8_SCHED; PG8_LDA(At, 1, 0); PG8_STAGE_A(PG8_SA(0, 1), 1, last, k2);
;             PG8_WAIT_L(8); PG8_BAR; PG8_WAIT_L(0); PG8_MMA(0, 0, At, B0); PG8_BAR; PG8_SCHED;
;             PG8_LDB(B1, 1, 1); PG8_STAGE(PG8_SB(1, 0), b3, voffB);
;             PG8_BAR; PG8_WAIT_L(0); PG8_MMA(0, 1, At, B1); PG8_BAR;
;             PG8_LDA(At, 1, 1); PG8_STAGE_A(PG8_SA(1, 0), 0, last, k3);
;             PG8_BAR; PG8_WAIT_L(0); PG8_MMA(1, 0, At, B0); PG8_BAR; PG8_SCHED;
;             PG8_STAGE(PG8_SB(1, 1), b3 + hstep, voffB);
	s_mov_b32 m0, s68
	v_add_u32_e32 v132, s65, v150
	v_lshl_add_u64 v[238:239], s[24:25], 0, v[128:129]
	ds_read_b128 v[222:225], v132
	ds_read_b128 v[226:229], v132 offset:1024
	ds_read_b128 v[230:233], v132 offset:2048
	ds_read_b128 v[234:237], v132 offset:3072
	global_load_lds_dwordx4 v[238:239], off
	v_lshl_add_u64 v[240:241], s[24:25], 0, v[130:131]
	s_mov_b32 m0, s69
	s_nop 0
	global_load_lds_dwordx4 v[240:241], off
	s_barrier
	s_waitcnt lgkmcnt(0)
	s_setprio 1
	s_waitcnt lgkmcnt(0)
	v_mfma_f32_16x16x32_bf16 v[112:115], v[222:225], v[190:193], v[112:115]
	v_mfma_f32_16x16x32_bf16 v[104:107], v[230:233], v[190:193], v[104:107]
	v_mfma_f32_16x16x32_bf16 v[96:99], v[222:225], v[198:201], v[96:99]
	v_mfma_f32_16x16x32_bf16 v[88:91], v[230:233], v[198:201], v[88:91]
	v_mfma_f32_16x16x32_bf16 v[80:83], v[222:225], v[206:209], v[80:83]
	v_mfma_f32_16x16x32_bf16 v[72:75], v[230:233], v[206:209], v[72:75]
	v_mfma_f32_16x16x32_bf16 v[52:55], v[222:225], v[214:217], v[52:55]
	v_mfma_f32_16x16x32_bf16 v[48:51], v[230:233], v[214:217], v[48:51]
	v_mfma_f32_16x16x32_bf16 v[112:115], v[226:229], v[194:197], v[112:115]
	v_mfma_f32_16x16x32_bf16 v[104:107], v[234:237], v[194:197], v[104:107]
	v_mfma_f32_16x16x32_bf16 v[96:99], v[226:229], v[202:205], v[96:99]
	v_mfma_f32_16x16x32_bf16 v[88:91], v[234:237], v[202:205], v[88:91]
	v_mfma_f32_16x16x32_bf16 v[80:83], v[226:229], v[210:213], v[80:83]
	v_mfma_f32_16x16x32_bf16 v[72:75], v[234:237], v[210:213], v[72:75]
	v_mfma_f32_16x16x32_bf16 v[52:55], v[226:229], v[218:221], v[52:55]
	v_mfma_f32_16x16x32_bf16 v[48:51], v[234:237], v[218:221], v[48:51]
	s_setprio 0
	s_add_u32 s0, s2, s83
	s_mov_b32 m0, s13
	s_addc_u32 s1, s3, 0
	v_cndmask_b32_e32 v132, v135, v170, vcc
	s_barrier
	ds_read_b128 v[190:193], v168 offset:16384
	ds_read_b128 v[194:197], v168 offset:17408
	ds_read_b128 v[198:201], v168 offset:18432
	ds_read_b128 v[202:205], v168 offset:19456
	ds_read_b128 v[206:209], v168 offset:20480
	ds_read_b128 v[210:213], v168 offset:21504
	ds_read_b128 v[214:217], v168 offset:22528
	ds_read_b128 v[218:221], v168 offset:23552
	v_cndmask_b32_e32 v242, v134, v172, vcc
	global_load_lds_dwordx4 v132, s[0:1]
	s_mov_b32 m0, s29
	v_mov_b32_e32 v243, v133
	global_load_lds_dwordx4 v242, s[0:1]
	s_barrier
	s_waitcnt lgkmcnt(0)
	v_lshl_add_u64 v[244:245], s[0:1], 0, v[132:133]
	v_lshl_add_u64 v[242:243], s[0:1], 0, v[242:243]
	s_setprio 1
	s_waitcnt lgkmcnt(0)
	v_mfma_f32_16x16x32_bf16 v[20:23], v[174:177], v[190:193], v[20:23]
	v_mfma_f32_16x16x32_bf16 v[8:11], v[182:185], v[190:193], v[8:11]
	v_mfma_f32_16x16x32_bf16 v[40:43], v[174:177], v[198:201], v[40:43]
	v_mfma_f32_16x16x32_bf16 v[44:47], v[182:185], v[198:201], v[44:47]
	v_mfma_f32_16x16x32_bf16 v[24:27], v[174:177], v[206:209], v[24:27]
	v_mfma_f32_16x16x32_bf16 v[28:31], v[182:185], v[206:209], v[28:31]
	v_mfma_f32_16x16x32_bf16 v[0:3], v[174:177], v[214:217], v[0:3]
	v_mfma_f32_16x16x32_bf16 v[4:7], v[182:185], v[214:217], v[4:7]
	v_mfma_f32_16x16x32_bf16 v[20:23], v[178:181], v[194:197], v[20:23]
	v_mfma_f32_16x16x32_bf16 v[8:11], v[186:189], v[194:197], v[8:11]
	v_mfma_f32_16x16x32_bf16 v[40:43], v[178:181], v[202:205], v[40:43]
	v_mfma_f32_16x16x32_bf16 v[44:47], v[186:189], v[202:205], v[44:47]
	v_mfma_f32_16x16x32_bf16 v[24:27], v[178:181], v[210:213], v[24:27]
	v_mfma_f32_16x16x32_bf16 v[28:31], v[186:189], v[210:213], v[28:31]
	v_mfma_f32_16x16x32_bf16 v[0:3], v[178:181], v[218:221], v[0:3]
	v_mfma_f32_16x16x32_bf16 v[4:7], v[186:189], v[218:221], v[4:7]
	s_setprio 0
	s_barrier
	s_add_u32 s82, s24, 0x40000
	s_addc_u32 s83, s25, 0
	s_mov_b32 m0, s70
	v_lshl_add_u64 v[174:175], s[82:83], 0, v[128:129]
	global_load_lds_dwordx4 v[174:175], off
	v_lshl_add_u64 v[174:175], s[82:83], 0, v[130:131]
	s_mov_b32 m0, s71
	s_nop 0
	global_load_lds_dwordx4 v[174:175], off
	s_waitcnt vmcnt(6)
	s_barrier
	s_setprio 1
	v_mfma_f32_16x16x32_bf16 v[64:67], v[222:225], v[190:193], v[64:67]
	v_mfma_f32_16x16x32_bf16 v[68:71], v[230:233], v[190:193], v[68:71]
	v_mfma_f32_16x16x32_bf16 v[56:59], v[222:225], v[198:201], v[56:59]
	v_mfma_f32_16x16x32_bf16 v[60:63], v[230:233], v[198:201], v[60:63]
	v_mfma_f32_16x16x32_bf16 v[32:35], v[222:225], v[206:209], v[32:35]
	v_mfma_f32_16x16x32_bf16 v[36:39], v[230:233], v[206:209], v[36:39]
	v_mfma_f32_16x16x32_bf16 v[12:15], v[222:225], v[214:217], v[12:15]
	v_mfma_f32_16x16x32_bf16 v[16:19], v[230:233], v[214:217], v[16:19]
	v_mfma_f32_16x16x32_bf16 v[64:67], v[226:229], v[194:197], v[64:67]
	v_mfma_f32_16x16x32_bf16 v[68:71], v[234:237], v[194:197], v[68:71]
	v_mfma_f32_16x16x32_bf16 v[56:59], v[226:229], v[202:205], v[56:59]
	v_mfma_f32_16x16x32_bf16 v[60:63], v[234:237], v[202:205], v[60:63]
	v_mfma_f32_16x16x32_bf16 v[32:35], v[226:229], v[210:213], v[32:35]
	v_mfma_f32_16x16x32_bf16 v[36:39], v[234:237], v[210:213], v[36:39]
	v_mfma_f32_16x16x32_bf16 v[12:15], v[226:229], v[218:221], v[12:15]
	v_mfma_f32_16x16x32_bf16 v[16:19], v[234:237], v[218:221], v[16:19]
	s_setprio 0
	v_add_u32_e32 v132, s72, v150
	s_barrier
	ds_read_b128 v[174:177], v132
	ds_read_b128 v[178:181], v132 offset:1024
	ds_read_b128 v[182:185], v132 offset:2048
	ds_read_b128 v[186:189], v132 offset:3072
	s_mov_b32 m0, s30
	v_cndmask_b32_e32 v132, v136, v171, vcc
	ds_read_b128 v[190:193], v168 offset:32768
	ds_read_b128 v[194:197], v168 offset:33792
	ds_read_b128 v[198:201], v168 offset:34816
	ds_read_b128 v[202:205], v168 offset:35840
	ds_read_b128 v[206:209], v168 offset:36864
	ds_read_b128 v[210:213], v168 offset:37888
	ds_read_b128 v[214:217], v168 offset:38912
	ds_read_b128 v[218:221], v168 offset:39936
	v_cndmask_b32_e32 v137, v138, v173, vcc
	global_load_lds_dwordx4 v132, s[0:1]
	s_mov_b32 m0, s31
	s_nop 0
	global_load_lds_dwordx4 v137, s[0:1]
	s_waitcnt lgkmcnt(8)
	s_barrier
; #define PG8_STAGE(bufoff, gbase, voff) do { _Pragma("unroll") for (int _i = 0; _i < 2; ++_i) \
;         __builtin_amdgcn_global_load_lds((const unsigned*)((const char*)(gbase) + (voff)[_i]), (LAS unsigned*)(lds + (bufoff) + ldsw + _i * 8192), 16, 0, 0); } while (0)
; #define PG8_LDA(dst, b, h) do { _Pragma("unroll") for (int m = 0; m < 4; ++m) _Pragma("unroll") for (int k = 0; k < 2; ++k) dst[m][k] = *(const LAS bf16x8*)(lds + PG8_SA(b, h) + aoff + m * 2048 + k * 1024); } while (0)
; #define PG8_LDB(dst, b, h) do { _Pragma("unroll") for (int n = 0; n < 2; ++n) _Pragma("unroll") for (int k = 0; k < 2; ++k) dst[n][k] = *(const LAS bf16x8*)(lds + PG8_SB(b, h) + boff + n * 2048 + k * 1024); } while (0)
; #define PG8_MMA(ai, bj, At, Bt) do { __builtin_amdgcn_s_setprio(1); _Pragma("unroll") for (int m = 0; m < 4; ++m) _Pragma("unroll") for (int n = 0; n < 2; ++n) _Pragma("unroll") for (int k = 0; k < 2; ++k) \
;         acc[ai][bj][m][n] = __builtin_amdgcn_mfma_f32_16x16x32_bf16(Bt[n][k], At[m][k], acc[ai][bj][m][n], 0, 0, 0); __builtin_amdgcn_s_setprio(0); } while (0)
; #define PG8_WAIT_V(n) asm volatile("s_waitcnt vmcnt(" #n ")" ::: "memory")
; #define PG8_WAIT_L(n) asm volatile("s_waitcnt lgkmcnt(" #n ")" ::: "memory")
; #define PG8_BAR __builtin_amdgcn_s_barrier()
; #define PG8_SCHED __builtin_amdgcn_sched_barrier(0)
; template <class Epi, class Sched>
; __device__ __forceinline__ void gemm_phase(LAS unsigned char* lds, const bf16_t* A, const int K, const Sched& S, const Epi& E, const int wv) {
;     ...
;             PG8_LDB(B0, 1, 0); PG8_SCHED; PG8_LDA(At, 1, 0); PG8_STAGE_A(PG8_SA(0, 1), 1, last, k2);
;             PG8_WAIT_L(8); PG8_BAR; PG8_WAIT_L(0); PG8_MMA(0, 0, At, B0); PG8_BAR; PG8_SCHED;
;             PG8_LDB(B1, 1, 1); PG8_STAGE(PG8_SB(1, 0), b3, voffB);
;             PG8_BAR; PG8_WAIT_L(0); PG8_MMA(0, 1, At, B1); PG8_BAR;
;             PG8_LDA(At, 1, 1); PG8_STAGE_A(PG8_SA(1, 0), 0, last, k3);
;             PG8_BAR; PG8_WAIT_L(0); PG8_MMA(1, 0, At, B0); PG8_BAR; PG8_SCHED;
;             PG8_STAGE(PG8_SB(1, 1), b3 + hstep, voffB);
;             PG8_WAIT_V(6); PG8_BAR; PG8_MMA(1, 1, At, B1); PG8_BAR;
;         }
	s_waitcnt lgkmcnt(0)
	s_setprio 1
	s_waitcnt lgkmcnt(0)
	v_mfma_f32_16x16x32_bf16 v[124:127], v[174:177], v[190:193], v[124:127]
	v_mfma_f32_16x16x32_bf16 v[120:123], v[182:185], v[190:193], v[120:123]
	v_mfma_f32_16x16x32_bf16 v[116:119], v[174:177], v[198:201], v[116:119]
	v_mfma_f32_16x16x32_bf16 v[108:111], v[182:185], v[198:201], v[108:111]
	v_mfma_f32_16x16x32_bf16 v[100:103], v[174:177], v[206:209], v[100:103]
	v_mfma_f32_16x16x32_bf16 v[92:95], v[182:185], v[206:209], v[92:95]
	v_mfma_f32_16x16x32_bf16 v[84:87], v[174:177], v[214:217], v[84:87]
	v_mfma_f32_16x16x32_bf16 v[76:79], v[182:185], v[214:217], v[76:79]
	v_mfma_f32_16x16x32_bf16 v[124:127], v[178:181], v[194:197], v[124:127]
	v_mfma_f32_16x16x32_bf16 v[120:123], v[186:189], v[194:197], v[120:123]
	v_mfma_f32_16x16x32_bf16 v[116:119], v[178:181], v[202:205], v[116:119]
	v_mfma_f32_16x16x32_bf16 v[108:111], v[186:189], v[202:205], v[108:111]
	v_mfma_f32_16x16x32_bf16 v[100:103], v[178:181], v[210:213], v[100:103]
	v_mfma_f32_16x16x32_bf16 v[92:95], v[186:189], v[210:213], v[92:95]
	v_mfma_f32_16x16x32_bf16 v[84:87], v[178:181], v[218:221], v[84:87]
	v_mfma_f32_16x16x32_bf16 v[76:79], v[186:189], v[218:221], v[76:79]
	s_setprio 0
	s_barrier
	s_mov_b32 m0, s74
	v_add_u32_e32 v132, s73, v150
	v_lshl_add_u64 v[238:239], v[238:239], 0, s[8:9]
	ds_read_b128 v[222:225], v132
	ds_read_b128 v[226:229], v132 offset:1024
	ds_read_b128 v[230:233], v132 offset:2048
	ds_read_b128 v[234:237], v132 offset:3072
	global_load_lds_dwordx4 v[238:239], off
	v_lshl_add_u64 v[238:239], v[240:241], 0, s[8:9]
	s_mov_b32 m0, s75
	s_nop 0
	global_load_lds_dwordx4 v[238:239], off
	s_barrier
	s_waitcnt lgkmcnt(0)
	s_setprio 1
	s_waitcnt lgkmcnt(0)
	v_mfma_f32_16x16x32_bf16 v[112:115], v[222:225], v[190:193], v[112:115]
	v_mfma_f32_16x16x32_bf16 v[104:107], v[230:233], v[190:193], v[104:107]
	v_mfma_f32_16x16x32_bf16 v[96:99], v[222:225], v[198:201], v[96:99]
	v_mfma_f32_16x16x32_bf16 v[88:91], v[230:233], v[198:201], v[88:91]
	v_mfma_f32_16x16x32_bf16 v[80:83], v[222:225], v[206:209], v[80:83]
	v_mfma_f32_16x16x32_bf16 v[72:75], v[230:233], v[206:209], v[72:75]
	v_mfma_f32_16x16x32_bf16 v[52:55], v[222:225], v[214:217], v[52:55]
	v_mfma_f32_16x16x32_bf16 v[48:51], v[230:233], v[214:217], v[48:51]
	v_mfma_f32_16x16x32_bf16 v[112:115], v[226:229], v[194:197], v[112:115]
	v_mfma_f32_16x16x32_bf16 v[104:107], v[234:237], v[194:197], v[104:107]
	v_mfma_f32_16x16x32_bf16 v[96:99], v[226:229], v[202:205], v[96:99]
	v_mfma_f32_16x16x32_bf16 v[88:91], v[234:237], v[202:205], v[88:91]
	v_mfma_f32_16x16x32_bf16 v[80:83], v[226:229], v[210:213], v[80:83]
	v_mfma_f32_16x16x32_bf16 v[72:75], v[234:237], v[210:213], v[72:75]
	v_mfma_f32_16x16x32_bf16 v[52:55], v[226:229], v[218:221], v[52:55]
	v_mfma_f32_16x16x32_bf16 v[48:51], v[234:237], v[218:221], v[48:51]
	s_setprio 0
	s_mov_b32 m0, s34
	v_lshl_add_u64 v[238:239], v[244:245], 0, s[8:9]
	s_barrier
	ds_read_b128 v[190:193], v168 offset:49152
	ds_read_b128 v[194:197], v168 offset:50176
	ds_read_b128 v[198:201], v168 offset:51200
	ds_read_b128 v[202:205], v168 offset:52224
	ds_read_b128 v[206:209], v168 offset:53248
	ds_read_b128 v[210:213], v168 offset:54272
	ds_read_b128 v[214:217], v168 offset:55296
	ds_read_b128 v[218:221], v168 offset:56320
	global_load_lds_dwordx4 v[238:239], off
	v_lshl_add_u64 v[238:239], v[242:243], 0, s[8:9]
	s_mov_b32 m0, s35
	s_nop 0
	global_load_lds_dwordx4 v[238:239], off
	s_barrier
	s_waitcnt lgkmcnt(0)
	s_setprio 1
	s_waitcnt lgkmcnt(0)
	v_mfma_f32_16x16x32_bf16 v[20:23], v[174:177], v[190:193], v[20:23]
	v_mfma_f32_16x16x32_bf16 v[8:11], v[182:185], v[190:193], v[8:11]
	v_mfma_f32_16x16x32_bf16 v[40:43], v[174:177], v[198:201], v[40:43]
	v_mfma_f32_16x16x32_bf16 v[44:47], v[182:185], v[198:201], v[44:47]
	v_mfma_f32_16x16x32_bf16 v[24:27], v[174:177], v[206:209], v[24:27]
	v_mfma_f32_16x16x32_bf16 v[28:31], v[182:185], v[206:209], v[28:31]
	v_mfma_f32_16x16x32_bf16 v[0:3], v[174:177], v[214:217], v[0:3]
	v_mfma_f32_16x16x32_bf16 v[4:7], v[182:185], v[214:217], v[4:7]
	v_mfma_f32_16x16x32_bf16 v[20:23], v[178:181], v[194:197], v[20:23]
	v_mfma_f32_16x16x32_bf16 v[8:11], v[186:189], v[194:197], v[8:11]
	v_mfma_f32_16x16x32_bf16 v[40:43], v[178:181], v[202:205], v[40:43]
	v_mfma_f32_16x16x32_bf16 v[44:47], v[186:189], v[202:205], v[44:47]
	v_mfma_f32_16x16x32_bf16 v[24:27], v[178:181], v[210:213], v[24:27]
	v_mfma_f32_16x16x32_bf16 v[28:31], v[186:189], v[210:213], v[28:31]
	v_mfma_f32_16x16x32_bf16 v[0:3], v[178:181], v[218:221], v[0:3]
	v_mfma_f32_16x16x32_bf16 v[4:7], v[186:189], v[218:221], v[4:7]
	s_setprio 0
	s_barrier
	s_add_u32 s0, s24, 0x40080
	s_addc_u32 s1, s25, 0
	s_mov_b32 m0, s76
	v_lshl_add_u64 v[174:175], s[0:1], 0, v[128:129]
	global_load_lds_dwordx4 v[174:175], off
	v_lshl_add_u64 v[174:175], s[0:1], 0, v[130:131]
	s_mov_b32 m0, s77
	s_nop 0
	global_load_lds_dwordx4 v[174:175], off
	s_waitcnt vmcnt(6)
	s_barrier
	s_setprio 1
	v_mfma_f32_16x16x32_bf16 v[64:67], v[222:225], v[190:193], v[64:67]
	v_mfma_f32_16x16x32_bf16 v[68:71], v[230:233], v[190:193], v[68:71]
	v_mfma_f32_16x16x32_bf16 v[56:59], v[222:225], v[198:201], v[56:59]
	v_mfma_f32_16x16x32_bf16 v[60:63], v[230:233], v[198:201], v[60:63]
	v_mfma_f32_16x16x32_bf16 v[32:35], v[222:225], v[206:209], v[32:35]
	v_mfma_f32_16x16x32_bf16 v[36:39], v[230:233], v[206:209], v[36:39]
	v_mfma_f32_16x16x32_bf16 v[12:15], v[222:225], v[214:217], v[12:15]
	v_mfma_f32_16x16x32_bf16 v[16:19], v[230:233], v[214:217], v[16:19]
	v_mfma_f32_16x16x32_bf16 v[64:67], v[226:229], v[194:197], v[64:67]
	v_mfma_f32_16x16x32_bf16 v[68:71], v[234:237], v[194:197], v[68:71]
	v_mfma_f32_16x16x32_bf16 v[56:59], v[226:229], v[202:205], v[56:59]
	v_mfma_f32_16x16x32_bf16 v[60:63], v[234:237], v[202:205], v[60:63]
	v_mfma_f32_16x16x32_bf16 v[32:35], v[226:229], v[210:213], v[32:35]
	v_mfma_f32_16x16x32_bf16 v[36:39], v[234:237], v[210:213], v[36:39]
	v_mfma_f32_16x16x32_bf16 v[12:15], v[226:229], v[218:221], v[12:15]
	v_mfma_f32_16x16x32_bf16 v[16:19], v[234:237], v[218:221], v[16:19]
	s_setprio 0
	s_add_i32 s80, s80, 2
	s_cmp_gt_u32 s80, 13
	s_mov_b64 s[0:1], s[22:23]
	s_cbranch_scc1 .Lmy_kx_3
	s_barrier
	s_branch .LBB0_1170

; __device__ __forceinline__ unsigned cvt_pk_bf16(float lo, float hi) { const bf16x2_t r = __builtin_convertvector((f32x2_t){lo, hi}, bf16x2_t); return __builtin_bit_cast(unsigned, r); }
;     __device__ __forceinline__ void operator()(const f32x4 (&acc)[2][2][4][2], const Unit& u, int wr, int wc, int fr, int fq) const {
;         const int lc = u.pn * 256 + wc * 32 + 8 * fq;
; #pragma unroll
;         for (int ai = 0; ai < 2; ++ai)
; #pragma unroll
;             for (int m = 0; m < 4; ++m) {
;                 const int r = ai * HALF + wr * 64 + m * 16 + fr;
;                 if (r < u.rows) {
;                     const int asg = rowtab[u.ui * 256 + r];
; #pragma unroll
;                     for (int bj = 0; bj < 2; ++bj) {
;                         const f32x4 v0 = acc[ai][bj][m][0], v1 = acc[ai][bj][m][1];
;                         u32x4 w; w[0] = cvt_pk_bf16(v0[0], v0[1]); w[1] = cvt_pk_bf16(v0[2], v0[3]); w[2] = cvt_pk_bf16(v1[0], v1[1]); w[3] = cvt_pk_bf16(v1[2], v1[3]);
;                         *(u32x4*)(yb + (size_t)asg * DM + lc + bj * HALF) = w;
;                     }
.Lmy_kxb_3:
	v_lshl_or_b32 v134, s12, 8, v159
	v_ashrrev_i32_e32 v135, 31, v134
	v_cmp_lt_i32_e32 vcc, v149, v145
	s_and_saveexec_b64 s[0:1], vcc
	s_cbranch_execz .LBB0_1179
	v_lshl_add_u32 v132, s33, 10, v151
	ds_read_b32 v136, v132
	v_cvt_pk_bf16_f32 v124, v124, v125
	v_cvt_pk_bf16_f32 v125, v126, v127
	v_cvt_pk_bf16_f32 v126, v120, v121
	v_cvt_pk_bf16_f32 v127, v122, v123
	s_waitcnt lgkmcnt(0)
	v_ashrrev_i32_e32 v137, 31, v136
	v_lshlrev_b64 v[120:121], 12, v[136:137]
	v_lshl_add_u64 v[120:121], s[6:7], 0, v[120:121]
	v_lshl_add_u64 v[120:121], v[134:135], 1, v[120:121]
	v_cvt_pk_bf16_f32 v112, v112, v113
	v_cvt_pk_bf16_f32 v113, v114, v115
	v_cvt_pk_bf16_f32 v114, v104, v105
	v_cvt_pk_bf16_f32 v115, v106, v107
	global_store_dwordx4 v[120:121], v[124:127], off
	global_store_dwordx4 v[120:121], v[112:115], off offset:256
	s_or_b64 exec, exec, s[0:1]
	v_cmp_lt_i32_e32 vcc, v152, v145
	s_and_saveexec_b64 s[0:1], vcc
	s_cbranch_execnz .LBB0_1180

; #define PG8_WAIT_V(n) asm volatile("s_waitcnt vmcnt(" #n ")" ::: "memory")
; #define PG8_BAR __builtin_amdgcn_s_barrier()
; template <class Epi, class Sched>
; __device__ __forceinline__ void gemm_phase(LAS unsigned char* lds, const bf16_t* A, const int K, const Sched& S, const Epi& E, const int wv) {
;     ...
;     PG8_WAIT_V(0);
;     if (wr == 0) PG8_BAR;
;     PG8_BAR;
.LBB0_1187:
	s_waitcnt vmcnt(0)
	v_readlane_b32 s84, v252, 20
	s_cmpk_gt_u32 s28, 0xff
	v_readlane_b32 s85, v252, 21
	v_readlane_b32 s86, v252, 22
	v_readlane_b32 s87, v252, 23
	v_readlane_b32 s88, v252, 24
	v_readlane_b32 s89, v252, 25
	v_readlane_b32 s90, v252, 26
	v_readlane_b32 s91, v252, 27
	s_cbranch_scc1 .LBB0_1189
.LBB0_1189:
	v_readlane_b32 s76, v252, 28
	v_readlane_b32 s77, v252, 29
	v_readlane_b32 s78, v252, 30
	v_readlane_b32 s79, v252, 31
	s_barrier

;     __device__ __forceinline__ unsigned arow(const Unit& u, int r) const { return (unsigned)(u.pm * 256 + r); }
; template <class Epi, class Sched>
; __device__ __forceinline__ void gemm_phase(LAS unsigned char* lds, const bf16_t* A, const int K, const Sched& S, const Epi& E, const int wv) {
;     ...
;     const int wid = __builtin_amdgcn_readfirstlane(tid >> 6), lane = tid & 63, wr = wid >> 2, wc = wid & 3, fr = lane & 15, fq = lane >> 4;
;     const int nt = K / BK;
;     unsigned voffA[2], voffB[2];
; #pragma unroll
;     for (int i = 0; i < 2; ++i) { int R, C; stage_rc(tid * 16 + i * 8192, R, C); const int Rb = Epi::PERM ? ((R & ~31) + perm32(R & 31)) : R;
;         voffA[i] = (unsigned)(R * K + C) * 2u; voffB[i] = (unsigned)(Rb * K + C) * 2u; }
;     const size_t kstep = (size_t)(BK * 2);
;     const size_t hstep = (size_t)HALF * K * 2;
;     const size_t tstep = 2 * hstep;
;     const unsigned ldsw = (unsigned)wid * 1024u;
;     const int aoff = lds_byte(wr * 64 + fr, fq * 8), boff = lds_byte(wc * 32 + fr, fq * 8);
;     Unit cur, nxt; int ui = 0;
;     if (!S.next(0, cur)) return;
;     f32x4 acc[2][2][4][2];
; #pragma unroll
;     for (int a_ = 0; a_ < 2; ++a_)
; #pragma unroll
;         for (int b_ = 0; b_ < 2; ++b_)
; #pragma unroll
;             for (int m = 0; m < 4; ++m)
; #pragma unroll
;                 for (int n = 0; n < 2; ++n) acc[a_][b_][m][n] = (f32x4){0.f, 0.f, 0.f, 0.f};
;     bf16x8 At[4][2], B0[2][2], B1[2][2];
;     unsigned ao0[2] = {0u, 0u}, ao1[2] = {0u, 0u}, no0[2] = {0u, 0u}, no1[2] = {0u, 0u};
;     const char* Ab = (const char*)A;
;     const char* cA = Ab; const char* nA = Ab;
;     if constexpr (Sched::GATHER) {
; #pragma unroll
;         for (int i = 0; i < 2; ++i) { int R, C; stage_rc(tid * 16 + i * 8192, R, C);
;             ao0[i] = (S.arow(cur, R) * (unsigned)K + (unsigned)C) * 2u; ao1[i] = (S.arow(cur, HALF + R) * (unsigned)K + (unsigned)C) * 2u; }
;     } else cA = Ab + (size_t)cur.pm * tstep;
;     const char* cB = S.bptr(cur);
;     PG8_STAGE(PG8_SB(0, 0), cB, voffB); PG8_STAGE_A(PG8_SA(0, 0), 0, false, 0); PG8_STAGE(PG8_SB(0, 1), cB + hstep, voffB); PG8_STAGE_A(PG8_SA(0, 1), 1, false, 0);
;     if (wr == 1) PG8_BAR;
;     PG8_WAIT_V(4); PG8_BAR;
;     PG8_STAGE(PG8_SB(1, 0), cB + kstep, voffB); PG8_STAGE_A(PG8_SA(1, 0), 0, false, kstep); PG8_STAGE(PG8_SB(1, 1), cB + hstep + kstep, voffB);
;     PG8_WAIT_V(6); PG8_BAR;
.LBB0_1367:
	s_andn2_b64 vcc, exec, s[0:1]
	s_cbranch_vccnz .LBB0_1632
	v_ashrrev_i32_e32 v1, 31, v8
	v_lshrrev_b32_e32 v1, 26, v1
	v_add_u32_e32 v1, v8, v1
	v_ashrrev_i32_e32 v9, 6, v1
	v_bfe_i32 v1, v8, 27, 1
	v_lshlrev_b32_e32 v0, 4, v8
	v_lshrrev_b32_e32 v1, 22, v1
	v_add_u32_e32 v1, v0, v1
	v_and_b32_e32 v1, 0xfffffc00, v1
	v_sub_u32_e32 v1, v0, v1
	v_lshrrev_b32_e32 v2, 4, v1
	v_bitop3_b32 v1, v2, v1, 32 bitop3:0x6c
	s_waitcnt lgkmcnt(0)
	v_ashrrev_i32_e32 v3, 31, v1
	v_lshrrev_b32_e32 v3, 26, v3
	v_add_u32_e32 v3, v1, v3
	v_lshlrev_b32_e32 v2, 3, v9
	v_ashrrev_i32_e32 v10, 6, v3
	v_and_b32_e32 v3, 0xc0, v3
	v_and_b32_e32 v2, -16, v2
	v_sub_u32_e32 v1, v1, v3
	v_mov_b32_e32 v3, 1
	v_add_u32_e32 v2, v10, v2
	v_ashrrev_i16_sdwa v1, v3, sext(v1) dst_sel:DWORD dst_unused:UNUSED_PAD src0_sel:DWORD src1_sel:BYTE_0
	v_lshlrev_b32_e32 v4, 5, v9
	v_bfe_i32 v11, v1, 0, 16
	v_lshlrev_b32_e32 v1, 1, v2
	v_lshrrev_b32_e32 v5, 2, v2
	v_and_b32_e32 v6, 3, v10
	s_mov_b32 s1, 0xfffe0
	v_and_b32_e32 v4, 32, v4
	v_and_b32_e32 v1, 24, v1
	v_and_b32_e32 v5, 4, v5
	v_and_or_b32 v6, v2, s1, v6
	v_or3_b32 v1, v6, v5, v1
	v_add_lshl_u32 v4, v4, v11, 1
	v_add_u32_e32 v0, 0x2000, v0
	v_lshl_add_u32 v162, v1, 12, v4
	v_ashrrev_i32_e32 v1, 31, v0
	v_lshrrev_b32_e32 v1, 22, v1
	v_add_u32_e32 v1, v0, v1
	v_ashrrev_i32_e32 v12, 10, v1
	v_mul_i32_i24_e32 v1, 0x400, v12
	v_sub_u32_e32 v0, v0, v1
	v_lshrrev_b32_e32 v1, 4, v0
	v_bitop3_b32 v0, v1, v0, 32 bitop3:0x6c
	v_lshl_add_u32 v160, v2, 12, v4
	v_ashrrev_i32_e32 v2, 31, v0
	v_lshrrev_b32_e32 v2, 26, v2
	s_add_u32 s50, s76, 0x1988000
	v_add_u32_e32 v2, v0, v2
	s_addc_u32 s51, s77, 0
	v_lshlrev_b32_e32 v1, 3, v12
	v_ashrrev_i32_e32 v13, 6, v2
	v_and_b32_e32 v2, 0xc0, v2
	s_add_u32 s54, s76, 0x3c188000
	v_and_b32_e32 v1, -16, v1
	v_sub_u32_e32 v0, v0, v2
	s_addc_u32 s55, s77, 0
	s_ashr_i32 s0, s35, 6
	v_add_u32_e32 v1, v13, v1
	v_ashrrev_i16_sdwa v0, v3, sext(v0) dst_sel:DWORD dst_unused:UNUSED_PAD src0_sel:DWORD src1_sel:BYTE_0
	v_and_b32_e32 v3, 3, v13
	s_ashr_i32 s17, s16, 31
	s_ashr_i32 s15, s14, 31
	v_and_or_b32 v3, v1, s1, v3
	s_ashr_i32 s1, s35, 8
	s_lshl_b32 s60, s0, 10
	s_lshl_b64 s[2:3], s[16:17], 20
	s_lshl_b64 s[4:5], s[14:15], 20
	s_add_u32 s24, s50, s4
	v_lshlrev_b32_e32 v4, 5, v12
	v_bfe_i32 v14, v0, 0, 16
	v_lshlrev_b32_e32 v0, 1, v1
	v_lshrrev_b32_e32 v2, 2, v1
	s_addc_u32 s25, s51, s5
	s_add_i32 s61, s60, 0
	v_and_b32_e32 v4, 32, v4
	v_and_b32_e32 v0, 24, v0
	v_and_b32_e32 v2, 4, v2
	s_add_i32 m0, s61, 0x10000
	v_or3_b32 v0, v3, v2, v0
	v_add_lshl_u32 v2, v4, v14, 1
	global_load_lds_dwordx4 v162, s[24:25]
	s_add_i32 m0, s61, 0x12000
	v_lshl_add_u32 v166, v0, 12, v2
	s_add_u32 s28, s54, s2
	global_load_lds_dwordx4 v166, s[24:25]
	s_addc_u32 s29, s55, s3
	s_mov_b32 m0, s61
	s_add_i32 s62, s61, 0x2000
	v_lshl_add_u32 v164, v1, 12, v2
	global_load_lds_dwordx4 v160, s[28:29]
	s_mov_b32 m0, s62
	s_add_u32 s2, s24, 0x80000
	global_load_lds_dwordx4 v164, s[28:29]
	s_addc_u32 s3, s25, 0
	s_add_i32 m0, s61, 0x14000
	v_mov_b32_e32 v169, 0
	global_load_lds_dwordx4 v162, s[2:3]
	s_add_i32 m0, s61, 0x16000
	v_mov_b32_e32 v163, v169
	global_load_lds_dwordx4 v166, s[2:3]
	s_add_u32 s2, s28, 0x80000
	s_addc_u32 s3, s29, 0
	s_add_i32 s63, s61, 0x4000
	s_mov_b32 m0, s63
	s_add_i32 s64, s61, 0x6000
	global_load_lds_dwordx4 v160, s[2:3]
	s_mov_b32 m0, s64
	v_mov_b32_e32 v167, v169
	global_load_lds_dwordx4 v164, s[2:3]
	v_mov_b32_e32 v161, v169
	v_mov_b32_e32 v165, v169
	s_mov_b32 s19, 0
	v_lshl_add_u64 v[6:7], s[24:25], 0, v[162:163]
	v_lshl_add_u64 v[4:5], s[24:25], 0, v[166:167]
	v_lshl_add_u64 v[2:3], s[28:29], 0, v[160:161]
	s_cmp_lg_u32 s1, 1
	v_lshl_add_u64 v[0:1], s[28:29], 0, v[164:165]
	s_cbranch_scc1 .LBB0_1370
.LBB0_1370:
	s_add_u32 s20, s76, 0xc8000
	s_addc_u32 s21, s77, 0
	s_add_u32 s22, s76, 0x4c188000
	s_mov_b64 s[26:27], 0x80
	s_addc_u32 s23, s77, 0
	s_and_b32 s4, s0, 3
	s_add_i32 m0, s61, 0x18000
	v_lshl_add_u64 v[6:7], v[6:7], 0, s[26:27]
	s_lshl_b32 s65, s1, 6
	s_lshl_b32 s2, s1, 13
	s_lshl_b32 s3, s4, 12
	s_waitcnt vmcnt(4)
	s_barrier
	global_load_lds_dwordx4 v[6:7], off
	v_lshl_add_u64 v[4:5], v[4:5], 0, s[26:27]
	s_add_i32 m0, s61, 0x1a000
	s_add_i32 s66, s61, 0x8000
	s_add_i32 s67, s61, 0xa000
	global_load_lds_dwordx4 v[4:5], off
	v_lshl_add_u64 v[2:3], v[2:3], 0, s[26:27]
	s_mov_b32 m0, s66
	s_add_u32 s0, s24, 0x80080
	global_load_lds_dwordx4 v[2:3], off
	v_lshl_add_u64 v[0:1], v[0:1], 0, s[26:27]
	s_mov_b32 m0, s67
	s_addc_u32 s1, s25, 0
	global_load_lds_dwordx4 v[0:1], off
	s_add_i32 m0, s61, 0x1c000
	v_lshl_add_u64 v[0:1], s[0:1], 0, v[162:163]
	global_load_lds_dwordx4 v[0:1], off
	v_lshl_add_u64 v[0:1], s[0:1], 0, v[166:167]
	s_add_i32 m0, s61, 0x1e000
	s_mov_b64 s[6:7], 0x148000
	global_load_lds_dwordx4 v[0:1], off
	v_bfe_u32 v0, v8, 4, 2
	v_lshlrev_b32_e32 v1, 3, v0
	v_lshl_or_b32 v170, s4, 5, v1
	v_and_b32_e32 v172, 8, v1
	v_lshlrev_b32_e32 v168, 1, v170
	v_lshl_add_u64 v[174:175], s[76:77], 0, v[168:169]
	v_lshlrev_b32_e32 v168, 2, v172
	v_lshl_add_u64 v[176:177], s[20:21], 0, v[168:169]
	v_lshlrev_b32_e32 v168, 2, v170
	v_lshlrev_b32_e32 v2, 4, v0
	v_cmp_gt_u32_e64 s[0:1], 2, v0
	v_lshl_add_u64 v[0:1], s[76:77], 0, v[168:169]
	v_lshl_add_u64 v[178:179], v[0:1], 0, s[6:7]
	v_lshlrev_b32_e32 v0, 15, v9
	v_and_b32_e32 v0, 0xffff0000, v0
	v_lshl_add_u32 v0, v10, 12, v0
	v_and_b32_e32 v1, 1, v9
	v_lshl_or_b32 v0, v1, 6, v0
	v_lshl_add_u32 v168, v11, 1, v0
	v_lshlrev_b32_e32 v0, 15, v12
	v_and_b32_e32 v171, 15, v8
	v_lshlrev_b32_e32 v3, 2, v8
	v_and_b32_e32 v0, 0xffff0000, v0
	v_lshl_or_b32 v2, v171, 6, v2
	v_and_b32_e32 v3, 32, v3
	v_lshl_add_u32 v0, v13, 12, v0
	v_and_b32_e32 v1, 1, v12
	v_bitop3_b32 v4, v2, s2, v3 bitop3:0xde
	v_bitop3_b32 v173, v2, s3, v3 bitop3:0xde
	s_mov_b64 s[2:3], 0x80080
	s_waitcnt vmcnt(6)
	s_cmp_eq_u32 s4, 0
	v_lshl_or_b32 v0, v1, 6, v0
	s_cselect_b64 s[30:31], -1, 0
	s_mov_b64 s[6:7], 0x44188000
	v_lshl_add_u64 v[182:183], v[168:169], 0, s[2:3]
	v_lshl_add_u32 v168, v14, 1, v0
	s_add_i32 s70, 0, 0x10000
	s_add_i32 s71, 0, 0x14000
	v_mbcnt_lo_u32_b32 v0, -1, 0
	v_cmp_eq_u32_e64 s[4:5], 0, v171
	s_ashr_i32 s68, s93, 31
	s_ashr_i32 s69, s94, 31
	v_lshl_add_u64 v[180:181], v[174:175], 0, s[6:7]
	v_lshl_add_u64 v[184:185], v[168:169], 0, s[2:3]
	v_mov_b64_e32 v[186:187], 0x600
	v_mov_b64_e32 v[188:189], 0x5ff
	v_add_u32_e32 v208, s70, v173
	v_add_u32_e32 v209, 0, v4
	v_add_u32_e32 v210, s71, v173
	s_mov_b32 s34, 0x3db504f3
	s_mov_b32 s72, 0x46188000
	s_mov_b64 s[36:37], 0x1000
	s_mov_b64 s[38:39], 0x2000
	s_mov_b64 s[40:41], 0x3000
	s_mov_b32 s73, 0x40188000
	s_mov_b64 s[44:45], 0x1800
	v_mov_b32_e32 v191, 0x3db504f3
	v_mbcnt_hi_u32_b32 v211, -1, v0
	v_mov_b32_e32 v212, 0x3e0293ee
	v_mov_b32_e32 v213, 0x1000
	s_mov_b32 s74, 0
	s_barrier
	s_branch .LBB0_1373

; #define PG8_LDA(dst, b, h) do { _Pragma("unroll") for (int m = 0; m < 4; ++m) _Pragma("unroll") for (int k = 0; k < 2; ++k) dst[m][k] = *(const LAS bf16x8*)(lds + PG8_SA(b, h) + aoff + m * 2048 + k * 1024); } while (0)
; #define PG8_LDB(dst, b, h) do { _Pragma("unroll") for (int n = 0; n < 2; ++n) _Pragma("unroll") for (int k = 0; k < 2; ++k) dst[n][k] = *(const LAS bf16x8*)(lds + PG8_SB(b, h) + boff + n * 2048 + k * 1024); } while (0)
; #define PG8_MMA(ai, bj, At, Bt) do { __builtin_amdgcn_s_setprio(1); _Pragma("unroll") for (int m = 0; m < 4; ++m) _Pragma("unroll") for (int n = 0; n < 2; ++n) _Pragma("unroll") for (int k = 0; k < 2; ++k) \
;         acc[ai][bj][m][n] = __builtin_amdgcn_mfma_f32_16x16x32_bf16(Bt[n][k], At[m][k], acc[ai][bj][m][n], 0, 0, 0); __builtin_amdgcn_s_setprio(0); } while (0)
; #define PG8_WAIT_L(n) asm volatile("s_waitcnt lgkmcnt(" #n ")" ::: "memory")
; #define PG8_BAR __builtin_amdgcn_s_barrier()
; #define PG8_SCHED __builtin_amdgcn_sched_barrier(0)
; template <class Epi, class Sched>
; __device__ __forceinline__ void gemm_phase(LAS unsigned char* lds, const bf16_t* A, const int K, const Sched& S, const Epi& E, const int wv) {
;     ...
;         for (int t = 0; t < nt; t += 2) {
;             const bool last = (t == nt - 2);
;             const size_t k1 = (size_t)(t + 1) * kstep;
;             const size_t k2 = last ? 0 : (size_t)(t + 2) * kstep, k3 = k2 + kstep;
;             const char* b2 = last ? nB : cB + (size_t)(t + 2) * kstep; const char* b3 = b2 + kstep;
;             PG8_LDB(B0, 0, 0); PG8_SCHED; PG8_LDA(At, 0, 0); PG8_STAGE_A(PG8_SA(1, 1), 1, false, k1);
;             PG8_WAIT_L(8); PG8_BAR; PG8_WAIT_L(0); PG8_MMA(0, 0, At, B0); PG8_BAR; PG8_SCHED;
;     ...
; #pragma unroll
;         for (int a_ = 0; a_ < 2; ++a_)
; #pragma unroll
;             for (int b_ = 0; b_ < 2; ++b_)
; #pragma unroll
;                 for (int m = 0; m < 4; ++m)
; #pragma unroll
;                     for (int n = 0; n < 2; ++n) acc[a_][b_][m][n] = (f32x4){0.f, 0.f, 0.f, 0.f};
;         cur = nxt; cB = nB; cA = nA; ++ui;
.LBB0_1375:
	s_ashr_i32 s15, s14, 31
	s_lshl_b64 s[24:25], s[14:15], 20
	s_add_u32 s24, s50, s24
	s_addc_u32 s25, s51, s25
	s_and_b64 s[28:29], s[8:9], exec
	s_cselect_b32 s15, s25, s11
	s_cselect_b32 s18, s24, s10
	s_ashr_i32 s17, s16, 31
	s_lshl_b64 s[28:29], s[16:17], 20
	s_add_u32 s28, s54, s28
	s_addc_u32 s29, s55, s29
	s_add_u32 s17, s10, 0x100
	v_mov_b32_e32 v0, 0
	s_addc_u32 s33, s11, 0
	s_waitcnt vmcnt(0)
	v_lshl_add_u64 v[128:129], s[2:3], 0, v[182:183]
	v_lshl_add_u64 v[130:131], s[2:3], 0, v[184:185]
	s_mov_b32 s77, -2
	s_mov_b64 s[10:11], 0
	v_mov_b32_e32 v1, v0
	v_mov_b32_e32 v2, v0
	s_waitcnt lgkmcnt(0)
	v_mov_b32_e32 v3, v0
	v_mov_b32_e32 v4, v0
	v_mov_b32_e32 v5, v0
	v_mov_b32_e32 v6, v0
	v_mov_b32_e32 v7, v0
	v_mov_b32_e32 v16, v0
	v_mov_b32_e32 v17, v0
	v_mov_b32_e32 v18, v0
	v_mov_b32_e32 v19, v0
	v_mov_b32_e32 v20, v0
	v_mov_b32_e32 v21, v0
	v_mov_b32_e32 v22, v0
	v_mov_b32_e32 v23, v0
	v_mov_b32_e32 v32, v0
	v_mov_b32_e32 v33, v0
	v_mov_b32_e32 v34, v0
	v_mov_b32_e32 v35, v0
	v_mov_b32_e32 v36, v0
	v_mov_b32_e32 v37, v0
	v_mov_b32_e32 v38, v0
	v_mov_b32_e32 v39, v0
	v_mov_b32_e32 v48, v0
	v_mov_b32_e32 v49, v0
	v_mov_b32_e32 v50, v0
	v_mov_b32_e32 v51, v0
	v_mov_b32_e32 v52, v0
	v_mov_b32_e32 v53, v0
	v_mov_b32_e32 v54, v0
	v_mov_b32_e32 v55, v0
	v_mov_b32_e32 v8, v0
	v_mov_b32_e32 v9, v0
	v_mov_b32_e32 v10, v0
	v_mov_b32_e32 v11, v0
	v_mov_b32_e32 v12, v0
	v_mov_b32_e32 v13, v0
	v_mov_b32_e32 v14, v0
	v_mov_b32_e32 v15, v0
	v_mov_b32_e32 v24, v0
	v_mov_b32_e32 v25, v0
	v_mov_b32_e32 v26, v0
	v_mov_b32_e32 v27, v0
	v_mov_b32_e32 v28, v0
	v_mov_b32_e32 v29, v0
	v_mov_b32_e32 v30, v0
	v_mov_b32_e32 v31, v0
	v_mov_b32_e32 v40, v0
	v_mov_b32_e32 v41, v0
	v_mov_b32_e32 v42, v0
	v_mov_b32_e32 v43, v0
	v_mov_b32_e32 v44, v0
	v_mov_b32_e32 v45, v0
	v_mov_b32_e32 v46, v0
	v_mov_b32_e32 v47, v0
	v_mov_b32_e32 v56, v0
	v_mov_b32_e32 v57, v0
	v_mov_b32_e32 v58, v0
	v_mov_b32_e32 v59, v0
	v_mov_b32_e32 v60, v0
	v_mov_b32_e32 v61, v0
	v_mov_b32_e32 v62, v0
	v_mov_b32_e32 v63, v0
	v_mov_b32_e32 v64, v0
	v_mov_b32_e32 v65, v0
	v_mov_b32_e32 v66, v0
	v_mov_b32_e32 v67, v0
	v_mov_b32_e32 v68, v0
	v_mov_b32_e32 v69, v0
	v_mov_b32_e32 v70, v0
	v_mov_b32_e32 v71, v0
	v_mov_b32_e32 v80, v0
	v_mov_b32_e32 v81, v0
	v_mov_b32_e32 v82, v0
	v_mov_b32_e32 v83, v0
	v_mov_b32_e32 v84, v0
	v_mov_b32_e32 v85, v0
	v_mov_b32_e32 v86, v0
	v_mov_b32_e32 v87, v0
	v_mov_b32_e32 v96, v0
	v_mov_b32_e32 v97, v0
	v_mov_b32_e32 v98, v0
	v_mov_b32_e32 v99, v0
	v_mov_b32_e32 v100, v0
	v_mov_b32_e32 v101, v0
	v_mov_b32_e32 v102, v0
	v_mov_b32_e32 v103, v0
	v_mov_b32_e32 v112, v0
	v_mov_b32_e32 v113, v0
	v_mov_b32_e32 v114, v0
	v_mov_b32_e32 v115, v0
	v_mov_b32_e32 v116, v0
	v_mov_b32_e32 v117, v0
	v_mov_b32_e32 v118, v0
	v_mov_b32_e32 v119, v0
	v_mov_b32_e32 v72, v0
	v_mov_b32_e32 v73, v0
	v_mov_b32_e32 v74, v0
	v_mov_b32_e32 v75, v0
	v_mov_b32_e32 v76, v0
	v_mov_b32_e32 v77, v0
	v_mov_b32_e32 v78, v0
	v_mov_b32_e32 v79, v0
	v_mov_b32_e32 v88, v0
	v_mov_b32_e32 v89, v0
	v_mov_b32_e32 v90, v0
	v_mov_b32_e32 v91, v0
	v_mov_b32_e32 v92, v0
	v_mov_b32_e32 v93, v0
	v_mov_b32_e32 v94, v0
	v_mov_b32_e32 v95, v0
	v_mov_b32_e32 v104, v0
	v_mov_b32_e32 v105, v0
	v_mov_b32_e32 v106, v0
	v_mov_b32_e32 v107, v0
	v_mov_b32_e32 v108, v0
	v_mov_b32_e32 v109, v0
	v_mov_b32_e32 v110, v0
	v_mov_b32_e32 v111, v0
	v_mov_b32_e32 v120, v0
	v_mov_b32_e32 v121, v0
	v_mov_b32_e32 v122, v0
	v_mov_b32_e32 v123, v0
	v_mov_b32_e32 v124, v0
	v_mov_b32_e32 v125, v0
	v_mov_b32_e32 v126, v0
	v_mov_b32_e32 v127, v0
	s_bitcmp1_b32 s92, 8
	s_cbranch_scc0 .Lmy_ph_4
	s_barrier
.Lmy_ph_4:
.LBB0_1376:
	s_add_u32 s42, s10, 0x100
	ds_read_b128 v[132:135], v208
	ds_read_b128 v[136:139], v208 offset:1024
	ds_read_b128 v[140:143], v208 offset:2048
	ds_read_b128 v[144:147], v208 offset:3072
	s_addc_u32 s43, s11, 0
	s_add_u32 s80, s17, s10
	s_addc_u32 s81, s33, s11
	s_cmp_eq_u32 s77, 28
	s_cselect_b64 s[78:79], -1, 0
	s_and_b64 s[48:49], s[78:79], exec
	s_cselect_b32 s82, 0, s42
	s_cselect_b32 s49, s15, s81
	s_cselect_b32 s48, s18, s80
	v_lshl_add_u64 v[218:219], v[128:129], 0, s[10:11]
	s_add_i32 m0, s61, 0xc000
	ds_read_b128 v[148:151], v209
	ds_read_b128 v[152:155], v209 offset:1024
	ds_read_b128 v[156:159], v209 offset:2048
	ds_read_b128 v[192:195], v209 offset:3072
	ds_read_b128 v[196:199], v209 offset:4096
	ds_read_b128 v[200:203], v209 offset:5120
	ds_read_b128 v[204:207], v209 offset:6144
	ds_read_b128 v[214:217], v209 offset:7168
	global_load_lds_dwordx4 v[218:219], off
	v_lshl_add_u64 v[218:219], v[130:131], 0, s[10:11]
	s_add_i32 m0, s61, 0xe000
	s_nop 0
	global_load_lds_dwordx4 v[218:219], off
	s_waitcnt lgkmcnt(8)
	s_barrier
	s_waitcnt lgkmcnt(0)
	s_setprio 1
	s_waitcnt lgkmcnt(0)
	v_mfma_f32_16x16x32_bf16 v[124:127], v[132:135], v[148:151], v[124:127]
	v_mfma_f32_16x16x32_bf16 v[120:123], v[140:143], v[148:151], v[120:123]
	v_mfma_f32_16x16x32_bf16 v[108:111], v[132:135], v[156:159], v[108:111]
	v_mfma_f32_16x16x32_bf16 v[104:107], v[140:143], v[156:159], v[104:107]
	v_mfma_f32_16x16x32_bf16 v[92:95], v[132:135], v[196:199], v[92:95]
	v_mfma_f32_16x16x32_bf16 v[88:91], v[140:143], v[196:199], v[88:91]
	v_mfma_f32_16x16x32_bf16 v[76:79], v[132:135], v[204:207], v[76:79]
	v_mfma_f32_16x16x32_bf16 v[72:75], v[140:143], v[204:207], v[72:75]
	v_mfma_f32_16x16x32_bf16 v[124:127], v[136:139], v[152:155], v[124:127]
	v_mfma_f32_16x16x32_bf16 v[120:123], v[144:147], v[152:155], v[120:123]
	v_mfma_f32_16x16x32_bf16 v[108:111], v[136:139], v[192:195], v[108:111]
	v_mfma_f32_16x16x32_bf16 v[104:107], v[144:147], v[192:195], v[104:107]
	v_mfma_f32_16x16x32_bf16 v[92:95], v[136:139], v[200:203], v[92:95]
	v_mfma_f32_16x16x32_bf16 v[88:91], v[144:147], v[200:203], v[88:91]
	v_mfma_f32_16x16x32_bf16 v[76:79], v[136:139], v[214:217], v[76:79]
	v_mfma_f32_16x16x32_bf16 v[72:75], v[144:147], v[214:217], v[72:75]
	s_setprio 0
	s_barrier
; #define PG8_STAGE(bufoff, gbase, voff) do { _Pragma("unroll") for (int _i = 0; _i < 2; ++_i) \
;         __builtin_amdgcn_global_load_lds((const unsigned*)((const char*)(gbase) + (voff)[_i]), (LAS unsigned*)(lds + (bufoff) + ldsw + _i * 8192), 16, 0, 0); } while (0)
; #define PG8_LDA(dst, b, h) do { _Pragma("unroll") for (int m = 0; m < 4; ++m) _Pragma("unroll") for (int k = 0; k < 2; ++k) dst[m][k] = *(const LAS bf16x8*)(lds + PG8_SA(b, h) + aoff + m * 2048 + k * 1024); } while (0)
; #define PG8_LDB(dst, b, h) do { _Pragma("unroll") for (int n = 0; n < 2; ++n) _Pragma("unroll") for (int k = 0; k < 2; ++k) dst[n][k] = *(const LAS bf16x8*)(lds + PG8_SB(b, h) + boff + n * 2048 + k * 1024); } while (0)
; #define PG8_MMA(ai, bj, At, Bt) do { __builtin_amdgcn_s_setprio(1); _Pragma("unroll") for (int m = 0; m < 4; ++m) _Pragma("unroll") for (int n = 0; n < 2; ++n) _Pragma("unroll") for (int k = 0; k < 2; ++k) \
;         acc[ai][bj][m][n] = __builtin_amdgcn_mfma_f32_16x16x32_bf16(Bt[n][k], At[m][k], acc[ai][bj][m][n], 0, 0, 0); __builtin_amdgcn_s_setprio(0); } while (0)
; #define PG8_WAIT_V(n) asm volatile("s_waitcnt vmcnt(" #n ")" ::: "memory")
; #define PG8_WAIT_L(n) asm volatile("s_waitcnt lgkmcnt(" #n ")" ::: "memory")
; template <class Epi, class Sched>
; __device__ __forceinline__ void gemm_phase(LAS unsigned char* lds, const bf16_t* A, const int K, const Sched& S, const Epi& E, const int wv) {
;     ...
;             PG8_LDB(B1, 0, 1); PG8_STAGE(PG8_SB(0, 0), b2, voffB);
;             PG8_BAR; PG8_WAIT_L(0); PG8_MMA(0, 1, At, B1); PG8_BAR;
;             PG8_LDA(At, 0, 1); PG8_STAGE_A(PG8_SA(0, 0), 0, last, k2);
;             PG8_BAR; PG8_WAIT_L(0); PG8_MMA(1, 0, At, B0); PG8_BAR; PG8_SCHED;
;             PG8_STAGE(PG8_SB(0, 1), b2 + hstep, voffB);
;             PG8_WAIT_V(6); PG8_BAR; PG8_MMA(1, 1, At, B1); PG8_BAR;
;             PG8_LDB(B0, 1, 0); PG8_SCHED; PG8_LDA(At, 1, 0); PG8_STAGE_A(PG8_SA(0, 1), 1, last, k2);
;             PG8_WAIT_L(8); PG8_BAR; PG8_WAIT_L(0); PG8_MMA(0, 0, At, B0); PG8_BAR; PG8_SCHED;
;             PG8_LDB(B1, 1, 1); PG8_STAGE(PG8_SB(1, 0), b3, voffB);
;             PG8_BAR; PG8_WAIT_L(0); PG8_MMA(0, 1, At, B1); PG8_BAR;
;             PG8_LDA(At, 1, 1); PG8_STAGE_A(PG8_SA(1, 0), 0, last, k3);
;             PG8_BAR; PG8_WAIT_L(0); PG8_MMA(1, 0, At, B0); PG8_BAR; PG8_SCHED;
;             PG8_STAGE(PG8_SB(1, 1), b3 + hstep, voffB);
	s_add_i32 s10, s70, s60
	v_lshl_add_u64 v[234:235], s[48:49], 0, v[162:163]
	s_mov_b32 m0, s10
	ds_read_b128 v[218:221], v210
	ds_read_b128 v[222:225], v210 offset:1024
	ds_read_b128 v[226:229], v210 offset:2048
	ds_read_b128 v[230:233], v210 offset:3072
	global_load_lds_dwordx4 v[234:235], off
	v_lshl_add_u64 v[236:237], s[48:49], 0, v[166:167]
	s_add_i32 m0, s10, 0x2000
	s_nop 0
	global_load_lds_dwordx4 v[236:237], off
	s_barrier
	s_waitcnt lgkmcnt(0)
	s_setprio 1
	s_waitcnt lgkmcnt(0)
	v_mfma_f32_16x16x32_bf16 v[116:119], v[218:221], v[148:151], v[116:119]
	v_mfma_f32_16x16x32_bf16 v[112:115], v[226:229], v[148:151], v[112:115]
	v_mfma_f32_16x16x32_bf16 v[100:103], v[218:221], v[156:159], v[100:103]
	v_mfma_f32_16x16x32_bf16 v[96:99], v[226:229], v[156:159], v[96:99]
	v_mfma_f32_16x16x32_bf16 v[84:87], v[218:221], v[196:199], v[84:87]
	v_mfma_f32_16x16x32_bf16 v[80:83], v[226:229], v[196:199], v[80:83]
	v_mfma_f32_16x16x32_bf16 v[68:71], v[218:221], v[204:207], v[68:71]
	v_mfma_f32_16x16x32_bf16 v[64:67], v[226:229], v[204:207], v[64:67]
	v_mfma_f32_16x16x32_bf16 v[116:119], v[222:225], v[152:155], v[116:119]
	v_mfma_f32_16x16x32_bf16 v[112:115], v[230:233], v[152:155], v[112:115]
	v_mfma_f32_16x16x32_bf16 v[100:103], v[222:225], v[192:195], v[100:103]
	v_mfma_f32_16x16x32_bf16 v[96:99], v[230:233], v[192:195], v[96:99]
	v_mfma_f32_16x16x32_bf16 v[84:87], v[222:225], v[200:203], v[84:87]
	v_mfma_f32_16x16x32_bf16 v[80:83], v[230:233], v[200:203], v[80:83]
	v_mfma_f32_16x16x32_bf16 v[68:71], v[222:225], v[214:217], v[68:71]
	v_mfma_f32_16x16x32_bf16 v[64:67], v[230:233], v[214:217], v[64:67]
	s_setprio 0
	s_and_b64 s[10:11], s[8:9], s[78:79]
	s_and_b64 s[10:11], s[10:11], exec
	s_cselect_b32 s10, s28, s2
	s_cselect_b32 s11, s29, s3
	s_add_u32 s10, s10, s82
	s_addc_u32 s11, s11, 0
	s_mov_b32 m0, s61
	v_lshl_add_u64 v[238:239], s[10:11], 0, v[160:161]
	s_barrier
	ds_read_b128 v[148:151], v209 offset:16384
	ds_read_b128 v[152:155], v209 offset:17408
	ds_read_b128 v[156:159], v209 offset:18432
	ds_read_b128 v[192:195], v209 offset:19456
	ds_read_b128 v[196:199], v209 offset:20480
	ds_read_b128 v[200:203], v209 offset:21504
	ds_read_b128 v[204:207], v209 offset:22528
	ds_read_b128 v[214:217], v209 offset:23552
	global_load_lds_dwordx4 v[238:239], off
	v_lshl_add_u64 v[240:241], s[10:11], 0, v[164:165]
	s_mov_b32 m0, s62
	s_nop 0
	global_load_lds_dwordx4 v[240:241], off
	s_barrier
	s_waitcnt lgkmcnt(0)
	s_setprio 1
	s_waitcnt lgkmcnt(0)
	v_mfma_f32_16x16x32_bf16 v[60:63], v[132:135], v[148:151], v[60:63]
	v_mfma_f32_16x16x32_bf16 v[56:59], v[140:143], v[148:151], v[56:59]
	v_mfma_f32_16x16x32_bf16 v[44:47], v[132:135], v[156:159], v[44:47]
	v_mfma_f32_16x16x32_bf16 v[40:43], v[140:143], v[156:159], v[40:43]
	v_mfma_f32_16x16x32_bf16 v[28:31], v[132:135], v[196:199], v[28:31]
	v_mfma_f32_16x16x32_bf16 v[24:27], v[140:143], v[196:199], v[24:27]
	v_mfma_f32_16x16x32_bf16 v[12:15], v[132:135], v[204:207], v[12:15]
	v_mfma_f32_16x16x32_bf16 v[8:11], v[140:143], v[204:207], v[8:11]
	v_mfma_f32_16x16x32_bf16 v[60:63], v[136:139], v[152:155], v[60:63]
	v_mfma_f32_16x16x32_bf16 v[56:59], v[144:147], v[152:155], v[56:59]
	v_mfma_f32_16x16x32_bf16 v[44:47], v[136:139], v[192:195], v[44:47]
	v_mfma_f32_16x16x32_bf16 v[40:43], v[144:147], v[192:195], v[40:43]
	v_mfma_f32_16x16x32_bf16 v[28:31], v[136:139], v[200:203], v[28:31]
	v_mfma_f32_16x16x32_bf16 v[24:27], v[144:147], v[200:203], v[24:27]
	v_mfma_f32_16x16x32_bf16 v[12:15], v[136:139], v[214:217], v[12:15]
	v_mfma_f32_16x16x32_bf16 v[8:11], v[144:147], v[214:217], v[8:11]
	s_setprio 0
	s_barrier
	s_add_u32 s78, s48, 0x80000
	s_addc_u32 s79, s49, 0
	s_add_i32 s80, s71, s60
	v_lshl_add_u64 v[132:133], s[78:79], 0, v[162:163]
	s_mov_b32 m0, s80
	s_nop 0
	global_load_lds_dwordx4 v[132:133], off
	v_lshl_add_u64 v[132:133], s[78:79], 0, v[166:167]
	s_add_i32 m0, s80, 0x2000
	s_nop 0
	global_load_lds_dwordx4 v[132:133], off
	s_waitcnt vmcnt(6)
	s_barrier
	s_setprio 1
	v_mfma_f32_16x16x32_bf16 v[52:55], v[218:221], v[148:151], v[52:55]
	v_mfma_f32_16x16x32_bf16 v[48:51], v[226:229], v[148:151], v[48:51]
	v_mfma_f32_16x16x32_bf16 v[36:39], v[218:221], v[156:159], v[36:39]
	v_mfma_f32_16x16x32_bf16 v[32:35], v[226:229], v[156:159], v[32:35]
	v_mfma_f32_16x16x32_bf16 v[20:23], v[218:221], v[196:199], v[20:23]
	v_mfma_f32_16x16x32_bf16 v[16:19], v[226:229], v[196:199], v[16:19]
	v_mfma_f32_16x16x32_bf16 v[4:7], v[218:221], v[204:207], v[4:7]
	v_mfma_f32_16x16x32_bf16 v[0:3], v[226:229], v[204:207], v[0:3]
	v_mfma_f32_16x16x32_bf16 v[52:55], v[222:225], v[152:155], v[52:55]
	v_mfma_f32_16x16x32_bf16 v[48:51], v[230:233], v[152:155], v[48:51]
	v_mfma_f32_16x16x32_bf16 v[36:39], v[222:225], v[192:195], v[36:39]
	v_mfma_f32_16x16x32_bf16 v[32:35], v[230:233], v[192:195], v[32:35]
	v_mfma_f32_16x16x32_bf16 v[20:23], v[222:225], v[200:203], v[20:23]
	v_mfma_f32_16x16x32_bf16 v[16:19], v[230:233], v[200:203], v[16:19]
	v_mfma_f32_16x16x32_bf16 v[4:7], v[222:225], v[214:217], v[4:7]
	v_mfma_f32_16x16x32_bf16 v[0:3], v[230:233], v[214:217], v[0:3]
	s_setprio 0
	s_add_i32 s78, 0, 0x18000
	v_add_u32_e32 v144, s78, v173
	s_barrier
	ds_read_b128 v[132:135], v144
	ds_read_b128 v[136:139], v144 offset:1024
	ds_read_b128 v[140:143], v144 offset:2048
	ds_read_b128 v[144:147], v144 offset:3072
	s_add_u32 s10, s10, 0x80000
	s_addc_u32 s11, s11, 0
	s_mov_b32 m0, s63
	v_lshl_add_u64 v[218:219], s[10:11], 0, v[160:161]
	ds_read_b128 v[148:151], v209 offset:32768
	ds_read_b128 v[152:155], v209 offset:33792
	ds_read_b128 v[156:159], v209 offset:34816
	ds_read_b128 v[192:195], v209 offset:35840
	ds_read_b128 v[196:199], v209 offset:36864
	ds_read_b128 v[200:203], v209 offset:37888
	ds_read_b128 v[204:207], v209 offset:38912
	ds_read_b128 v[214:217], v209 offset:39936
	global_load_lds_dwordx4 v[218:219], off
	v_lshl_add_u64 v[218:219], s[10:11], 0, v[164:165]
	s_mov_b32 m0, s64
	s_nop 0
	global_load_lds_dwordx4 v[218:219], off
	s_waitcnt lgkmcnt(8)
	s_barrier
; #define PG8_STAGE(bufoff, gbase, voff) do { _Pragma("unroll") for (int _i = 0; _i < 2; ++_i) \
;         __builtin_amdgcn_global_load_lds((const unsigned*)((const char*)(gbase) + (voff)[_i]), (LAS unsigned*)(lds + (bufoff) + ldsw + _i * 8192), 16, 0, 0); } while (0)
; #define PG8_LDA(dst, b, h) do { _Pragma("unroll") for (int m = 0; m < 4; ++m) _Pragma("unroll") for (int k = 0; k < 2; ++k) dst[m][k] = *(const LAS bf16x8*)(lds + PG8_SA(b, h) + aoff + m * 2048 + k * 1024); } while (0)
; #define PG8_LDB(dst, b, h) do { _Pragma("unroll") for (int n = 0; n < 2; ++n) _Pragma("unroll") for (int k = 0; k < 2; ++k) dst[n][k] = *(const LAS bf16x8*)(lds + PG8_SB(b, h) + boff + n * 2048 + k * 1024); } while (0)
; #define PG8_WAIT_V(n) asm volatile("s_waitcnt vmcnt(" #n ")" ::: "memory")
; #define PG8_WAIT_L(n) asm volatile("s_waitcnt lgkmcnt(" #n ")" ::: "memory")
; #define PG8_BAR __builtin_amdgcn_s_barrier()
; template <class Epi, class Sched>
; __device__ __forceinline__ void gemm_phase(LAS unsigned char* lds, const bf16_t* A, const int K, const Sched& S, const Epi& E, const int wv) {
;     ...
;             PG8_LDB(B0, 0, 0); PG8_SCHED; PG8_LDA(At, 0, 0); PG8_STAGE_A(PG8_SA(1, 1), 1, false, k1);
;             PG8_WAIT_L(8); PG8_BAR; PG8_WAIT_L(0); PG8_MMA(0, 0, At, B0); PG8_BAR; PG8_SCHED;
;             PG8_LDB(B1, 0, 1); PG8_STAGE(PG8_SB(0, 0), b2, voffB);
;             PG8_BAR; PG8_WAIT_L(0); PG8_MMA(0, 1, At, B1); PG8_BAR;
;             PG8_LDA(At, 0, 1); PG8_STAGE_A(PG8_SA(0, 0), 0, last, k2);
;             PG8_BAR; PG8_WAIT_L(0); PG8_MMA(1, 0, At, B0); PG8_BAR; PG8_SCHED;
;             PG8_STAGE(PG8_SB(0, 1), b2 + hstep, voffB);
;             PG8_WAIT_V(6); PG8_BAR; PG8_MMA(1, 1, At, B1); PG8_BAR;
;             PG8_LDB(B0, 1, 0); PG8_SCHED; PG8_LDA(At, 1, 0); PG8_STAGE_A(PG8_SA(0, 1), 1, last, k2);
;             PG8_WAIT_L(8); PG8_BAR; PG8_WAIT_L(0); PG8_MMA(0, 0, At, B0); PG8_BAR; PG8_SCHED;
;             PG8_LDB(B1, 1, 1); PG8_STAGE(PG8_SB(1, 0), b3, voffB);
;             PG8_BAR; PG8_WAIT_L(0); PG8_MMA(0, 1, At, B1); PG8_BAR;
;             PG8_LDA(At, 1, 1); PG8_STAGE_A(PG8_SA(1, 0), 0, last, k3);
;             PG8_BAR; PG8_WAIT_L(0); PG8_MMA(1, 0, At, B0); PG8_BAR; PG8_SCHED;
;             PG8_STAGE(PG8_SB(1, 1), b3 + hstep, voffB);
;             PG8_WAIT_V(6); PG8_BAR; PG8_MMA(1, 1, At, B1); PG8_BAR;
;         }
	s_waitcnt lgkmcnt(0)
	s_setprio 1
	s_waitcnt lgkmcnt(0)
	v_mfma_f32_16x16x32_bf16 v[124:127], v[132:135], v[148:151], v[124:127]
	v_mfma_f32_16x16x32_bf16 v[120:123], v[140:143], v[148:151], v[120:123]
	v_mfma_f32_16x16x32_bf16 v[108:111], v[132:135], v[156:159], v[108:111]
	v_mfma_f32_16x16x32_bf16 v[104:107], v[140:143], v[156:159], v[104:107]
	v_mfma_f32_16x16x32_bf16 v[92:95], v[132:135], v[196:199], v[92:95]
	v_mfma_f32_16x16x32_bf16 v[88:91], v[140:143], v[196:199], v[88:91]
	v_mfma_f32_16x16x32_bf16 v[76:79], v[132:135], v[204:207], v[76:79]
	v_mfma_f32_16x16x32_bf16 v[72:75], v[140:143], v[204:207], v[72:75]
	v_mfma_f32_16x16x32_bf16 v[124:127], v[136:139], v[152:155], v[124:127]
	v_mfma_f32_16x16x32_bf16 v[120:123], v[144:147], v[152:155], v[120:123]
	v_mfma_f32_16x16x32_bf16 v[108:111], v[136:139], v[192:195], v[108:111]
	v_mfma_f32_16x16x32_bf16 v[104:107], v[144:147], v[192:195], v[104:107]
	v_mfma_f32_16x16x32_bf16 v[92:95], v[136:139], v[200:203], v[92:95]
	v_mfma_f32_16x16x32_bf16 v[88:91], v[144:147], v[200:203], v[88:91]
	v_mfma_f32_16x16x32_bf16 v[76:79], v[136:139], v[214:217], v[76:79]
	v_mfma_f32_16x16x32_bf16 v[72:75], v[144:147], v[214:217], v[72:75]
	s_setprio 0
	s_barrier
	s_add_i32 s79, 0, 0x1c000
	s_add_i32 s10, s78, s60
	v_add_u32_e32 v168, s79, v173
	v_lshl_add_u64 v[234:235], v[234:235], 0, s[26:27]
	s_mov_b32 m0, s10
	ds_read_b128 v[218:221], v168
	ds_read_b128 v[222:225], v168 offset:1024
	ds_read_b128 v[226:229], v168 offset:2048
	ds_read_b128 v[230:233], v168 offset:3072
	global_load_lds_dwordx4 v[234:235], off
	v_lshl_add_u64 v[234:235], v[236:237], 0, s[26:27]
	s_add_i32 m0, s10, 0x2000
	s_nop 0
	global_load_lds_dwordx4 v[234:235], off
	s_barrier
	s_waitcnt lgkmcnt(0)
	s_setprio 1
	s_waitcnt lgkmcnt(0)
	v_mfma_f32_16x16x32_bf16 v[116:119], v[218:221], v[148:151], v[116:119]
	v_mfma_f32_16x16x32_bf16 v[112:115], v[226:229], v[148:151], v[112:115]
	v_mfma_f32_16x16x32_bf16 v[100:103], v[218:221], v[156:159], v[100:103]
	v_mfma_f32_16x16x32_bf16 v[96:99], v[226:229], v[156:159], v[96:99]
	v_mfma_f32_16x16x32_bf16 v[84:87], v[218:221], v[196:199], v[84:87]
	v_mfma_f32_16x16x32_bf16 v[80:83], v[226:229], v[196:199], v[80:83]
	v_mfma_f32_16x16x32_bf16 v[68:71], v[218:221], v[204:207], v[68:71]
	v_mfma_f32_16x16x32_bf16 v[64:67], v[226:229], v[204:207], v[64:67]
	v_mfma_f32_16x16x32_bf16 v[116:119], v[222:225], v[152:155], v[116:119]
	v_mfma_f32_16x16x32_bf16 v[112:115], v[230:233], v[152:155], v[112:115]
	v_mfma_f32_16x16x32_bf16 v[100:103], v[222:225], v[192:195], v[100:103]
	v_mfma_f32_16x16x32_bf16 v[96:99], v[230:233], v[192:195], v[96:99]
	v_mfma_f32_16x16x32_bf16 v[84:87], v[222:225], v[200:203], v[84:87]
	v_mfma_f32_16x16x32_bf16 v[80:83], v[230:233], v[200:203], v[80:83]
	v_mfma_f32_16x16x32_bf16 v[68:71], v[222:225], v[214:217], v[68:71]
	v_mfma_f32_16x16x32_bf16 v[64:67], v[230:233], v[214:217], v[64:67]
	s_setprio 0
	s_mov_b32 m0, s66
	v_lshl_add_u64 v[234:235], v[238:239], 0, s[26:27]
	s_barrier
	ds_read_b128 v[148:151], v209 offset:49152
	ds_read_b128 v[152:155], v209 offset:50176
	ds_read_b128 v[156:159], v209 offset:51200
	ds_read_b128 v[192:195], v209 offset:52224
	ds_read_b128 v[196:199], v209 offset:53248
	ds_read_b128 v[200:203], v209 offset:54272
	ds_read_b128 v[204:207], v209 offset:55296
	ds_read_b128 v[214:217], v209 offset:56320
	global_load_lds_dwordx4 v[234:235], off
	v_lshl_add_u64 v[234:235], v[240:241], 0, s[26:27]
	s_mov_b32 m0, s67
	s_nop 0
	global_load_lds_dwordx4 v[234:235], off
	s_barrier
	s_waitcnt lgkmcnt(0)
	s_setprio 1
	s_waitcnt lgkmcnt(0)
	v_mfma_f32_16x16x32_bf16 v[60:63], v[132:135], v[148:151], v[60:63]
	v_mfma_f32_16x16x32_bf16 v[56:59], v[140:143], v[148:151], v[56:59]
	v_mfma_f32_16x16x32_bf16 v[44:47], v[132:135], v[156:159], v[44:47]
	v_mfma_f32_16x16x32_bf16 v[40:43], v[140:143], v[156:159], v[40:43]
	v_mfma_f32_16x16x32_bf16 v[28:31], v[132:135], v[196:199], v[28:31]
	v_mfma_f32_16x16x32_bf16 v[24:27], v[140:143], v[196:199], v[24:27]
	v_mfma_f32_16x16x32_bf16 v[12:15], v[132:135], v[204:207], v[12:15]
	v_mfma_f32_16x16x32_bf16 v[8:11], v[140:143], v[204:207], v[8:11]
	v_mfma_f32_16x16x32_bf16 v[60:63], v[136:139], v[152:155], v[60:63]
	v_mfma_f32_16x16x32_bf16 v[56:59], v[144:147], v[152:155], v[56:59]
	v_mfma_f32_16x16x32_bf16 v[44:47], v[136:139], v[192:195], v[44:47]
	v_mfma_f32_16x16x32_bf16 v[40:43], v[144:147], v[192:195], v[40:43]
	v_mfma_f32_16x16x32_bf16 v[28:31], v[136:139], v[200:203], v[28:31]
	v_mfma_f32_16x16x32_bf16 v[24:27], v[144:147], v[200:203], v[24:27]
	v_mfma_f32_16x16x32_bf16 v[12:15], v[136:139], v[214:217], v[12:15]
	v_mfma_f32_16x16x32_bf16 v[8:11], v[144:147], v[214:217], v[8:11]
	s_setprio 0
	s_barrier
	s_add_u32 s10, s48, 0x80080
	s_addc_u32 s11, s49, 0
	s_add_i32 s48, s79, s60
	v_lshl_add_u64 v[132:133], s[10:11], 0, v[162:163]
	s_mov_b32 m0, s48
	s_nop 0
	global_load_lds_dwordx4 v[132:133], off
	v_lshl_add_u64 v[132:133], s[10:11], 0, v[166:167]
	s_add_i32 m0, s48, 0x2000
	s_nop 0
	global_load_lds_dwordx4 v[132:133], off
	s_waitcnt vmcnt(6)
	s_barrier
	s_setprio 1
	v_mfma_f32_16x16x32_bf16 v[52:55], v[218:221], v[148:151], v[52:55]
	v_mfma_f32_16x16x32_bf16 v[48:51], v[226:229], v[148:151], v[48:51]
	v_mfma_f32_16x16x32_bf16 v[36:39], v[218:221], v[156:159], v[36:39]
	v_mfma_f32_16x16x32_bf16 v[32:35], v[226:229], v[156:159], v[32:35]
	v_mfma_f32_16x16x32_bf16 v[20:23], v[218:221], v[196:199], v[20:23]
	v_mfma_f32_16x16x32_bf16 v[16:19], v[226:229], v[196:199], v[16:19]
	v_mfma_f32_16x16x32_bf16 v[4:7], v[218:221], v[204:207], v[4:7]
	v_mfma_f32_16x16x32_bf16 v[0:3], v[226:229], v[204:207], v[0:3]
	v_mfma_f32_16x16x32_bf16 v[52:55], v[222:225], v[152:155], v[52:55]
	v_mfma_f32_16x16x32_bf16 v[48:51], v[230:233], v[152:155], v[48:51]
	v_mfma_f32_16x16x32_bf16 v[36:39], v[222:225], v[192:195], v[36:39]
	v_mfma_f32_16x16x32_bf16 v[32:35], v[230:233], v[192:195], v[32:35]
	v_mfma_f32_16x16x32_bf16 v[20:23], v[222:225], v[200:203], v[20:23]
	v_mfma_f32_16x16x32_bf16 v[16:19], v[230:233], v[200:203], v[16:19]
	v_mfma_f32_16x16x32_bf16 v[4:7], v[222:225], v[214:217], v[4:7]
	v_mfma_f32_16x16x32_bf16 v[0:3], v[230:233], v[214:217], v[0:3]
	s_setprio 0
	s_add_i32 s77, s77, 2
	s_cmp_gt_u32 s77, 29
	s_mov_b64 s[10:11], s[42:43]
	s_cbranch_scc1 .Lmy_kx_4
	s_barrier
	s_branch .LBB0_1376

; __device__ __forceinline__ unsigned cvt_pk_bf16(float lo, float hi) { const bf16x2_t r = __builtin_convertvector((f32x2_t){lo, hi}, bf16x2_t); return __builtin_bit_cast(unsigned, r); }
; __device__ __forceinline__ float silu_fast(float x) { return x * __builtin_amdgcn_rcpf(1.0f + __builtin_amdgcn_exp2f(-x * 1.4426950408889634f)); }
;     __device__ __forceinline__ void operator()(const f32x4 (&acc)[2][2][4][2], const Unit& u, int wr, int wc, int fr, int fq) const {
;     ...
;         } else {
;             const bool isog = u.pn >= 20;
;             size_t woff; int cb;
;             if (u.pn < 20) { woff = WS_VG; cb = (u.pn - 16) * 256; }
;             else { woff = WS_OG; cb = (u.pn - 20) * 256; }
;             bf16_t* dst = (bf16_t*)(ws + woff);
; #pragma unroll
;             for (int ai = 0; ai < 2; ++ai)
; #pragma unroll
;                 for (int m = 0; m < 4; ++m) {
;                     const int r = row0 + ai * HALF + m * 16;
; #pragma unroll
;                     for (int bj = 0; bj < 2; ++bj) {
;                         f32x4 v0 = acc[ai][bj][m][0], v1 = acc[ai][bj][m][1];
;                         if (isog) {
; #pragma unroll
;                             for (int i = 0; i < 4; ++i) { v0[i] = silu_fast(v0[i]); v1[i] = silu_fast(v1[i]); }
;                         }
;                         u32x4 o; o[0] = cvt_pk_bf16(v0[0], v0[1]); o[1] = cvt_pk_bf16(v0[2], v0[3]); o[2] = cvt_pk_bf16(v1[0], v1[1]); o[3] = cvt_pk_bf16(v1[2], v1[3]);
;                         __builtin_nontemporal_store(o, (u32x4*)(dst + ((size_t)((r >> 11) * 4 + (cb >> 8)) * SEQ + (r & (SEQ - 1))) * 256 + bj * HALF + lc));
.Lmy_kxb_4:
	s_lshl_b32 s15, s75, 8
	s_add_i32 s15, s15, s65
	v_or_b32_e32 v192, s15, v171
	s_cmp_gt_i32 s76, 7
	s_mov_b64 s[2:3], -1
	s_cbranch_scc0 .LBB0_1482
	s_cmp_gt_u32 s76, 11
	s_cbranch_scc0 .LBB0_1479
	s_cmp_gt_u32 s76, 15
	s_cbranch_scc0 .LBB0_1413
	s_cmp_gt_u32 s76, 19
	v_mov_b64_e32 v[130:131], v[126:127]
	v_mov_b64_e32 v[134:135], v[122:123]
	s_cselect_b64 s[2:3], -1, 0
	s_cmp_lt_u32 s76, 20
	v_mov_b64_e32 v[128:129], v[124:125]
	v_mov_b64_e32 v[132:133], v[120:121]
	s_cbranch_scc1 .LBB0_1382
	v_mul_f32_e32 v129, 0xbfb8aa3b, v120
	v_mul_f32_e32 v130, 0xbfb8aa3b, v125
	v_exp_f32_e32 v129, v129
	v_exp_f32_e32 v130, v130
	v_mul_f32_e32 v131, 0xbfb8aa3b, v126
	v_mul_f32_e32 v133, 0xbfb8aa3b, v122
	v_add_f32_e32 v129, 1.0, v129
	v_rcp_f32_e32 v132, v129
	v_add_f32_e32 v129, 1.0, v130
	v_mul_f32_e32 v130, 0xbfb8aa3b, v121
	v_exp_f32_e32 v130, v130
	v_exp_f32_e32 v131, v131
	v_exp_f32_e32 v133, v133
	v_mul_f32_e32 v128, 0xbfb8aa3b, v124
	v_add_f32_e32 v136, 1.0, v130
	v_add_f32_e32 v130, 1.0, v131
	v_add_f32_e32 v131, 1.0, v133
	v_mul_f32_e32 v133, 0xbfb8aa3b, v127
	v_mul_f32_e32 v134, 0xbfb8aa3b, v123
	v_exp_f32_e32 v128, v128
	v_exp_f32_e32 v133, v133
	v_exp_f32_e32 v135, v134
	v_rcp_f32_e32 v134, v131
	v_add_f32_e32 v128, 1.0, v128
	v_add_f32_e32 v131, 1.0, v133
	v_add_f32_e32 v133, 1.0, v135
	v_rcp_f32_e32 v128, v128
	v_rcp_f32_e32 v129, v129
	v_rcp_f32_e32 v130, v130
	v_rcp_f32_e32 v131, v131
	v_rcp_f32_e32 v135, v133
	v_rcp_f32_e32 v133, v136
	v_pk_mul_f32 v[128:129], v[124:125], v[128:129]
	v_pk_mul_f32 v[130:131], v[126:127], v[130:131]
	v_pk_mul_f32 v[134:135], v[122:123], v[134:135]
	v_pk_mul_f32 v[132:133], v[120:121], v[132:133]

; #define PG8_WAIT_V(n) asm volatile("s_waitcnt vmcnt(" #n ")" ::: "memory")
; #define PG8_BAR __builtin_amdgcn_s_barrier()
; template <class Epi, class Sched>
; __device__ __forceinline__ void gemm_phase(LAS unsigned char* lds, const bf16_t* A, const int K, const Sched& S, const Epi& E, const int wv) {
;     ...
;     PG8_WAIT_V(0);
;     if (wr == 0) PG8_BAR;
;     PG8_BAR;
.LBB0_1629:
	s_waitcnt vmcnt(0)
	s_cmpk_gt_u32 s35, 0xff
	s_cbranch_scc1 .LBB0_1631
.LBB0_1631:
	v_readlane_b32 s84, v252, 20
	v_readlane_b32 s76, v252, 28
	v_readlane_b32 s85, v252, 21
	v_readlane_b32 s86, v252, 22
	v_readlane_b32 s87, v252, 23
	v_readlane_b32 s88, v252, 24
	v_readlane_b32 s89, v252, 25
	v_readlane_b32 s90, v252, 26
	v_readlane_b32 s91, v252, 27
	v_readlane_b32 s77, v252, 29
	v_readlane_b32 s78, v252, 30
	v_readlane_b32 s79, v252, 31
	s_barrier

; #define PG8_BAR __builtin_amdgcn_s_barrier()
; template <class Epi, class Sched>
; __device__ __forceinline__ void gemm_phase(LAS unsigned char* lds, const bf16_t* A, const int K, const Sched& S, const Epi& E, const int wv) {
;     int tid = mk_tid(wv); asm volatile("" : "+v"(tid));
;     const int wid = __builtin_amdgcn_readfirstlane(tid >> 6), lane = tid & 63, wr = wid >> 2, wc = wid & 3, fr = lane & 15, fq = lane >> 4;
;     const int nt = K / BK;
;     unsigned voffA[2], voffB[2];
; #pragma unroll
;     for (int i = 0; i < 2; ++i) { int R, C; stage_rc(tid * 16 + i * 8192, R, C); const int Rb = Epi::PERM ? ((R & ~31) + perm32(R & 31)) : R;
;         voffA[i] = (unsigned)(R * K + C) * 2u; voffB[i] = (unsigned)(Rb * K + C) * 2u; }
;     const size_t kstep = (size_t)(BK * 2);
;     const size_t hstep = (size_t)HALF * K * 2;
;     const size_t tstep = 2 * hstep;
;     const unsigned ldsw = (unsigned)wid * 1024u;
;     const int aoff = lds_byte(wr * 64 + fr, fq * 8), boff = lds_byte(wc * 32 + fr, fq * 8);
;     Unit cur, nxt; int ui = 0;
;     if (!S.next(0, cur)) return;
;     f32x4 acc[2][2][4][2];
; #pragma unroll
;     for (int a_ = 0; a_ < 2; ++a_)
; #pragma unroll
;         for (int b_ = 0; b_ < 2; ++b_)
; #pragma unroll
;             for (int m = 0; m < 4; ++m)
; #pragma unroll
;                 for (int n = 0; n < 2; ++n) acc[a_][b_][m][n] = (f32x4){0.f, 0.f, 0.f, 0.f};
;     bf16x8 At[4][2], B0[2][2], B1[2][2];
;     unsigned ao0[2] = {0u, 0u}, ao1[2] = {0u, 0u}, no0[2] = {0u, 0u}, no1[2] = {0u, 0u};
;     const char* Ab = (const char*)A;
;     const char* cA = Ab; const char* nA = Ab;
;     if constexpr (Sched::GATHER) {
; #pragma unroll
;         for (int i = 0; i < 2; ++i) { int R, C; stage_rc(tid * 16 + i * 8192, R, C);
;             ao0[i] = (S.arow(cur, R) * (unsigned)K + (unsigned)C) * 2u; ao1[i] = (S.arow(cur, HALF + R) * (unsigned)K + (unsigned)C) * 2u; }
;     } else cA = Ab + (size_t)cur.pm * tstep;
;     const char* cB = S.bptr(cur);
;     PG8_STAGE(PG8_SB(0, 0), cB, voffB); PG8_STAGE_A(PG8_SA(0, 0), 0, false, 0); PG8_STAGE(PG8_SB(0, 1), cB + hstep, voffB); PG8_STAGE_A(PG8_SA(0, 1), 1, false, 0);
;     if (wr == 1) PG8_BAR;
;     PG8_WAIT_V(4); PG8_BAR;
;     PG8_STAGE(PG8_SB(1, 0), cB + kstep, voffB); PG8_STAGE_A(PG8_SA(1, 0), 0, false, kstep); PG8_STAGE(PG8_SB(1, 1), cB + hstep + kstep, voffB);
;     PG8_WAIT_V(6); PG8_BAR;
.LBB0_1895:
	v_ashrrev_i32_e32 v1, 31, v8
	v_lshrrev_b32_e32 v1, 26, v1
	v_add_u32_e32 v1, v8, v1
	v_ashrrev_i32_e32 v9, 6, v1
	v_bfe_i32 v1, v8, 27, 1
	v_lshlrev_b32_e32 v0, 4, v8
	v_lshrrev_b32_e32 v1, 22, v1
	v_add_u32_e32 v1, v0, v1
	v_and_b32_e32 v1, 0xfffffc00, v1
	v_sub_u32_e32 v1, v0, v1
	v_lshrrev_b32_e32 v2, 4, v1
	v_bitop3_b32 v1, v2, v1, 32 bitop3:0x6c
	s_waitcnt lgkmcnt(0)
	v_ashrrev_i32_e32 v3, 31, v1
	v_lshrrev_b32_e32 v3, 26, v3
	s_add_u32 s39, s76, 0x3988000
	v_add_u32_e32 v3, v1, v3
	s_addc_u32 s40, s77, 0
	v_ashrrev_i32_e32 v10, 6, v3
	v_and_b32_e32 v3, 0xc0, v3
	s_add_u32 s41, s76, 0x4e188000
	v_sub_u32_e32 v1, v1, v3
	v_mov_b32_e32 v3, 1
	s_addc_u32 s42, s77, 0
	v_lshlrev_b32_e32 v2, 3, v9
	v_lshlrev_b32_e32 v4, 5, v9
	v_ashrrev_i16_sdwa v1, v3, sext(v1) dst_sel:DWORD dst_unused:UNUSED_PAD src0_sel:DWORD src1_sel:BYTE_0
	s_add_i32 s0, s5, s0
	v_and_b32_e32 v2, 0xffff0, v2
	v_and_b32_e32 v4, 32, v4
	v_bfe_i32 v11, v1, 0, 16
	s_ashr_i32 s5, s0, 31
	v_add_u32_e32 v1, v4, v11
	v_add_lshl_u32 v2, v10, v2, 12
	v_add_u32_e32 v0, 0x2000, v0
	s_lshr_b32 s5, s5, 26
	v_lshl_add_u32 v144, v1, 1, v2
	v_ashrrev_i32_e32 v1, 31, v0
	s_add_i32 s5, s0, s5
	v_lshrrev_b32_e32 v1, 22, v1
	s_ashr_i32 s6, s5, 6
	s_and_b32 s5, s5, 0xffc0
	v_add_u32_e32 v1, v0, v1
	s_sub_i32 s5, s0, s5
	v_ashrrev_i32_e32 v12, 10, v1
	s_bfe_i32 s0, s5, 0x80000
	v_mul_i32_i24_e32 v1, 0x400, v12
	s_bfe_u32 s0, s0, 0x3000c
	v_sub_u32_e32 v0, v0, v1
	s_add_i32 s7, s5, s0
	v_lshrrev_b32_e32 v1, 4, v0
	s_bfe_i32 s0, s7, 0x80000
	s_and_b32 s7, s7, 0xf8
	v_bitop3_b32 v0, v1, v0, 32 bitop3:0x6c
	s_sub_i32 s5, s5, s7
	v_ashrrev_i32_e32 v2, 31, v0
	s_lshl_b32 s6, s6, 3
	s_sext_i32_i16 s0, s0
	s_sext_i32_i8 s5, s5
	s_ashr_i32 s1, s33, 8
	v_lshrrev_b32_e32 v2, 26, v2
	s_lshr_b32 s0, s0, 3
	s_add_i32 s26, s6, s5
	v_add_u32_e32 v2, v0, v2
	s_ashr_i32 s4, s33, 6
	s_ashr_i32 s27, s26, 31
	s_bfe_i64 s[8:9], s[0:1], 0x100000
	v_ashrrev_i32_e32 v13, 6, v2
	v_and_b32_e32 v2, 0xc0, v2
	s_lshl_b32 s43, s4, 10
	s_lshl_b64 s[6:7], s[26:27], 20
	s_lshl_b64 s[8:9], s[8:9], 20
	v_sub_u32_e32 v0, v0, v2
	s_add_u32 s30, s39, s8
	v_lshlrev_b32_e32 v1, 3, v12
	v_lshlrev_b32_e32 v4, 5, v12
	v_ashrrev_i16_sdwa v0, v3, sext(v0) dst_sel:DWORD dst_unused:UNUSED_PAD src0_sel:DWORD src1_sel:BYTE_0
	s_addc_u32 s31, s40, s9
	s_add_i32 s27, s43, 0
	v_and_b32_e32 v1, 0xffff0, v1
	v_and_b32_e32 v4, 32, v4
	v_bfe_i32 v14, v0, 0, 16
	s_add_i32 m0, s27, 0x10000
	v_add_u32_e32 v0, v4, v14
	v_add_lshl_u32 v1, v13, v1, 12
	global_load_lds_dwordx4 v144, s[30:31]
	s_add_i32 m0, s27, 0x12000
	v_lshl_add_u32 v146, v0, 1, v1
	s_add_u32 s28, s41, s6
	global_load_lds_dwordx4 v146, s[30:31]
	s_addc_u32 s29, s42, s7
	s_mov_b32 m0, s27
	s_add_i32 s44, s27, 0x2000
	global_load_lds_dwordx4 v144, s[28:29]
	s_mov_b32 m0, s44
	s_add_u32 s6, s30, 0x80000
	global_load_lds_dwordx4 v146, s[28:29]
	s_addc_u32 s7, s31, 0
	s_add_i32 m0, s27, 0x14000
	v_mov_b32_e32 v145, 0
	global_load_lds_dwordx4 v144, s[6:7]
	s_add_i32 m0, s27, 0x16000
	v_mov_b32_e32 v147, v145
	global_load_lds_dwordx4 v146, s[6:7]
	s_add_u32 s6, s28, 0x80000
	s_addc_u32 s7, s29, 0
	s_add_i32 s45, s27, 0x4000
	s_mov_b32 m0, s45
	s_add_i32 s46, s27, 0x6000
	global_load_lds_dwordx4 v144, s[6:7]
	s_mov_b32 m0, s46
	s_mov_b32 s47, 0
	global_load_lds_dwordx4 v146, s[6:7]
	v_lshl_add_u64 v[6:7], s[30:31], 0, v[144:145]
	v_lshl_add_u64 v[4:5], s[30:31], 0, v[146:147]
	v_lshl_add_u64 v[2:3], s[28:29], 0, v[144:145]
	s_cmp_lg_u32 s1, 1
	v_lshl_add_u64 v[0:1], s[28:29], 0, v[146:147]
	s_cbranch_scc1 .LBB0_1897
.LBB0_1897:
	s_add_u32 s6, s76, 0x34188000
	s_addc_u32 s7, s77, 0
	s_add_u32 s48, s76, 0x6c000
	s_addc_u32 s49, s77, 0
	s_lshl_b32 s4, s4, 5
	s_mov_b64 s[8:9], 0x80
	s_and_b32 s11, s4, 0x60
	s_add_i32 m0, s27, 0x18000
	v_lshl_add_u64 v[6:7], v[6:7], 0, s[8:9]
	s_lshl_b32 s10, s1, 13
	s_lshl_b32 s12, s11, 7
	s_waitcnt vmcnt(4)
	s_barrier
	global_load_lds_dwordx4 v[6:7], off
	v_lshl_add_u64 v[4:5], v[4:5], 0, s[8:9]
	s_add_i32 m0, s27, 0x1a000
	s_add_i32 s50, s27, 0x8000
	s_add_i32 s51, s27, 0xa000
	global_load_lds_dwordx4 v[4:5], off
	v_lshl_add_u64 v[2:3], v[2:3], 0, s[8:9]
	s_mov_b32 m0, s50
	s_add_u32 s4, s30, 0x80080
	global_load_lds_dwordx4 v[2:3], off
	v_lshl_add_u64 v[0:1], v[0:1], 0, s[8:9]
	s_mov_b32 m0, s51
	s_addc_u32 s5, s31, 0
	global_load_lds_dwordx4 v[0:1], off
	s_add_i32 m0, s27, 0x1c000
	v_lshl_add_u64 v[0:1], s[4:5], 0, v[144:145]
	global_load_lds_dwordx4 v[0:1], off
	v_lshl_add_u64 v[0:1], s[4:5], 0, v[146:147]
	s_add_i32 m0, s27, 0x1e000
	s_sext_i32_i8 s61, s0
	global_load_lds_dwordx4 v[0:1], off
	v_bfe_u32 v1, v8, 4, 2
	v_and_b32_e32 v0, 15, v8
	v_lshlrev_b32_e32 v2, 4, v1
	v_lshl_or_b32 v162, s1, 6, v0
	v_lshl_or_b32 v0, v0, 6, v2
	v_lshlrev_b32_e32 v2, 2, v8
	v_and_b32_e32 v2, 32, v2
	v_bitop3_b32 v3, v0, s10, v2 bitop3:0xde
	v_bitop3_b32 v163, v0, s12, v2 bitop3:0xde
	v_lshlrev_b32_e32 v0, 15, v9
	v_and_b32_e32 v0, 0xffff0000, v0
	v_lshl_or_b32 v164, v1, 2, s11
	v_lshl_add_u32 v0, v10, 12, v0
	v_and_b32_e32 v1, 1, v9
	v_lshl_or_b32 v0, v1, 6, v0
	s_mov_b64 s[0:1], 0x80080
	v_lshl_add_u32 v0, v11, 1, v0
	v_mov_b32_e32 v1, v145
	v_lshl_add_u64 v[148:149], v[0:1], 0, s[0:1]
	v_lshlrev_b32_e32 v0, 15, v12
	v_and_b32_e32 v0, 0xffff0000, v0
	v_lshl_add_u32 v0, v13, 12, v0
	v_and_b32_e32 v1, 1, v12
	s_waitcnt vmcnt(6)
	v_lshl_or_b32 v0, v1, 6, v0
	v_lshl_add_u32 v0, v14, 1, v0
	v_mov_b32_e32 v1, v145
	s_add_i32 s55, 0, 0x10000
	s_add_i32 s60, 0, 0x14000
	s_ashr_i32 s54, s93, 31
	v_lshl_add_u64 v[150:151], v[0:1], 0, s[0:1]
	v_mov_b64_e32 v[152:153], 0x200
	v_mov_b64_e32 v[154:155], 0x1ff
	v_add_u32_e32 v165, s55, v163
	v_add_u32_e32 v166, 0, v3
	v_add_u32_e32 v167, s60, v163
	s_mov_b64 s[10:11], 0x100000
	s_mov_b64 s[12:13], 0x120000
	s_mov_b64 s[14:15], 0x140000
	s_mov_b64 s[16:17], 0x160000
	s_barrier

; #define PG8_LDA(dst, b, h) do { _Pragma("unroll") for (int m = 0; m < 4; ++m) _Pragma("unroll") for (int k = 0; k < 2; ++k) dst[m][k] = *(const LAS bf16x8*)(lds + PG8_SA(b, h) + aoff + m * 2048 + k * 1024); } while (0)
; #define PG8_LDB(dst, b, h) do { _Pragma("unroll") for (int n = 0; n < 2; ++n) _Pragma("unroll") for (int k = 0; k < 2; ++k) dst[n][k] = *(const LAS bf16x8*)(lds + PG8_SB(b, h) + boff + n * 2048 + k * 1024); } while (0)
; #define PG8_MMA(ai, bj, At, Bt) do { __builtin_amdgcn_s_setprio(1); _Pragma("unroll") for (int m = 0; m < 4; ++m) _Pragma("unroll") for (int n = 0; n < 2; ++n) _Pragma("unroll") for (int k = 0; k < 2; ++k) \
;         acc[ai][bj][m][n] = __builtin_amdgcn_mfma_f32_16x16x32_bf16(Bt[n][k], At[m][k], acc[ai][bj][m][n], 0, 0, 0); __builtin_amdgcn_s_setprio(0); } while (0)
; #define PG8_WAIT_L(n) asm volatile("s_waitcnt lgkmcnt(" #n ")" ::: "memory")
; #define PG8_BAR __builtin_amdgcn_s_barrier()
; #define PG8_SCHED __builtin_amdgcn_sched_barrier(0)
; template <class Epi, class Sched>
; __device__ __forceinline__ void gemm_phase(LAS unsigned char* lds, const bf16_t* A, const int K, const Sched& S, const Epi& E, const int wv) {
;     ...
;         } else nA = has_next ? Ab + (size_t)nxt.pm * tstep : cA;
;         for (int t = 0; t < nt; t += 2) {
;             const bool last = (t == nt - 2);
;             const size_t k1 = (size_t)(t + 1) * kstep;
;             const size_t k2 = last ? 0 : (size_t)(t + 2) * kstep, k3 = k2 + kstep;
;             const char* b2 = last ? nB : cB + (size_t)(t + 2) * kstep; const char* b3 = b2 + kstep;
;             PG8_LDB(B0, 0, 0); PG8_SCHED; PG8_LDA(At, 0, 0); PG8_STAGE_A(PG8_SA(1, 1), 1, false, k1);
;             PG8_WAIT_L(8); PG8_BAR; PG8_WAIT_L(0); PG8_MMA(0, 0, At, B0); PG8_BAR; PG8_SCHED;
;     ...
; #pragma unroll
;         for (int a_ = 0; a_ < 2; ++a_)
; #pragma unroll
;             for (int b_ = 0; b_ < 2; ++b_)
; #pragma unroll
;                 for (int m = 0; m < 4; ++m)
; #pragma unroll
;                     for (int n = 0; n < 2; ++n) acc[a_][b_][m][n] = (f32x4){0.f, 0.f, 0.f, 0.f};
.LBB0_1904:
	s_ashr_i32 s19, s18, 31
	s_lshl_b64 s[22:23], s[18:19], 20
	s_add_u32 s22, s39, s22
	s_addc_u32 s23, s40, s23
	s_and_b64 s[24:25], s[4:5], exec
	s_cselect_b32 s19, s23, s31
	s_cselect_b32 s62, s22, s30
	s_ashr_i32 s21, s20, 31
	s_lshl_b64 s[24:25], s[20:21], 20
	s_add_u32 s24, s41, s24
	s_addc_u32 s25, s42, s25
	s_add_u32 s21, s30, 0x100
	v_mov_b32_e32 v0, 0
	s_addc_u32 s63, s31, 0
	v_lshl_add_u64 v[128:129], s[28:29], 0, v[148:149]
	v_lshl_add_u64 v[130:131], s[28:29], 0, v[150:151]
	s_mov_b32 s64, -2
	s_mov_b64 s[30:31], 0
	v_mov_b32_e32 v1, v0
	v_mov_b32_e32 v2, v0
	v_mov_b32_e32 v3, v0
	v_mov_b32_e32 v4, v0
	v_mov_b32_e32 v5, v0
	v_mov_b32_e32 v6, v0
	v_mov_b32_e32 v7, v0
	v_mov_b32_e32 v12, v0
	v_mov_b32_e32 v13, v0
	v_mov_b32_e32 v14, v0
	v_mov_b32_e32 v15, v0
	v_mov_b32_e32 v20, v0
	v_mov_b32_e32 v21, v0
	v_mov_b32_e32 v22, v0
	v_mov_b32_e32 v23, v0
	v_mov_b32_e32 v24, v0
	v_mov_b32_e32 v25, v0
	v_mov_b32_e32 v26, v0
	v_mov_b32_e32 v27, v0
	v_mov_b32_e32 v28, v0
	v_mov_b32_e32 v29, v0
	v_mov_b32_e32 v30, v0
	v_mov_b32_e32 v31, v0
	v_mov_b32_e32 v36, v0
	v_mov_b32_e32 v37, v0
	v_mov_b32_e32 v38, v0
	v_mov_b32_e32 v39, v0
	v_mov_b32_e32 v40, v0
	v_mov_b32_e32 v41, v0
	v_mov_b32_e32 v42, v0
	v_mov_b32_e32 v43, v0
	v_mov_b32_e32 v8, v0
	v_mov_b32_e32 v9, v0
	v_mov_b32_e32 v10, v0
	v_mov_b32_e32 v11, v0
	v_mov_b32_e32 v16, v0
	v_mov_b32_e32 v17, v0
	v_mov_b32_e32 v18, v0
	v_mov_b32_e32 v19, v0
	v_mov_b32_e32 v32, v0
	v_mov_b32_e32 v33, v0
	v_mov_b32_e32 v34, v0
	v_mov_b32_e32 v35, v0
	v_mov_b32_e32 v44, v0
	v_mov_b32_e32 v45, v0
	v_mov_b32_e32 v46, v0
	v_mov_b32_e32 v47, v0
	v_mov_b32_e32 v48, v0
	v_mov_b32_e32 v49, v0
	v_mov_b32_e32 v50, v0
	v_mov_b32_e32 v51, v0
	v_mov_b32_e32 v52, v0
	v_mov_b32_e32 v53, v0
	v_mov_b32_e32 v54, v0
	v_mov_b32_e32 v55, v0
	v_mov_b32_e32 v56, v0
	v_mov_b32_e32 v57, v0
	v_mov_b32_e32 v58, v0
	v_mov_b32_e32 v59, v0
	v_mov_b32_e32 v60, v0
	v_mov_b32_e32 v61, v0
	v_mov_b32_e32 v62, v0
	v_mov_b32_e32 v63, v0
	v_mov_b32_e32 v64, v0
	v_mov_b32_e32 v65, v0
	v_mov_b32_e32 v66, v0
	v_mov_b32_e32 v67, v0
	v_mov_b32_e32 v68, v0
	v_mov_b32_e32 v69, v0
	v_mov_b32_e32 v70, v0
	v_mov_b32_e32 v71, v0
	v_mov_b32_e32 v76, v0
	v_mov_b32_e32 v77, v0
	v_mov_b32_e32 v78, v0
	v_mov_b32_e32 v79, v0
	v_mov_b32_e32 v84, v0
	v_mov_b32_e32 v85, v0
	v_mov_b32_e32 v86, v0
	v_mov_b32_e32 v87, v0
	v_mov_b32_e32 v88, v0
	v_mov_b32_e32 v89, v0
	v_mov_b32_e32 v90, v0
	v_mov_b32_e32 v91, v0
	v_mov_b32_e32 v92, v0
	v_mov_b32_e32 v93, v0
	v_mov_b32_e32 v94, v0
	v_mov_b32_e32 v95, v0
	v_mov_b32_e32 v100, v0
	v_mov_b32_e32 v101, v0
	v_mov_b32_e32 v102, v0
	v_mov_b32_e32 v103, v0
	v_mov_b32_e32 v104, v0
	v_mov_b32_e32 v105, v0
	v_mov_b32_e32 v106, v0
	v_mov_b32_e32 v107, v0
	v_mov_b32_e32 v72, v0
	v_mov_b32_e32 v73, v0
	v_mov_b32_e32 v74, v0
	v_mov_b32_e32 v75, v0
	v_mov_b32_e32 v80, v0
	v_mov_b32_e32 v81, v0
	v_mov_b32_e32 v82, v0
	v_mov_b32_e32 v83, v0
	v_mov_b32_e32 v96, v0
	v_mov_b32_e32 v97, v0
	v_mov_b32_e32 v98, v0
	v_mov_b32_e32 v99, v0
	v_mov_b32_e32 v108, v0
	v_mov_b32_e32 v109, v0
	v_mov_b32_e32 v110, v0
	v_mov_b32_e32 v111, v0
	v_mov_b32_e32 v112, v0
	v_mov_b32_e32 v113, v0
	v_mov_b32_e32 v114, v0
	v_mov_b32_e32 v115, v0
	v_mov_b32_e32 v116, v0
	v_mov_b32_e32 v117, v0
	v_mov_b32_e32 v118, v0
	v_mov_b32_e32 v119, v0
	v_mov_b32_e32 v120, v0
	v_mov_b32_e32 v121, v0
	v_mov_b32_e32 v122, v0
	v_mov_b32_e32 v123, v0
	v_mov_b32_e32 v124, v0
	v_mov_b32_e32 v125, v0
	v_mov_b32_e32 v126, v0
	v_mov_b32_e32 v127, v0
	s_bitcmp1_b32 s92, 8
	s_cbranch_scc0 .Lmy_ph_5
	s_barrier
.Lmy_ph_5:
.LBB0_1905:
	s_add_u32 s34, s30, 0x100
	ds_read_b128 v[132:135], v165
	ds_read_b128 v[136:139], v165 offset:1024
	ds_read_b128 v[140:143], v165 offset:2048
	ds_read_b128 v[156:159], v165 offset:3072
	s_addc_u32 s35, s31, 0
	s_add_u32 s65, s21, s30
	s_addc_u32 s68, s63, s31
	s_cmp_eq_u32 s64, 28
	s_cselect_b64 s[66:67], -1, 0
	s_and_b64 s[36:37], s[66:67], exec
	s_cselect_b32 s69, 0, s34
	s_cselect_b32 s37, s19, s68
	s_cselect_b32 s36, s62, s65
	v_lshl_add_u64 v[160:161], v[128:129], 0, s[30:31]
	s_add_i32 m0, s27, 0xc000
	ds_read_b128 v[168:171], v166
	ds_read_b128 v[172:175], v166 offset:1024
	ds_read_b128 v[176:179], v166 offset:2048
	ds_read_b128 v[180:183], v166 offset:3072
	ds_read_b128 v[184:187], v166 offset:4096
	ds_read_b128 v[188:191], v166 offset:5120
	ds_read_b128 v[192:195], v166 offset:6144
	ds_read_b128 v[196:199], v166 offset:7168
	global_load_lds_dwordx4 v[160:161], off
	v_lshl_add_u64 v[160:161], v[130:131], 0, s[30:31]
	s_add_i32 m0, s27, 0xe000
	s_nop 0
	global_load_lds_dwordx4 v[160:161], off
	s_waitcnt lgkmcnt(8)
	s_barrier
	s_waitcnt lgkmcnt(0)
	s_setprio 1
	s_waitcnt lgkmcnt(0)
	v_mfma_f32_16x16x32_bf16 v[124:127], v[132:135], v[168:171], v[124:127]
	v_mfma_f32_16x16x32_bf16 v[120:123], v[140:143], v[168:171], v[120:123]
	v_mfma_f32_16x16x32_bf16 v[116:119], v[132:135], v[176:179], v[116:119]
	v_mfma_f32_16x16x32_bf16 v[112:115], v[140:143], v[176:179], v[112:115]
	v_mfma_f32_16x16x32_bf16 v[108:111], v[132:135], v[184:187], v[108:111]
	v_mfma_f32_16x16x32_bf16 v[96:99], v[140:143], v[184:187], v[96:99]
	v_mfma_f32_16x16x32_bf16 v[80:83], v[132:135], v[192:195], v[80:83]
	v_mfma_f32_16x16x32_bf16 v[72:75], v[140:143], v[192:195], v[72:75]
	v_mfma_f32_16x16x32_bf16 v[124:127], v[136:139], v[172:175], v[124:127]
	v_mfma_f32_16x16x32_bf16 v[120:123], v[156:159], v[172:175], v[120:123]
	v_mfma_f32_16x16x32_bf16 v[116:119], v[136:139], v[180:183], v[116:119]
	v_mfma_f32_16x16x32_bf16 v[112:115], v[156:159], v[180:183], v[112:115]
	v_mfma_f32_16x16x32_bf16 v[108:111], v[136:139], v[188:191], v[108:111]
	v_mfma_f32_16x16x32_bf16 v[96:99], v[156:159], v[188:191], v[96:99]
	v_mfma_f32_16x16x32_bf16 v[80:83], v[136:139], v[196:199], v[80:83]
	v_mfma_f32_16x16x32_bf16 v[72:75], v[156:159], v[196:199], v[72:75]
	s_setprio 0
	s_barrier
; #define PG8_STAGE(bufoff, gbase, voff) do { _Pragma("unroll") for (int _i = 0; _i < 2; ++_i) \
;         __builtin_amdgcn_global_load_lds((const unsigned*)((const char*)(gbase) + (voff)[_i]), (LAS unsigned*)(lds + (bufoff) + ldsw + _i * 8192), 16, 0, 0); } while (0)
; #define PG8_LDA(dst, b, h) do { _Pragma("unroll") for (int m = 0; m < 4; ++m) _Pragma("unroll") for (int k = 0; k < 2; ++k) dst[m][k] = *(const LAS bf16x8*)(lds + PG8_SA(b, h) + aoff + m * 2048 + k * 1024); } while (0)
; #define PG8_LDB(dst, b, h) do { _Pragma("unroll") for (int n = 0; n < 2; ++n) _Pragma("unroll") for (int k = 0; k < 2; ++k) dst[n][k] = *(const LAS bf16x8*)(lds + PG8_SB(b, h) + boff + n * 2048 + k * 1024); } while (0)
; #define PG8_MMA(ai, bj, At, Bt) do { __builtin_amdgcn_s_setprio(1); _Pragma("unroll") for (int m = 0; m < 4; ++m) _Pragma("unroll") for (int n = 0; n < 2; ++n) _Pragma("unroll") for (int k = 0; k < 2; ++k) \
;         acc[ai][bj][m][n] = __builtin_amdgcn_mfma_f32_16x16x32_bf16(Bt[n][k], At[m][k], acc[ai][bj][m][n], 0, 0, 0); __builtin_amdgcn_s_setprio(0); } while (0)
; #define PG8_WAIT_V(n) asm volatile("s_waitcnt vmcnt(" #n ")" ::: "memory")
; #define PG8_WAIT_L(n) asm volatile("s_waitcnt lgkmcnt(" #n ")" ::: "memory")
; #define PG8_BAR __builtin_amdgcn_s_barrier()
; #define PG8_SCHED __builtin_amdgcn_sched_barrier(0)
; template <class Epi, class Sched>
; __device__ __forceinline__ void gemm_phase(LAS unsigned char* lds, const bf16_t* A, const int K, const Sched& S, const Epi& E, const int wv) {
;     ...
;             PG8_LDB(B1, 0, 1); PG8_STAGE(PG8_SB(0, 0), b2, voffB);
;             PG8_BAR; PG8_WAIT_L(0); PG8_MMA(0, 1, At, B1); PG8_BAR;
;             PG8_LDA(At, 0, 1); PG8_STAGE_A(PG8_SA(0, 0), 0, last, k2);
;             PG8_BAR; PG8_WAIT_L(0); PG8_MMA(1, 0, At, B0); PG8_BAR; PG8_SCHED;
;             PG8_STAGE(PG8_SB(0, 1), b2 + hstep, voffB);
;             PG8_WAIT_V(6); PG8_BAR; PG8_MMA(1, 1, At, B1); PG8_BAR;
;             PG8_LDB(B0, 1, 0); PG8_SCHED; PG8_LDA(At, 1, 0); PG8_STAGE_A(PG8_SA(0, 1), 1, last, k2);
;             PG8_WAIT_L(8); PG8_BAR; PG8_WAIT_L(0); PG8_MMA(0, 0, At, B0); PG8_BAR; PG8_SCHED;
;             PG8_LDB(B1, 1, 1); PG8_STAGE(PG8_SB(1, 0), b3, voffB);
	s_add_i32 s30, s55, s43
	v_lshl_add_u64 v[160:161], s[36:37], 0, v[144:145]
	s_mov_b32 m0, s30
	ds_read_b128 v[200:203], v167
	ds_read_b128 v[204:207], v167 offset:1024
	ds_read_b128 v[208:211], v167 offset:2048
	ds_read_b128 v[212:215], v167 offset:3072
	global_load_lds_dwordx4 v[160:161], off
	v_lshl_add_u64 v[216:217], s[36:37], 0, v[146:147]
	s_add_i32 m0, s30, 0x2000
	s_nop 0
	global_load_lds_dwordx4 v[216:217], off
	s_barrier
	s_waitcnt lgkmcnt(0)
	s_setprio 1
	s_waitcnt lgkmcnt(0)
	v_mfma_f32_16x16x32_bf16 v[104:107], v[200:203], v[168:171], v[104:107]
	v_mfma_f32_16x16x32_bf16 v[100:103], v[208:211], v[168:171], v[100:103]
	v_mfma_f32_16x16x32_bf16 v[92:95], v[200:203], v[176:179], v[92:95]
	v_mfma_f32_16x16x32_bf16 v[88:91], v[208:211], v[176:179], v[88:91]
	v_mfma_f32_16x16x32_bf16 v[84:87], v[200:203], v[184:187], v[84:87]
	v_mfma_f32_16x16x32_bf16 v[76:79], v[208:211], v[184:187], v[76:79]
	v_mfma_f32_16x16x32_bf16 v[68:71], v[200:203], v[192:195], v[68:71]
	v_mfma_f32_16x16x32_bf16 v[64:67], v[208:211], v[192:195], v[64:67]
	v_mfma_f32_16x16x32_bf16 v[104:107], v[204:207], v[172:175], v[104:107]
	v_mfma_f32_16x16x32_bf16 v[100:103], v[212:215], v[172:175], v[100:103]
	v_mfma_f32_16x16x32_bf16 v[92:95], v[204:207], v[180:183], v[92:95]
	v_mfma_f32_16x16x32_bf16 v[88:91], v[212:215], v[180:183], v[88:91]
	v_mfma_f32_16x16x32_bf16 v[84:87], v[204:207], v[188:191], v[84:87]
	v_mfma_f32_16x16x32_bf16 v[76:79], v[212:215], v[188:191], v[76:79]
	v_mfma_f32_16x16x32_bf16 v[68:71], v[204:207], v[196:199], v[68:71]
	v_mfma_f32_16x16x32_bf16 v[64:67], v[212:215], v[196:199], v[64:67]
	s_setprio 0
	s_and_b64 s[30:31], s[4:5], s[66:67]
	s_and_b64 s[30:31], s[30:31], exec
	s_cselect_b32 s30, s24, s28
	s_cselect_b32 s31, s25, s29
	s_add_u32 s30, s30, s69
	s_addc_u32 s31, s31, 0
	s_mov_b32 m0, s27
	v_lshl_add_u64 v[218:219], s[30:31], 0, v[144:145]
	s_barrier
	ds_read_b128 v[168:171], v166 offset:16384
	ds_read_b128 v[172:175], v166 offset:17408
	ds_read_b128 v[176:179], v166 offset:18432
	ds_read_b128 v[180:183], v166 offset:19456
	ds_read_b128 v[184:187], v166 offset:20480
	ds_read_b128 v[188:191], v166 offset:21504
	ds_read_b128 v[192:195], v166 offset:22528
	ds_read_b128 v[196:199], v166 offset:23552
	global_load_lds_dwordx4 v[218:219], off
	v_lshl_add_u64 v[220:221], s[30:31], 0, v[146:147]
	s_mov_b32 m0, s44
	s_nop 0
	global_load_lds_dwordx4 v[220:221], off
	s_barrier
	s_waitcnt lgkmcnt(0)
	s_setprio 1
	s_waitcnt lgkmcnt(0)
	v_mfma_f32_16x16x32_bf16 v[60:63], v[132:135], v[168:171], v[60:63]
	v_mfma_f32_16x16x32_bf16 v[56:59], v[140:143], v[168:171], v[56:59]
	v_mfma_f32_16x16x32_bf16 v[52:55], v[132:135], v[176:179], v[52:55]
	v_mfma_f32_16x16x32_bf16 v[48:51], v[140:143], v[176:179], v[48:51]
	v_mfma_f32_16x16x32_bf16 v[44:47], v[132:135], v[184:187], v[44:47]
	v_mfma_f32_16x16x32_bf16 v[32:35], v[140:143], v[184:187], v[32:35]
	v_mfma_f32_16x16x32_bf16 v[16:19], v[132:135], v[192:195], v[16:19]
	v_mfma_f32_16x16x32_bf16 v[8:11], v[140:143], v[192:195], v[8:11]
	v_mfma_f32_16x16x32_bf16 v[60:63], v[136:139], v[172:175], v[60:63]
	v_mfma_f32_16x16x32_bf16 v[56:59], v[156:159], v[172:175], v[56:59]
	v_mfma_f32_16x16x32_bf16 v[52:55], v[136:139], v[180:183], v[52:55]
	v_mfma_f32_16x16x32_bf16 v[48:51], v[156:159], v[180:183], v[48:51]
	v_mfma_f32_16x16x32_bf16 v[44:47], v[136:139], v[188:191], v[44:47]
	v_mfma_f32_16x16x32_bf16 v[32:35], v[156:159], v[188:191], v[32:35]
	v_mfma_f32_16x16x32_bf16 v[16:19], v[136:139], v[196:199], v[16:19]
	v_mfma_f32_16x16x32_bf16 v[8:11], v[156:159], v[196:199], v[8:11]
	s_setprio 0
	s_barrier
	s_add_u32 s66, s36, 0x80000
	s_addc_u32 s67, s37, 0
	s_add_i32 s65, s60, s43
	v_lshl_add_u64 v[132:133], s[66:67], 0, v[144:145]
	s_mov_b32 m0, s65
	s_nop 0
	global_load_lds_dwordx4 v[132:133], off
	v_lshl_add_u64 v[132:133], s[66:67], 0, v[146:147]
	s_add_i32 m0, s65, 0x2000
	s_nop 0
	global_load_lds_dwordx4 v[132:133], off
	s_waitcnt vmcnt(6)
	s_barrier
	s_setprio 1
	v_mfma_f32_16x16x32_bf16 v[40:43], v[200:203], v[168:171], v[40:43]
	v_mfma_f32_16x16x32_bf16 v[36:39], v[208:211], v[168:171], v[36:39]
	v_mfma_f32_16x16x32_bf16 v[28:31], v[200:203], v[176:179], v[28:31]
	v_mfma_f32_16x16x32_bf16 v[24:27], v[208:211], v[176:179], v[24:27]
	v_mfma_f32_16x16x32_bf16 v[20:23], v[200:203], v[184:187], v[20:23]
	v_mfma_f32_16x16x32_bf16 v[12:15], v[208:211], v[184:187], v[12:15]
	v_mfma_f32_16x16x32_bf16 v[4:7], v[200:203], v[192:195], v[4:7]
	v_mfma_f32_16x16x32_bf16 v[0:3], v[208:211], v[192:195], v[0:3]
	v_mfma_f32_16x16x32_bf16 v[40:43], v[204:207], v[172:175], v[40:43]
	v_mfma_f32_16x16x32_bf16 v[36:39], v[212:215], v[172:175], v[36:39]
	v_mfma_f32_16x16x32_bf16 v[28:31], v[204:207], v[180:183], v[28:31]
	v_mfma_f32_16x16x32_bf16 v[24:27], v[212:215], v[180:183], v[24:27]
	v_mfma_f32_16x16x32_bf16 v[20:23], v[204:207], v[188:191], v[20:23]
	v_mfma_f32_16x16x32_bf16 v[12:15], v[212:215], v[188:191], v[12:15]
	v_mfma_f32_16x16x32_bf16 v[4:7], v[204:207], v[196:199], v[4:7]
	v_mfma_f32_16x16x32_bf16 v[0:3], v[212:215], v[196:199], v[0:3]
	s_setprio 0
	s_add_i32 s65, 0, 0x18000
	v_add_u32_e32 v156, s65, v163
	s_barrier
	ds_read_b128 v[132:135], v156
	ds_read_b128 v[136:139], v156 offset:1024
	ds_read_b128 v[140:143], v156 offset:2048
	ds_read_b128 v[156:159], v156 offset:3072
	s_add_u32 s30, s30, 0x80000
	s_addc_u32 s31, s31, 0
	s_mov_b32 m0, s45
	v_lshl_add_u64 v[200:201], s[30:31], 0, v[144:145]
	ds_read_b128 v[168:171], v166 offset:32768
	ds_read_b128 v[172:175], v166 offset:33792
	ds_read_b128 v[176:179], v166 offset:34816
	ds_read_b128 v[180:183], v166 offset:35840
	ds_read_b128 v[184:187], v166 offset:36864
	ds_read_b128 v[188:191], v166 offset:37888
	ds_read_b128 v[192:195], v166 offset:38912
	ds_read_b128 v[196:199], v166 offset:39936
	global_load_lds_dwordx4 v[200:201], off
	v_lshl_add_u64 v[200:201], s[30:31], 0, v[146:147]
	s_mov_b32 m0, s46
	s_nop 0
	global_load_lds_dwordx4 v[200:201], off
	s_waitcnt lgkmcnt(8)
	s_barrier
; #define PG8_STAGE(bufoff, gbase, voff) do { _Pragma("unroll") for (int _i = 0; _i < 2; ++_i) \
;         __builtin_amdgcn_global_load_lds((const unsigned*)((const char*)(gbase) + (voff)[_i]), (LAS unsigned*)(lds + (bufoff) + ldsw + _i * 8192), 16, 0, 0); } while (0)
; #define PG8_LDA(dst, b, h) do { _Pragma("unroll") for (int m = 0; m < 4; ++m) _Pragma("unroll") for (int k = 0; k < 2; ++k) dst[m][k] = *(const LAS bf16x8*)(lds + PG8_SA(b, h) + aoff + m * 2048 + k * 1024); } while (0)
; #define PG8_LDB(dst, b, h) do { _Pragma("unroll") for (int n = 0; n < 2; ++n) _Pragma("unroll") for (int k = 0; k < 2; ++k) dst[n][k] = *(const LAS bf16x8*)(lds + PG8_SB(b, h) + boff + n * 2048 + k * 1024); } while (0)
; #define PG8_MMA(ai, bj, At, Bt) do { __builtin_amdgcn_s_setprio(1); _Pragma("unroll") for (int m = 0; m < 4; ++m) _Pragma("unroll") for (int n = 0; n < 2; ++n) _Pragma("unroll") for (int k = 0; k < 2; ++k) \
;         acc[ai][bj][m][n] = __builtin_amdgcn_mfma_f32_16x16x32_bf16(Bt[n][k], At[m][k], acc[ai][bj][m][n], 0, 0, 0); __builtin_amdgcn_s_setprio(0); } while (0)
; #define PG8_WAIT_V(n) asm volatile("s_waitcnt vmcnt(" #n ")" ::: "memory")
; #define PG8_WAIT_L(n) asm volatile("s_waitcnt lgkmcnt(" #n ")" ::: "memory")
; #define PG8_BAR __builtin_amdgcn_s_barrier()
; #define PG8_SCHED __builtin_amdgcn_sched_barrier(0)
; template <class Epi, class Sched>
; __device__ __forceinline__ void gemm_phase(LAS unsigned char* lds, const bf16_t* A, const int K, const Sched& S, const Epi& E, const int wv) {
;     ...
;             PG8_LDB(B0, 1, 0); PG8_SCHED; PG8_LDA(At, 1, 0); PG8_STAGE_A(PG8_SA(0, 1), 1, last, k2);
;             PG8_WAIT_L(8); PG8_BAR; PG8_WAIT_L(0); PG8_MMA(0, 0, At, B0); PG8_BAR; PG8_SCHED;
;             PG8_LDB(B1, 1, 1); PG8_STAGE(PG8_SB(1, 0), b3, voffB);
;             PG8_BAR; PG8_WAIT_L(0); PG8_MMA(0, 1, At, B1); PG8_BAR;
;             PG8_LDA(At, 1, 1); PG8_STAGE_A(PG8_SA(1, 0), 0, last, k3);
;             PG8_BAR; PG8_WAIT_L(0); PG8_MMA(1, 0, At, B0); PG8_BAR; PG8_SCHED;
;             PG8_STAGE(PG8_SB(1, 1), b3 + hstep, voffB);
;             PG8_WAIT_V(6); PG8_BAR; PG8_MMA(1, 1, At, B1); PG8_BAR;
;         }
	s_waitcnt lgkmcnt(0)
	s_setprio 1
	s_waitcnt lgkmcnt(0)
	v_mfma_f32_16x16x32_bf16 v[124:127], v[132:135], v[168:171], v[124:127]
	v_mfma_f32_16x16x32_bf16 v[120:123], v[140:143], v[168:171], v[120:123]
	v_mfma_f32_16x16x32_bf16 v[116:119], v[132:135], v[176:179], v[116:119]
	v_mfma_f32_16x16x32_bf16 v[112:115], v[140:143], v[176:179], v[112:115]
	v_mfma_f32_16x16x32_bf16 v[108:111], v[132:135], v[184:187], v[108:111]
	v_mfma_f32_16x16x32_bf16 v[96:99], v[140:143], v[184:187], v[96:99]
	v_mfma_f32_16x16x32_bf16 v[80:83], v[132:135], v[192:195], v[80:83]
	v_mfma_f32_16x16x32_bf16 v[72:75], v[140:143], v[192:195], v[72:75]
	v_mfma_f32_16x16x32_bf16 v[124:127], v[136:139], v[172:175], v[124:127]
	v_mfma_f32_16x16x32_bf16 v[120:123], v[156:159], v[172:175], v[120:123]
	v_mfma_f32_16x16x32_bf16 v[116:119], v[136:139], v[180:183], v[116:119]
	v_mfma_f32_16x16x32_bf16 v[112:115], v[156:159], v[180:183], v[112:115]
	v_mfma_f32_16x16x32_bf16 v[108:111], v[136:139], v[188:191], v[108:111]
	v_mfma_f32_16x16x32_bf16 v[96:99], v[156:159], v[188:191], v[96:99]
	v_mfma_f32_16x16x32_bf16 v[80:83], v[136:139], v[196:199], v[80:83]
	v_mfma_f32_16x16x32_bf16 v[72:75], v[156:159], v[196:199], v[72:75]
	s_setprio 0
	s_barrier
	s_add_i32 s66, 0, 0x1c000
	s_add_i32 s30, s65, s43
	v_add_u32_e32 v212, s66, v163
	v_lshl_add_u64 v[160:161], v[160:161], 0, s[8:9]
	s_mov_b32 m0, s30
	ds_read_b128 v[200:203], v212
	ds_read_b128 v[204:207], v212 offset:1024
	ds_read_b128 v[208:211], v212 offset:2048
	ds_read_b128 v[212:215], v212 offset:3072
	global_load_lds_dwordx4 v[160:161], off
	v_lshl_add_u64 v[160:161], v[216:217], 0, s[8:9]
	s_add_i32 m0, s30, 0x2000
	s_nop 0
	global_load_lds_dwordx4 v[160:161], off
	s_barrier
	s_waitcnt lgkmcnt(0)
	s_setprio 1
	s_waitcnt lgkmcnt(0)
	v_mfma_f32_16x16x32_bf16 v[104:107], v[200:203], v[168:171], v[104:107]
	v_mfma_f32_16x16x32_bf16 v[100:103], v[208:211], v[168:171], v[100:103]
	v_mfma_f32_16x16x32_bf16 v[92:95], v[200:203], v[176:179], v[92:95]
	v_mfma_f32_16x16x32_bf16 v[88:91], v[208:211], v[176:179], v[88:91]
	v_mfma_f32_16x16x32_bf16 v[84:87], v[200:203], v[184:187], v[84:87]
	v_mfma_f32_16x16x32_bf16 v[76:79], v[208:211], v[184:187], v[76:79]
	v_mfma_f32_16x16x32_bf16 v[68:71], v[200:203], v[192:195], v[68:71]
	v_mfma_f32_16x16x32_bf16 v[64:67], v[208:211], v[192:195], v[64:67]
	v_mfma_f32_16x16x32_bf16 v[104:107], v[204:207], v[172:175], v[104:107]
	v_mfma_f32_16x16x32_bf16 v[100:103], v[212:215], v[172:175], v[100:103]
	v_mfma_f32_16x16x32_bf16 v[92:95], v[204:207], v[180:183], v[92:95]
	v_mfma_f32_16x16x32_bf16 v[88:91], v[212:215], v[180:183], v[88:91]
	v_mfma_f32_16x16x32_bf16 v[84:87], v[204:207], v[188:191], v[84:87]
	v_mfma_f32_16x16x32_bf16 v[76:79], v[212:215], v[188:191], v[76:79]
	v_mfma_f32_16x16x32_bf16 v[68:71], v[204:207], v[196:199], v[68:71]
	v_mfma_f32_16x16x32_bf16 v[64:67], v[212:215], v[196:199], v[64:67]
	s_setprio 0
	s_mov_b32 m0, s50
	v_lshl_add_u64 v[160:161], v[218:219], 0, s[8:9]
	s_barrier
	ds_read_b128 v[168:171], v166 offset:49152
	ds_read_b128 v[172:175], v166 offset:50176
	ds_read_b128 v[176:179], v166 offset:51200
	ds_read_b128 v[180:183], v166 offset:52224
	ds_read_b128 v[184:187], v166 offset:53248
	ds_read_b128 v[188:191], v166 offset:54272
	ds_read_b128 v[192:195], v166 offset:55296
	ds_read_b128 v[196:199], v166 offset:56320
	global_load_lds_dwordx4 v[160:161], off
	v_lshl_add_u64 v[160:161], v[220:221], 0, s[8:9]
	s_mov_b32 m0, s51
	s_nop 0
	global_load_lds_dwordx4 v[160:161], off
	s_barrier
	s_waitcnt lgkmcnt(0)
	s_setprio 1
	s_waitcnt lgkmcnt(0)
	v_mfma_f32_16x16x32_bf16 v[60:63], v[132:135], v[168:171], v[60:63]
	v_mfma_f32_16x16x32_bf16 v[56:59], v[140:143], v[168:171], v[56:59]
	v_mfma_f32_16x16x32_bf16 v[52:55], v[132:135], v[176:179], v[52:55]
	v_mfma_f32_16x16x32_bf16 v[48:51], v[140:143], v[176:179], v[48:51]
	v_mfma_f32_16x16x32_bf16 v[44:47], v[132:135], v[184:187], v[44:47]
	v_mfma_f32_16x16x32_bf16 v[32:35], v[140:143], v[184:187], v[32:35]
	v_mfma_f32_16x16x32_bf16 v[16:19], v[132:135], v[192:195], v[16:19]
	v_mfma_f32_16x16x32_bf16 v[8:11], v[140:143], v[192:195], v[8:11]
	v_mfma_f32_16x16x32_bf16 v[60:63], v[136:139], v[172:175], v[60:63]
	v_mfma_f32_16x16x32_bf16 v[56:59], v[156:159], v[172:175], v[56:59]
	v_mfma_f32_16x16x32_bf16 v[52:55], v[136:139], v[180:183], v[52:55]
	v_mfma_f32_16x16x32_bf16 v[48:51], v[156:159], v[180:183], v[48:51]
	v_mfma_f32_16x16x32_bf16 v[44:47], v[136:139], v[188:191], v[44:47]
	v_mfma_f32_16x16x32_bf16 v[32:35], v[156:159], v[188:191], v[32:35]
	v_mfma_f32_16x16x32_bf16 v[16:19], v[136:139], v[196:199], v[16:19]
	v_mfma_f32_16x16x32_bf16 v[8:11], v[156:159], v[196:199], v[8:11]
	s_setprio 0
	s_barrier
	s_add_u32 s30, s36, 0x80080
	s_addc_u32 s31, s37, 0
	s_add_i32 s36, s66, s43
	v_lshl_add_u64 v[132:133], s[30:31], 0, v[144:145]
	s_mov_b32 m0, s36
	s_nop 0
	global_load_lds_dwordx4 v[132:133], off
	v_lshl_add_u64 v[132:133], s[30:31], 0, v[146:147]
	s_add_i32 m0, s36, 0x2000
	s_nop 0
	global_load_lds_dwordx4 v[132:133], off
	s_waitcnt vmcnt(6)
	s_barrier
	s_setprio 1
	v_mfma_f32_16x16x32_bf16 v[40:43], v[200:203], v[168:171], v[40:43]
	v_mfma_f32_16x16x32_bf16 v[36:39], v[208:211], v[168:171], v[36:39]
	v_mfma_f32_16x16x32_bf16 v[28:31], v[200:203], v[176:179], v[28:31]
	v_mfma_f32_16x16x32_bf16 v[24:27], v[208:211], v[176:179], v[24:27]
	v_mfma_f32_16x16x32_bf16 v[20:23], v[200:203], v[184:187], v[20:23]
	v_mfma_f32_16x16x32_bf16 v[12:15], v[208:211], v[184:187], v[12:15]
	v_mfma_f32_16x16x32_bf16 v[4:7], v[200:203], v[192:195], v[4:7]
	v_mfma_f32_16x16x32_bf16 v[0:3], v[208:211], v[192:195], v[0:3]
	v_mfma_f32_16x16x32_bf16 v[40:43], v[204:207], v[172:175], v[40:43]
	v_mfma_f32_16x16x32_bf16 v[36:39], v[212:215], v[172:175], v[36:39]
	v_mfma_f32_16x16x32_bf16 v[28:31], v[204:207], v[180:183], v[28:31]
	v_mfma_f32_16x16x32_bf16 v[24:27], v[212:215], v[180:183], v[24:27]
	v_mfma_f32_16x16x32_bf16 v[20:23], v[204:207], v[188:191], v[20:23]
	v_mfma_f32_16x16x32_bf16 v[12:15], v[212:215], v[188:191], v[12:15]
	v_mfma_f32_16x16x32_bf16 v[4:7], v[204:207], v[196:199], v[4:7]
	v_mfma_f32_16x16x32_bf16 v[0:3], v[212:215], v[196:199], v[0:3]
	s_setprio 0
	s_add_i32 s64, s64, 2
	s_cmp_gt_u32 s64, 29
	s_mov_b64 s[30:31], s[34:35]
	s_cbranch_scc1 .Lmy_kx_5
	s_barrier
	s_branch .LBB0_1905

;     __device__ __forceinline__ void operator()(const f32x4 (&acc)[2][2][4][2], const Unit& u, int wr, int wc, int fr, int fq) const {
;         const int row0 = u.pm * BM + wr * 64 + fr, col0 = u.pn * BM + wc * 32 + 4 * fq;
;         const int b = u.pm >> 3;
;         f32x4 gv[2][2];
; #pragma unroll
;         for (int bj = 0; bj < 2; ++bj)
; #pragma unroll
;             for (int n = 0; n < 2; ++n) gv[bj][n] = *(const f32x4*)(gate + (size_t)b * (6 * DM) + col0 + bj * HALF + n * 16);
; #pragma unroll
;         for (int ai = 0; ai < 2; ++ai) {
;             f32x4 rv[4][2][2];
; #pragma unroll
;             for (int m = 0; m < 4; ++m) { const size_t off = (size_t)(row0 + ai * HALF + m * 16) * DM + col0;
; #pragma unroll
;                 for (int bj = 0; bj < 2; ++bj)
; #pragma unroll
;                     for (int n = 0; n < 2; ++n) rv[m][bj][n] = *(const f32x4*)(res + off + bj * HALF + n * 16); }
; #pragma unroll
;             for (int m = 0; m < 4; ++m) { const size_t off = (size_t)(row0 + ai * HALF + m * 16) * DM + col0;
; #pragma unroll
;                 for (int bj = 0; bj < 2; ++bj)
; #pragma unroll
;                     for (int n = 0; n < 2; ++n) *(f32x4*)(out + off + bj * HALF + n * 16) = rv[m][bj][n] + gv[bj][n] * acc[ai][bj][m][n]; }
.Lmy_kxb_5:
	v_lshl_or_b32 v128, s61, 8, v164
	s_ashr_i32 s4, s26, 3
	v_lshl_add_u32 v216, s26, 8, v162
	s_mul_hi_i32 s5, s4, 0xc000
	s_mul_i32 s4, s4, 0xc000
	v_ashrrev_i32_e32 v129, 31, v128
	v_or_b32_e32 v184, 16, v216
	v_or_b32_e32 v200, 32, v216
	s_add_u32 s4, s48, s4
	v_lshlrev_b64 v[156:157], 2, v[128:129]
	v_ashrrev_i32_e32 v217, 31, v216
	v_ashrrev_i32_e32 v185, 31, v184
	v_ashrrev_i32_e32 v201, 31, v200
	s_addc_u32 s5, s49, s5
	v_lshl_add_u64 v[158:159], s[6:7], 0, v[156:157]
	v_lshlrev_b64 v[160:161], 13, v[216:217]
	v_lshlrev_b64 v[232:233], 13, v[184:185]
	v_lshlrev_b64 v[234:235], 13, v[200:201]
	v_or_b32_e32 v216, 48, v216
	v_lshl_add_u64 v[128:129], s[4:5], 0, v[156:157]
	v_lshl_add_u64 v[180:181], v[158:159], 0, v[160:161]
	v_lshl_add_u64 v[196:197], v[158:159], 0, v[232:233]
	v_lshl_add_u64 v[212:213], v[158:159], 0, v[234:235]
	v_ashrrev_i32_e32 v217, 31, v216
	global_load_dwordx4 v[140:143], v[128:129], off
	global_load_dwordx4 v[136:139], v[128:129], off offset:64
	global_load_dwordx4 v[132:135], v[128:129], off offset:512
	s_nop 0
	global_load_dwordx4 v[128:131], v[128:129], off offset:576
	s_nop 0
	global_load_dwordx4 v[168:171], v[180:181], off
	global_load_dwordx4 v[172:175], v[180:181], off offset:64
	global_load_dwordx4 v[176:179], v[180:181], off offset:512
	s_nop 0
	global_load_dwordx4 v[180:183], v[180:181], off offset:576
	s_nop 0
	global_load_dwordx4 v[184:187], v[196:197], off
	global_load_dwordx4 v[188:191], v[196:197], off offset:64
	global_load_dwordx4 v[192:195], v[196:197], off offset:512
	s_nop 0
	global_load_dwordx4 v[196:199], v[196:197], off offset:576
	s_nop 0
	global_load_dwordx4 v[200:203], v[212:213], off
	global_load_dwordx4 v[204:207], v[212:213], off offset:64
	global_load_dwordx4 v[208:211], v[212:213], off offset:512
	s_nop 0
	global_load_dwordx4 v[212:215], v[212:213], off offset:576
	v_lshlrev_b64 v[236:237], 13, v[216:217]
	v_lshl_add_u64 v[228:229], v[158:159], 0, v[236:237]
	global_load_dwordx4 v[216:219], v[228:229], off
	global_load_dwordx4 v[220:223], v[228:229], off offset:64
	global_load_dwordx4 v[224:227], v[228:229], off offset:512
	s_nop 0
	global_load_dwordx4 v[228:231], v[228:229], off offset:576
	v_lshl_add_u64 v[238:239], s[6:7], 0, v[160:161]
	v_lshl_add_u64 v[238:239], v[238:239], 0, v[156:157]
	v_lshl_add_u64 v[232:233], s[6:7], 0, v[232:233]
	v_lshl_add_u64 v[234:235], s[6:7], 0, v[234:235]
	v_lshl_add_u64 v[232:233], v[232:233], 0, v[156:157]
	v_lshl_add_u64 v[234:235], v[234:235], 0, v[156:157]
	s_and_b64 vcc, exec, s[0:1]
	s_mov_b32 s61, s18
	s_mov_b32 s26, s20
	s_mov_b64 s[30:31], s[22:23]
	s_mov_b64 s[28:29], s[24:25]
	s_waitcnt vmcnt(0)
	v_pk_fma_f32 v[126:127], v[126:127], v[142:143], v[170:171]
	v_pk_fma_f32 v[124:125], v[124:125], v[140:141], v[168:169]
	v_pk_fma_f32 v[122:123], v[122:123], v[138:139], v[174:175]
	v_pk_fma_f32 v[120:121], v[120:121], v[136:137], v[172:173]
	v_pk_fma_f32 v[106:107], v[106:107], v[134:135], v[178:179]
	v_pk_fma_f32 v[76:77], v[76:77], v[128:129], v[212:213]
	v_pk_fma_f32 v[104:105], v[104:105], v[132:133], v[176:177]
	v_pk_fma_f32 v[102:103], v[102:103], v[130:131], v[182:183]
	v_pk_fma_f32 v[100:101], v[100:101], v[128:129], v[180:181]
	v_pk_fma_f32 v[118:119], v[118:119], v[142:143], v[186:187]
	v_pk_fma_f32 v[116:117], v[116:117], v[140:141], v[184:185]
	v_pk_fma_f32 v[114:115], v[114:115], v[138:139], v[190:191]
	v_pk_fma_f32 v[112:113], v[112:113], v[136:137], v[188:189]
	v_pk_fma_f32 v[94:95], v[94:95], v[134:135], v[194:195]
	v_pk_fma_f32 v[92:93], v[92:93], v[132:133], v[192:193]
	v_pk_fma_f32 v[90:91], v[90:91], v[130:131], v[198:199]
	v_pk_fma_f32 v[88:89], v[88:89], v[128:129], v[196:197]
	v_pk_fma_f32 v[110:111], v[110:111], v[142:143], v[202:203]
	v_pk_fma_f32 v[108:109], v[108:109], v[140:141], v[200:201]
	v_pk_fma_f32 v[98:99], v[98:99], v[138:139], v[206:207]
	v_pk_fma_f32 v[96:97], v[96:97], v[136:137], v[204:205]
	v_pk_fma_f32 v[86:87], v[86:87], v[134:135], v[210:211]
	v_pk_fma_f32 v[84:85], v[84:85], v[132:133], v[208:209]
	v_pk_fma_f32 v[78:79], v[78:79], v[130:131], v[214:215]
	global_store_dwordx4 v[238:239], v[124:127], off
	global_store_dwordx4 v[238:239], v[120:123], off offset:64
	global_store_dwordx4 v[238:239], v[104:107], off offset:512
	global_store_dwordx4 v[238:239], v[100:103], off offset:576
	global_store_dwordx4 v[232:233], v[116:119], off
	global_store_dwordx4 v[232:233], v[112:115], off offset:64
	global_store_dwordx4 v[232:233], v[92:95], off offset:512
	global_store_dwordx4 v[232:233], v[88:91], off offset:576
	global_store_dwordx4 v[234:235], v[108:111], off
	global_store_dwordx4 v[234:235], v[96:99], off offset:64
	global_store_dwordx4 v[234:235], v[84:87], off offset:512
	global_store_dwordx4 v[234:235], v[76:79], off offset:576
	v_pk_fma_f32 v[74:75], v[74:75], v[138:139], v[222:223]
	v_pk_fma_f32 v[72:73], v[72:73], v[136:137], v[220:221]
	v_pk_fma_f32 v[76:77], v[80:81], v[140:141], v[216:217]
	v_lshl_add_u64 v[80:81], s[6:7], 0, v[236:237]
	v_pk_fma_f32 v[78:79], v[82:83], v[142:143], v[218:219]
; #define PG8_WAIT_V(n) asm volatile("s_waitcnt vmcnt(" #n ")" ::: "memory")
; #define PG8_BAR __builtin_amdgcn_s_barrier()
; template <class Epi, class Sched>
; __device__ __forceinline__ void gemm_phase(LAS unsigned char* lds, const bf16_t* A, const int K, const Sched& S, const Epi& E, const int wv) {
;     ...
;     PG8_WAIT_V(0);
;     if (wr == 0) PG8_BAR;
;     PG8_BAR;
;     __device__ __forceinline__ void operator()(const f32x4 (&acc)[2][2][4][2], const Unit& u, int wr, int wc, int fr, int fq) const {
;     ...
;         for (int ai = 0; ai < 2; ++ai) {
;             f32x4 rv[4][2][2];
; #pragma unroll
;             for (int m = 0; m < 4; ++m) { const size_t off = (size_t)(row0 + ai * HALF + m * 16) * DM + col0;
; #pragma unroll
;                 for (int bj = 0; bj < 2; ++bj)
; #pragma unroll
;                     for (int n = 0; n < 2; ++n) rv[m][bj][n] = *(const f32x4*)(res + off + bj * HALF + n * 16); }
; #pragma unroll
;             for (int m = 0; m < 4; ++m) { const size_t off = (size_t)(row0 + ai * HALF + m * 16) * DM + col0;
; #pragma unroll
;                 for (int bj = 0; bj < 2; ++bj)
; #pragma unroll
;                     for (int n = 0; n < 2; ++n) *(f32x4*)(out + off + bj * HALF + n * 16) = rv[m][bj][n] + gv[bj][n] * acc[ai][bj][m][n]; }
	v_lshl_add_u64 v[80:81], v[80:81], 0, v[156:157]
	v_pk_fma_f32 v[70:71], v[70:71], v[134:135], v[226:227]
	v_pk_fma_f32 v[68:69], v[68:69], v[132:133], v[224:225]
	v_pk_fma_f32 v[66:67], v[66:67], v[130:131], v[230:231]
	v_pk_fma_f32 v[64:65], v[64:65], v[128:129], v[228:229]
	global_store_dwordx4 v[80:81], v[76:79], off
	global_store_dwordx4 v[80:81], v[72:75], off offset:64
	global_store_dwordx4 v[80:81], v[68:71], off offset:512
	global_store_dwordx4 v[80:81], v[64:67], off offset:576
	v_lshl_add_u64 v[168:169], v[160:161], 0, s[10:11]
	v_lshl_add_u64 v[170:171], v[160:161], 0, s[12:13]
	v_lshl_add_u64 v[172:173], v[160:161], 0, s[14:15]
	v_lshl_add_u64 v[76:77], v[158:159], 0, v[168:169]
	v_lshl_add_u64 v[92:93], v[158:159], 0, v[170:171]
	v_lshl_add_u64 v[108:109], v[158:159], 0, v[172:173]
	global_load_dwordx4 v[64:67], v[76:77], off
	global_load_dwordx4 v[68:71], v[76:77], off offset:64
	global_load_dwordx4 v[72:75], v[76:77], off offset:512
	s_nop 0
	global_load_dwordx4 v[76:79], v[76:77], off offset:576
	s_nop 0
	global_load_dwordx4 v[80:83], v[92:93], off
	global_load_dwordx4 v[84:87], v[92:93], off offset:64
	global_load_dwordx4 v[88:91], v[92:93], off offset:512
	s_nop 0
	global_load_dwordx4 v[92:95], v[92:93], off offset:576
	s_nop 0
	global_load_dwordx4 v[96:99], v[108:109], off
	global_load_dwordx4 v[100:103], v[108:109], off offset:64
	global_load_dwordx4 v[104:107], v[108:109], off offset:512
	s_nop 0
	global_load_dwordx4 v[108:111], v[108:109], off offset:576
	v_lshl_add_u64 v[160:161], v[160:161], 0, s[16:17]
	v_lshl_add_u64 v[124:125], v[158:159], 0, v[160:161]
	global_load_dwordx4 v[112:115], v[124:125], off
	global_load_dwordx4 v[116:119], v[124:125], off offset:64
	global_load_dwordx4 v[120:123], v[124:125], off offset:512
	s_nop 0
	global_load_dwordx4 v[124:127], v[124:125], off offset:576
	v_lshl_add_u64 v[158:159], s[6:7], 0, v[168:169]
	v_lshl_add_u64 v[168:169], s[6:7], 0, v[170:171]
	v_lshl_add_u64 v[170:171], s[6:7], 0, v[172:173]
	v_lshl_add_u64 v[158:159], v[158:159], 0, v[156:157]
	v_lshl_add_u64 v[168:169], v[168:169], 0, v[156:157]
	v_lshl_add_u64 v[170:171], v[170:171], 0, v[156:157]
	s_waitcnt vmcnt(0)
	v_pk_fma_f32 v[62:63], v[62:63], v[142:143], v[66:67]
	v_pk_fma_f32 v[60:61], v[60:61], v[140:141], v[64:65]
	v_pk_fma_f32 v[58:59], v[58:59], v[138:139], v[70:71]
	v_pk_fma_f32 v[56:57], v[56:57], v[136:137], v[68:69]
	v_pk_fma_f32 v[42:43], v[42:43], v[134:135], v[74:75]
	v_pk_fma_f32 v[12:13], v[12:13], v[128:129], v[108:109]
	v_pk_fma_f32 v[40:41], v[40:41], v[132:133], v[72:73]
	v_pk_fma_f32 v[38:39], v[38:39], v[130:131], v[78:79]
	v_pk_fma_f32 v[36:37], v[36:37], v[128:129], v[76:77]
	v_pk_fma_f32 v[54:55], v[54:55], v[142:143], v[82:83]
	v_pk_fma_f32 v[52:53], v[52:53], v[140:141], v[80:81]
	v_pk_fma_f32 v[50:51], v[50:51], v[138:139], v[86:87]
	v_pk_fma_f32 v[48:49], v[48:49], v[136:137], v[84:85]
	v_pk_fma_f32 v[30:31], v[30:31], v[134:135], v[90:91]
	v_pk_fma_f32 v[28:29], v[28:29], v[132:133], v[88:89]
	v_pk_fma_f32 v[26:27], v[26:27], v[130:131], v[94:95]
	v_pk_fma_f32 v[24:25], v[24:25], v[128:129], v[92:93]
	v_pk_fma_f32 v[46:47], v[46:47], v[142:143], v[98:99]
	v_pk_fma_f32 v[44:45], v[44:45], v[140:141], v[96:97]
	v_pk_fma_f32 v[34:35], v[34:35], v[138:139], v[102:103]
	v_pk_fma_f32 v[32:33], v[32:33], v[136:137], v[100:101]
	v_pk_fma_f32 v[22:23], v[22:23], v[134:135], v[106:107]
	v_pk_fma_f32 v[20:21], v[20:21], v[132:133], v[104:105]
	v_pk_fma_f32 v[14:15], v[14:15], v[130:131], v[110:111]
	global_store_dwordx4 v[158:159], v[60:63], off
	global_store_dwordx4 v[158:159], v[56:59], off offset:64
	global_store_dwordx4 v[158:159], v[40:43], off offset:512
	global_store_dwordx4 v[158:159], v[36:39], off offset:576
	global_store_dwordx4 v[168:169], v[52:55], off
	global_store_dwordx4 v[168:169], v[48:51], off offset:64
	global_store_dwordx4 v[168:169], v[28:31], off offset:512
	global_store_dwordx4 v[168:169], v[24:27], off offset:576
	global_store_dwordx4 v[170:171], v[44:47], off
	global_store_dwordx4 v[170:171], v[32:35], off offset:64
	global_store_dwordx4 v[170:171], v[20:23], off offset:512
	global_store_dwordx4 v[170:171], v[12:15], off offset:576
	v_pk_fma_f32 v[18:19], v[18:19], v[142:143], v[114:115]
	v_pk_fma_f32 v[16:17], v[16:17], v[140:141], v[112:113]
	v_lshl_add_u64 v[12:13], s[6:7], 0, v[160:161]
	v_lshl_add_u64 v[12:13], v[12:13], 0, v[156:157]
	v_pk_fma_f32 v[10:11], v[10:11], v[138:139], v[118:119]
	v_pk_fma_f32 v[8:9], v[8:9], v[136:137], v[116:117]
	v_pk_fma_f32 v[6:7], v[6:7], v[134:135], v[122:123]
	v_pk_fma_f32 v[4:5], v[4:5], v[132:133], v[120:121]
	v_pk_fma_f32 v[2:3], v[2:3], v[130:131], v[126:127]
	v_pk_fma_f32 v[0:1], v[0:1], v[128:129], v[124:125]
	global_store_dwordx4 v[12:13], v[16:19], off
	global_store_dwordx4 v[12:13], v[8:11], off offset:64
	global_store_dwordx4 v[12:13], v[4:7], off offset:512
	global_store_dwordx4 v[12:13], v[0:3], off offset:576
	s_cbranch_vccz .LBB0_1898
	s_waitcnt vmcnt(0)
	s_cmpk_gt_u32 s33, 0xff
	s_cbranch_scc1 .LBB0_1909

; #define PG8_BAR __builtin_amdgcn_s_barrier()
; template <class Epi, class Sched>
; __device__ __forceinline__ void gemm_phase(LAS unsigned char* lds, const bf16_t* A, const int K, const Sched& S, const Epi& E, const int wv) {
;     int tid = mk_tid(wv); asm volatile("" : "+v"(tid));
;     const int wid = __builtin_amdgcn_readfirstlane(tid >> 6), lane = tid & 63, wr = wid >> 2, wc = wid & 3, fr = lane & 15, fq = lane >> 4;
;     const int nt = K / BK;
;     unsigned voffA[2], voffB[2];
; #pragma unroll
;     for (int i = 0; i < 2; ++i) { int R, C; stage_rc(tid * 16 + i * 8192, R, C); const int Rb = Epi::PERM ? ((R & ~31) + perm32(R & 31)) : R;
;         voffA[i] = (unsigned)(R * K + C) * 2u; voffB[i] = (unsigned)(Rb * K + C) * 2u; }
;     const size_t kstep = (size_t)(BK * 2);
;     const size_t hstep = (size_t)HALF * K * 2;
;     const size_t tstep = 2 * hstep;
;     const unsigned ldsw = (unsigned)wid * 1024u;
;     const int aoff = lds_byte(wr * 64 + fr, fq * 8), boff = lds_byte(wc * 32 + fr, fq * 8);
;     Unit cur, nxt; int ui = 0;
;     if (!S.next(0, cur)) return;
;     f32x4 acc[2][2][4][2];
; #pragma unroll
;     for (int a_ = 0; a_ < 2; ++a_)
; #pragma unroll
;         for (int b_ = 0; b_ < 2; ++b_)
; #pragma unroll
;             for (int m = 0; m < 4; ++m)
; #pragma unroll
;                 for (int n = 0; n < 2; ++n) acc[a_][b_][m][n] = (f32x4){0.f, 0.f, 0.f, 0.f};
;     bf16x8 At[4][2], B0[2][2], B1[2][2];
;     unsigned ao0[2] = {0u, 0u}, ao1[2] = {0u, 0u}, no0[2] = {0u, 0u}, no1[2] = {0u, 0u};
;     const char* Ab = (const char*)A;
;     const char* cA = Ab; const char* nA = Ab;
;     if constexpr (Sched::GATHER) {
; #pragma unroll
;         for (int i = 0; i < 2; ++i) { int R, C; stage_rc(tid * 16 + i * 8192, R, C);
;             ao0[i] = (S.arow(cur, R) * (unsigned)K + (unsigned)C) * 2u; ao1[i] = (S.arow(cur, HALF + R) * (unsigned)K + (unsigned)C) * 2u; }
;     } else cA = Ab + (size_t)cur.pm * tstep;
;     const char* cB = S.bptr(cur);
;     PG8_STAGE(PG8_SB(0, 0), cB, voffB); PG8_STAGE_A(PG8_SA(0, 0), 0, false, 0); PG8_STAGE(PG8_SB(0, 1), cB + hstep, voffB); PG8_STAGE_A(PG8_SA(0, 1), 1, false, 0);
;     if (wr == 1) PG8_BAR;
;     PG8_WAIT_V(4); PG8_BAR;
;     PG8_STAGE(PG8_SB(1, 0), cB + kstep, voffB); PG8_STAGE_A(PG8_SA(1, 0), 0, false, kstep); PG8_STAGE(PG8_SB(1, 1), cB + hstep + kstep, voffB);
;     PG8_WAIT_V(6); PG8_BAR;
.LBB0_2069:
	v_bfe_i32 v2, v4, 27, 1
	v_lshlrev_b32_e32 v0, 4, v4
	v_lshrrev_b32_e32 v2, 22, v2
	v_add_u32_e32 v2, v0, v2
	v_and_b32_e32 v2, 0xfffffc00, v2
	v_sub_u32_e32 v2, v0, v2
	v_ashrrev_i32_e32 v1, 31, v4
	v_lshrrev_b32_e32 v3, 4, v2
	v_lshrrev_b32_e32 v1, 26, v1
	v_bitop3_b32 v2, v3, v2, 32 bitop3:0x6c
	v_add_u32_e32 v1, v4, v1
	v_ashrrev_i32_e32 v5, 31, v2
	v_ashrrev_i32_e32 v1, 6, v1
	v_lshrrev_b32_e32 v5, 26, v5
	v_lshlrev_b32_e32 v3, 3, v1
	v_add_u32_e32 v5, v2, v5
	v_and_b32_e32 v3, -16, v3
	v_ashrrev_i32_e32 v6, 6, v5
	v_add_u32_e32 v144, v6, v3
	v_and_b32_e32 v3, 0xc0, v5
	v_sub_u32_e32 v2, v2, v3
	v_mov_b32_e32 v3, 1
	v_lshlrev_b32_e32 v1, 5, v1
	v_ashrrev_i16_sdwa v2, v3, sext(v2) dst_sel:DWORD dst_unused:UNUSED_PAD src0_sel:DWORD src1_sel:BYTE_0
	v_and_b32_e32 v1, 32, v1
	v_bfe_i32 v2, v2, 0, 16
	v_add_u32_e32 v0, 0x2000, v0
	v_add_lshl_u32 v145, v1, v2, 1
	v_ashrrev_i32_e32 v1, 31, v0
	v_lshrrev_b32_e32 v1, 22, v1
	v_add_u32_e32 v1, v0, v1
	v_ashrrev_i32_e32 v1, 10, v1
	v_mul_i32_i24_e32 v2, 0x400, v1
	v_lshlrev_b32_e32 v5, 1, v144
	v_lshrrev_b32_e32 v7, 2, v144
	v_and_b32_e32 v6, 3, v6
	s_mov_b32 s9, 0xfffe0
	v_sub_u32_e32 v0, v0, v2
	v_and_b32_e32 v5, 24, v5
	v_and_b32_e32 v7, 4, v7
	v_and_or_b32 v6, v144, s9, v6
	v_lshrrev_b32_e32 v2, 4, v0
	v_or3_b32 v5, v6, v7, v5
	v_bitop3_b32 v0, v2, v0, 32 bitop3:0x6c
	v_lshl_add_u32 v128, v5, 12, v145
	v_ashrrev_i32_e32 v5, 31, v0
	v_lshrrev_b32_e32 v5, 26, v5
	v_lshlrev_b32_e32 v2, 3, v1
	v_add_u32_e32 v5, v0, v5
	v_and_b32_e32 v2, -16, v2
	v_ashrrev_i32_e32 v6, 6, v5
	v_lshlrev_b32_e32 v1, 5, v1
	s_add_u32 s2, s76, 0x3c188000
	v_add_u32_e32 v146, v6, v2
	v_and_b32_e32 v2, 32, v1
	v_and_b32_e32 v1, 0xc0, v5
	s_addc_u32 s3, s77, 0
	v_sub_u32_e32 v0, v0, v1
	s_ashr_i32 s8, s26, 6
	s_ashr_i32 s0, s26, 8
	v_ashrrev_i16_sdwa v0, v3, sext(v0) dst_sel:DWORD dst_unused:UNUSED_PAD src0_sel:DWORD src1_sel:BYTE_0
	s_lshl_b32 s1, s8, 10
	v_bfe_i32 v3, v0, 0, 16
	v_lshlrev_b32_e32 v0, 1, v146
	s_add_u32 s27, s76, 0x14188000
	v_and_b32_e32 v5, 24, v0
	v_lshrrev_b32_e32 v0, 2, v146
	s_addc_u32 s28, s77, 0
	s_add_i32 s12, 0, 0x20800
	v_and_b32_e32 v7, 4, v0
	v_lshl_add_u32 v0, v144, 2, s12
	ds_read2st64_b32 v[0:1], v0 offset1:2
	s_ashr_i32 s21, s20, 31
	v_and_b32_e32 v6, 3, v6
	v_add_lshl_u32 v147, v2, v3, 1
	v_lshl_add_u32 v2, v146, 2, s12
	s_lshl_b64 s[10:11], s[20:21], 20
	v_and_or_b32 v6, v146, s9, v6
	ds_read2st64_b32 v[2:3], v2 offset1:2
	s_add_u32 s9, s27, s10
	s_waitcnt lgkmcnt(1)
	v_lshlrev_b32_e32 v0, 11, v0
	s_addc_u32 s10, s28, s11
	v_and_b32_e32 v0, 0xfffff000, v0
	s_add_u32 s22, s9, s6
	v_add_u32_e32 v132, v0, v145
	v_lshlrev_b32_e32 v0, 11, v1
	s_addc_u32 s23, s10, s7
	s_add_i32 s21, s1, 0
	v_or3_b32 v5, v6, v7, v5
	v_and_b32_e32 v0, 0xfffff000, v0
	s_add_i32 m0, s21, 0x10000
	v_lshl_add_u32 v130, v5, 12, v147
	v_add_u32_e32 v134, v0, v145
	s_waitcnt lgkmcnt(0)
	v_lshlrev_b32_e32 v0, 11, v2
	global_load_lds_dwordx4 v128, s[22:23]
	s_add_i32 m0, s21, 0x12000
	v_and_b32_e32 v0, 0xfffff000, v0
	global_load_lds_dwordx4 v130, s[22:23]
	s_mov_b32 m0, s21
	s_add_i32 s29, s21, 0x2000
	v_add_u32_e32 v136, v0, v147
	global_load_lds_dwordx4 v132, s[2:3]
	s_mov_b32 m0, s29
	s_add_u32 s6, s22, 0x80000
	global_load_lds_dwordx4 v136, s[2:3]
	s_addc_u32 s7, s23, 0
	s_add_i32 m0, s21, 0x14000
	v_lshlrev_b32_e32 v0, 11, v3
	global_load_lds_dwordx4 v128, s[6:7]
	s_add_i32 m0, s21, 0x16000
	s_add_i32 s30, s21, 0x4000
	v_and_b32_e32 v0, 0xfffff000, v0
	global_load_lds_dwordx4 v130, s[6:7]
	s_mov_b32 m0, s30
	s_add_i32 s31, s21, 0x6000
	v_add_u32_e32 v138, v0, v147
	global_load_lds_dwordx4 v134, s[2:3]
	s_mov_b32 m0, s31
	v_mov_b32_e32 v133, 0
	global_load_lds_dwordx4 v138, s[2:3]
	v_mov_b32_e32 v129, v133
	v_mov_b32_e32 v131, v133
	s_mov_b32 s38, 0
	v_lshl_add_u64 v[2:3], s[22:23], 0, v[128:129]
	v_lshl_add_u64 v[0:1], s[22:23], 0, v[130:131]
	s_cmp_lg_u32 s0, 1
	v_mov_b32_e32 v137, v133
	s_cbranch_scc1 .LBB0_2071
.LBB0_2071:
	s_add_u32 s6, s76, 0x52188000
	s_addc_u32 s7, s77, 0
	s_lshl_b32 s8, s8, 5
	s_and_b32 s16, s8, 0x60
	s_mov_b64 s[8:9], 0x80
	s_add_i32 m0, s21, 0x18000
	v_lshl_add_u64 v[2:3], v[2:3], 0, s[8:9]
	s_lshl_b32 s13, s0, 13
	s_lshl_b32 s17, s16, 7
	s_waitcnt vmcnt(4)
	s_barrier
	global_load_lds_dwordx4 v[2:3], off
	s_add_i32 m0, s21, 0x1a000
	s_add_u32 s10, s76, 0x3c188080
	v_lshl_add_u64 v[0:1], v[0:1], 0, s[8:9]
	s_addc_u32 s11, s77, 0
	s_add_i32 s33, s21, 0x8000
	s_add_i32 s34, s21, 0xa000
	global_load_lds_dwordx4 v[0:1], off
	v_lshl_add_u64 v[0:1], s[10:11], 0, v[132:133]
	s_mov_b32 m0, s33
	s_add_u32 s14, s22, 0x80080
	global_load_lds_dwordx4 v[0:1], off
	v_lshl_add_u64 v[0:1], s[10:11], 0, v[136:137]
	s_mov_b32 m0, s34
	s_addc_u32 s15, s23, 0
	global_load_lds_dwordx4 v[0:1], off
	s_add_i32 m0, s21, 0x1c000
	v_lshl_add_u64 v[0:1], s[14:15], 0, v[128:129]
	global_load_lds_dwordx4 v[0:1], off
	v_lshl_add_u64 v[0:1], s[14:15], 0, v[130:131]
	s_add_i32 m0, s21, 0x1e000
	s_add_i32 s52, 0, 0x10000
	global_load_lds_dwordx4 v[0:1], off
	v_lshrrev_b32_e32 v1, 1, v4
	v_and_b32_e32 v0, 15, v4
	v_and_b32_e32 v1, 24, v1
	v_lshl_or_b32 v137, s0, 6, v0
	v_lshlrev_b32_e32 v2, 1, v1
	v_lshl_or_b32 v0, v0, 6, v2
	v_lshlrev_b32_e32 v2, 2, v137
	v_and_b32_e32 v3, 32, v2
	v_lshlrev_b32_e32 v4, 2, v4
	s_waitcnt vmcnt(6)
	s_add_i32 s53, 0, 0x14000
	s_add_i32 s62, 0, 0x18000
	s_add_i32 s63, 0, 0x1c000
	v_bitop3_b32 v3, v0, s13, v3 bitop3:0xde
	v_and_b32_e32 v4, 32, v4
	v_or_b32_e32 v151, 16, v137
	v_or_b32_e32 v152, 32, v137
	v_or_b32_e32 v153, 48, v137
	v_add_u32_e32 v154, 0x80, v137
	v_add_u32_e32 v155, 0x90, v137
	v_add_u32_e32 v156, 0xa0, v137
	v_add_u32_e32 v157, 0xb0, v137
	s_add_i32 s0, 0, 0x20480
	s_add_i32 s56, s52, s1
	s_add_i32 s60, s53, s1
	s_add_i32 s64, s62, s1
	s_add_i32 s66, s63, s1
	v_bitop3_b32 v149, v0, s17, v4 bitop3:0xde
	v_add_u32_e32 v150, s12, v2
	v_or_b32_e32 v158, s16, v1
	v_lshl_add_u32 v159, v151, 2, s12
	v_lshl_add_u32 v160, v152, 2, s12
	v_lshl_add_u32 v161, v153, 2, s12
	v_lshl_add_u32 v162, v154, 2, s12
	v_lshl_add_u32 v163, v155, 2, s12
	v_lshl_add_u32 v164, v156, 2, s12
	v_lshl_add_u32 v165, v157, 2, s12
	v_mov_b32_e32 v166, s0
	s_add_i32 s35, 0, 0x20404
	s_add_i32 s36, 0, 0x2040c
	s_add_i32 s37, 0, 0x20414
	s_add_i32 s39, 0, 0x2041c
	s_add_i32 s40, 0, 0x20424
	s_add_i32 s41, 0, 0x2042c
	s_add_i32 s42, 0, 0x20434
	s_add_i32 s43, 0, 0x2043c
	s_add_i32 s44, 0, 0x20444
	s_add_i32 s45, 0, 0x2044c
	s_add_i32 s46, 0, 0x20454
	s_add_i32 s47, 0, 0x2045c
	s_add_i32 s48, 0, 0x20464
	s_add_i32 s49, 0, 0x2046c
	s_add_i32 s50, 0, 0x20474
	s_add_i32 s51, 0, 0x2047c
	v_add_u32_e32 v167, 0, v3
	s_add_i32 s54, s21, 0xc000
	s_add_i32 s55, s21, 0xe000
	s_add_i32 s57, s56, 0x2000
	s_add_i32 s61, s60, 0x2000
	s_add_i32 s65, s64, 0x2000
	s_add_i32 s67, s66, 0x2000
	v_mov_b32_e32 v173, v132
	s_mov_b32 s68, 0
	s_barrier
	s_branch .LBB0_2073

;     __device__ __forceinline__ const char* bptr(const Unit& u) const { return (const char*)Bt + (size_t)u.pn * 256 * K * 2; }
;     __device__ __forceinline__ unsigned arow(const Unit& u, int r) const { return (unsigned)(u.pm * 256 + r); }
; #define PG8_LDA(dst, b, h) do { _Pragma("unroll") for (int m = 0; m < 4; ++m) _Pragma("unroll") for (int k = 0; k < 2; ++k) dst[m][k] = *(const LAS bf16x8*)(lds + PG8_SA(b, h) + aoff + m * 2048 + k * 1024); } while (0)
; #define PG8_WAIT_L(n) asm volatile("s_waitcnt lgkmcnt(" #n ")" ::: "memory")
; template <class Epi, class Sched>
; __device__ __forceinline__ void gemm_phase(LAS unsigned char* lds, const bf16_t* A, const int K, const Sched& S, const Epi& E, const int wv) {
;     ...
;         const bool has_next = S.next(ui + 1, nxt);
;         const char* nB = has_next ? S.bptr(nxt) : cB;
;         if constexpr (Sched::GATHER) {
;             if (has_next) {
; #pragma unroll
;                 for (int i = 0; i < 2; ++i) { int R, C; stage_rc(tid * 16 + i * 8192, R, C);
;                     no0[i] = (S.arow(nxt, R) * (unsigned)K + (unsigned)C) * 2u; no1[i] = (S.arow(nxt, HALF + R) * (unsigned)K + (unsigned)C) * 2u; }
;             } else {
; #pragma unroll
;                 for (int i = 0; i < 2; ++i) { no0[i] = ao0[i]; no1[i] = ao1[i]; }
;             }
;             asm volatile("s_waitcnt lgkmcnt(0)" ::: "memory");
;             asm volatile("" : "+v"(no0[0]), "+v"(no0[1]), "+v"(no1[0]), "+v"(no1[1]));
;         } else nA = has_next ? Ab + (size_t)nxt.pm * tstep : cA;
;         for (int t = 0; t < nt; t += 2) {
;             const bool last = (t == nt - 2);
;             const size_t k1 = (size_t)(t + 1) * kstep;
;             const size_t k2 = last ? 0 : (size_t)(t + 2) * kstep, k3 = k2 + kstep;
;             const char* b2 = last ? nB : cB + (size_t)(t + 2) * kstep; const char* b3 = b2 + kstep;
;             PG8_LDB(B0, 0, 0); PG8_SCHED; PG8_LDA(At, 0, 0); PG8_STAGE_A(PG8_SA(1, 1), 1, false, k1);
;             PG8_WAIT_L(8); PG8_BAR; PG8_WAIT_L(0); PG8_MMA(0, 0, At, B0); PG8_BAR; PG8_SCHED;
;     ...
; #pragma unroll
;         for (int a_ = 0; a_ < 2; ++a_)
; #pragma unroll
;             for (int b_ = 0; b_ < 2; ++b_)
; #pragma unroll
;                 for (int m = 0; m < 4; ++m)
; #pragma unroll
;                     for (int n = 0; n < 2; ++n) acc[a_][b_][m][n] = (f32x4){0.f, 0.f, 0.f, 0.f};
.LBB0_2079:
	s_waitcnt lgkmcnt(0)
	v_mov_b32_e32 v135, v133
	v_mov_b32_e32 v139, v133
	s_add_u32 s15, s22, 0x100
	v_mov_b32_e32 v36, 0
	s_addc_u32 s17, s23, 0
	v_lshl_add_u64 v[140:141], s[10:11], 0, v[138:139]
	v_lshl_add_u64 v[142:143], s[10:11], 0, v[134:135]
	s_mov_b32 s70, -2
	s_mov_b64 s[0:1], 0
	v_mov_b32_e32 v37, v36
	v_mov_b32_e32 v38, v36
	v_mov_b32_e32 v39, v36
	v_mov_b32_e32 v52, v36
	v_mov_b32_e32 v53, v36
	v_mov_b32_e32 v54, v36
	v_mov_b32_e32 v55, v36
	v_mov_b32_e32 v64, v36
	v_mov_b32_e32 v65, v36
	v_mov_b32_e32 v66, v36
	v_mov_b32_e32 v67, v36
	v_mov_b32_e32 v68, v36
	v_mov_b32_e32 v69, v36
	v_mov_b32_e32 v70, v36
	v_mov_b32_e32 v71, v36
	v_mov_b32_e32 v80, v36
	v_mov_b32_e32 v81, v36
	v_mov_b32_e32 v82, v36
	v_mov_b32_e32 v83, v36
	v_mov_b32_e32 v84, v36
	v_mov_b32_e32 v85, v36
	v_mov_b32_e32 v86, v36
	v_mov_b32_e32 v87, v36
	v_mov_b32_e32 v96, v36
	v_mov_b32_e32 v97, v36
	v_mov_b32_e32 v98, v36
	v_mov_b32_e32 v99, v36
	v_mov_b32_e32 v100, v36
	v_mov_b32_e32 v101, v36
	v_mov_b32_e32 v102, v36
	v_mov_b32_e32 v103, v36
	v_mov_b32_e32 v112, v36
	v_mov_b32_e32 v113, v36
	v_mov_b32_e32 v114, v36
	v_mov_b32_e32 v115, v36
	v_mov_b32_e32 v116, v36
	v_mov_b32_e32 v117, v36
	v_mov_b32_e32 v118, v36
	v_mov_b32_e32 v119, v36
	v_mov_b32_e32 v72, v36
	v_mov_b32_e32 v73, v36
	v_mov_b32_e32 v74, v36
	v_mov_b32_e32 v75, v36
	v_mov_b32_e32 v76, v36
	v_mov_b32_e32 v77, v36
	v_mov_b32_e32 v78, v36
	v_mov_b32_e32 v79, v36
	v_mov_b32_e32 v88, v36
	v_mov_b32_e32 v89, v36
	v_mov_b32_e32 v90, v36
	v_mov_b32_e32 v91, v36
	v_mov_b32_e32 v92, v36
	v_mov_b32_e32 v93, v36
	v_mov_b32_e32 v94, v36
	v_mov_b32_e32 v95, v36
	v_mov_b32_e32 v104, v36
	v_mov_b32_e32 v105, v36
	v_mov_b32_e32 v106, v36
	v_mov_b32_e32 v107, v36
	v_mov_b32_e32 v108, v36
	v_mov_b32_e32 v109, v36
	v_mov_b32_e32 v110, v36
	v_mov_b32_e32 v111, v36
	v_mov_b32_e32 v120, v36
	v_mov_b32_e32 v121, v36
	v_mov_b32_e32 v122, v36
	v_mov_b32_e32 v123, v36
	v_mov_b32_e32 v124, v36
	v_mov_b32_e32 v125, v36
	v_mov_b32_e32 v126, v36
	v_mov_b32_e32 v127, v36
	v_mov_b32_e32 v40, v36
	v_mov_b32_e32 v41, v36
	v_mov_b32_e32 v42, v36
	v_mov_b32_e32 v43, v36
	v_mov_b32_e32 v32, v36
	v_mov_b32_e32 v33, v36
	v_mov_b32_e32 v34, v36
	v_mov_b32_e32 v35, v36
	v_mov_b32_e32 v20, v36
	v_mov_b32_e32 v21, v36
	v_mov_b32_e32 v22, v36
	v_mov_b32_e32 v23, v36
	v_mov_b32_e32 v16, v36
	v_mov_b32_e32 v17, v36
	v_mov_b32_e32 v18, v36
	v_mov_b32_e32 v19, v36
	v_mov_b32_e32 v4, v36
	v_mov_b32_e32 v5, v36
	v_mov_b32_e32 v6, v36
	v_mov_b32_e32 v7, v36
	v_mov_b32_e32 v0, v36
	v_mov_b32_e32 v1, v36
	v_mov_b32_e32 v2, v36
	v_mov_b32_e32 v3, v36
	v_mov_b32_e32 v60, v36
	v_mov_b32_e32 v61, v36
	v_mov_b32_e32 v62, v36
	v_mov_b32_e32 v63, v36
	v_mov_b32_e32 v56, v36
	v_mov_b32_e32 v57, v36
	v_mov_b32_e32 v58, v36
	v_mov_b32_e32 v59, v36
	v_mov_b32_e32 v48, v36
	v_mov_b32_e32 v49, v36
	v_mov_b32_e32 v50, v36
	v_mov_b32_e32 v51, v36
	v_mov_b32_e32 v44, v36
	v_mov_b32_e32 v45, v36
	v_mov_b32_e32 v46, v36
	v_mov_b32_e32 v47, v36
	v_mov_b32_e32 v28, v36
	v_mov_b32_e32 v29, v36
	v_mov_b32_e32 v30, v36
	v_mov_b32_e32 v31, v36
	v_mov_b32_e32 v24, v36
	v_mov_b32_e32 v25, v36
	v_mov_b32_e32 v26, v36
	v_mov_b32_e32 v27, v36
	v_mov_b32_e32 v12, v36
	v_mov_b32_e32 v13, v36
	v_mov_b32_e32 v14, v36
	v_mov_b32_e32 v15, v36
	v_mov_b32_e32 v8, v36
	v_mov_b32_e32 v9, v36
	v_mov_b32_e32 v10, v36
	v_mov_b32_e32 v11, v36
	s_bitcmp1_b32 s92, 8
	s_cbranch_scc0 .Lmy_ph_6
	s_barrier
.Lmy_ph_6:
.LBB0_2080:
	v_add_u32_e32 v132, s52, v149
	s_add_u32 s22, s0, 0x100
	ds_read_b128 v[174:177], v132
	ds_read_b128 v[178:181], v132 offset:1024
	ds_read_b128 v[182:185], v132 offset:2048
	ds_read_b128 v[186:189], v132 offset:3072
	s_addc_u32 s23, s1, 0
	s_add_u32 s71, s15, s0
	s_addc_u32 s72, s17, s1
	s_cmpk_eq_i32 s0, 0xf00
	s_cselect_b64 vcc, -1, 0
	s_and_b64 s[24:25], vcc, exec
	s_cselect_b32 s73, 0, s22
	s_cselect_b32 s25, s19, s72
	s_cselect_b32 s24, s18, s71
	s_mov_b32 m0, s54
	v_lshl_add_u64 v[222:223], v[142:143], 0, s[0:1]
	ds_read_b128 v[190:193], v167
	ds_read_b128 v[194:197], v167 offset:1024
	ds_read_b128 v[198:201], v167 offset:2048
	ds_read_b128 v[202:205], v167 offset:3072
	ds_read_b128 v[206:209], v167 offset:4096
	ds_read_b128 v[210:213], v167 offset:5120
	ds_read_b128 v[214:217], v167 offset:6144
	ds_read_b128 v[218:221], v167 offset:7168
	global_load_lds_dwordx4 v[222:223], off
	v_lshl_add_u64 v[222:223], v[140:141], 0, s[0:1]
	s_mov_b32 m0, s55
	s_nop 0
	global_load_lds_dwordx4 v[222:223], off
	s_waitcnt lgkmcnt(8)
	s_barrier
	s_waitcnt lgkmcnt(0)
	s_setprio 1
	s_waitcnt lgkmcnt(0)
	v_mfma_f32_16x16x32_bf16 v[124:127], v[174:177], v[190:193], v[124:127]
	v_mfma_f32_16x16x32_bf16 v[120:123], v[182:185], v[190:193], v[120:123]
	v_mfma_f32_16x16x32_bf16 v[108:111], v[174:177], v[198:201], v[108:111]
	v_mfma_f32_16x16x32_bf16 v[104:107], v[182:185], v[198:201], v[104:107]
	v_mfma_f32_16x16x32_bf16 v[92:95], v[174:177], v[206:209], v[92:95]
	v_mfma_f32_16x16x32_bf16 v[88:91], v[182:185], v[206:209], v[88:91]
	v_mfma_f32_16x16x32_bf16 v[76:79], v[174:177], v[214:217], v[76:79]
	v_mfma_f32_16x16x32_bf16 v[72:75], v[182:185], v[214:217], v[72:75]
	v_mfma_f32_16x16x32_bf16 v[124:127], v[178:181], v[194:197], v[124:127]
	v_mfma_f32_16x16x32_bf16 v[120:123], v[186:189], v[194:197], v[120:123]
	v_mfma_f32_16x16x32_bf16 v[108:111], v[178:181], v[202:205], v[108:111]
	v_mfma_f32_16x16x32_bf16 v[104:107], v[186:189], v[202:205], v[104:107]
	v_mfma_f32_16x16x32_bf16 v[92:95], v[178:181], v[210:213], v[92:95]
	v_mfma_f32_16x16x32_bf16 v[88:91], v[186:189], v[210:213], v[88:91]
	v_mfma_f32_16x16x32_bf16 v[76:79], v[178:181], v[218:221], v[76:79]
	v_mfma_f32_16x16x32_bf16 v[72:75], v[186:189], v[218:221], v[72:75]
	s_setprio 0
	s_barrier
; #define PG8_STAGE(bufoff, gbase, voff) do { _Pragma("unroll") for (int _i = 0; _i < 2; ++_i) \
;         __builtin_amdgcn_global_load_lds((const unsigned*)((const char*)(gbase) + (voff)[_i]), (LAS unsigned*)(lds + (bufoff) + ldsw + _i * 8192), 16, 0, 0); } while (0)
; #define PG8_LDA(dst, b, h) do { _Pragma("unroll") for (int m = 0; m < 4; ++m) _Pragma("unroll") for (int k = 0; k < 2; ++k) dst[m][k] = *(const LAS bf16x8*)(lds + PG8_SA(b, h) + aoff + m * 2048 + k * 1024); } while (0)
; #define PG8_LDB(dst, b, h) do { _Pragma("unroll") for (int n = 0; n < 2; ++n) _Pragma("unroll") for (int k = 0; k < 2; ++k) dst[n][k] = *(const LAS bf16x8*)(lds + PG8_SB(b, h) + boff + n * 2048 + k * 1024); } while (0)
; #define PG8_MMA(ai, bj, At, Bt) do { __builtin_amdgcn_s_setprio(1); _Pragma("unroll") for (int m = 0; m < 4; ++m) _Pragma("unroll") for (int n = 0; n < 2; ++n) _Pragma("unroll") for (int k = 0; k < 2; ++k) \
;         acc[ai][bj][m][n] = __builtin_amdgcn_mfma_f32_16x16x32_bf16(Bt[n][k], At[m][k], acc[ai][bj][m][n], 0, 0, 0); __builtin_amdgcn_s_setprio(0); } while (0)
; #define PG8_WAIT_V(n) asm volatile("s_waitcnt vmcnt(" #n ")" ::: "memory")
; #define PG8_WAIT_L(n) asm volatile("s_waitcnt lgkmcnt(" #n ")" ::: "memory")
; #define PG8_BAR __builtin_amdgcn_s_barrier()
; #define PG8_SCHED __builtin_amdgcn_sched_barrier(0)
; template <class Epi, class Sched>
; __device__ __forceinline__ void gemm_phase(LAS unsigned char* lds, const bf16_t* A, const int K, const Sched& S, const Epi& E, const int wv) {
;     ...
;             PG8_LDB(B1, 0, 1); PG8_STAGE(PG8_SB(0, 0), b2, voffB);
;             PG8_BAR; PG8_WAIT_L(0); PG8_MMA(0, 1, At, B1); PG8_BAR;
;             PG8_LDA(At, 0, 1); PG8_STAGE_A(PG8_SA(0, 0), 0, last, k2);
;             PG8_BAR; PG8_WAIT_L(0); PG8_MMA(1, 0, At, B0); PG8_BAR; PG8_SCHED;
;             PG8_STAGE(PG8_SB(0, 1), b2 + hstep, voffB);
;             PG8_WAIT_V(6); PG8_BAR; PG8_MMA(1, 1, At, B1); PG8_BAR;
;             PG8_LDB(B0, 1, 0); PG8_SCHED; PG8_LDA(At, 1, 0); PG8_STAGE_A(PG8_SA(0, 1), 1, last, k2);
;             PG8_WAIT_L(8); PG8_BAR; PG8_WAIT_L(0); PG8_MMA(0, 0, At, B0); PG8_BAR; PG8_SCHED;
;             PG8_LDB(B1, 1, 1); PG8_STAGE(PG8_SB(1, 0), b3, voffB);
	s_mov_b32 m0, s56
	v_add_u32_e32 v132, s53, v149
	v_lshl_add_u64 v[238:239], s[24:25], 0, v[128:129]
	ds_read_b128 v[222:225], v132
	ds_read_b128 v[226:229], v132 offset:1024
	ds_read_b128 v[230:233], v132 offset:2048
	ds_read_b128 v[234:237], v132 offset:3072
	global_load_lds_dwordx4 v[238:239], off
	v_lshl_add_u64 v[240:241], s[24:25], 0, v[130:131]
	s_mov_b32 m0, s57
	s_nop 0
	global_load_lds_dwordx4 v[240:241], off
	s_barrier
	s_waitcnt lgkmcnt(0)
	s_setprio 1
	s_waitcnt lgkmcnt(0)
	v_mfma_f32_16x16x32_bf16 v[116:119], v[222:225], v[190:193], v[116:119]
	v_mfma_f32_16x16x32_bf16 v[112:115], v[230:233], v[190:193], v[112:115]
	v_mfma_f32_16x16x32_bf16 v[100:103], v[222:225], v[198:201], v[100:103]
	v_mfma_f32_16x16x32_bf16 v[96:99], v[230:233], v[198:201], v[96:99]
	v_mfma_f32_16x16x32_bf16 v[84:87], v[222:225], v[206:209], v[84:87]
	v_mfma_f32_16x16x32_bf16 v[80:83], v[230:233], v[206:209], v[80:83]
	v_mfma_f32_16x16x32_bf16 v[68:71], v[222:225], v[214:217], v[68:71]
	v_mfma_f32_16x16x32_bf16 v[64:67], v[230:233], v[214:217], v[64:67]
	v_mfma_f32_16x16x32_bf16 v[116:119], v[226:229], v[194:197], v[116:119]
	v_mfma_f32_16x16x32_bf16 v[112:115], v[234:237], v[194:197], v[112:115]
	v_mfma_f32_16x16x32_bf16 v[100:103], v[226:229], v[202:205], v[100:103]
	v_mfma_f32_16x16x32_bf16 v[96:99], v[234:237], v[202:205], v[96:99]
	v_mfma_f32_16x16x32_bf16 v[84:87], v[226:229], v[210:213], v[84:87]
	v_mfma_f32_16x16x32_bf16 v[80:83], v[234:237], v[210:213], v[80:83]
	v_mfma_f32_16x16x32_bf16 v[68:71], v[226:229], v[218:221], v[68:71]
	v_mfma_f32_16x16x32_bf16 v[64:67], v[234:237], v[218:221], v[64:67]
	s_setprio 0
	s_add_u32 s0, s2, s73
	s_mov_b32 m0, s21
	s_addc_u32 s1, s3, 0
	v_cndmask_b32_e32 v132, v173, v169, vcc
	s_barrier
	ds_read_b128 v[190:193], v167 offset:16384
	ds_read_b128 v[194:197], v167 offset:17408
	ds_read_b128 v[198:201], v167 offset:18432
	ds_read_b128 v[202:205], v167 offset:19456
	ds_read_b128 v[206:209], v167 offset:20480
	ds_read_b128 v[210:213], v167 offset:21504
	ds_read_b128 v[214:217], v167 offset:22528
	ds_read_b128 v[218:221], v167 offset:23552
	v_cndmask_b32_e32 v242, v136, v171, vcc
	global_load_lds_dwordx4 v132, s[0:1]
	s_mov_b32 m0, s29
	v_mov_b32_e32 v243, v133
	global_load_lds_dwordx4 v242, s[0:1]
	s_barrier
	s_waitcnt lgkmcnt(0)
	v_lshl_add_u64 v[244:245], s[0:1], 0, v[132:133]
	v_lshl_add_u64 v[242:243], s[0:1], 0, v[242:243]
	s_setprio 1
	s_waitcnt lgkmcnt(0)
	v_mfma_f32_16x16x32_bf16 v[52:55], v[174:177], v[190:193], v[52:55]
	v_mfma_f32_16x16x32_bf16 v[36:39], v[182:185], v[190:193], v[36:39]
	v_mfma_f32_16x16x32_bf16 v[40:43], v[174:177], v[198:201], v[40:43]
	v_mfma_f32_16x16x32_bf16 v[32:35], v[182:185], v[198:201], v[32:35]
	v_mfma_f32_16x16x32_bf16 v[20:23], v[174:177], v[206:209], v[20:23]
	v_mfma_f32_16x16x32_bf16 v[16:19], v[182:185], v[206:209], v[16:19]
	v_mfma_f32_16x16x32_bf16 v[4:7], v[174:177], v[214:217], v[4:7]
	v_mfma_f32_16x16x32_bf16 v[0:3], v[182:185], v[214:217], v[0:3]
	v_mfma_f32_16x16x32_bf16 v[52:55], v[178:181], v[194:197], v[52:55]
	v_mfma_f32_16x16x32_bf16 v[36:39], v[186:189], v[194:197], v[36:39]
	v_mfma_f32_16x16x32_bf16 v[40:43], v[178:181], v[202:205], v[40:43]
	v_mfma_f32_16x16x32_bf16 v[32:35], v[186:189], v[202:205], v[32:35]
	v_mfma_f32_16x16x32_bf16 v[20:23], v[178:181], v[210:213], v[20:23]
	v_mfma_f32_16x16x32_bf16 v[16:19], v[186:189], v[210:213], v[16:19]
	v_mfma_f32_16x16x32_bf16 v[4:7], v[178:181], v[218:221], v[4:7]
	v_mfma_f32_16x16x32_bf16 v[0:3], v[186:189], v[218:221], v[0:3]
	s_setprio 0
	s_barrier
	s_add_u32 s72, s24, 0x80000
	s_addc_u32 s73, s25, 0
	s_mov_b32 m0, s60
	v_lshl_add_u64 v[174:175], s[72:73], 0, v[128:129]
	global_load_lds_dwordx4 v[174:175], off
	v_lshl_add_u64 v[174:175], s[72:73], 0, v[130:131]
	s_mov_b32 m0, s61
	s_nop 0
	global_load_lds_dwordx4 v[174:175], off
	s_waitcnt vmcnt(6)
	s_barrier
	s_setprio 1
	v_mfma_f32_16x16x32_bf16 v[60:63], v[222:225], v[190:193], v[60:63]
	v_mfma_f32_16x16x32_bf16 v[56:59], v[230:233], v[190:193], v[56:59]
	v_mfma_f32_16x16x32_bf16 v[48:51], v[222:225], v[198:201], v[48:51]
	v_mfma_f32_16x16x32_bf16 v[44:47], v[230:233], v[198:201], v[44:47]
	v_mfma_f32_16x16x32_bf16 v[28:31], v[222:225], v[206:209], v[28:31]
	v_mfma_f32_16x16x32_bf16 v[24:27], v[230:233], v[206:209], v[24:27]
	v_mfma_f32_16x16x32_bf16 v[12:15], v[222:225], v[214:217], v[12:15]
	v_mfma_f32_16x16x32_bf16 v[8:11], v[230:233], v[214:217], v[8:11]
	v_mfma_f32_16x16x32_bf16 v[60:63], v[226:229], v[194:197], v[60:63]
	v_mfma_f32_16x16x32_bf16 v[56:59], v[234:237], v[194:197], v[56:59]
	v_mfma_f32_16x16x32_bf16 v[48:51], v[226:229], v[202:205], v[48:51]
	v_mfma_f32_16x16x32_bf16 v[44:47], v[234:237], v[202:205], v[44:47]
	v_mfma_f32_16x16x32_bf16 v[28:31], v[226:229], v[210:213], v[28:31]
	v_mfma_f32_16x16x32_bf16 v[24:27], v[234:237], v[210:213], v[24:27]
	v_mfma_f32_16x16x32_bf16 v[12:15], v[226:229], v[218:221], v[12:15]
	v_mfma_f32_16x16x32_bf16 v[8:11], v[234:237], v[218:221], v[8:11]
	s_setprio 0
	v_add_u32_e32 v132, s62, v149
	s_barrier
	ds_read_b128 v[174:177], v132
	ds_read_b128 v[178:181], v132 offset:1024
	ds_read_b128 v[182:185], v132 offset:2048
	ds_read_b128 v[186:189], v132 offset:3072
	s_mov_b32 m0, s30
	v_cndmask_b32_e32 v132, v134, v170, vcc
	ds_read_b128 v[190:193], v167 offset:32768
	ds_read_b128 v[194:197], v167 offset:33792
	ds_read_b128 v[198:201], v167 offset:34816
	ds_read_b128 v[202:205], v167 offset:35840
	ds_read_b128 v[206:209], v167 offset:36864
	ds_read_b128 v[210:213], v167 offset:37888
	ds_read_b128 v[214:217], v167 offset:38912
	ds_read_b128 v[218:221], v167 offset:39936
	v_cndmask_b32_e32 v135, v138, v172, vcc
	global_load_lds_dwordx4 v132, s[0:1]
	s_mov_b32 m0, s31
	s_nop 0
	global_load_lds_dwordx4 v135, s[0:1]
	s_waitcnt lgkmcnt(8)
	s_barrier
; #define PG8_STAGE(bufoff, gbase, voff) do { _Pragma("unroll") for (int _i = 0; _i < 2; ++_i) \
;         __builtin_amdgcn_global_load_lds((const unsigned*)((const char*)(gbase) + (voff)[_i]), (LAS unsigned*)(lds + (bufoff) + ldsw + _i * 8192), 16, 0, 0); } while (0)
; #define PG8_LDA(dst, b, h) do { _Pragma("unroll") for (int m = 0; m < 4; ++m) _Pragma("unroll") for (int k = 0; k < 2; ++k) dst[m][k] = *(const LAS bf16x8*)(lds + PG8_SA(b, h) + aoff + m * 2048 + k * 1024); } while (0)
; #define PG8_LDB(dst, b, h) do { _Pragma("unroll") for (int n = 0; n < 2; ++n) _Pragma("unroll") for (int k = 0; k < 2; ++k) dst[n][k] = *(const LAS bf16x8*)(lds + PG8_SB(b, h) + boff + n * 2048 + k * 1024); } while (0)
; #define PG8_MMA(ai, bj, At, Bt) do { __builtin_amdgcn_s_setprio(1); _Pragma("unroll") for (int m = 0; m < 4; ++m) _Pragma("unroll") for (int n = 0; n < 2; ++n) _Pragma("unroll") for (int k = 0; k < 2; ++k) \
;         acc[ai][bj][m][n] = __builtin_amdgcn_mfma_f32_16x16x32_bf16(Bt[n][k], At[m][k], acc[ai][bj][m][n], 0, 0, 0); __builtin_amdgcn_s_setprio(0); } while (0)
; #define PG8_WAIT_V(n) asm volatile("s_waitcnt vmcnt(" #n ")" ::: "memory")
; #define PG8_WAIT_L(n) asm volatile("s_waitcnt lgkmcnt(" #n ")" ::: "memory")
; #define PG8_BAR __builtin_amdgcn_s_barrier()
; #define PG8_SCHED __builtin_amdgcn_sched_barrier(0)
; template <class Epi, class Sched>
; __device__ __forceinline__ void gemm_phase(LAS unsigned char* lds, const bf16_t* A, const int K, const Sched& S, const Epi& E, const int wv) {
;     ...
;             PG8_LDB(B0, 1, 0); PG8_SCHED; PG8_LDA(At, 1, 0); PG8_STAGE_A(PG8_SA(0, 1), 1, last, k2);
;             PG8_WAIT_L(8); PG8_BAR; PG8_WAIT_L(0); PG8_MMA(0, 0, At, B0); PG8_BAR; PG8_SCHED;
;             PG8_LDB(B1, 1, 1); PG8_STAGE(PG8_SB(1, 0), b3, voffB);
;             PG8_BAR; PG8_WAIT_L(0); PG8_MMA(0, 1, At, B1); PG8_BAR;
;             PG8_LDA(At, 1, 1); PG8_STAGE_A(PG8_SA(1, 0), 0, last, k3);
;             PG8_BAR; PG8_WAIT_L(0); PG8_MMA(1, 0, At, B0); PG8_BAR; PG8_SCHED;
;             PG8_STAGE(PG8_SB(1, 1), b3 + hstep, voffB);
;             PG8_WAIT_V(6); PG8_BAR; PG8_MMA(1, 1, At, B1); PG8_BAR;
;         }
	s_waitcnt lgkmcnt(0)
	s_setprio 1
	s_waitcnt lgkmcnt(0)
	v_mfma_f32_16x16x32_bf16 v[124:127], v[174:177], v[190:193], v[124:127]
	v_mfma_f32_16x16x32_bf16 v[120:123], v[182:185], v[190:193], v[120:123]
	v_mfma_f32_16x16x32_bf16 v[108:111], v[174:177], v[198:201], v[108:111]
	v_mfma_f32_16x16x32_bf16 v[104:107], v[182:185], v[198:201], v[104:107]
	v_mfma_f32_16x16x32_bf16 v[92:95], v[174:177], v[206:209], v[92:95]
	v_mfma_f32_16x16x32_bf16 v[88:91], v[182:185], v[206:209], v[88:91]
	v_mfma_f32_16x16x32_bf16 v[76:79], v[174:177], v[214:217], v[76:79]
	v_mfma_f32_16x16x32_bf16 v[72:75], v[182:185], v[214:217], v[72:75]
	v_mfma_f32_16x16x32_bf16 v[124:127], v[178:181], v[194:197], v[124:127]
	v_mfma_f32_16x16x32_bf16 v[120:123], v[186:189], v[194:197], v[120:123]
	v_mfma_f32_16x16x32_bf16 v[108:111], v[178:181], v[202:205], v[108:111]
	v_mfma_f32_16x16x32_bf16 v[104:107], v[186:189], v[202:205], v[104:107]
	v_mfma_f32_16x16x32_bf16 v[92:95], v[178:181], v[210:213], v[92:95]
	v_mfma_f32_16x16x32_bf16 v[88:91], v[186:189], v[210:213], v[88:91]
	v_mfma_f32_16x16x32_bf16 v[76:79], v[178:181], v[218:221], v[76:79]
	v_mfma_f32_16x16x32_bf16 v[72:75], v[186:189], v[218:221], v[72:75]
	s_setprio 0
	s_barrier
	s_mov_b32 m0, s64
	v_add_u32_e32 v132, s63, v149
	v_lshl_add_u64 v[238:239], v[238:239], 0, s[8:9]
	ds_read_b128 v[222:225], v132
	ds_read_b128 v[226:229], v132 offset:1024
	ds_read_b128 v[230:233], v132 offset:2048
	ds_read_b128 v[234:237], v132 offset:3072
	global_load_lds_dwordx4 v[238:239], off
	v_lshl_add_u64 v[238:239], v[240:241], 0, s[8:9]
	s_mov_b32 m0, s65
	s_nop 0
	global_load_lds_dwordx4 v[238:239], off
	s_barrier
	s_waitcnt lgkmcnt(0)
	s_setprio 1
	s_waitcnt lgkmcnt(0)
	v_mfma_f32_16x16x32_bf16 v[116:119], v[222:225], v[190:193], v[116:119]
	v_mfma_f32_16x16x32_bf16 v[112:115], v[230:233], v[190:193], v[112:115]
	v_mfma_f32_16x16x32_bf16 v[100:103], v[222:225], v[198:201], v[100:103]
	v_mfma_f32_16x16x32_bf16 v[96:99], v[230:233], v[198:201], v[96:99]
	v_mfma_f32_16x16x32_bf16 v[84:87], v[222:225], v[206:209], v[84:87]
	v_mfma_f32_16x16x32_bf16 v[80:83], v[230:233], v[206:209], v[80:83]
	v_mfma_f32_16x16x32_bf16 v[68:71], v[222:225], v[214:217], v[68:71]
	v_mfma_f32_16x16x32_bf16 v[64:67], v[230:233], v[214:217], v[64:67]
	v_mfma_f32_16x16x32_bf16 v[116:119], v[226:229], v[194:197], v[116:119]
	v_mfma_f32_16x16x32_bf16 v[112:115], v[234:237], v[194:197], v[112:115]
	v_mfma_f32_16x16x32_bf16 v[100:103], v[226:229], v[202:205], v[100:103]
	v_mfma_f32_16x16x32_bf16 v[96:99], v[234:237], v[202:205], v[96:99]
	v_mfma_f32_16x16x32_bf16 v[84:87], v[226:229], v[210:213], v[84:87]
	v_mfma_f32_16x16x32_bf16 v[80:83], v[234:237], v[210:213], v[80:83]
	v_mfma_f32_16x16x32_bf16 v[68:71], v[226:229], v[218:221], v[68:71]
	v_mfma_f32_16x16x32_bf16 v[64:67], v[234:237], v[218:221], v[64:67]
	s_setprio 0
	s_mov_b32 m0, s33
	v_lshl_add_u64 v[238:239], v[244:245], 0, s[8:9]
	s_barrier
	ds_read_b128 v[190:193], v167 offset:49152
	ds_read_b128 v[194:197], v167 offset:50176
	ds_read_b128 v[198:201], v167 offset:51200
	ds_read_b128 v[202:205], v167 offset:52224
	ds_read_b128 v[206:209], v167 offset:53248
	ds_read_b128 v[210:213], v167 offset:54272
	ds_read_b128 v[214:217], v167 offset:55296
	ds_read_b128 v[218:221], v167 offset:56320
	global_load_lds_dwordx4 v[238:239], off
	v_lshl_add_u64 v[238:239], v[242:243], 0, s[8:9]
	s_mov_b32 m0, s34
	s_nop 0
	global_load_lds_dwordx4 v[238:239], off
	s_barrier
	s_waitcnt lgkmcnt(0)
	s_setprio 1
	s_waitcnt lgkmcnt(0)
	v_mfma_f32_16x16x32_bf16 v[52:55], v[174:177], v[190:193], v[52:55]
	v_mfma_f32_16x16x32_bf16 v[36:39], v[182:185], v[190:193], v[36:39]
	v_mfma_f32_16x16x32_bf16 v[40:43], v[174:177], v[198:201], v[40:43]
	v_mfma_f32_16x16x32_bf16 v[32:35], v[182:185], v[198:201], v[32:35]
	v_mfma_f32_16x16x32_bf16 v[20:23], v[174:177], v[206:209], v[20:23]
	v_mfma_f32_16x16x32_bf16 v[16:19], v[182:185], v[206:209], v[16:19]
	v_mfma_f32_16x16x32_bf16 v[4:7], v[174:177], v[214:217], v[4:7]
	v_mfma_f32_16x16x32_bf16 v[0:3], v[182:185], v[214:217], v[0:3]
	v_mfma_f32_16x16x32_bf16 v[52:55], v[178:181], v[194:197], v[52:55]
	v_mfma_f32_16x16x32_bf16 v[36:39], v[186:189], v[194:197], v[36:39]
	v_mfma_f32_16x16x32_bf16 v[40:43], v[178:181], v[202:205], v[40:43]
	v_mfma_f32_16x16x32_bf16 v[32:35], v[186:189], v[202:205], v[32:35]
	v_mfma_f32_16x16x32_bf16 v[20:23], v[178:181], v[210:213], v[20:23]
	v_mfma_f32_16x16x32_bf16 v[16:19], v[186:189], v[210:213], v[16:19]
	v_mfma_f32_16x16x32_bf16 v[4:7], v[178:181], v[218:221], v[4:7]
	v_mfma_f32_16x16x32_bf16 v[0:3], v[186:189], v[218:221], v[0:3]
	s_setprio 0
	s_barrier
	s_add_u32 s0, s24, 0x80080
	s_addc_u32 s1, s25, 0
	s_mov_b32 m0, s66
	v_lshl_add_u64 v[174:175], s[0:1], 0, v[128:129]
	global_load_lds_dwordx4 v[174:175], off
	v_lshl_add_u64 v[174:175], s[0:1], 0, v[130:131]
	s_mov_b32 m0, s67
	s_nop 0
	global_load_lds_dwordx4 v[174:175], off
	s_waitcnt vmcnt(6)
	s_barrier
	s_setprio 1
	v_mfma_f32_16x16x32_bf16 v[60:63], v[222:225], v[190:193], v[60:63]
	v_mfma_f32_16x16x32_bf16 v[56:59], v[230:233], v[190:193], v[56:59]
	v_mfma_f32_16x16x32_bf16 v[48:51], v[222:225], v[198:201], v[48:51]
	v_mfma_f32_16x16x32_bf16 v[44:47], v[230:233], v[198:201], v[44:47]
	v_mfma_f32_16x16x32_bf16 v[28:31], v[222:225], v[206:209], v[28:31]
	v_mfma_f32_16x16x32_bf16 v[24:27], v[230:233], v[206:209], v[24:27]
	v_mfma_f32_16x16x32_bf16 v[12:15], v[222:225], v[214:217], v[12:15]
	v_mfma_f32_16x16x32_bf16 v[8:11], v[230:233], v[214:217], v[8:11]
	v_mfma_f32_16x16x32_bf16 v[60:63], v[226:229], v[194:197], v[60:63]
	v_mfma_f32_16x16x32_bf16 v[56:59], v[234:237], v[194:197], v[56:59]
	v_mfma_f32_16x16x32_bf16 v[48:51], v[226:229], v[202:205], v[48:51]
	v_mfma_f32_16x16x32_bf16 v[44:47], v[234:237], v[202:205], v[44:47]
	v_mfma_f32_16x16x32_bf16 v[28:31], v[226:229], v[210:213], v[28:31]
	v_mfma_f32_16x16x32_bf16 v[24:27], v[234:237], v[210:213], v[24:27]
	v_mfma_f32_16x16x32_bf16 v[12:15], v[226:229], v[218:221], v[12:15]
	v_mfma_f32_16x16x32_bf16 v[8:11], v[234:237], v[218:221], v[8:11]
	s_setprio 0
	s_add_i32 s70, s70, 2
	s_cmp_gt_u32 s70, 29
	s_mov_b64 s[0:1], s[22:23]
	s_cbranch_scc1 .Lmy_kx_6
	s_barrier
	s_branch .LBB0_2080

; #define PG8_WAIT_V(n) asm volatile("s_waitcnt vmcnt(" #n ")" ::: "memory")
; #define PG8_BAR __builtin_amdgcn_s_barrier()
; template <class Epi, class Sched>
; __device__ __forceinline__ void gemm_phase(LAS unsigned char* lds, const bf16_t* A, const int K, const Sched& S, const Epi& E, const int wv) {
;     ...
;     PG8_WAIT_V(0);
;     if (wr == 0) PG8_BAR;
;     PG8_BAR;
.LBB0_2097:
	s_waitcnt vmcnt(0)
	s_cmpk_gt_u32 s26, 0xff
	s_cbranch_scc1 .LBB0_2099
.LBB0_2099:
	s_barrier

; #define PG8_BAR __builtin_amdgcn_s_barrier()
; template <class Epi, class Sched>
; __device__ __forceinline__ void gemm_phase(LAS unsigned char* lds, const bf16_t* A, const int K, const Sched& S, const Epi& E, const int wv) {
;     int tid = mk_tid(wv); asm volatile("" : "+v"(tid));
;     const int wid = __builtin_amdgcn_readfirstlane(tid >> 6), lane = tid & 63, wr = wid >> 2, wc = wid & 3, fr = lane & 15, fq = lane >> 4;
;     const int nt = K / BK;
;     unsigned voffA[2], voffB[2];
; #pragma unroll
;     for (int i = 0; i < 2; ++i) { int R, C; stage_rc(tid * 16 + i * 8192, R, C); const int Rb = Epi::PERM ? ((R & ~31) + perm32(R & 31)) : R;
;         voffA[i] = (unsigned)(R * K + C) * 2u; voffB[i] = (unsigned)(Rb * K + C) * 2u; }
;     const size_t kstep = (size_t)(BK * 2);
;     const size_t hstep = (size_t)HALF * K * 2;
;     const size_t tstep = 2 * hstep;
;     const unsigned ldsw = (unsigned)wid * 1024u;
;     const int aoff = lds_byte(wr * 64 + fr, fq * 8), boff = lds_byte(wc * 32 + fr, fq * 8);
;     Unit cur, nxt; int ui = 0;
;     if (!S.next(0, cur)) return;
;     f32x4 acc[2][2][4][2];
; #pragma unroll
;     for (int a_ = 0; a_ < 2; ++a_)
; #pragma unroll
;         for (int b_ = 0; b_ < 2; ++b_)
; #pragma unroll
;             for (int m = 0; m < 4; ++m)
; #pragma unroll
;                 for (int n = 0; n < 2; ++n) acc[a_][b_][m][n] = (f32x4){0.f, 0.f, 0.f, 0.f};
;     bf16x8 At[4][2], B0[2][2], B1[2][2];
;     unsigned ao0[2] = {0u, 0u}, ao1[2] = {0u, 0u}, no0[2] = {0u, 0u}, no1[2] = {0u, 0u};
;     const char* Ab = (const char*)A;
;     const char* cA = Ab; const char* nA = Ab;
;     if constexpr (Sched::GATHER) {
; #pragma unroll
;         for (int i = 0; i < 2; ++i) { int R, C; stage_rc(tid * 16 + i * 8192, R, C);
;             ao0[i] = (S.arow(cur, R) * (unsigned)K + (unsigned)C) * 2u; ao1[i] = (S.arow(cur, HALF + R) * (unsigned)K + (unsigned)C) * 2u; }
;     } else cA = Ab + (size_t)cur.pm * tstep;
;     const char* cB = S.bptr(cur);
;     PG8_STAGE(PG8_SB(0, 0), cB, voffB); PG8_STAGE_A(PG8_SA(0, 0), 0, false, 0); PG8_STAGE(PG8_SB(0, 1), cB + hstep, voffB); PG8_STAGE_A(PG8_SA(0, 1), 1, false, 0);
;     if (wr == 1) PG8_BAR;
;     PG8_WAIT_V(4); PG8_BAR;
;     PG8_STAGE(PG8_SB(1, 0), cB + kstep, voffB); PG8_STAGE_A(PG8_SA(1, 0), 0, false, kstep); PG8_STAGE(PG8_SB(1, 1), cB + hstep + kstep, voffB);
;     PG8_WAIT_V(6); PG8_BAR;
.LBB0_2210:
	v_bfe_i32 v2, v4, 27, 1
	v_lshlrev_b32_e32 v0, 4, v4
	v_lshrrev_b32_e32 v2, 22, v2
	v_add_u32_e32 v2, v0, v2
	v_and_b32_e32 v2, 0xfffffc00, v2
	v_sub_u32_e32 v2, v0, v2
	v_ashrrev_i32_e32 v1, 31, v4
	v_lshrrev_b32_e32 v3, 4, v2
	v_lshrrev_b32_e32 v1, 26, v1
	v_bitop3_b32 v2, v3, v2, 32 bitop3:0x6c
	v_add_u32_e32 v1, v4, v1
	v_ashrrev_i32_e32 v5, 31, v2
	v_ashrrev_i32_e32 v1, 6, v1
	v_lshrrev_b32_e32 v5, 26, v5
	v_lshlrev_b32_e32 v3, 3, v1
	v_add_u32_e32 v5, v2, v5
	v_and_b32_e32 v3, -16, v3
	v_ashrrev_i32_e32 v6, 6, v5
	v_add_u32_e32 v144, v6, v3
	v_and_b32_e32 v3, 0xc0, v5
	v_sub_u32_e32 v2, v2, v3
	v_mov_b32_e32 v3, 1
	v_lshlrev_b32_e32 v1, 5, v1
	v_ashrrev_i16_sdwa v2, v3, sext(v2) dst_sel:DWORD dst_unused:UNUSED_PAD src0_sel:DWORD src1_sel:BYTE_0
	v_and_b32_e32 v1, 32, v1
	v_bfe_i32 v2, v2, 0, 16
	v_add_u32_e32 v0, 0x2000, v0
	v_add_lshl_u32 v146, v1, v2, 1
	v_ashrrev_i32_e32 v1, 31, v0
	v_lshrrev_b32_e32 v1, 22, v1
	v_add_u32_e32 v1, v0, v1
	v_ashrrev_i32_e32 v1, 10, v1
	v_mul_i32_i24_e32 v2, 0x400, v1
	v_lshlrev_b32_e32 v5, 1, v144
	v_lshrrev_b32_e32 v7, 2, v144
	v_and_b32_e32 v6, 3, v6
	s_mov_b32 s1, 0x1fffe0
	v_sub_u32_e32 v0, v0, v2
	v_and_b32_e32 v5, 24, v5
	v_and_b32_e32 v7, 4, v7
	v_and_or_b32 v6, v144, s1, v6
	v_lshrrev_b32_e32 v2, 4, v0
	v_or3_b32 v5, v6, v7, v5
	v_bitop3_b32 v0, v2, v0, 32 bitop3:0x6c
	v_lshl_add_u32 v128, v5, 11, v146
	v_ashrrev_i32_e32 v5, 31, v0
	v_lshrrev_b32_e32 v5, 26, v5
	v_lshlrev_b32_e32 v2, 3, v1
	v_add_u32_e32 v5, v0, v5
	s_add_u32 s2, s76, 0x52188000
	v_and_b32_e32 v2, -16, v2
	v_ashrrev_i32_e32 v6, 6, v5
	v_lshlrev_b32_e32 v1, 5, v1
	s_addc_u32 s3, s77, 0
	v_add_u32_e32 v147, v6, v2
	v_and_b32_e32 v7, 32, v1
	v_and_b32_e32 v1, 0xc0, v5
	v_and_b32_e32 v2, 3, v6
	s_ashr_i32 s8, s26, 6
	s_ashr_i32 s0, s26, 8
	v_sub_u32_e32 v0, v0, v1
	v_and_or_b32 v2, v147, s1, v2
	s_lshl_b32 s1, s8, 10
	v_ashrrev_i16_sdwa v0, v3, sext(v0) dst_sel:DWORD dst_unused:UNUSED_PAD src0_sel:DWORD src1_sel:BYTE_0
	s_add_u32 s27, s76, 0x2c188000
	v_bfe_i32 v5, v0, 0, 16
	v_lshlrev_b32_e32 v0, 1, v147
	v_lshrrev_b32_e32 v1, 2, v147
	s_addc_u32 s28, s77, 0
	s_ashr_i32 s13, s12, 31
	v_and_b32_e32 v0, 24, v0
	v_and_b32_e32 v1, 4, v1
	s_add_i32 s14, 0, 0x20800
	s_lshl_b64 s[10:11], s[12:13], 19
	v_or3_b32 v6, v2, v1, v0
	v_lshl_add_u32 v0, v144, 2, s14
	s_add_u32 s9, s27, s10
	ds_read2st64_b32 v[0:1], v0 offset1:2
	v_lshl_add_u32 v2, v147, 2, s14
	s_addc_u32 s10, s28, s11
	ds_read2st64_b32 v[2:3], v2 offset1:2
	s_add_u32 s22, s9, s6
	s_addc_u32 s23, s10, s7
	s_add_i32 s13, s1, 0
	v_add_lshl_u32 v148, v7, v5, 1
	s_add_i32 m0, s13, 0x10000
	v_lshl_add_u32 v130, v6, 11, v148
	global_load_lds_dwordx4 v128, s[22:23]
	s_add_i32 m0, s13, 0x12000
	s_waitcnt lgkmcnt(0)
	v_lshl_add_u32 v132, v0, 11, v146
	global_load_lds_dwordx4 v130, s[22:23]
	s_mov_b32 m0, s13
	s_add_i32 s29, s13, 0x2000
	v_lshl_add_u32 v134, v2, 11, v148
	global_load_lds_dwordx4 v132, s[2:3]
	s_mov_b32 m0, s29
	s_add_u32 s6, s22, 0x40000
	global_load_lds_dwordx4 v134, s[2:3]
	s_addc_u32 s7, s23, 0
	s_add_i32 m0, s13, 0x14000
	s_add_i32 s30, s13, 0x4000
	global_load_lds_dwordx4 v128, s[6:7]
	s_add_i32 m0, s13, 0x16000
	v_lshl_add_u32 v136, v1, 11, v146
	global_load_lds_dwordx4 v130, s[6:7]
	s_mov_b32 m0, s30
	s_add_i32 s31, s13, 0x6000
	v_lshl_add_u32 v138, v3, 11, v148
	global_load_lds_dwordx4 v136, s[2:3]
	s_mov_b32 m0, s31
	v_mov_b32_e32 v133, 0
	global_load_lds_dwordx4 v138, s[2:3]
	v_mov_b32_e32 v129, v133
	v_mov_b32_e32 v131, v133
	s_mov_b32 s33, 0
	v_lshl_add_u64 v[2:3], s[22:23], 0, v[128:129]
	v_lshl_add_u64 v[0:1], s[22:23], 0, v[130:131]
	s_cmp_lg_u32 s0, 1
	v_mov_b32_e32 v135, v133
	s_cbranch_scc1 .LBB0_2212
.LBB0_2212:
	s_add_u32 s6, s76, 0x56188000
	s_addc_u32 s7, s77, 0
	s_lshl_b32 s8, s8, 5
	s_and_b32 s18, s8, 0x60
	s_mov_b64 s[8:9], 0x80
	s_add_i32 m0, s13, 0x18000
	v_lshl_add_u64 v[2:3], v[2:3], 0, s[8:9]
	s_lshl_b32 s15, s0, 13
	s_lshl_b32 s19, s18, 7
	s_waitcnt vmcnt(4)
	s_barrier
	global_load_lds_dwordx4 v[2:3], off
	s_add_i32 m0, s13, 0x1a000
	s_add_u32 s10, s76, 0x52188080
	v_lshl_add_u64 v[0:1], v[0:1], 0, s[8:9]
	s_addc_u32 s11, s77, 0
	s_add_i32 s34, s13, 0x8000
	s_add_i32 s35, s13, 0xa000
	global_load_lds_dwordx4 v[0:1], off
	v_lshl_add_u64 v[0:1], s[10:11], 0, v[132:133]
	s_mov_b32 m0, s34
	s_add_u32 s16, s22, 0x40080
	global_load_lds_dwordx4 v[0:1], off
	v_lshl_add_u64 v[0:1], s[10:11], 0, v[134:135]
	s_mov_b32 m0, s35
	s_addc_u32 s17, s23, 0
	global_load_lds_dwordx4 v[0:1], off
	s_add_i32 m0, s13, 0x1c000
	v_lshl_add_u64 v[0:1], s[16:17], 0, v[128:129]
	global_load_lds_dwordx4 v[0:1], off
	v_lshl_add_u64 v[0:1], s[16:17], 0, v[130:131]
	s_add_i32 m0, s13, 0x1e000
	s_add_i32 s52, 0, 0x10000
	global_load_lds_dwordx4 v[0:1], off
	v_lshrrev_b32_e32 v1, 1, v4
	v_and_b32_e32 v0, 15, v4
	v_and_b32_e32 v1, 24, v1
	v_lshl_or_b32 v149, s0, 6, v0
	v_lshlrev_b32_e32 v2, 1, v1
	v_lshl_or_b32 v0, v0, 6, v2
	v_lshlrev_b32_e32 v2, 2, v149
	v_and_b32_e32 v3, 32, v2
	v_lshlrev_b32_e32 v4, 2, v4
	s_waitcnt vmcnt(6)
	s_add_i32 s53, 0, 0x14000
	s_add_i32 s60, 0, 0x18000
	s_add_i32 s61, 0, 0x1c000
	v_bitop3_b32 v3, v0, s15, v3 bitop3:0xde
	v_and_b32_e32 v4, 32, v4
	v_or_b32_e32 v152, 16, v149
	v_or_b32_e32 v153, 32, v149
	v_or_b32_e32 v154, 48, v149
	v_add_u32_e32 v155, 0x80, v149
	v_add_u32_e32 v156, 0x90, v149
	v_add_u32_e32 v157, 0xa0, v149
	v_add_u32_e32 v158, 0xb0, v149
	s_add_i32 s0, 0, 0x20480
	s_add_i32 s56, s52, s1
	s_add_i32 s58, s53, s1
	s_add_i32 s62, s60, s1
	s_add_i32 s64, s61, s1
	v_bitop3_b32 v150, v0, s19, v4 bitop3:0xde
	v_add_u32_e32 v151, s14, v2
	v_or_b32_e32 v159, s18, v1
	v_lshl_add_u32 v160, v152, 2, s14
	v_lshl_add_u32 v161, v153, 2, s14
	v_lshl_add_u32 v162, v154, 2, s14
	v_lshl_add_u32 v163, v155, 2, s14
	v_lshl_add_u32 v164, v156, 2, s14
	v_lshl_add_u32 v165, v157, 2, s14
	v_lshl_add_u32 v166, v158, 2, s14
	v_mov_b32_e32 v167, s0
	s_add_i32 s36, 0, 0x20404
	s_add_i32 s37, 0, 0x2040c
	s_add_i32 s38, 0, 0x20414
	s_add_i32 s39, 0, 0x2041c
	s_add_i32 s40, 0, 0x20424
	s_add_i32 s41, 0, 0x2042c
	s_add_i32 s42, 0, 0x20434
	s_add_i32 s43, 0, 0x2043c
	s_add_i32 s44, 0, 0x20444
	s_add_i32 s45, 0, 0x2044c
	s_add_i32 s46, 0, 0x20454
	s_add_i32 s47, 0, 0x2045c
	s_add_i32 s48, 0, 0x20464
	s_add_i32 s49, 0, 0x2046c
	s_add_i32 s50, 0, 0x20474
	s_add_i32 s51, 0, 0x2047c
	v_add_u32_e32 v168, 0, v3
	s_add_i32 s54, s13, 0xc000
	s_add_i32 s55, s13, 0xe000
	s_add_i32 s57, s56, 0x2000
	s_add_i32 s59, s58, 0x2000
	s_add_i32 s63, s62, 0x2000
	s_add_i32 s65, s64, 0x2000
	v_mov_b32_e32 v135, v132
	s_mov_b32 s66, 0
	s_barrier
	s_branch .LBB0_2214

;     __device__ __forceinline__ const char* bptr(const Unit& u) const { return (const char*)Bt + (size_t)u.pn * 256 * K * 2; }
;     __device__ __forceinline__ unsigned arow(const Unit& u, int r) const { return (unsigned)(u.pm * 256 + r); }
; #define PG8_LDA(dst, b, h) do { _Pragma("unroll") for (int m = 0; m < 4; ++m) _Pragma("unroll") for (int k = 0; k < 2; ++k) dst[m][k] = *(const LAS bf16x8*)(lds + PG8_SA(b, h) + aoff + m * 2048 + k * 1024); } while (0)
; #define PG8_WAIT_L(n) asm volatile("s_waitcnt lgkmcnt(" #n ")" ::: "memory")
; template <class Epi, class Sched>
; __device__ __forceinline__ void gemm_phase(LAS unsigned char* lds, const bf16_t* A, const int K, const Sched& S, const Epi& E, const int wv) {
;     ...
;         const bool has_next = S.next(ui + 1, nxt);
;         const char* nB = has_next ? S.bptr(nxt) : cB;
;         if constexpr (Sched::GATHER) {
;             if (has_next) {
; #pragma unroll
;                 for (int i = 0; i < 2; ++i) { int R, C; stage_rc(tid * 16 + i * 8192, R, C);
;                     no0[i] = (S.arow(nxt, R) * (unsigned)K + (unsigned)C) * 2u; no1[i] = (S.arow(nxt, HALF + R) * (unsigned)K + (unsigned)C) * 2u; }
;             } else {
; #pragma unroll
;                 for (int i = 0; i < 2; ++i) { no0[i] = ao0[i]; no1[i] = ao1[i]; }
;             }
;             asm volatile("s_waitcnt lgkmcnt(0)" ::: "memory");
;             asm volatile("" : "+v"(no0[0]), "+v"(no0[1]), "+v"(no1[0]), "+v"(no1[1]));
;         } else nA = has_next ? Ab + (size_t)nxt.pm * tstep : cA;
;         for (int t = 0; t < nt; t += 2) {
;             const bool last = (t == nt - 2);
;             const size_t k1 = (size_t)(t + 1) * kstep;
;             const size_t k2 = last ? 0 : (size_t)(t + 2) * kstep, k3 = k2 + kstep;
;             const char* b2 = last ? nB : cB + (size_t)(t + 2) * kstep; const char* b3 = b2 + kstep;
;             PG8_LDB(B0, 0, 0); PG8_SCHED; PG8_LDA(At, 0, 0); PG8_STAGE_A(PG8_SA(1, 1), 1, false, k1);
;             PG8_WAIT_L(8); PG8_BAR; PG8_WAIT_L(0); PG8_MMA(0, 0, At, B0); PG8_BAR; PG8_SCHED;
;     ...
; #pragma unroll
;         for (int a_ = 0; a_ < 2; ++a_)
; #pragma unroll
;             for (int b_ = 0; b_ < 2; ++b_)
; #pragma unroll
;                 for (int m = 0; m < 4; ++m)
; #pragma unroll
;                     for (int n = 0; n < 2; ++n) acc[a_][b_][m][n] = (f32x4){0.f, 0.f, 0.f, 0.f};
.LBB0_2220:
	s_waitcnt lgkmcnt(0)
	v_mov_b32_e32 v137, v133
	v_mov_b32_e32 v139, v133
	s_add_u32 s17, s22, 0x100
	v_mov_b32_e32 v8, 0
	s_addc_u32 s19, s23, 0
	v_lshl_add_u64 v[140:141], s[10:11], 0, v[138:139]
	v_lshl_add_u64 v[142:143], s[10:11], 0, v[136:137]
	s_mov_b32 s68, -2
	s_mov_b64 s[0:1], 0
	v_mov_b32_e32 v9, v8
	v_mov_b32_e32 v10, v8
	v_mov_b32_e32 v11, v8
	v_mov_b32_e32 v20, v8
	v_mov_b32_e32 v21, v8
	v_mov_b32_e32 v22, v8
	v_mov_b32_e32 v23, v8
	v_mov_b32_e32 v48, v8
	v_mov_b32_e32 v49, v8
	v_mov_b32_e32 v50, v8
	v_mov_b32_e32 v51, v8
	v_mov_b32_e32 v52, v8
	v_mov_b32_e32 v53, v8
	v_mov_b32_e32 v54, v8
	v_mov_b32_e32 v55, v8
	v_mov_b32_e32 v72, v8
	v_mov_b32_e32 v73, v8
	v_mov_b32_e32 v74, v8
	v_mov_b32_e32 v75, v8
	v_mov_b32_e32 v80, v8
	v_mov_b32_e32 v81, v8
	v_mov_b32_e32 v82, v8
	v_mov_b32_e32 v83, v8
	v_mov_b32_e32 v88, v8
	v_mov_b32_e32 v89, v8
	v_mov_b32_e32 v90, v8
	v_mov_b32_e32 v91, v8
	v_mov_b32_e32 v96, v8
	v_mov_b32_e32 v97, v8
	v_mov_b32_e32 v98, v8
	v_mov_b32_e32 v99, v8
	v_mov_b32_e32 v104, v8
	v_mov_b32_e32 v105, v8
	v_mov_b32_e32 v106, v8
	v_mov_b32_e32 v107, v8
	v_mov_b32_e32 v112, v8
	v_mov_b32_e32 v113, v8
	v_mov_b32_e32 v114, v8
	v_mov_b32_e32 v115, v8
	v_mov_b32_e32 v76, v8
	v_mov_b32_e32 v77, v8
	v_mov_b32_e32 v78, v8
	v_mov_b32_e32 v79, v8
	v_mov_b32_e32 v84, v8
	v_mov_b32_e32 v85, v8
	v_mov_b32_e32 v86, v8
	v_mov_b32_e32 v87, v8
	v_mov_b32_e32 v92, v8
	v_mov_b32_e32 v93, v8
	v_mov_b32_e32 v94, v8
	v_mov_b32_e32 v95, v8
	v_mov_b32_e32 v100, v8
	v_mov_b32_e32 v101, v8
	v_mov_b32_e32 v102, v8
	v_mov_b32_e32 v103, v8
	v_mov_b32_e32 v108, v8
	v_mov_b32_e32 v109, v8
	v_mov_b32_e32 v110, v8
	v_mov_b32_e32 v111, v8
	v_mov_b32_e32 v116, v8
	v_mov_b32_e32 v117, v8
	v_mov_b32_e32 v118, v8
	v_mov_b32_e32 v119, v8
	v_mov_b32_e32 v120, v8
	v_mov_b32_e32 v121, v8
	v_mov_b32_e32 v122, v8
	v_mov_b32_e32 v123, v8
	v_mov_b32_e32 v124, v8
	v_mov_b32_e32 v125, v8
	v_mov_b32_e32 v126, v8
	v_mov_b32_e32 v127, v8
	v_mov_b32_e32 v40, v8
	v_mov_b32_e32 v41, v8
	v_mov_b32_e32 v42, v8
	v_mov_b32_e32 v43, v8
	v_mov_b32_e32 v44, v8
	v_mov_b32_e32 v45, v8
	v_mov_b32_e32 v46, v8
	v_mov_b32_e32 v47, v8
	v_mov_b32_e32 v24, v8
	v_mov_b32_e32 v25, v8
	v_mov_b32_e32 v26, v8
	v_mov_b32_e32 v27, v8
	v_mov_b32_e32 v28, v8
	v_mov_b32_e32 v29, v8
	v_mov_b32_e32 v30, v8
	v_mov_b32_e32 v31, v8
	v_mov_b32_e32 v0, v8
	v_mov_b32_e32 v1, v8
	v_mov_b32_e32 v2, v8
	v_mov_b32_e32 v3, v8
	v_mov_b32_e32 v4, v8
	v_mov_b32_e32 v5, v8
	v_mov_b32_e32 v6, v8
	v_mov_b32_e32 v7, v8
	v_mov_b32_e32 v64, v8
	v_mov_b32_e32 v65, v8
	v_mov_b32_e32 v66, v8
	v_mov_b32_e32 v67, v8
	v_mov_b32_e32 v68, v8
	v_mov_b32_e32 v69, v8
	v_mov_b32_e32 v70, v8
	v_mov_b32_e32 v71, v8
	v_mov_b32_e32 v56, v8
	v_mov_b32_e32 v57, v8
	v_mov_b32_e32 v58, v8
	v_mov_b32_e32 v59, v8
	v_mov_b32_e32 v60, v8
	v_mov_b32_e32 v61, v8
	v_mov_b32_e32 v62, v8
	v_mov_b32_e32 v63, v8
	v_mov_b32_e32 v32, v8
	v_mov_b32_e32 v33, v8
	v_mov_b32_e32 v34, v8
	v_mov_b32_e32 v35, v8
	v_mov_b32_e32 v36, v8
	v_mov_b32_e32 v37, v8
	v_mov_b32_e32 v38, v8
	v_mov_b32_e32 v39, v8
	v_mov_b32_e32 v12, v8
	v_mov_b32_e32 v13, v8
	v_mov_b32_e32 v14, v8
	v_mov_b32_e32 v15, v8
	v_mov_b32_e32 v16, v8
	v_mov_b32_e32 v17, v8
	v_mov_b32_e32 v18, v8
	v_mov_b32_e32 v19, v8
	s_bitcmp1_b32 s92, 8
	s_cbranch_scc0 .Lmy_ph_7
	s_barrier
.Lmy_ph_7:
.LBB0_2221:
	v_add_u32_e32 v132, s52, v150
	s_add_u32 s22, s0, 0x100
	ds_read_b128 v[174:177], v132
	ds_read_b128 v[178:181], v132 offset:1024
	ds_read_b128 v[182:185], v132 offset:2048
	ds_read_b128 v[186:189], v132 offset:3072
	s_addc_u32 s23, s1, 0
	s_add_u32 s69, s17, s0
	s_addc_u32 s70, s19, s1
	s_cmpk_eq_i32 s0, 0x700
	s_cselect_b64 vcc, -1, 0
	s_and_b64 s[24:25], vcc, exec
	s_cselect_b32 s71, 0, s22
	s_cselect_b32 s25, s21, s70
	s_cselect_b32 s24, s20, s69
	s_mov_b32 m0, s54
	v_lshl_add_u64 v[222:223], v[142:143], 0, s[0:1]
	ds_read_b128 v[190:193], v168
	ds_read_b128 v[194:197], v168 offset:1024
	ds_read_b128 v[198:201], v168 offset:2048
	ds_read_b128 v[202:205], v168 offset:3072
	ds_read_b128 v[206:209], v168 offset:4096
	ds_read_b128 v[210:213], v168 offset:5120
	ds_read_b128 v[214:217], v168 offset:6144
	ds_read_b128 v[218:221], v168 offset:7168
	global_load_lds_dwordx4 v[222:223], off
	v_lshl_add_u64 v[222:223], v[140:141], 0, s[0:1]
	s_mov_b32 m0, s55
	s_nop 0
	global_load_lds_dwordx4 v[222:223], off
	s_waitcnt lgkmcnt(8)
	s_barrier
	s_waitcnt lgkmcnt(0)
	s_setprio 1
	s_waitcnt lgkmcnt(0)
	v_mfma_f32_16x16x32_bf16 v[124:127], v[174:177], v[190:193], v[124:127]
	v_mfma_f32_16x16x32_bf16 v[120:123], v[182:185], v[190:193], v[120:123]
	v_mfma_f32_16x16x32_bf16 v[116:119], v[174:177], v[198:201], v[116:119]
	v_mfma_f32_16x16x32_bf16 v[108:111], v[182:185], v[198:201], v[108:111]
	v_mfma_f32_16x16x32_bf16 v[100:103], v[174:177], v[206:209], v[100:103]
	v_mfma_f32_16x16x32_bf16 v[92:95], v[182:185], v[206:209], v[92:95]
	v_mfma_f32_16x16x32_bf16 v[84:87], v[174:177], v[214:217], v[84:87]
	v_mfma_f32_16x16x32_bf16 v[76:79], v[182:185], v[214:217], v[76:79]
	v_mfma_f32_16x16x32_bf16 v[124:127], v[178:181], v[194:197], v[124:127]
	v_mfma_f32_16x16x32_bf16 v[120:123], v[186:189], v[194:197], v[120:123]
	v_mfma_f32_16x16x32_bf16 v[116:119], v[178:181], v[202:205], v[116:119]
	v_mfma_f32_16x16x32_bf16 v[108:111], v[186:189], v[202:205], v[108:111]
	v_mfma_f32_16x16x32_bf16 v[100:103], v[178:181], v[210:213], v[100:103]
	v_mfma_f32_16x16x32_bf16 v[92:95], v[186:189], v[210:213], v[92:95]
	v_mfma_f32_16x16x32_bf16 v[84:87], v[178:181], v[218:221], v[84:87]
	v_mfma_f32_16x16x32_bf16 v[76:79], v[186:189], v[218:221], v[76:79]
	s_setprio 0
	s_barrier
; #define PG8_STAGE(bufoff, gbase, voff) do { _Pragma("unroll") for (int _i = 0; _i < 2; ++_i) \
;         __builtin_amdgcn_global_load_lds((const unsigned*)((const char*)(gbase) + (voff)[_i]), (LAS unsigned*)(lds + (bufoff) + ldsw + _i * 8192), 16, 0, 0); } while (0)
; #define PG8_LDA(dst, b, h) do { _Pragma("unroll") for (int m = 0; m < 4; ++m) _Pragma("unroll") for (int k = 0; k < 2; ++k) dst[m][k] = *(const LAS bf16x8*)(lds + PG8_SA(b, h) + aoff + m * 2048 + k * 1024); } while (0)
; #define PG8_LDB(dst, b, h) do { _Pragma("unroll") for (int n = 0; n < 2; ++n) _Pragma("unroll") for (int k = 0; k < 2; ++k) dst[n][k] = *(const LAS bf16x8*)(lds + PG8_SB(b, h) + boff + n * 2048 + k * 1024); } while (0)
; #define PG8_MMA(ai, bj, At, Bt) do { __builtin_amdgcn_s_setprio(1); _Pragma("unroll") for (int m = 0; m < 4; ++m) _Pragma("unroll") for (int n = 0; n < 2; ++n) _Pragma("unroll") for (int k = 0; k < 2; ++k) \
;         acc[ai][bj][m][n] = __builtin_amdgcn_mfma_f32_16x16x32_bf16(Bt[n][k], At[m][k], acc[ai][bj][m][n], 0, 0, 0); __builtin_amdgcn_s_setprio(0); } while (0)
; #define PG8_WAIT_V(n) asm volatile("s_waitcnt vmcnt(" #n ")" ::: "memory")
; #define PG8_WAIT_L(n) asm volatile("s_waitcnt lgkmcnt(" #n ")" ::: "memory")
; #define PG8_BAR __builtin_amdgcn_s_barrier()
; #define PG8_SCHED __builtin_amdgcn_sched_barrier(0)
; template <class Epi, class Sched>
; __device__ __forceinline__ void gemm_phase(LAS unsigned char* lds, const bf16_t* A, const int K, const Sched& S, const Epi& E, const int wv) {
;     ...
;             PG8_LDB(B1, 0, 1); PG8_STAGE(PG8_SB(0, 0), b2, voffB);
;             PG8_BAR; PG8_WAIT_L(0); PG8_MMA(0, 1, At, B1); PG8_BAR;
;             PG8_LDA(At, 0, 1); PG8_STAGE_A(PG8_SA(0, 0), 0, last, k2);
;             PG8_BAR; PG8_WAIT_L(0); PG8_MMA(1, 0, At, B0); PG8_BAR; PG8_SCHED;
;             PG8_STAGE(PG8_SB(0, 1), b2 + hstep, voffB);
;             PG8_WAIT_V(6); PG8_BAR; PG8_MMA(1, 1, At, B1); PG8_BAR;
;             PG8_LDB(B0, 1, 0); PG8_SCHED; PG8_LDA(At, 1, 0); PG8_STAGE_A(PG8_SA(0, 1), 1, last, k2);
;             PG8_WAIT_L(8); PG8_BAR; PG8_WAIT_L(0); PG8_MMA(0, 0, At, B0); PG8_BAR; PG8_SCHED;
;             PG8_LDB(B1, 1, 1); PG8_STAGE(PG8_SB(1, 0), b3, voffB);
	s_mov_b32 m0, s56
	v_add_u32_e32 v132, s53, v150
	v_lshl_add_u64 v[238:239], s[24:25], 0, v[128:129]
	ds_read_b128 v[222:225], v132
	ds_read_b128 v[226:229], v132 offset:1024
	ds_read_b128 v[230:233], v132 offset:2048
	ds_read_b128 v[234:237], v132 offset:3072
	global_load_lds_dwordx4 v[238:239], off
	v_lshl_add_u64 v[240:241], s[24:25], 0, v[130:131]
	s_mov_b32 m0, s57
	s_nop 0
	global_load_lds_dwordx4 v[240:241], off
	s_barrier
	s_waitcnt lgkmcnt(0)
	s_setprio 1
	s_waitcnt lgkmcnt(0)
	v_mfma_f32_16x16x32_bf16 v[112:115], v[222:225], v[190:193], v[112:115]
	v_mfma_f32_16x16x32_bf16 v[104:107], v[230:233], v[190:193], v[104:107]
	v_mfma_f32_16x16x32_bf16 v[96:99], v[222:225], v[198:201], v[96:99]
	v_mfma_f32_16x16x32_bf16 v[88:91], v[230:233], v[198:201], v[88:91]
	v_mfma_f32_16x16x32_bf16 v[80:83], v[222:225], v[206:209], v[80:83]
	v_mfma_f32_16x16x32_bf16 v[72:75], v[230:233], v[206:209], v[72:75]
	v_mfma_f32_16x16x32_bf16 v[52:55], v[222:225], v[214:217], v[52:55]
	v_mfma_f32_16x16x32_bf16 v[48:51], v[230:233], v[214:217], v[48:51]
	v_mfma_f32_16x16x32_bf16 v[112:115], v[226:229], v[194:197], v[112:115]
	v_mfma_f32_16x16x32_bf16 v[104:107], v[234:237], v[194:197], v[104:107]
	v_mfma_f32_16x16x32_bf16 v[96:99], v[226:229], v[202:205], v[96:99]
	v_mfma_f32_16x16x32_bf16 v[88:91], v[234:237], v[202:205], v[88:91]
	v_mfma_f32_16x16x32_bf16 v[80:83], v[226:229], v[210:213], v[80:83]
	v_mfma_f32_16x16x32_bf16 v[72:75], v[234:237], v[210:213], v[72:75]
	v_mfma_f32_16x16x32_bf16 v[52:55], v[226:229], v[218:221], v[52:55]
	v_mfma_f32_16x16x32_bf16 v[48:51], v[234:237], v[218:221], v[48:51]
	s_setprio 0
	s_add_u32 s0, s2, s71
	s_mov_b32 m0, s13
	s_addc_u32 s1, s3, 0
	v_cndmask_b32_e32 v132, v135, v170, vcc
	s_barrier
	ds_read_b128 v[190:193], v168 offset:16384
	ds_read_b128 v[194:197], v168 offset:17408
	ds_read_b128 v[198:201], v168 offset:18432
	ds_read_b128 v[202:205], v168 offset:19456
	ds_read_b128 v[206:209], v168 offset:20480
	ds_read_b128 v[210:213], v168 offset:21504
	ds_read_b128 v[214:217], v168 offset:22528
	ds_read_b128 v[218:221], v168 offset:23552
	v_cndmask_b32_e32 v242, v134, v172, vcc
	global_load_lds_dwordx4 v132, s[0:1]
	s_mov_b32 m0, s29
	v_mov_b32_e32 v243, v133
	global_load_lds_dwordx4 v242, s[0:1]
	s_barrier
	s_waitcnt lgkmcnt(0)
	v_lshl_add_u64 v[244:245], s[0:1], 0, v[132:133]
	v_lshl_add_u64 v[242:243], s[0:1], 0, v[242:243]
	s_setprio 1
	s_waitcnt lgkmcnt(0)
	v_mfma_f32_16x16x32_bf16 v[20:23], v[174:177], v[190:193], v[20:23]
	v_mfma_f32_16x16x32_bf16 v[8:11], v[182:185], v[190:193], v[8:11]
	v_mfma_f32_16x16x32_bf16 v[40:43], v[174:177], v[198:201], v[40:43]
	v_mfma_f32_16x16x32_bf16 v[44:47], v[182:185], v[198:201], v[44:47]
	v_mfma_f32_16x16x32_bf16 v[24:27], v[174:177], v[206:209], v[24:27]
	v_mfma_f32_16x16x32_bf16 v[28:31], v[182:185], v[206:209], v[28:31]
	v_mfma_f32_16x16x32_bf16 v[0:3], v[174:177], v[214:217], v[0:3]
	v_mfma_f32_16x16x32_bf16 v[4:7], v[182:185], v[214:217], v[4:7]
	v_mfma_f32_16x16x32_bf16 v[20:23], v[178:181], v[194:197], v[20:23]
	v_mfma_f32_16x16x32_bf16 v[8:11], v[186:189], v[194:197], v[8:11]
	v_mfma_f32_16x16x32_bf16 v[40:43], v[178:181], v[202:205], v[40:43]
	v_mfma_f32_16x16x32_bf16 v[44:47], v[186:189], v[202:205], v[44:47]
	v_mfma_f32_16x16x32_bf16 v[24:27], v[178:181], v[210:213], v[24:27]
	v_mfma_f32_16x16x32_bf16 v[28:31], v[186:189], v[210:213], v[28:31]
	v_mfma_f32_16x16x32_bf16 v[0:3], v[178:181], v[218:221], v[0:3]
	v_mfma_f32_16x16x32_bf16 v[4:7], v[186:189], v[218:221], v[4:7]
	s_setprio 0
	s_barrier
	s_add_u32 s70, s24, 0x40000
	s_addc_u32 s71, s25, 0
	s_mov_b32 m0, s58
	v_lshl_add_u64 v[174:175], s[70:71], 0, v[128:129]
	global_load_lds_dwordx4 v[174:175], off
	v_lshl_add_u64 v[174:175], s[70:71], 0, v[130:131]
	s_mov_b32 m0, s59
	s_nop 0
	global_load_lds_dwordx4 v[174:175], off
	s_waitcnt vmcnt(6)
	s_barrier
	s_setprio 1
	v_mfma_f32_16x16x32_bf16 v[64:67], v[222:225], v[190:193], v[64:67]
	v_mfma_f32_16x16x32_bf16 v[68:71], v[230:233], v[190:193], v[68:71]
	v_mfma_f32_16x16x32_bf16 v[56:59], v[222:225], v[198:201], v[56:59]
	v_mfma_f32_16x16x32_bf16 v[60:63], v[230:233], v[198:201], v[60:63]
	v_mfma_f32_16x16x32_bf16 v[32:35], v[222:225], v[206:209], v[32:35]
	v_mfma_f32_16x16x32_bf16 v[36:39], v[230:233], v[206:209], v[36:39]
	v_mfma_f32_16x16x32_bf16 v[12:15], v[222:225], v[214:217], v[12:15]
	v_mfma_f32_16x16x32_bf16 v[16:19], v[230:233], v[214:217], v[16:19]
	v_mfma_f32_16x16x32_bf16 v[64:67], v[226:229], v[194:197], v[64:67]
	v_mfma_f32_16x16x32_bf16 v[68:71], v[234:237], v[194:197], v[68:71]
	v_mfma_f32_16x16x32_bf16 v[56:59], v[226:229], v[202:205], v[56:59]
	v_mfma_f32_16x16x32_bf16 v[60:63], v[234:237], v[202:205], v[60:63]
	v_mfma_f32_16x16x32_bf16 v[32:35], v[226:229], v[210:213], v[32:35]
	v_mfma_f32_16x16x32_bf16 v[36:39], v[234:237], v[210:213], v[36:39]
	v_mfma_f32_16x16x32_bf16 v[12:15], v[226:229], v[218:221], v[12:15]
	v_mfma_f32_16x16x32_bf16 v[16:19], v[234:237], v[218:221], v[16:19]
	s_setprio 0
	v_add_u32_e32 v132, s60, v150
	s_barrier
	ds_read_b128 v[174:177], v132
	ds_read_b128 v[178:181], v132 offset:1024
	ds_read_b128 v[182:185], v132 offset:2048
	ds_read_b128 v[186:189], v132 offset:3072
	s_mov_b32 m0, s30
	v_cndmask_b32_e32 v132, v136, v171, vcc
	ds_read_b128 v[190:193], v168 offset:32768
	ds_read_b128 v[194:197], v168 offset:33792
	ds_read_b128 v[198:201], v168 offset:34816
	ds_read_b128 v[202:205], v168 offset:35840
	ds_read_b128 v[206:209], v168 offset:36864
	ds_read_b128 v[210:213], v168 offset:37888
	ds_read_b128 v[214:217], v168 offset:38912
	ds_read_b128 v[218:221], v168 offset:39936
	v_cndmask_b32_e32 v137, v138, v173, vcc
	global_load_lds_dwordx4 v132, s[0:1]
	s_mov_b32 m0, s31
	s_nop 0
	global_load_lds_dwordx4 v137, s[0:1]
	s_waitcnt lgkmcnt(8)
	s_barrier
; #define PG8_STAGE(bufoff, gbase, voff) do { _Pragma("unroll") for (int _i = 0; _i < 2; ++_i) \
;         __builtin_amdgcn_global_load_lds((const unsigned*)((const char*)(gbase) + (voff)[_i]), (LAS unsigned*)(lds + (bufoff) + ldsw + _i * 8192), 16, 0, 0); } while (0)
; #define PG8_LDA(dst, b, h) do { _Pragma("unroll") for (int m = 0; m < 4; ++m) _Pragma("unroll") for (int k = 0; k < 2; ++k) dst[m][k] = *(const LAS bf16x8*)(lds + PG8_SA(b, h) + aoff + m * 2048 + k * 1024); } while (0)
; #define PG8_LDB(dst, b, h) do { _Pragma("unroll") for (int n = 0; n < 2; ++n) _Pragma("unroll") for (int k = 0; k < 2; ++k) dst[n][k] = *(const LAS bf16x8*)(lds + PG8_SB(b, h) + boff + n * 2048 + k * 1024); } while (0)
; #define PG8_MMA(ai, bj, At, Bt) do { __builtin_amdgcn_s_setprio(1); _Pragma("unroll") for (int m = 0; m < 4; ++m) _Pragma("unroll") for (int n = 0; n < 2; ++n) _Pragma("unroll") for (int k = 0; k < 2; ++k) \
;         acc[ai][bj][m][n] = __builtin_amdgcn_mfma_f32_16x16x32_bf16(Bt[n][k], At[m][k], acc[ai][bj][m][n], 0, 0, 0); __builtin_amdgcn_s_setprio(0); } while (0)
; #define PG8_WAIT_V(n) asm volatile("s_waitcnt vmcnt(" #n ")" ::: "memory")
; #define PG8_WAIT_L(n) asm volatile("s_waitcnt lgkmcnt(" #n ")" ::: "memory")
; #define PG8_BAR __builtin_amdgcn_s_barrier()
; #define PG8_SCHED __builtin_amdgcn_sched_barrier(0)
; template <class Epi, class Sched>
; __device__ __forceinline__ void gemm_phase(LAS unsigned char* lds, const bf16_t* A, const int K, const Sched& S, const Epi& E, const int wv) {
;     ...
;             PG8_LDB(B0, 1, 0); PG8_SCHED; PG8_LDA(At, 1, 0); PG8_STAGE_A(PG8_SA(0, 1), 1, last, k2);
;             PG8_WAIT_L(8); PG8_BAR; PG8_WAIT_L(0); PG8_MMA(0, 0, At, B0); PG8_BAR; PG8_SCHED;
;             PG8_LDB(B1, 1, 1); PG8_STAGE(PG8_SB(1, 0), b3, voffB);
;             PG8_BAR; PG8_WAIT_L(0); PG8_MMA(0, 1, At, B1); PG8_BAR;
;             PG8_LDA(At, 1, 1); PG8_STAGE_A(PG8_SA(1, 0), 0, last, k3);
;             PG8_BAR; PG8_WAIT_L(0); PG8_MMA(1, 0, At, B0); PG8_BAR; PG8_SCHED;
;             PG8_STAGE(PG8_SB(1, 1), b3 + hstep, voffB);
;             PG8_WAIT_V(6); PG8_BAR; PG8_MMA(1, 1, At, B1); PG8_BAR;
;         }
	s_waitcnt lgkmcnt(0)
	s_setprio 1
	s_waitcnt lgkmcnt(0)
	v_mfma_f32_16x16x32_bf16 v[124:127], v[174:177], v[190:193], v[124:127]
	v_mfma_f32_16x16x32_bf16 v[120:123], v[182:185], v[190:193], v[120:123]
	v_mfma_f32_16x16x32_bf16 v[116:119], v[174:177], v[198:201], v[116:119]
	v_mfma_f32_16x16x32_bf16 v[108:111], v[182:185], v[198:201], v[108:111]
	v_mfma_f32_16x16x32_bf16 v[100:103], v[174:177], v[206:209], v[100:103]
	v_mfma_f32_16x16x32_bf16 v[92:95], v[182:185], v[206:209], v[92:95]
	v_mfma_f32_16x16x32_bf16 v[84:87], v[174:177], v[214:217], v[84:87]
	v_mfma_f32_16x16x32_bf16 v[76:79], v[182:185], v[214:217], v[76:79]
	v_mfma_f32_16x16x32_bf16 v[124:127], v[178:181], v[194:197], v[124:127]
	v_mfma_f32_16x16x32_bf16 v[120:123], v[186:189], v[194:197], v[120:123]
	v_mfma_f32_16x16x32_bf16 v[116:119], v[178:181], v[202:205], v[116:119]
	v_mfma_f32_16x16x32_bf16 v[108:111], v[186:189], v[202:205], v[108:111]
	v_mfma_f32_16x16x32_bf16 v[100:103], v[178:181], v[210:213], v[100:103]
	v_mfma_f32_16x16x32_bf16 v[92:95], v[186:189], v[210:213], v[92:95]
	v_mfma_f32_16x16x32_bf16 v[84:87], v[178:181], v[218:221], v[84:87]
	v_mfma_f32_16x16x32_bf16 v[76:79], v[186:189], v[218:221], v[76:79]
	s_setprio 0
	s_barrier
	s_mov_b32 m0, s62
	v_add_u32_e32 v132, s61, v150
	v_lshl_add_u64 v[238:239], v[238:239], 0, s[8:9]
	ds_read_b128 v[222:225], v132
	ds_read_b128 v[226:229], v132 offset:1024
	ds_read_b128 v[230:233], v132 offset:2048
	ds_read_b128 v[234:237], v132 offset:3072
	global_load_lds_dwordx4 v[238:239], off
	v_lshl_add_u64 v[238:239], v[240:241], 0, s[8:9]
	s_mov_b32 m0, s63
	s_nop 0
	global_load_lds_dwordx4 v[238:239], off
	s_barrier
	s_waitcnt lgkmcnt(0)
	s_setprio 1
	s_waitcnt lgkmcnt(0)
	v_mfma_f32_16x16x32_bf16 v[112:115], v[222:225], v[190:193], v[112:115]
	v_mfma_f32_16x16x32_bf16 v[104:107], v[230:233], v[190:193], v[104:107]
	v_mfma_f32_16x16x32_bf16 v[96:99], v[222:225], v[198:201], v[96:99]
	v_mfma_f32_16x16x32_bf16 v[88:91], v[230:233], v[198:201], v[88:91]
	v_mfma_f32_16x16x32_bf16 v[80:83], v[222:225], v[206:209], v[80:83]
	v_mfma_f32_16x16x32_bf16 v[72:75], v[230:233], v[206:209], v[72:75]
	v_mfma_f32_16x16x32_bf16 v[52:55], v[222:225], v[214:217], v[52:55]
	v_mfma_f32_16x16x32_bf16 v[48:51], v[230:233], v[214:217], v[48:51]
	v_mfma_f32_16x16x32_bf16 v[112:115], v[226:229], v[194:197], v[112:115]
	v_mfma_f32_16x16x32_bf16 v[104:107], v[234:237], v[194:197], v[104:107]
	v_mfma_f32_16x16x32_bf16 v[96:99], v[226:229], v[202:205], v[96:99]
	v_mfma_f32_16x16x32_bf16 v[88:91], v[234:237], v[202:205], v[88:91]
	v_mfma_f32_16x16x32_bf16 v[80:83], v[226:229], v[210:213], v[80:83]
	v_mfma_f32_16x16x32_bf16 v[72:75], v[234:237], v[210:213], v[72:75]
	v_mfma_f32_16x16x32_bf16 v[52:55], v[226:229], v[218:221], v[52:55]
	v_mfma_f32_16x16x32_bf16 v[48:51], v[234:237], v[218:221], v[48:51]
	s_setprio 0
	s_mov_b32 m0, s34
	v_lshl_add_u64 v[238:239], v[244:245], 0, s[8:9]
	s_barrier
	ds_read_b128 v[190:193], v168 offset:49152
	ds_read_b128 v[194:197], v168 offset:50176
	ds_read_b128 v[198:201], v168 offset:51200
	ds_read_b128 v[202:205], v168 offset:52224
	ds_read_b128 v[206:209], v168 offset:53248
	ds_read_b128 v[210:213], v168 offset:54272
	ds_read_b128 v[214:217], v168 offset:55296
	ds_read_b128 v[218:221], v168 offset:56320
	global_load_lds_dwordx4 v[238:239], off
	v_lshl_add_u64 v[238:239], v[242:243], 0, s[8:9]
	s_mov_b32 m0, s35
	s_nop 0
	global_load_lds_dwordx4 v[238:239], off
	s_barrier
	s_waitcnt lgkmcnt(0)
	s_setprio 1
	s_waitcnt lgkmcnt(0)
	v_mfma_f32_16x16x32_bf16 v[20:23], v[174:177], v[190:193], v[20:23]
	v_mfma_f32_16x16x32_bf16 v[8:11], v[182:185], v[190:193], v[8:11]
	v_mfma_f32_16x16x32_bf16 v[40:43], v[174:177], v[198:201], v[40:43]
	v_mfma_f32_16x16x32_bf16 v[44:47], v[182:185], v[198:201], v[44:47]
	v_mfma_f32_16x16x32_bf16 v[24:27], v[174:177], v[206:209], v[24:27]
	v_mfma_f32_16x16x32_bf16 v[28:31], v[182:185], v[206:209], v[28:31]
	v_mfma_f32_16x16x32_bf16 v[0:3], v[174:177], v[214:217], v[0:3]
	v_mfma_f32_16x16x32_bf16 v[4:7], v[182:185], v[214:217], v[4:7]
	v_mfma_f32_16x16x32_bf16 v[20:23], v[178:181], v[194:197], v[20:23]
	v_mfma_f32_16x16x32_bf16 v[8:11], v[186:189], v[194:197], v[8:11]
	v_mfma_f32_16x16x32_bf16 v[40:43], v[178:181], v[202:205], v[40:43]
	v_mfma_f32_16x16x32_bf16 v[44:47], v[186:189], v[202:205], v[44:47]
	v_mfma_f32_16x16x32_bf16 v[24:27], v[178:181], v[210:213], v[24:27]
	v_mfma_f32_16x16x32_bf16 v[28:31], v[186:189], v[210:213], v[28:31]
	v_mfma_f32_16x16x32_bf16 v[0:3], v[178:181], v[218:221], v[0:3]
	v_mfma_f32_16x16x32_bf16 v[4:7], v[186:189], v[218:221], v[4:7]
	s_setprio 0
	s_barrier
	s_add_u32 s0, s24, 0x40080
	s_addc_u32 s1, s25, 0
	s_mov_b32 m0, s64
	v_lshl_add_u64 v[174:175], s[0:1], 0, v[128:129]
	global_load_lds_dwordx4 v[174:175], off
	v_lshl_add_u64 v[174:175], s[0:1], 0, v[130:131]
	s_mov_b32 m0, s65
	s_nop 0
	global_load_lds_dwordx4 v[174:175], off
	s_waitcnt vmcnt(6)
	s_barrier
	s_setprio 1
	v_mfma_f32_16x16x32_bf16 v[64:67], v[222:225], v[190:193], v[64:67]
	v_mfma_f32_16x16x32_bf16 v[68:71], v[230:233], v[190:193], v[68:71]
	v_mfma_f32_16x16x32_bf16 v[56:59], v[222:225], v[198:201], v[56:59]
	v_mfma_f32_16x16x32_bf16 v[60:63], v[230:233], v[198:201], v[60:63]
	v_mfma_f32_16x16x32_bf16 v[32:35], v[222:225], v[206:209], v[32:35]
	v_mfma_f32_16x16x32_bf16 v[36:39], v[230:233], v[206:209], v[36:39]
	v_mfma_f32_16x16x32_bf16 v[12:15], v[222:225], v[214:217], v[12:15]
	v_mfma_f32_16x16x32_bf16 v[16:19], v[230:233], v[214:217], v[16:19]
	v_mfma_f32_16x16x32_bf16 v[64:67], v[226:229], v[194:197], v[64:67]
	v_mfma_f32_16x16x32_bf16 v[68:71], v[234:237], v[194:197], v[68:71]
	v_mfma_f32_16x16x32_bf16 v[56:59], v[226:229], v[202:205], v[56:59]
	v_mfma_f32_16x16x32_bf16 v[60:63], v[234:237], v[202:205], v[60:63]
	v_mfma_f32_16x16x32_bf16 v[32:35], v[226:229], v[210:213], v[32:35]
	v_mfma_f32_16x16x32_bf16 v[36:39], v[234:237], v[210:213], v[36:39]
	v_mfma_f32_16x16x32_bf16 v[12:15], v[226:229], v[218:221], v[12:15]
	v_mfma_f32_16x16x32_bf16 v[16:19], v[234:237], v[218:221], v[16:19]
	s_setprio 0
	s_add_i32 s68, s68, 2
	s_cmp_gt_u32 s68, 13
	s_mov_b64 s[0:1], s[22:23]
	s_cbranch_scc1 .Lmy_kx_7
	s_barrier
	s_branch .LBB0_2221

; #define PG8_WAIT_V(n) asm volatile("s_waitcnt vmcnt(" #n ")" ::: "memory")
; #define PG8_BAR __builtin_amdgcn_s_barrier()
; template <class Epi, class Sched>
; __device__ __forceinline__ void gemm_phase(LAS unsigned char* lds, const bf16_t* A, const int K, const Sched& S, const Epi& E, const int wv) {
;     ...
;     PG8_WAIT_V(0);
;     if (wr == 0) PG8_BAR;
;     PG8_BAR;
.LBB0_2238:
	s_waitcnt vmcnt(0)
	s_cmpk_gt_u32 s26, 0xff
	s_cbranch_scc1 .LBB0_2240
.LBB0_2240:
	s_barrier
